# speedup vs baseline: 1.0925x; 1.0789x over previous
.LBB0_9:
	s_or_b64 exec, exec, s[22:23]
	v_ashrrev_i32_e32 v5, 31, v4
	s_waitcnt lgkmcnt(0)
	v_lshl_add_u64 v[4:5], v[4:5], 4, s[20:21]
	global_store_dwordx4 v[4:5], v[0:3], off sc1

.LBB0_11:
	s_andn2_saveexec_b64 s[20:21], s[8:9]
	s_cbranch_execz .LBB0_13
	s_load_dwordx4 s[8:11], s[0:1], 0x48
	v_subrev_u32_e32 v0, s17, v0
	v_ashrrev_i32_e32 v4, 2, v0
	v_ashrrev_i32_e32 v5, 31, v4
	v_and_b32_e32 v10, 3, v0
	v_lshlrev_b64 v[0:1], 6, v[4:5]
	s_waitcnt lgkmcnt(0)
	v_lshl_add_u64 v[0:1], s[8:9], 0, v[0:1]
	v_lshlrev_b32_e32 v6, 4, v10
	v_mov_b32_e32 v7, 0
	v_lshl_add_u64 v[0:1], v[0:1], 0, v[6:7]
	global_load_dwordx4 v[0:3], v[0:1], off
	v_lshrrev_b32_e32 v5, 23, v5
	v_add_u32_e32 v5, v4, v5
	v_ashrrev_i32_e32 v8, 9, v5
	v_mul_i32_i24_e32 v5, 0x200, v8
	v_ashrrev_i32_e32 v9, 31, v8
	v_sub_u32_e32 v4, v4, v5
	v_lshlrev_b32_e32 v6, 9, v10
	v_lshlrev_b64 v[8:9], 15, v[8:9]
	v_ashrrev_i32_e32 v5, 31, v4
	s_mov_b32 s8, 0xbfb8aa3b
	v_lshl_add_u64 v[8:9], s[10:11], 0, v[8:9]
	v_lshl_add_u64 v[4:5], v[4:5], 0, v[6:7]
	v_lshl_add_u64 v[4:5], v[4:5], 4, v[8:9]
	s_waitcnt vmcnt(0)
	v_mul_f32_e32 v0, 0x3fb8aa3b, v0
	v_mul_f32_e32 v1, 0x3fb8aa3b, v1
	v_mul_f32_e32 v2, 0x3fb8aa3b, v2
	v_mul_f32_e32 v3, 0x3fb8aa3b, v3
	v_exp_f32_e32 v0, v0
	v_exp_f32_e32 v1, v1
	v_exp_f32_e32 v2, v2
	v_exp_f32_e32 v3, v3
	v_pk_mul_f32 v[0:1], v[0:1], s[8:9] op_sel_hi:[1,0]
	v_pk_mul_f32 v[2:3], v[2:3], s[8:9] op_sel_hi:[1,0]
	global_store_dwordx4 v[4:5], v[0:3], off sc1

.LBB0_20:
	v_ashrrev_i32_e32 v6, 5, v1
	v_sub_u32_e32 v7, 0, v6
	v_max_i32_e32 v7, v6, v7
	v_cvt_f32_u32_e32 v8, v7
	v_sub_u32_e32 v12, 0, v7
	v_ashrrev_i32_e32 v9, 6, v0
	v_sub_u32_e32 v11, 0, v9
	v_rcp_iflag_f32_e32 v8, v8
	v_max_i32_e32 v11, v9, v11
	v_xor_b32_e32 v10, v9, v6
	v_ashrrev_i32_e32 v10, 31, v10
	v_mul_f32_e32 v8, 0x4f7ffffe, v8
	v_cvt_u32_f32_e32 v8, v8
	v_mul_lo_u32 v12, v12, v8
	v_mul_hi_u32 v12, v8, v12
	v_add_u32_e32 v8, v8, v12
	v_mul_hi_u32 v8, v11, v8
	v_mul_lo_u32 v12, v8, v7
	v_sub_u32_e32 v11, v11, v12
	v_add_u32_e32 v13, 1, v8
	v_cmp_ge_u32_e32 vcc, v11, v7
	v_sub_u32_e32 v12, v11, v7
	s_nop 0
	v_cndmask_b32_e32 v8, v8, v13, vcc
	v_cndmask_b32_e32 v11, v11, v12, vcc
	v_add_u32_e32 v12, 1, v8
	v_cmp_ge_u32_e32 vcc, v11, v7
	s_nop 1
	v_cndmask_b32_e32 v7, v8, v12, vcc
	v_xor_b32_e32 v7, v7, v10
	v_sub_u32_e32 v7, v7, v10
	v_mul_lo_u32 v6, v7, v6
	v_sub_u32_e32 v8, v9, v6
	v_and_b32_e32 v6, 15, v0
	v_lshl_or_b32 v6, v7, 4, v6
	v_mad_i64_i32 v[6:7], s[0:1], v6, v1, 0
	v_lshl_add_u64 v[4:5], v[6:7], 2, v[4:5]
	v_lshlrev_b32_e32 v6, 5, v8
	v_ashrrev_i32_e32 v7, 31, v6
	v_lshlrev_b32_e32 v1, 1, v0
	v_lshl_add_u64 v[4:5], v[6:7], 2, v[4:5]
	v_and_b32_e32 v6, 0x60, v1
	v_mov_b32_e32 v7, 0
	v_lshl_add_u64 v[12:13], v[4:5], 0, v[6:7]
	global_load_dwordx4 v[4:7], v[12:13], off
	global_load_dwordx4 v[8:11], v[12:13], off offset:16
	v_ashrrev_i32_e32 v1, 31, v0
	v_lshl_add_u64 v[0:1], v[0:1], 4, v[2:3]
	s_waitcnt vmcnt(1)
	v_cvt_f16_f32_e32 v4, v4
	v_cvt_pk_f16_f32 v12, v5, v6
	s_waitcnt vmcnt(0)
	v_cvt_pk_f16_f32 v6, v7, v8
	v_cvt_f16_f32_e32 v8, v11
	v_cvt_pk_f16_f32 v7, v9, v10
	v_alignbit_b32 v5, v6, v12, 16
	v_alignbit_b32 v6, v7, v6, 16
	v_pack_b32_f16 v4, v4, v12
	v_alignbit_b32 v7, v8, v7, 16
	global_store_dwordx4 v[0:1], v[4:7], off sc1
	s_endpgm

_Z10k_ka_firstPKfPKiPfS0_S0_PKDF16_PDF16_:
	s_load_dwordx8 s[4:11], s[0:1], 0x0
	s_lshl_b32 s3, s2, 5
	s_and_b32 s3, s3, 0xe0
	s_lshr_b32 s12, s2, 3
	s_or_b32 s14, s3, s12
	v_or_b32_e32 v1, 0x200, v0
	s_lshl_b32 s51, s14, 5
	v_mov_b32_e32 v75, 0
	v_lshrrev_b32_e32 v26, 6, v0
	v_lshrrev_b32_e32 v27, 6, v1
	v_or_b32_e32 v1, 0x600, v0
	v_or_b32_e32 v2, s51, v26
	v_mov_b32_e32 v3, v75
	v_lshrrev_b32_e32 v28, 6, v1
	s_waitcnt lgkmcnt(0)
	v_lshl_add_u64 v[2:3], v[2:3], 2, s[6:7]
	v_or_b32_e32 v4, s51, v27
	v_mov_b32_e32 v5, v75
	v_or_b32_e32 v6, s51, v28
	v_mov_b32_e32 v7, v75
	v_lshl_add_u64 v[4:5], v[4:5], 2, s[6:7]
	v_lshl_add_u64 v[6:7], v[6:7], 2, s[6:7]
	global_load_dword v8, v[2:3], off
	global_load_dword v10, v[4:5], off
	global_load_dword v12, v[6:7], off
	global_load_dword v14, v[2:3], off offset:64
	v_and_b32_e32 v29, 63, v0
	v_lshlrev_b32_e32 v74, 4, v29
	v_lshl_add_u64 v[2:3], s[4:5], 0, v[74:75]
	s_movk_i32 s16, 0x410
	s_bfe_u32 s40, s2, 0x30003
	s_mov_b32 s3, 0
	s_lshl_b32 s2, s40, 10
	s_movk_i32 s48, 0x2000
	s_movk_i32 s49, 0x4000
	s_movk_i32 s33, 0x6000
	s_movk_i32 s18, 0x210
	s_mov_b32 s21, s3
	s_mov_b32 s27, s3
	v_mov_b32_e32 v80, 0x3727c5ac
	s_mov_b32 s39, 0x800000
	s_mov_b32 s23, s3
	s_mov_b32 s25, s3
	s_mov_b64 s[36:37], 0x40000
	s_mov_b32 s29, s3
	s_mov_b32 s31, s3
	s_mov_b32 s35, 0x14000
	s_mov_b32 s34, 0x3b800000
	v_and_b32_e32 v86, 15, v0
	s_mov_b32 s17, s3
	s_mov_b32 s15, s3
	s_lshl_b32 s52, s40, 5
	v_lshl_add_u64 v[102:103], s[8:9], 0, v[74:75]
	s_xor_b32 s44, s2, 0x1000
	s_mov_b32 s45, s3
	s_mov_b32 s43, s3
	s_mov_b32 s47, s3
	s_movk_i32 s50, 0x1c0
	s_waitcnt vmcnt(3)
	v_ashrrev_i32_e32 v9, 31, v8
	s_waitcnt vmcnt(2)
	v_ashrrev_i32_e32 v11, 31, v10
	s_waitcnt vmcnt(1)
	v_ashrrev_i32_e32 v13, 31, v12
	s_waitcnt vmcnt(0)
	v_ashrrev_i32_e32 v15, 31, v14
	v_lshlrev_b64 v[4:5], 10, v[8:9]
	v_lshlrev_b64 v[6:7], 10, v[10:11]
	v_lshlrev_b64 v[8:9], 10, v[14:15]
	v_lshlrev_b64 v[10:11], 10, v[12:13]
	v_lshl_add_u64 v[18:19], v[2:3], 0, v[4:5]
	v_lshl_add_u64 v[20:21], v[2:3], 0, v[6:7]
	v_lshl_add_u64 v[22:23], v[2:3], 0, v[8:9]
	v_lshl_add_u64 v[24:25], v[2:3], 0, v[10:11]
	global_load_dwordx4 v[2:5], v[18:19], off
	global_load_dwordx4 v[6:9], v[20:21], off
	global_load_dwordx4 v[10:13], v[22:23], off
	global_load_dwordx4 v[14:17], v[24:25], off
	s_load_dwordx4 s[4:7], s[0:1], 0x20
	s_load_dwordx2 s[12:13], s[0:1], 0x30
	v_lshrrev_b32_e32 v21, 1, v0
	v_and_b32_e32 v81, 24, v21
	v_mad_u32_u24 v21, v26, s16, v74
	v_mad_u32_u24 v23, v27, s16, v74
	v_mad_u32_u24 v24, v28, s16, v74
	v_lshrrev_b32_e32 v20, 4, v0
	v_mov_b32_e32 v18, 0x14000
	v_and_b32_e32 v1, 28, v20
	v_mov_b32_e32 v19, v75
	v_lshl_or_b32 v22, v29, 3, v18
	v_lshlrev_b32_e32 v18, 13, v1
	s_waitcnt lgkmcnt(0)
	v_lshl_add_u64 v[18:19], s[6:7], 0, v[18:19]
	v_lshl_add_u64 v[78:79], v[18:19], 0, v[74:75]
	v_mad_u32_u24 v54, v1, s16, v74
	v_lshl_add_u64 v[30:31], v[78:79], 0, s[2:3]
	v_or_b32_e32 v20, 3, v20
	v_mad_u32_u24 v87, v1, s18, v22
	v_mad_u32_u24 v100, v20, s16, v74
	v_mad_u32_u24 v101, v20, s18, v22
	s_lshl_b32 s1, s40, 6
	s_add_i32 s38, s1, 64
	s_and_b32 s18, s38, 0x1c0
	s_add_i32 s0, s1, 0x80
	s_lshl_b32 s20, s18, 4
	s_and_b32 s26, s0, 0x1c0
	v_lshl_add_u64 v[46:47], v[78:79], 0, s[20:21]
	s_lshl_b32 s26, s26, 4
	v_lshl_add_u64 v[52:53], v[78:79], 0, s[26:27]
	s_lshl_b32 s19, s38, 4
	s_or_b32 s22, s19, 0x2000
	s_or_b32 s24, s19, 0x6000
	v_lshl_add_u64 v[48:49], v[78:79], 0, s[22:23]
	v_lshl_add_u64 v[50:51], v[78:79], 0, s[24:25]
	s_lshl_b32 s30, s0, 4
	s_or_b32 s28, s30, 0x2000
	s_or_b32 s30, s30, 0x6000
	v_lshl_add_u64 v[76:77], v[78:79], 0, s[36:37]
	v_lshl_add_u64 v[88:89], v[78:79], 0, s[28:29]
	v_lshl_add_u64 v[90:91], v[78:79], 0, s[30:31]
	s_add_i32 s16, s1, 0xc0
	s_and_b32 s0, s14, 0x7ffffff
	s_and_b32 s14, s16, 0x1c0
	s_lshl_b32 s41, s16, 4
	s_lshl_b32 s16, s14, 4
	v_lshl_add_u64 v[82:83], v[78:79], 0, s[16:17]
	s_or_b32 s14, s41, 0x2000
	s_or_b32 s18, s41, 0x6000
	v_lshl_add_u64 v[84:85], v[78:79], 0, s[14:15]
	s_mov_b32 s41, s3
	s_mov_b32 s37, s3
	v_lshl_add_u64 v[120:121], v[78:79], 0, s[44:45]
	v_lshl_add_u64 v[148:149], v[76:77], 0, s[2:3]
	v_lshl_add_u64 v[150:151], v[76:77], 0, s[20:21]
	v_lshl_add_u64 v[152:153], v[76:77], 0, s[22:23]
	v_lshl_add_u64 v[154:155], v[76:77], 0, s[24:25]
	v_lshl_add_u64 v[156:157], v[76:77], 0, s[26:27]
	s_waitcnt vmcnt(3)
	ds_write_b128 v21, v[2:5] offset:37376
	s_waitcnt vmcnt(2)
	ds_write_b128 v23, v[6:9] offset:37376
	s_waitcnt vmcnt(1)
	ds_write_b128 v21, v[10:13] offset:54016
	s_waitcnt vmcnt(0)
	ds_write_b128 v24, v[14:17] offset:37376
	s_waitcnt lgkmcnt(0)
	s_barrier
	global_load_dwordx4 v[66:69], v74, s[10:11]
	global_load_dwordx4 v[70:73], v74, s[4:5]
	v_add_co_u32_e32 v6, vcc, s48, v30
	ds_read_b128 v[2:5], v54 offset:37376
	s_nop 0
	v_addc_co_u32_e32 v7, vcc, 0, v31, vcc
	v_add_co_u32_e32 v8, vcc, s49, v30
	v_lshl_add_u64 v[158:159], v[76:77], 0, s[28:29]
	s_nop 0
	v_addc_co_u32_e32 v9, vcc, 0, v31, vcc
	v_add_co_u32_e32 v10, vcc, s33, v30
	v_lshl_add_u64 v[160:161], v[76:77], 0, s[30:31]
	s_nop 0
	v_addc_co_u32_e32 v11, vcc, 0, v31, vcc
	global_load_dwordx4 v[26:29], v[30:31], off
	global_load_dwordx4 v[22:25], v[6:7], off
	global_load_dwordx4 v[18:21], v[8:9], off
	global_load_dwordx4 v[14:17], v[10:11], off
	s_waitcnt lgkmcnt(0)
	v_add_f32_e32 v6, v2, v3
	v_add_f32_e32 v6, v6, v4
	v_add_f32_e32 v6, v6, v5
	v_add_co_u32_e32 v12, vcc, s49, v46
	s_nop 0
	v_add_f32_dpp v6, v6, v6 quad_perm:[1,0,3,2] row_mask:0xf bank_mask:0xf bound_ctrl:1
	v_addc_co_u32_e32 v13, vcc, 0, v47, vcc
	s_nop 0
	v_add_f32_dpp v6, v6, v6 quad_perm:[2,3,0,1] row_mask:0xf bank_mask:0xf bound_ctrl:1
	v_add_co_u32_e32 v92, vcc, s49, v52
	s_nop 0
	v_add_f32_dpp v6, v6, v6 row_half_mirror row_mask:0xf bank_mask:0xf bound_ctrl:1
	v_addc_co_u32_e32 v93, vcc, 0, v53, vcc
	s_nop 0
	v_add_f32_dpp v6, v6, v6 row_mirror row_mask:0xf bank_mask:0xf bound_ctrl:1
	s_nop 0
	v_readlane_b32 s6, v6, 16
	v_readlane_b32 s7, v6, 48
	v_readlane_b32 s4, v6, 0
	v_readlane_b32 s5, v6, 32
	v_mov_b32_e32 v6, s6
	v_mov_b32_e32 v7, s7
	v_pk_add_f32 v[6:7], s[4:5], v[6:7]
	s_nop 0
	v_add_f32_e32 v6, v6, v7
	v_mul_f32_e32 v6, 0x3b800000, v6
	v_pk_add_f32 v[8:9], v[2:3], v[6:7] op_sel_hi:[1,0] neg_lo:[0,1] neg_hi:[0,1]
	v_pk_add_f32 v[6:7], v[4:5], v[6:7] op_sel_hi:[1,0] neg_lo:[0,1] neg_hi:[0,1]
	v_pk_mul_f32 v[10:11], v[8:9], v[8:9]
	v_pk_mul_f32 v[30:31], v[6:7], v[6:7]
	v_add_f32_e32 v10, v10, v11
	v_add_f32_e32 v10, v30, v10
	v_add_f32_e32 v10, v31, v10
	global_load_dwordx4 v[42:45], v[46:47], off
	global_load_dwordx4 v[38:41], v[48:49], off
	global_load_dwordx4 v[34:37], v[12:13], off
	global_load_dwordx4 v[30:33], v[50:51], off
	v_add_f32_dpp v10, v10, v10 quad_perm:[1,0,3,2] row_mask:0xf bank_mask:0xf bound_ctrl:1
	s_nop 1
	v_add_f32_dpp v10, v10, v10 quad_perm:[2,3,0,1] row_mask:0xf bank_mask:0xf bound_ctrl:1
	s_nop 1
	v_add_f32_dpp v10, v10, v10 row_half_mirror row_mask:0xf bank_mask:0xf bound_ctrl:1
	s_nop 1
	v_add_f32_dpp v10, v10, v10 row_mirror row_mask:0xf bank_mask:0xf bound_ctrl:1
	s_nop 0
	v_readlane_b32 s6, v10, 16
	v_readlane_b32 s7, v10, 48
	v_readlane_b32 s4, v10, 0
	v_readlane_b32 s5, v10, 32
	v_mov_b32_e32 v10, s6
	v_mov_b32_e32 v11, s7
	v_pk_add_f32 v[10:11], s[4:5], v[10:11]
	s_nop 0
	v_add_f32_e32 v10, v10, v11
	v_fmamk_f32 v10, v10, 0x3b800000, v80
	v_mul_f32_e32 v11, 0x4b800000, v10
	v_cmp_gt_f32_e32 vcc, s39, v10
	s_nop 1
	v_cndmask_b32_e32 v10, v10, v11, vcc
	v_rsq_f32_e32 v10, v10
	s_nop 0
	v_mul_f32_e32 v11, 0x45800000, v10
	v_cndmask_b32_e32 v10, v10, v11, vcc
	v_pk_mul_f32 v[8:9], v[8:9], v[10:11] op_sel_hi:[1,0]
	v_pk_mul_f32 v[6:7], v[6:7], v[10:11] op_sel_hi:[1,0]
	s_waitcnt vmcnt(8)
	v_pk_fma_f32 v[8:9], v[66:67], v[8:9], v[70:71]
	v_pk_fma_f32 v[6:7], v[68:69], v[6:7], v[72:73]
	v_cvt_pk_f16_f32 v8, v8, v9
	v_cvt_pk_f16_f32 v9, v6, v7
	ds_write_b64 v87, v[8:9]
	ds_read_b128 v[6:9], v54 offset:38416
	ds_read_b128 v[10:13], v54 offset:39456
	global_load_dwordx4 v[62:65], v[52:53], off
	global_load_dwordx4 v[58:61], v[88:89], off
	global_load_dwordx4 v[54:57], v[92:93], off
	global_load_dwordx4 v[46:49], v[90:91], off
	s_waitcnt lgkmcnt(1)
	v_add_f32_e32 v50, v6, v7
	s_waitcnt lgkmcnt(0)
	v_add_f32_e32 v51, v10, v11
	v_add_f32_e32 v50, v50, v8
	v_add_f32_e32 v51, v51, v12
	v_add_f32_e32 v50, v50, v9
	v_add_f32_e32 v51, v51, v13
	s_nop 0
	v_add_f32_dpp v50, v50, v50 quad_perm:[1,0,3,2] row_mask:0xf bank_mask:0xf bound_ctrl:1
	v_add_f32_dpp v51, v51, v51 quad_perm:[1,0,3,2] row_mask:0xf bank_mask:0xf bound_ctrl:1
	s_nop 0
	v_add_f32_dpp v50, v50, v50 quad_perm:[2,3,0,1] row_mask:0xf bank_mask:0xf bound_ctrl:1
	v_add_f32_dpp v51, v51, v51 quad_perm:[2,3,0,1] row_mask:0xf bank_mask:0xf bound_ctrl:1
	s_nop 0
	v_add_f32_dpp v50, v50, v50 row_half_mirror row_mask:0xf bank_mask:0xf bound_ctrl:1
	v_add_f32_dpp v51, v51, v51 row_half_mirror row_mask:0xf bank_mask:0xf bound_ctrl:1
	s_nop 0
	v_add_f32_dpp v50, v50, v50 row_mirror row_mask:0xf bank_mask:0xf bound_ctrl:1
	v_add_f32_dpp v51, v51, v51 row_mirror row_mask:0xf bank_mask:0xf bound_ctrl:1
	v_readlane_b32 s10, v50, 16
	v_readlane_b32 s11, v50, 48
	v_readlane_b32 s19, v51, 16
	v_readlane_b32 s36, v51, 48
	v_readlane_b32 s4, v50, 0
	v_readlane_b32 s5, v50, 32
	v_readlane_b32 s6, v51, 0
	v_readlane_b32 s7, v51, 32
	v_mov_b32_e32 v50, s10
	v_mov_b32_e32 v51, s11
	v_mov_b32_e32 v52, s19
	v_mov_b32_e32 v53, s36
	v_pk_add_f32 v[50:51], s[4:5], v[50:51]
	v_pk_add_f32 v[52:53], s[6:7], v[52:53]
	v_add_f32_e32 v50, v50, v51
	v_add_f32_e32 v51, v52, v53
	v_mul_f32_e32 v50, 0x3b800000, v50
	v_mul_f32_e32 v52, 0x3b800000, v51
	v_pk_add_f32 v[88:89], v[6:7], v[50:51] op_sel_hi:[1,0] neg_lo:[0,1] neg_hi:[0,1]
	v_pk_add_f32 v[90:91], v[10:11], v[52:53] op_sel_hi:[1,0] neg_lo:[0,1] neg_hi:[0,1]
	v_pk_add_f32 v[50:51], v[8:9], v[50:51] op_sel_hi:[1,0] neg_lo:[0,1] neg_hi:[0,1]
	v_pk_add_f32 v[52:53], v[12:13], v[52:53] op_sel_hi:[1,0] neg_lo:[0,1] neg_hi:[0,1]
	v_pk_mul_f32 v[92:93], v[88:89], v[88:89]
	v_pk_mul_f32 v[96:97], v[90:91], v[90:91]
	v_pk_mul_f32 v[94:95], v[50:51], v[50:51]
	v_pk_mul_f32 v[98:99], v[52:53], v[52:53]
	v_add_f32_e32 v92, v92, v93
	v_add_f32_e32 v93, v96, v97
	v_add_f32_e32 v92, v94, v92
	v_add_f32_e32 v93, v98, v93
	v_add_f32_e32 v92, v95, v92
	v_add_f32_e32 v93, v99, v93
	s_nop 0
	v_add_f32_dpp v92, v92, v92 quad_perm:[1,0,3,2] row_mask:0xf bank_mask:0xf bound_ctrl:1
	v_add_f32_dpp v93, v93, v93 quad_perm:[1,0,3,2] row_mask:0xf bank_mask:0xf bound_ctrl:1
	s_nop 0
	v_add_f32_dpp v92, v92, v92 quad_perm:[2,3,0,1] row_mask:0xf bank_mask:0xf bound_ctrl:1
	v_add_f32_dpp v93, v93, v93 quad_perm:[2,3,0,1] row_mask:0xf bank_mask:0xf bound_ctrl:1
	s_nop 0
	v_add_f32_dpp v92, v92, v92 row_half_mirror row_mask:0xf bank_mask:0xf bound_ctrl:1
	v_add_f32_dpp v93, v93, v93 row_half_mirror row_mask:0xf bank_mask:0xf bound_ctrl:1
	s_nop 0
	v_add_f32_dpp v92, v92, v92 row_mirror row_mask:0xf bank_mask:0xf bound_ctrl:1
	v_add_f32_dpp v93, v93, v93 row_mirror row_mask:0xf bank_mask:0xf bound_ctrl:1
	v_readlane_b32 s10, v92, 16
	v_readlane_b32 s11, v92, 48
	v_readlane_b32 s19, v93, 16
	v_readlane_b32 s36, v93, 48
	v_readlane_b32 s4, v92, 0
	v_readlane_b32 s5, v92, 32
	v_readlane_b32 s6, v93, 0
	v_readlane_b32 s7, v93, 32
	v_mov_b32_e32 v92, s10
	v_mov_b32_e32 v93, s11
	v_mov_b32_e32 v94, s19
	v_mov_b32_e32 v95, s36
	v_pk_add_f32 v[92:93], s[4:5], v[92:93]
	v_pk_add_f32 v[94:95], s[6:7], v[94:95]
	v_mov_b32_e32 v97, v92
	v_mov_b32_e32 v96, v94
	v_mov_b32_e32 v92, v95
	v_pk_add_f32 v[92:93], v[96:97], v[92:93]
	s_mov_b32 s19, s3
	v_pk_fma_f32 v[92:93], v[92:93], s[34:35], v[80:81] op_sel_hi:[1,0,0]
	s_mov_b32 s11, s3
	v_mul_f32_e32 v94, 0x4b800000, v93
	v_cmp_gt_f32_e32 vcc, s39, v93
	s_nop 1
	v_cndmask_b32_e32 v93, v93, v94, vcc
	v_rsq_f32_e32 v93, v93
	v_lshl_add_u64 v[94:95], v[78:79], 0, s[18:19]
	v_mul_f32_e32 v96, 0x45800000, v93
	v_cndmask_b32_e32 v96, v93, v96, vcc
	v_pk_mul_f32 v[88:89], v[88:89], v[96:97] op_sel_hi:[1,0]
	v_cmp_gt_f32_e32 vcc, s39, v92
	v_pk_fma_f32 v[88:89], v[66:67], v[88:89], v[70:71]
	v_pk_mul_f32 v[50:51], v[50:51], v[96:97] op_sel_hi:[1,0]
	v_cvt_pk_f16_f32 v88, v88, v89
	v_mul_f32_e32 v89, 0x4b800000, v92
	v_cndmask_b32_e32 v89, v92, v89, vcc
	v_rsq_f32_e32 v92, v89
	v_pk_fma_f32 v[50:51], v[68:69], v[50:51], v[72:73]
	s_nop 0
	v_cvt_pk_f16_f32 v89, v50, v51
	v_mul_f32_e32 v50, 0x45800000, v92
	v_cndmask_b32_e32 v50, v92, v50, vcc
	v_pk_mul_f32 v[90:91], v[90:91], v[50:51] op_sel_hi:[1,0]
	v_pk_mul_f32 v[50:51], v[52:53], v[50:51] op_sel_hi:[1,0]
	v_pk_fma_f32 v[90:91], v[66:67], v[90:91], v[70:71]
	v_pk_fma_f32 v[50:51], v[68:69], v[50:51], v[72:73]
	v_cvt_pk_f16_f32 v90, v90, v91
	v_cvt_pk_f16_f32 v91, v50, v51
	ds_write2_b64 v87, v[88:89], v[90:91] offset0:66 offset1:132
	ds_read_b128 v[50:53], v100 offset:37376
	v_lshlrev_b32_e32 v87, 1, v81
	v_mul_u32_u24_e32 v88, 0x210, v86
	v_add3_u32 v87, v88, v87, s35
	v_or_b32_e32 v100, s51, v1
	s_waitcnt lgkmcnt(0)
	v_add_f32_e32 v88, v50, v51
	v_add_f32_e32 v88, v88, v52
	v_add_f32_e32 v88, v88, v53
	v_or_b32_e32 v74, 1, v100
	v_add_u32_e32 v168, s1, v87
	v_add_f32_dpp v88, v88, v88 quad_perm:[1,0,3,2] row_mask:0xf bank_mask:0xf bound_ctrl:1
	s_mov_b32 s35, s3
	s_nop 0
	v_add_f32_dpp v88, v88, v88 quad_perm:[2,3,0,1] row_mask:0xf bank_mask:0xf bound_ctrl:1
	s_nop 1
	v_add_f32_dpp v88, v88, v88 row_half_mirror row_mask:0xf bank_mask:0xf bound_ctrl:1
	s_nop 1
	v_add_f32_dpp v88, v88, v88 row_mirror row_mask:0xf bank_mask:0xf bound_ctrl:1
	s_nop 0
	v_readlane_b32 s6, v88, 16
	v_readlane_b32 s7, v88, 48
	v_readlane_b32 s4, v88, 0
	v_readlane_b32 s5, v88, 32
	v_mov_b32_e32 v88, s6
	v_mov_b32_e32 v89, s7
	v_pk_add_f32 v[88:89], s[4:5], v[88:89]
	s_nop 0
	v_add_f32_e32 v88, v88, v89
	v_mul_f32_e32 v88, 0x3b800000, v88
	v_pk_add_f32 v[90:91], v[50:51], v[88:89] op_sel_hi:[1,0] neg_lo:[0,1] neg_hi:[0,1]
	v_pk_add_f32 v[88:89], v[52:53], v[88:89] op_sel_hi:[1,0] neg_lo:[0,1] neg_hi:[0,1]
	v_pk_mul_f32 v[92:93], v[90:91], v[90:91]
	v_pk_mul_f32 v[96:97], v[88:89], v[88:89]
	v_add_f32_e32 v92, v92, v93
	v_add_f32_e32 v92, v96, v92
	v_add_f32_e32 v92, v97, v92
	s_nop 1
	v_add_f32_dpp v92, v92, v92 quad_perm:[1,0,3,2] row_mask:0xf bank_mask:0xf bound_ctrl:1
	s_nop 1
	v_add_f32_dpp v92, v92, v92 quad_perm:[2,3,0,1] row_mask:0xf bank_mask:0xf bound_ctrl:1
	s_nop 1
	v_add_f32_dpp v92, v92, v92 row_half_mirror row_mask:0xf bank_mask:0xf bound_ctrl:1
	s_nop 1
	v_add_f32_dpp v92, v92, v92 row_mirror row_mask:0xf bank_mask:0xf bound_ctrl:1
	s_nop 0
	v_readlane_b32 s6, v92, 16
	v_readlane_b32 s7, v92, 48
	v_readlane_b32 s4, v92, 0
	v_readlane_b32 s5, v92, 32
	v_mov_b32_e32 v92, s6
	v_mov_b32_e32 v93, s7
	v_pk_add_f32 v[92:93], s[4:5], v[92:93]
	s_add_i32 s4, s52, 32
	v_add_f32_e32 v92, v92, v93
	v_fmac_f32_e32 v80, 0x3b800000, v92
	v_mul_f32_e32 v92, 0x4b800000, v80
	v_cmp_gt_f32_e32 vcc, s39, v80
	s_and_b32 s4, s4, 0xe0
	s_mov_b32 s39, s3
	v_cndmask_b32_e32 v80, v80, v92, vcc
	v_rsq_f32_e32 v80, v80
	s_mov_b32 s7, s3
	v_mul_f32_e32 v92, 0x45800000, v80
	v_cndmask_b32_e32 v80, v80, v92, vcc
	v_pk_mul_f32 v[90:91], v[90:91], v[80:81] op_sel_hi:[1,0]
	v_add_co_u32_e32 v92, vcc, s49, v82
	v_pk_fma_f32 v[66:67], v[66:67], v[90:91], v[70:71]
	v_pk_mul_f32 v[70:71], v[88:89], v[80:81] op_sel_hi:[1,0]
	v_cvt_pk_f16_f32 v66, v66, v67
	v_pk_fma_f32 v[68:69], v[68:69], v[70:71], v[72:73]
	v_addc_co_u32_e32 v93, vcc, 0, v83, vcc
	v_cvt_pk_f16_f32 v67, v68, v69
	ds_write_b64 v101, v[66:67]
	s_waitcnt lgkmcnt(0)
	s_barrier
	global_load_dwordx4 v[66:69], v[82:83], off
	global_load_dwordx4 v[70:73], v[84:85], off
	s_nop 0
	global_load_dwordx4 v[82:85], v[92:93], off
	global_load_dwordx4 v[88:91], v[94:95], off
	v_lshl_add_u32 v80, s4, 1, v87
	s_add_i32 s4, s1, 0x140
	s_and_b32 s5, s4, 0x1c0
	s_lshl_b32 s4, s4, 4
	s_or_b32 s46, s4, 0x2000
	s_or_b32 s40, s4, 0x6000
	s_sub_i32 s4, s38, s52
	s_and_b32 s4, s4, 0xe0
	v_lshl_add_u32 v169, s4, 1, v87
	s_add_i32 s4, s1, 0x180
	s_lshl_b32 s42, s5, 4
	s_and_b32 s5, s4, 0x1c0
	s_lshl_b32 s4, s4, 4
	s_or_b32 s38, s4, 0x2000
	s_or_b32 s34, s4, 0x6000
	s_add_i32 s4, s52, 0x60
	v_mov_b32_e32 v101, v75
	s_and_b32 s4, s4, 0xe0
	v_lshlrev_b64 v[92:93], 10, v[100:101]
	v_lshl_add_u32 v170, s4, 1, v87
	s_add_i32 s4, s1, 0x1c0
	s_xor_b32 s1, s1, 0x100
	v_lshl_add_u64 v[162:163], v[102:103], 0, v[92:93]
	v_lshlrev_b64 v[92:93], 10, v[74:75]
	v_add_u32_e32 v171, s1, v87
	s_add_i32 s1, s52, 0xa0
	v_lshl_add_u64 v[164:165], v[102:103], 0, v[92:93]
	ds_read_b128 v[92:95], v168
	ds_read_b128 v[96:99], v168 offset:8448
	s_and_b32 s1, s1, 0xe0
	v_lshl_add_u32 v172, s1, 1, v87
	s_add_i32 s1, s52, 0xc0
	v_or_b32_e32 v74, 2, v100
	s_lshl_b32 s36, s5, 4
	s_and_b32 s5, s4, 0x1c0
	s_lshl_b32 s4, s4, 4
	s_and_b32 s1, s1, 0xe0
	s_addk_i32 s52, 0xe0
	v_lshlrev_b64 v[104:105], 10, v[74:75]
	v_or_b32_e32 v74, 3, v100
	s_lshl_b32 s6, s5, 4
	s_or_b32 s10, s4, 0x2000
	s_or_b32 s4, s4, 0x6000
	s_mov_b32 s5, s3
	v_lshl_add_u32 v173, s1, 1, v87
	s_and_b32 s1, s52, 0xe0
	v_lshlrev_b64 v[74:75], 10, v[74:75]
	v_lshl_add_u64 v[132:133], v[78:79], 0, s[42:43]
	v_lshl_add_u64 v[134:135], v[78:79], 0, s[46:47]
	v_lshl_add_u64 v[136:137], v[78:79], 0, s[40:41]
	v_lshl_add_u64 v[138:139], v[78:79], 0, s[36:37]
	v_lshl_add_u64 v[140:141], v[78:79], 0, s[38:39]
	v_lshl_add_u64 v[142:143], v[78:79], 0, s[34:35]
	v_lshl_add_u64 v[144:145], v[78:79], 0, s[6:7]
	v_lshl_add_u64 v[146:147], v[78:79], 0, s[10:11]
	v_lshl_add_u64 v[78:79], v[78:79], 0, s[4:5]
	v_lshl_add_u32 v87, s1, 1, v87
	v_lshl_add_u64 v[166:167], v[102:103], 0, v[104:105]
	v_lshl_add_u64 v[74:75], v[102:103], 0, v[74:75]
	s_setprio 1
	s_waitcnt vmcnt(15) lgkmcnt(1)
	v_mfma_f32_16x16x32_f16 v[100:103], v[92:95], v[26:29], 0
	s_waitcnt lgkmcnt(0)
	v_mfma_f32_16x16x32_f16 v[26:29], v[96:99], v[26:29], 0
	s_waitcnt vmcnt(14)
	v_mfma_f32_16x16x32_f16 v[104:107], v[92:95], v[22:25], 0
	v_mfma_f32_16x16x32_f16 v[22:25], v[96:99], v[22:25], 0
	s_waitcnt vmcnt(13)
	v_mfma_f32_16x16x32_f16 v[108:111], v[92:95], v[18:21], 0
	v_mfma_f32_16x16x32_f16 v[18:21], v[96:99], v[18:21], 0
	s_waitcnt vmcnt(12)
	v_mfma_f32_16x16x32_f16 v[92:95], v[92:95], v[14:17], 0
	v_mfma_f32_16x16x32_f16 v[14:17], v[96:99], v[14:17], 0
	s_setprio 0
	v_add_co_u32_e32 v112, vcc, s48, v120
	global_load_dwordx4 v[96:99], v[120:121], off
	s_nop 0
	v_addc_co_u32_e32 v113, vcc, 0, v121, vcc
	v_add_co_u32_e32 v116, vcc, s49, v120
	s_nop 1
	v_addc_co_u32_e32 v117, vcc, 0, v121, vcc
	v_add_co_u32_e32 v120, vcc, s33, v120
	global_load_dwordx4 v[112:115], v[112:113], off
	s_nop 0
	global_load_dwordx4 v[116:119], v[116:117], off
	v_addc_co_u32_e32 v121, vcc, 0, v121, vcc
	global_load_dwordx4 v[120:123], v[120:121], off
	ds_read_b128 v[124:127], v80
	ds_read_b128 v[128:131], v80 offset:8448
	s_setprio 1
	s_waitcnt vmcnt(15) lgkmcnt(1)
	v_mfma_f32_16x16x32_f16 v[100:103], v[124:127], v[42:45], v[100:103]
	s_waitcnt lgkmcnt(0)
	v_mfma_f32_16x16x32_f16 v[26:29], v[128:131], v[42:45], v[26:29]
	s_waitcnt vmcnt(14)
	v_mfma_f32_16x16x32_f16 v[42:45], v[124:127], v[38:41], v[104:107]
	v_mfma_f32_16x16x32_f16 v[22:25], v[128:131], v[38:41], v[22:25]
	s_waitcnt vmcnt(13)
	v_mfma_f32_16x16x32_f16 v[38:41], v[124:127], v[34:37], v[108:111]
	v_mfma_f32_16x16x32_f16 v[18:21], v[128:131], v[34:37], v[18:21]
	s_waitcnt vmcnt(12)
	v_mfma_f32_16x16x32_f16 v[34:37], v[124:127], v[30:33], v[92:95]
	v_mfma_f32_16x16x32_f16 v[14:17], v[128:131], v[30:33], v[14:17]
	s_setprio 0
	v_add_co_u32_e32 v104, vcc, s49, v132
	global_load_dwordx4 v[30:33], v[132:133], off
	global_load_dwordx4 v[92:95], v[134:135], off
	v_addc_co_u32_e32 v105, vcc, 0, v133, vcc
	global_load_dwordx4 v[104:107], v[104:105], off
	s_nop 0
	global_load_dwordx4 v[108:111], v[136:137], off
	ds_read_b128 v[124:127], v169
	ds_read_b128 v[128:131], v169 offset:8448
	s_setprio 1
	s_waitcnt vmcnt(15) lgkmcnt(1)
	v_mfma_f32_16x16x32_f16 v[100:103], v[124:127], v[62:65], v[100:103]
	s_waitcnt lgkmcnt(0)
	v_mfma_f32_16x16x32_f16 v[26:29], v[128:131], v[62:65], v[26:29]
	s_waitcnt vmcnt(14)
	v_mfma_f32_16x16x32_f16 v[42:45], v[124:127], v[58:61], v[42:45]
	v_mfma_f32_16x16x32_f16 v[22:25], v[128:131], v[58:61], v[22:25]
	s_waitcnt vmcnt(13)
	v_mfma_f32_16x16x32_f16 v[38:41], v[124:127], v[54:57], v[38:41]
	v_mfma_f32_16x16x32_f16 v[18:21], v[128:131], v[54:57], v[18:21]
	s_waitcnt vmcnt(12)
	v_mfma_f32_16x16x32_f16 v[34:37], v[124:127], v[46:49], v[34:37]
	v_mfma_f32_16x16x32_f16 v[14:17], v[128:131], v[46:49], v[14:17]
	s_setprio 0
	v_add_co_u32_e32 v58, vcc, s49, v138
	global_load_dwordx4 v[46:49], v[138:139], off
	global_load_dwordx4 v[54:57], v[140:141], off
	v_addc_co_u32_e32 v59, vcc, 0, v139, vcc
	global_load_dwordx4 v[58:61], v[58:59], off
	s_nop 0
	global_load_dwordx4 v[62:65], v[142:143], off
	ds_read_b128 v[124:127], v170
	ds_read_b128 v[128:131], v170 offset:8448
	s_setprio 1
	s_waitcnt vmcnt(15) lgkmcnt(1)
	v_mfma_f32_16x16x32_f16 v[100:103], v[124:127], v[66:69], v[100:103]
	s_waitcnt lgkmcnt(0)
	v_mfma_f32_16x16x32_f16 v[26:29], v[128:131], v[66:69], v[26:29]
	s_waitcnt vmcnt(14)
	v_mfma_f32_16x16x32_f16 v[42:45], v[124:127], v[70:73], v[42:45]
	v_mfma_f32_16x16x32_f16 v[22:25], v[128:131], v[70:73], v[22:25]
	s_waitcnt vmcnt(13)
	v_mfma_f32_16x16x32_f16 v[38:41], v[124:127], v[82:85], v[38:41]
	v_mfma_f32_16x16x32_f16 v[18:21], v[128:131], v[82:85], v[18:21]
	s_waitcnt vmcnt(12)
	v_mfma_f32_16x16x32_f16 v[34:37], v[124:127], v[88:91], v[34:37]
	v_mfma_f32_16x16x32_f16 v[14:17], v[128:131], v[88:91], v[14:17]
	s_setprio 0
	v_add_co_u32_e32 v82, vcc, s49, v144
	global_load_dwordx4 v[66:69], v[144:145], off
	global_load_dwordx4 v[70:73], v[146:147], off
	v_addc_co_u32_e32 v83, vcc, 0, v145, vcc
	global_load_dwordx4 v[82:85], v[82:83], off
	s_nop 0
	global_load_dwordx4 v[88:91], v[78:79], off
	ds_read_b128 v[124:127], v171
	ds_read_b128 v[128:131], v171 offset:8448
	s_setprio 1
	s_waitcnt vmcnt(15) lgkmcnt(1)
	v_mfma_f32_16x16x32_f16 v[100:103], v[124:127], v[96:99], v[100:103]
	s_waitcnt lgkmcnt(0)
	v_mfma_f32_16x16x32_f16 v[26:29], v[128:131], v[96:99], v[26:29]
	s_waitcnt vmcnt(14)
	v_mfma_f32_16x16x32_f16 v[42:45], v[124:127], v[112:115], v[42:45]
	v_mfma_f32_16x16x32_f16 v[22:25], v[128:131], v[112:115], v[22:25]
	s_waitcnt vmcnt(13)
	v_mfma_f32_16x16x32_f16 v[38:41], v[124:127], v[116:119], v[38:41]
	v_mfma_f32_16x16x32_f16 v[18:21], v[128:131], v[116:119], v[18:21]
	s_waitcnt vmcnt(12)
	v_mfma_f32_16x16x32_f16 v[34:37], v[124:127], v[120:123], v[34:37]
	v_mfma_f32_16x16x32_f16 v[14:17], v[128:131], v[120:123], v[14:17]
	s_setprio 0
	ds_read_b128 v[96:99], v172
	ds_read_b128 v[112:115], v172 offset:8448
	s_setprio 1
	s_waitcnt vmcnt(11) lgkmcnt(1)
	v_mfma_f32_16x16x32_f16 v[100:103], v[96:99], v[30:33], v[100:103]
	s_waitcnt lgkmcnt(0)
	v_mfma_f32_16x16x32_f16 v[26:29], v[112:115], v[30:33], v[26:29]
	s_waitcnt vmcnt(10)
	v_mfma_f32_16x16x32_f16 v[30:33], v[96:99], v[92:95], v[42:45]
	v_mfma_f32_16x16x32_f16 v[22:25], v[112:115], v[92:95], v[22:25]
	s_waitcnt vmcnt(9)
	v_mfma_f32_16x16x32_f16 v[38:41], v[96:99], v[104:107], v[38:41]
	v_mfma_f32_16x16x32_f16 v[18:21], v[112:115], v[104:107], v[18:21]
	s_waitcnt vmcnt(8)
	v_mfma_f32_16x16x32_f16 v[34:37], v[96:99], v[108:111], v[34:37]
	v_mfma_f32_16x16x32_f16 v[14:17], v[112:115], v[108:111], v[14:17]
	s_setprio 0
	ds_read_b128 v[42:45], v173
	ds_read_b128 v[92:95], v173 offset:8448
	s_setprio 1
	s_waitcnt vmcnt(7) lgkmcnt(1)
	v_mfma_f32_16x16x32_f16 v[96:99], v[42:45], v[46:49], v[100:103]
	s_waitcnt lgkmcnt(0)
	v_mfma_f32_16x16x32_f16 v[26:29], v[92:95], v[46:49], v[26:29]
	s_waitcnt vmcnt(6)
	v_mfma_f32_16x16x32_f16 v[30:33], v[42:45], v[54:57], v[30:33]
	v_mfma_f32_16x16x32_f16 v[22:25], v[92:95], v[54:57], v[22:25]
	s_waitcnt vmcnt(5)
	v_mfma_f32_16x16x32_f16 v[38:41], v[42:45], v[58:61], v[38:41]
	v_mfma_f32_16x16x32_f16 v[18:21], v[92:95], v[58:61], v[18:21]
	s_waitcnt vmcnt(4)
	v_mfma_f32_16x16x32_f16 v[34:37], v[42:45], v[62:65], v[34:37]
	v_mfma_f32_16x16x32_f16 v[14:17], v[92:95], v[62:65], v[14:17]
	s_setprio 0
	ds_read_b128 v[42:45], v87
	ds_read_b128 v[46:49], v87 offset:8448
	s_setprio 1
	s_waitcnt vmcnt(3) lgkmcnt(1)
	v_mfma_f32_16x16x32_f16 v[54:57], v[42:45], v[66:69], v[96:99]
	s_waitcnt lgkmcnt(0)
	v_mfma_f32_16x16x32_f16 v[26:29], v[46:49], v[66:69], v[26:29]
	s_waitcnt vmcnt(2)
	v_mfma_f32_16x16x32_f16 v[30:33], v[42:45], v[70:73], v[30:33]
	v_mfma_f32_16x16x32_f16 v[22:25], v[46:49], v[70:73], v[22:25]
	s_waitcnt vmcnt(1)
	v_mfma_f32_16x16x32_f16 v[38:41], v[42:45], v[82:85], v[38:41]
	v_mfma_f32_16x16x32_f16 v[18:21], v[46:49], v[82:85], v[18:21]
	s_waitcnt vmcnt(0)
	v_mfma_f32_16x16x32_f16 v[34:37], v[42:45], v[88:91], v[34:37]
	v_mfma_f32_16x16x32_f16 v[14:17], v[46:49], v[88:91], v[14:17]
	s_setprio 0
	v_add_co_u32_e32 v78, vcc, s48, v148
	v_lshlrev_b32_e32 v116, 4, v1
	s_nop 0
	v_addc_co_u32_e32 v79, vcc, 0, v149, vcc
	v_add_co_u32_e32 v42, vcc, s49, v148
	v_or_b32_e32 v1, v116, v86
	s_nop 0
	v_addc_co_u32_e32 v43, vcc, 0, v149, vcc
	v_add_co_u32_e32 v66, vcc, s33, v148
	s_movk_i32 s2, 0x50
	s_nop 0
	v_addc_co_u32_e32 v67, vcc, 0, v149, vcc
	v_add_co_u32_e32 v108, vcc, s49, v150
	v_or_b32_e32 v117, 16, v116
	s_nop 0
	v_addc_co_u32_e32 v109, vcc, 0, v151, vcc
	v_add_co_u32_e32 v110, vcc, s49, v156
	global_load_dwordx4 v[42:45], v[42:43], off
	s_nop 0
	global_load_dwordx4 v[46:49], v[66:67], off
	global_load_dwordx4 v[58:61], v[148:149], off
	global_load_dwordx4 v[62:65], v[150:151], off
	s_nop 0
	global_load_dwordx4 v[66:69], v[152:153], off
	global_load_dwordx4 v[70:73], v[154:155], off
	global_load_dwordx4 v[82:85], v[156:157], off
	global_load_dwordx4 v[88:91], v[158:159], off
	v_addc_co_u32_e32 v111, vcc, 0, v157, vcc
	global_load_dwordx4 v[92:95], v[108:109], off
	global_load_dwordx4 v[96:99], v[110:111], off
	global_load_dwordx4 v[100:103], v[78:79], off
	global_load_dwordx4 v[104:107], v[160:161], off
	s_nop 0
	global_store_dwordx4 v[162:163], v[2:5], off sc1
	global_store_dwordx4 v[164:165], v[6:9], off sc1
	global_store_dwordx4 v[166:167], v[10:13], off sc1
	global_store_dwordx4 v[74:75], v[50:53], off sc1
	v_cvt_pk_f16_f32 v3, v56, v57
	v_cvt_pk_f16_f32 v2, v54, v55
	v_mad_u32_u24 v1, v1, s2, v81
	v_or_b32_e32 v4, v117, v86
	v_or_b32_e32 v118, 32, v116
	ds_write_b64 v1, v[2:3]
	v_cvt_pk_f16_f32 v3, v32, v33
	v_cvt_pk_f16_f32 v2, v30, v31
	v_mad_u32_u24 v4, v4, s2, v81
	v_or_b32_e32 v5, v118, v86
	v_and_or_b32 v119, v0, s50, 48
	ds_write_b64 v4, v[2:3]
	v_cvt_pk_f16_f32 v3, v40, v41
	v_cvt_pk_f16_f32 v2, v38, v39
	v_mad_u32_u24 v5, v5, s2, v81
	v_or_b32_e32 v6, v119, v86
	ds_write_b64 v5, v[2:3]
	v_cvt_pk_f16_f32 v3, v36, v37
	v_cvt_pk_f16_f32 v2, v34, v35
	v_mad_u32_u24 v6, v6, s2, v81
	ds_write_b64 v6, v[2:3]
	v_cvt_pk_f16_f32 v3, v28, v29
	v_cvt_pk_f16_f32 v2, v26, v27
	ds_write_b64 v1, v[2:3] offset:32
	v_cvt_pk_f16_f32 v3, v24, v25
	v_cvt_pk_f16_f32 v2, v22, v23
	v_lshl_add_u64 v[10:11], v[76:77], 0, s[16:17]
	ds_write_b64 v4, v[2:3] offset:32
	v_cvt_pk_f16_f32 v3, v20, v21
	v_cvt_pk_f16_f32 v2, v18, v19
	v_add_co_u32_e32 v18, vcc, s49, v10
	ds_write_b64 v5, v[2:3] offset:32
	v_cvt_pk_f16_f32 v3, v16, v17
	v_cvt_pk_f16_f32 v2, v14, v15
	v_lshl_add_u64 v[12:13], v[76:77], 0, s[14:15]
	v_addc_co_u32_e32 v19, vcc, 0, v11, vcc
	ds_write_b64 v6, v[2:3] offset:32
	s_waitcnt lgkmcnt(0)
	s_barrier
	global_load_dwordx4 v[2:5], v[10:11], off
	global_load_dwordx4 v[6:9], v[12:13], off
	v_lshl_add_u64 v[20:21], v[76:77], 0, s[18:19]
	global_load_dwordx4 v[10:13], v[18:19], off
	global_load_dwordx4 v[14:17], v[20:21], off
	ds_read_b128 v[18:21], v168
	ds_read_b128 v[22:25], v168 offset:8448
	s_mov_b32 s1, s3
	s_setprio 1
	s_waitcnt vmcnt(17) lgkmcnt(1)
	v_mfma_f32_16x16x32_f16 v[26:29], v[18:21], v[58:61], 0
	s_waitcnt lgkmcnt(0)
	v_mfma_f32_16x16x32_f16 v[30:33], v[22:25], v[58:61], 0
	s_waitcnt vmcnt(9)
	v_mfma_f32_16x16x32_f16 v[34:37], v[18:21], v[100:103], 0
	v_mfma_f32_16x16x32_f16 v[38:41], v[22:25], v[100:103], 0
	v_mfma_f32_16x16x32_f16 v[50:53], v[18:21], v[42:45], 0
	v_mfma_f32_16x16x32_f16 v[42:45], v[22:25], v[42:45], 0
	v_mfma_f32_16x16x32_f16 v[18:21], v[18:21], v[46:49], 0
	v_mfma_f32_16x16x32_f16 v[22:25], v[22:25], v[46:49], 0
	s_setprio 0
	v_lshl_add_u64 v[58:59], v[76:77], 0, s[44:45]
	v_add_co_u32_e32 v60, vcc, s48, v58
	s_nop 1
	v_addc_co_u32_e32 v61, vcc, 0, v59, vcc
	v_add_co_u32_e32 v74, vcc, s49, v58
	global_load_dwordx4 v[46:49], v[58:59], off
	global_load_dwordx4 v[54:57], v[60:61], off
	v_addc_co_u32_e32 v75, vcc, 0, v59, vcc
	v_add_co_u32_e32 v78, vcc, s33, v58
	s_nop 1
	v_addc_co_u32_e32 v79, vcc, 0, v59, vcc
	global_load_dwordx4 v[58:61], v[74:75], off
	global_load_dwordx4 v[100:103], v[78:79], off
	ds_read_b128 v[108:111], v80
	ds_read_b128 v[112:115], v80 offset:8448
	s_setprio 1
	s_waitcnt lgkmcnt(1)
	v_mfma_f32_16x16x32_f16 v[26:29], v[108:111], v[62:65], v[26:29]
	s_waitcnt lgkmcnt(0)
	v_mfma_f32_16x16x32_f16 v[30:33], v[112:115], v[62:65], v[30:33]
	v_mfma_f32_16x16x32_f16 v[34:37], v[108:111], v[66:69], v[34:37]
	v_mfma_f32_16x16x32_f16 v[38:41], v[112:115], v[66:69], v[38:41]
	v_mfma_f32_16x16x32_f16 v[50:53], v[108:111], v[92:95], v[50:53]
	v_mfma_f32_16x16x32_f16 v[42:45], v[112:115], v[92:95], v[42:45]
	v_mfma_f32_16x16x32_f16 v[18:21], v[108:111], v[70:73], v[18:21]
	v_mfma_f32_16x16x32_f16 v[22:25], v[112:115], v[70:73], v[22:25]
	s_setprio 0
	v_lshl_add_u64 v[70:71], v[76:77], 0, s[42:43]
	v_add_co_u32_e32 v74, vcc, s49, v70
	v_lshl_add_u64 v[72:73], v[76:77], 0, s[46:47]
	s_nop 0
	v_addc_co_u32_e32 v75, vcc, 0, v71, vcc
	global_load_dwordx4 v[62:65], v[70:71], off
	global_load_dwordx4 v[66:69], v[72:73], off
	v_lshl_add_u64 v[78:79], v[76:77], 0, s[40:41]
	global_load_dwordx4 v[70:73], v[74:75], off
	global_load_dwordx4 v[92:95], v[78:79], off
	ds_read_b128 v[108:111], v169
	ds_read_b128 v[112:115], v169 offset:8448
	s_setprio 1
	s_waitcnt lgkmcnt(1)
	v_mfma_f32_16x16x32_f16 v[26:29], v[108:111], v[82:85], v[26:29]
	s_waitcnt lgkmcnt(0)
	v_mfma_f32_16x16x32_f16 v[30:33], v[112:115], v[82:85], v[30:33]
	v_mfma_f32_16x16x32_f16 v[34:37], v[108:111], v[88:91], v[34:37]
	v_mfma_f32_16x16x32_f16 v[38:41], v[112:115], v[88:91], v[38:41]
	v_mfma_f32_16x16x32_f16 v[50:53], v[108:111], v[96:99], v[50:53]
	v_mfma_f32_16x16x32_f16 v[42:45], v[112:115], v[96:99], v[42:45]
	s_waitcnt vmcnt(16)
	v_mfma_f32_16x16x32_f16 v[18:21], v[108:111], v[104:107], v[18:21]
	v_mfma_f32_16x16x32_f16 v[22:25], v[112:115], v[104:107], v[22:25]
	s_setprio 0
	v_lshl_add_u64 v[74:75], v[76:77], 0, s[36:37]
	v_lshl_add_u64 v[78:79], v[76:77], 0, s[38:39]
	global_load_dwordx4 v[82:85], v[74:75], off
	global_load_dwordx4 v[88:91], v[78:79], off
	v_add_co_u32_e32 v74, vcc, s49, v74
	v_lshl_add_u64 v[78:79], v[76:77], 0, s[34:35]
	s_nop 0
	v_addc_co_u32_e32 v75, vcc, 0, v75, vcc
	global_load_dwordx4 v[96:99], v[74:75], off
	global_load_dwordx4 v[104:107], v[78:79], off
	ds_read_b128 v[108:111], v170
	ds_read_b128 v[112:115], v170 offset:8448
	s_setprio 1
	s_waitcnt vmcnt(15) lgkmcnt(1)
	v_mfma_f32_16x16x32_f16 v[26:29], v[108:111], v[2:5], v[26:29]
	s_waitcnt lgkmcnt(0)
	v_mfma_f32_16x16x32_f16 v[2:5], v[112:115], v[2:5], v[30:33]
	s_waitcnt vmcnt(14)
	v_mfma_f32_16x16x32_f16 v[30:33], v[108:111], v[6:9], v[34:37]
	v_mfma_f32_16x16x32_f16 v[6:9], v[112:115], v[6:9], v[38:41]
	s_waitcnt vmcnt(13)
	v_mfma_f32_16x16x32_f16 v[34:37], v[108:111], v[10:13], v[50:53]
	v_mfma_f32_16x16x32_f16 v[10:13], v[112:115], v[10:13], v[42:45]
	s_waitcnt vmcnt(12)
	v_mfma_f32_16x16x32_f16 v[18:21], v[108:111], v[14:17], v[18:21]
	v_mfma_f32_16x16x32_f16 v[14:17], v[112:115], v[14:17], v[22:25]
	s_setprio 0
	v_lshl_add_u64 v[42:43], v[76:77], 0, s[6:7]
	v_add_co_u32_e32 v74, vcc, s49, v42
	v_lshl_add_u64 v[44:45], v[76:77], 0, s[10:11]
	s_nop 0
	v_addc_co_u32_e32 v75, vcc, 0, v43, vcc
	global_load_dwordx4 v[22:25], v[42:43], off
	global_load_dwordx4 v[38:41], v[44:45], off
	v_lshl_add_u64 v[76:77], v[76:77], 0, s[4:5]
	global_load_dwordx4 v[42:45], v[74:75], off
	global_load_dwordx4 v[50:53], v[76:77], off
	ds_read_b128 v[74:77], v171
	ds_read_b128 v[108:111], v171 offset:8448
	s_setprio 1
	s_waitcnt vmcnt(15) lgkmcnt(1)
	v_mfma_f32_16x16x32_f16 v[26:29], v[74:77], v[46:49], v[26:29]
	s_waitcnt lgkmcnt(0)
	v_mfma_f32_16x16x32_f16 v[2:5], v[108:111], v[46:49], v[2:5]
	s_waitcnt vmcnt(14)
	v_mfma_f32_16x16x32_f16 v[30:33], v[74:77], v[54:57], v[30:33]
	v_mfma_f32_16x16x32_f16 v[6:9], v[108:111], v[54:57], v[6:9]
	s_waitcnt vmcnt(13)
	v_mfma_f32_16x16x32_f16 v[34:37], v[74:77], v[58:61], v[34:37]
	v_mfma_f32_16x16x32_f16 v[10:13], v[108:111], v[58:61], v[10:13]
	s_waitcnt vmcnt(12)
	v_mfma_f32_16x16x32_f16 v[18:21], v[74:77], v[100:103], v[18:21]
	v_mfma_f32_16x16x32_f16 v[14:17], v[108:111], v[100:103], v[14:17]
	s_setprio 0
	ds_read_b128 v[46:49], v172
	ds_read_b128 v[54:57], v172 offset:8448
	s_setprio 1
	s_waitcnt vmcnt(11) lgkmcnt(1)
	v_mfma_f32_16x16x32_f16 v[26:29], v[46:49], v[62:65], v[26:29]
	s_waitcnt lgkmcnt(0)
	v_mfma_f32_16x16x32_f16 v[2:5], v[54:57], v[62:65], v[2:5]
	s_waitcnt vmcnt(10)
	v_mfma_f32_16x16x32_f16 v[30:33], v[46:49], v[66:69], v[30:33]
	v_mfma_f32_16x16x32_f16 v[6:9], v[54:57], v[66:69], v[6:9]
	s_waitcnt vmcnt(9)
	v_mfma_f32_16x16x32_f16 v[34:37], v[46:49], v[70:73], v[34:37]
	v_mfma_f32_16x16x32_f16 v[10:13], v[54:57], v[70:73], v[10:13]
	s_waitcnt vmcnt(8)
	v_mfma_f32_16x16x32_f16 v[18:21], v[46:49], v[92:95], v[18:21]
	v_mfma_f32_16x16x32_f16 v[14:17], v[54:57], v[92:95], v[14:17]
	s_setprio 0
	ds_read_b128 v[46:49], v173
	ds_read_b128 v[54:57], v173 offset:8448
	s_setprio 1
	s_waitcnt vmcnt(7) lgkmcnt(1)
	v_mfma_f32_16x16x32_f16 v[26:29], v[46:49], v[82:85], v[26:29]
	s_waitcnt lgkmcnt(0)
	v_mfma_f32_16x16x32_f16 v[2:5], v[54:57], v[82:85], v[2:5]
	s_waitcnt vmcnt(6)
	v_mfma_f32_16x16x32_f16 v[30:33], v[46:49], v[88:91], v[30:33]
	v_mfma_f32_16x16x32_f16 v[6:9], v[54:57], v[88:91], v[6:9]
	s_waitcnt vmcnt(5)
	v_mfma_f32_16x16x32_f16 v[34:37], v[46:49], v[96:99], v[34:37]
	v_mfma_f32_16x16x32_f16 v[58:61], v[54:57], v[96:99], v[10:13]
	s_waitcnt vmcnt(4)
	v_mfma_f32_16x16x32_f16 v[18:21], v[46:49], v[104:107], v[18:21]
	v_mfma_f32_16x16x32_f16 v[46:49], v[54:57], v[104:107], v[14:17]
	s_setprio 0
	ds_read_b128 v[54:57], v87
	ds_read_b128 v[62:65], v87 offset:8448
	s_setprio 1
	s_waitcnt vmcnt(3) lgkmcnt(1)
	v_mfma_f32_16x16x32_f16 v[26:29], v[54:57], v[22:25], v[26:29]
	s_waitcnt lgkmcnt(0)
	v_mfma_f32_16x16x32_f16 v[14:17], v[62:65], v[22:25], v[2:5]
	s_waitcnt vmcnt(2)
	v_mfma_f32_16x16x32_f16 v[22:25], v[54:57], v[38:41], v[30:33]
	v_mfma_f32_16x16x32_f16 v[10:13], v[62:65], v[38:41], v[6:9]
	s_waitcnt vmcnt(1)
	v_mfma_f32_16x16x32_f16 v[30:33], v[54:57], v[42:45], v[34:37]
	v_mfma_f32_16x16x32_f16 v[6:9], v[62:65], v[42:45], v[58:61]
	s_waitcnt vmcnt(0)
	v_mfma_f32_16x16x32_f16 v[34:37], v[54:57], v[50:53], v[18:21]
	v_mfma_f32_16x16x32_f16 v[2:5], v[62:65], v[50:53], v[46:49]
	s_setprio 0
	v_mul_u32_u24_e32 v52, 0x50, v0
	ds_read_b128 v[18:21], v52
	s_lshl_b64 s[0:1], s[0:1], 15
	v_lshl_or_b32 v0, v0, 4, s0
	v_mov_b32_e32 v1, s1
	v_lshl_add_u64 v[50:51], s[12:13], 0, v[0:1]
	ds_read_b128 v[38:41], v52 offset:16
	ds_read_b128 v[42:45], v52 offset:32
	ds_read_b128 v[46:49], v52 offset:48
	s_waitcnt lgkmcnt(3)
	global_store_dwordx4 v[50:51], v[18:21], off sc1
	s_add_u32 s0, s12, 0x800000
	s_nop 0
	v_add_co_u32_e32 v18, vcc, s48, v50
	s_nop 1
	v_addc_co_u32_e32 v19, vcc, 0, v51, vcc
	s_waitcnt lgkmcnt(2)
	global_store_dwordx4 v[18:19], v[38:41], off sc1
	v_or_b32_e32 v18, 0x4000, v0
	v_mov_b32_e32 v19, s1
	v_lshl_add_u64 v[20:21], s[12:13], 0, v[18:19]
	s_waitcnt lgkmcnt(1)
	global_store_dwordx4 v[20:21], v[42:45], off sc1
	v_mul_f32_e32 v20, 0xbfb8aa3b, v26
	v_exp_f32_e32 v38, v20
	v_add_co_u32_e32 v20, vcc, s33, v50
	v_or_b32_e32 v39, 0x200, v86
	s_nop 0
	v_addc_co_u32_e32 v21, vcc, 0, v51, vcc
	s_waitcnt lgkmcnt(0)
	global_store_dwordx4 v[20:21], v[46:49], off sc1
	v_add_f32_e32 v20, 1.0, v38
	v_rcp_f32_e32 v20, v20
	v_mul_f32_e32 v21, 0xbfb8aa3b, v27
	v_mul_f32_e32 v38, 0xbfb8aa3b, v28
	v_exp_f32_e32 v21, v21
	v_exp_f32_e32 v38, v38
	v_fma_mixlo_f16 v40, v26, v20, 0
	v_mul_f32_e32 v26, 0xbfb8aa3b, v29
	v_add_f32_e32 v20, 1.0, v21
	v_add_f32_e32 v21, 1.0, v38
	v_exp_f32_e32 v38, v26
	v_rcp_f32_e32 v20, v20
	v_rcp_f32_e32 v21, v21
	v_mov_b32_e32 v26, v27
	v_mov_b32_e32 v27, v28
	v_add_f32_e32 v28, 1.0, v38
	v_rcp_f32_e32 v28, v28
	v_pk_mul_f32 v[20:21], v[26:27], v[20:21]
	v_or_b32_e32 v27, v116, v39
	v_cvt_pk_f16_f32 v21, v20, v21
	v_fma_mixlo_f16 v26, v29, v28, 0
	v_pack_b32_f16 v20, v40, v21
	v_alignbit_b32 v21, v26, v21, 16
	v_mul_f32_e32 v26, 0xbfb8aa3b, v22
	v_exp_f32_e32 v26, v26
	v_mad_u32_u24 v27, v27, s2, v81
	ds_write_b64 v27, v[20:21]
	v_mul_f32_e32 v21, 0xbfb8aa3b, v23
	v_add_f32_e32 v20, 1.0, v26
	v_rcp_f32_e32 v20, v20
	v_mul_f32_e32 v26, 0xbfb8aa3b, v24
	v_exp_f32_e32 v21, v21
	v_exp_f32_e32 v26, v26
	v_fma_mixlo_f16 v28, v22, v20, 0
	v_mul_f32_e32 v22, 0xbfb8aa3b, v25
	v_add_f32_e32 v20, 1.0, v21
	v_add_f32_e32 v21, 1.0, v26
	v_exp_f32_e32 v26, v22
	v_rcp_f32_e32 v20, v20
	v_rcp_f32_e32 v21, v21
	v_mov_b32_e32 v22, v23
	v_mov_b32_e32 v23, v24
	v_add_f32_e32 v24, 1.0, v26
	v_rcp_f32_e32 v24, v24
	v_pk_mul_f32 v[20:21], v[22:23], v[20:21]
	v_or_b32_e32 v23, v117, v39
	v_cvt_pk_f16_f32 v21, v20, v21
	v_fma_mixlo_f16 v22, v25, v24, 0
	v_pack_b32_f16 v20, v28, v21
	v_alignbit_b32 v21, v22, v21, 16
	v_mul_f32_e32 v22, 0xbfb8aa3b, v30
	v_exp_f32_e32 v22, v22
	v_mad_u32_u24 v24, v23, s2, v81
	ds_write_b64 v24, v[20:21]
	v_mul_f32_e32 v21, 0xbfb8aa3b, v31
	v_add_f32_e32 v20, 1.0, v22
	v_mul_f32_e32 v22, 0xbfb8aa3b, v32
	v_rcp_f32_e32 v20, v20
	v_exp_f32_e32 v21, v21
	v_exp_f32_e32 v22, v22
	v_mov_b32_e32 v23, v32
	v_fma_mixlo_f16 v25, v30, v20, 0
	v_add_f32_e32 v20, 1.0, v21
	v_add_f32_e32 v21, 1.0, v22
	v_mul_f32_e32 v22, 0xbfb8aa3b, v33
	v_exp_f32_e32 v26, v22
	v_rcp_f32_e32 v20, v20
	v_rcp_f32_e32 v21, v21
	v_mov_b32_e32 v22, v31
	v_add_f32_e32 v26, 1.0, v26
	v_rcp_f32_e32 v26, v26
	v_pk_mul_f32 v[20:21], v[22:23], v[20:21]
	v_or_b32_e32 v23, v118, v39
	v_cvt_pk_f16_f32 v21, v20, v21
	v_fma_mixlo_f16 v22, v33, v26, 0
	v_pack_b32_f16 v20, v25, v21
	v_alignbit_b32 v21, v22, v21, 16
	v_mul_f32_e32 v22, 0xbfb8aa3b, v34
	v_exp_f32_e32 v22, v22
	v_mad_u32_u24 v25, v23, s2, v81
	ds_write_b64 v25, v[20:21]
	v_mul_f32_e32 v21, 0xbfb8aa3b, v35
	v_add_f32_e32 v20, 1.0, v22
	v_mul_f32_e32 v22, 0xbfb8aa3b, v36
	v_rcp_f32_e32 v20, v20
	v_exp_f32_e32 v21, v21
	v_exp_f32_e32 v22, v22
	v_mov_b32_e32 v23, v36
	v_fma_mixlo_f16 v26, v34, v20, 0
	v_add_f32_e32 v20, 1.0, v21
	v_add_f32_e32 v21, 1.0, v22
	v_mul_f32_e32 v22, 0xbfb8aa3b, v37
	v_exp_f32_e32 v28, v22
	v_rcp_f32_e32 v20, v20
	v_rcp_f32_e32 v21, v21
	v_mov_b32_e32 v22, v35
	v_add_f32_e32 v28, 1.0, v28
	v_rcp_f32_e32 v28, v28
	v_pk_mul_f32 v[20:21], v[22:23], v[20:21]
	v_or_b32_e32 v23, v119, v39
	v_cvt_pk_f16_f32 v21, v20, v21
	v_fma_mixlo_f16 v22, v37, v28, 0
	v_pack_b32_f16 v20, v26, v21
	v_alignbit_b32 v21, v22, v21, 16
	v_mul_f32_e32 v22, 0xbfb8aa3b, v14
	v_exp_f32_e32 v22, v22
	v_mad_u32_u24 v23, v23, s2, v81
	ds_write_b64 v23, v[20:21]
	v_mul_f32_e32 v21, 0xbfb8aa3b, v15
	v_add_f32_e32 v20, 1.0, v22
	v_rcp_f32_e32 v20, v20
	v_exp_f32_e32 v21, v21
	v_mul_f32_e32 v22, 0xbfb8aa3b, v16
	v_exp_f32_e32 v22, v22
	v_fma_mixlo_f16 v26, v14, v20, 0
	v_add_f32_e32 v14, 1.0, v21
	v_rcp_f32_e32 v20, v14
	v_add_f32_e32 v14, 1.0, v22
	v_rcp_f32_e32 v21, v14
	v_mov_b32_e32 v14, v15
	v_mul_f32_e32 v15, 0xbfb8aa3b, v17
	v_exp_f32_e32 v22, v15
	v_mov_b32_e32 v15, v16
	v_pk_mul_f32 v[14:15], v[14:15], v[20:21]
	v_mul_f32_e32 v20, 0xbfb8aa3b, v10
	v_cvt_pk_f16_f32 v15, v14, v15
	v_add_f32_e32 v14, 1.0, v22
	v_rcp_f32_e32 v16, v14
	v_exp_f32_e32 v20, v20
	v_pack_b32_f16 v14, v26, v15
	s_addc_u32 s1, s13, 0
	v_fma_mixlo_f16 v16, v17, v16, 0
	v_alignbit_b32 v15, v16, v15, 16
	ds_write_b64 v27, v[14:15] offset:32
	v_add_f32_e32 v14, 1.0, v20
	v_mul_f32_e32 v15, 0xbfb8aa3b, v11
	v_rcp_f32_e32 v14, v14
	v_exp_f32_e32 v15, v15
	v_mul_f32_e32 v16, 0xbfb8aa3b, v12
	v_exp_f32_e32 v16, v16
	v_fma_mixlo_f16 v17, v10, v14, 0
	v_add_f32_e32 v10, 1.0, v15
	v_rcp_f32_e32 v14, v10
	v_add_f32_e32 v10, 1.0, v16
	v_rcp_f32_e32 v15, v10
	v_mov_b32_e32 v10, v11
	v_mul_f32_e32 v11, 0xbfb8aa3b, v13
	v_exp_f32_e32 v16, v11
	v_mov_b32_e32 v11, v12
	v_pk_mul_f32 v[10:11], v[10:11], v[14:15]
	v_mul_f32_e32 v14, 0xbfb8aa3b, v6
	v_cvt_pk_f16_f32 v11, v10, v11
	v_add_f32_e32 v10, 1.0, v16
	v_rcp_f32_e32 v12, v10
	v_exp_f32_e32 v14, v14
	v_pack_b32_f16 v10, v17, v11
	v_lshl_add_u64 v[0:1], s[0:1], 0, v[0:1]
	v_fma_mixlo_f16 v12, v13, v12, 0
	v_alignbit_b32 v11, v12, v11, 16
	ds_write_b64 v24, v[10:11] offset:32
	v_add_f32_e32 v10, 1.0, v14
	v_mul_f32_e32 v11, 0xbfb8aa3b, v7
	v_rcp_f32_e32 v10, v10
	v_exp_f32_e32 v11, v11
	v_mul_f32_e32 v12, 0xbfb8aa3b, v8
	v_exp_f32_e32 v12, v12
	v_fma_mixlo_f16 v13, v6, v10, 0
	v_add_f32_e32 v6, 1.0, v11
	v_rcp_f32_e32 v10, v6
	v_add_f32_e32 v6, 1.0, v12
	v_rcp_f32_e32 v11, v6
	v_mov_b32_e32 v6, v7
	v_mul_f32_e32 v7, 0xbfb8aa3b, v9
	v_exp_f32_e32 v12, v7
	v_mov_b32_e32 v7, v8
	v_pk_mul_f32 v[6:7], v[6:7], v[10:11]
	v_mul_f32_e32 v10, 0xbfb8aa3b, v2
	v_cvt_pk_f16_f32 v7, v6, v7
	v_add_f32_e32 v6, 1.0, v12
	v_rcp_f32_e32 v8, v6
	v_exp_f32_e32 v10, v10
	v_pack_b32_f16 v6, v13, v7
	v_fma_mixlo_f16 v8, v9, v8, 0
	v_alignbit_b32 v7, v8, v7, 16
	ds_write_b64 v25, v[6:7] offset:32
	v_add_f32_e32 v6, 1.0, v10
	v_mul_f32_e32 v7, 0xbfb8aa3b, v3
	v_rcp_f32_e32 v6, v6
	v_exp_f32_e32 v7, v7
	v_mul_f32_e32 v8, 0xbfb8aa3b, v4
	v_exp_f32_e32 v8, v8
	v_fma_mixlo_f16 v9, v2, v6, 0
	v_add_f32_e32 v2, 1.0, v7
	v_mul_f32_e32 v7, 0xbfb8aa3b, v5
	v_rcp_f32_e32 v6, v2
	v_add_f32_e32 v2, 1.0, v8
	v_exp_f32_e32 v8, v7
	v_rcp_f32_e32 v7, v2
	v_mov_b32_e32 v2, v3
	v_mov_b32_e32 v3, v4
	v_add_f32_e32 v4, 1.0, v8
	v_rcp_f32_e32 v4, v4
	v_pk_mul_f32 v[2:3], v[2:3], v[6:7]
	v_fma_mixlo_f16 v4, v5, v4, 0
	v_cvt_pk_f16_f32 v3, v2, v3
	v_pack_b32_f16 v2, v9, v3
	v_alignbit_b32 v3, v4, v3, 16
	ds_write_b64 v23, v[2:3] offset:32
	s_waitcnt lgkmcnt(0)
	s_barrier
	ds_read_b128 v[2:5], v52 offset:40960
	ds_read_b128 v[6:9], v52 offset:40976
	ds_read_b128 v[10:13], v52 offset:40992
	ds_read_b128 v[14:17], v52 offset:41008
	s_waitcnt lgkmcnt(3)
	global_store_dwordx4 v[0:1], v[2:5], off sc1
	s_nop 1
	v_add_co_u32_e32 v2, vcc, 0x2000, v0
	s_nop 1
	v_addc_co_u32_e32 v3, vcc, 0, v1, vcc
	v_add_co_u32_e32 v0, vcc, 0x6000, v0
	s_waitcnt lgkmcnt(2)
	global_store_dwordx4 v[2:3], v[6:9], off sc1
	v_lshl_add_u64 v[2:3], s[0:1], 0, v[18:19]
	v_addc_co_u32_e32 v1, vcc, 0, v1, vcc
	s_waitcnt lgkmcnt(1)
	global_store_dwordx4 v[2:3], v[10:13], off sc1
	s_waitcnt lgkmcnt(0)
	global_store_dwordx4 v[0:1], v[14:17], off sc1
	s_endpgm

.LBB2_5:
	v_and_b32_e32 v136, 0x1cf, v0
	v_lshlrev_b32_e32 v4, 6, v0
	s_movk_i32 s12, 0x7000
	v_lshlrev_b32_e32 v3, 2, v136
	v_and_or_b32 v2, v4, s12, v2
	v_or_b32_e32 v135, 48, v0
	global_load_dwordx4 v[34:37], v2, s[8:9]
	global_load_dwordx4 v[30:33], v2, s[8:9] offset:1024
	global_load_dword v134, v3, s[10:11]
	global_load_dword v133, v3, s[10:11] offset:64
	global_load_dword v131, v3, s[10:11] offset:128
	v_lshlrev_b32_e32 v3, 2, v135
	global_load_dword v121, v3, s[10:11]
	global_load_dwordx4 v[26:29], v2, s[8:9] offset:2048
	global_load_dwordx4 v[18:21], v2, s[8:9] offset:3072
	s_waitcnt lgkmcnt(0)
	v_lshl_add_u64 v[2:3], s[20:21], 0, v[118:119]
	s_movk_i32 s8, 0x2000
	v_add_co_u32_e32 v4, vcc, s8, v2
	s_movk_i32 s8, 0x4000
	s_nop 0
	v_addc_co_u32_e32 v5, vcc, 0, v3, vcc
	global_load_dwordx4 v[14:17], v[2:3], off
	global_load_dwordx4 v[10:13], v[4:5], off
	v_add_co_u32_e32 v4, vcc, s8, v2
	s_movk_i32 s8, 0x6000
	s_nop 0
	v_addc_co_u32_e32 v5, vcc, 0, v3, vcc
	v_add_co_u32_e32 v2, vcc, s8, v2
	s_nop 1
	v_addc_co_u32_e32 v3, vcc, 0, v3, vcc
	global_load_dwordx4 v[6:9], v[4:5], off
	s_nop 0
	global_load_dwordx4 v[2:5], v[2:3], off
	s_waitcnt vmcnt(12)
	v_cvt_f32_f16_sdwa v124, v122 dst_sel:DWORD dst_unused:UNUSED_PAD src0_sel:WORD_1
	v_cvt_f32_f16_e32 v125, v123
	v_cvt_f32_f16_sdwa v128, v123 dst_sel:DWORD dst_unused:UNUSED_PAD src0_sel:WORD_1
	v_cvt_f32_f16_e32 v129, v22
	v_cvt_f32_f16_sdwa v138, v22 dst_sel:DWORD dst_unused:UNUSED_PAD src0_sel:WORD_1
	v_cvt_f32_f16_e32 v139, v23
	s_waitcnt vmcnt(6)
	v_pk_fma_f32 v[122:123], v[106:107], v[124:125], v[120:121] op_sel_hi:[0,1,0]
	v_pk_mov_b32 v[124:125], v[124:125], v[128:129] op_sel:[1,0]
	v_cvt_f32_f16_sdwa v141, v25 dst_sel:DWORD dst_unused:UNUSED_PAD src0_sel:WORD_1
	v_pk_fma_f32 v[122:123], v[106:107], v[124:125], v[122:123] op_sel:[1,0,0]
	v_pk_mov_b32 v[148:149], v[128:129], v[138:139] op_sel:[1,0]
	v_pk_fma_f32 v[124:125], v[108:109], v[128:129], v[122:123] op_sel_hi:[0,1,1]
	v_mov_b32_e32 v122, v109
	v_pk_fma_f32 v[150:151], v[122:123], v[148:149], v[124:125] op_sel_hi:[0,1,1]
	v_mul_f32_e32 v22, 0xbfb8aa3b, v150
	v_exp_f32_e32 v22, v22
	v_mul_f32_e32 v123, 0xbfb8aa3b, v151
	v_exp_f32_e32 v123, v123
	v_cvt_f32_f16_sdwa v157, v102 dst_sel:DWORD dst_unused:UNUSED_PAD src0_sel:WORD_1
	v_add_f32_e32 v22, 1.0, v22
	v_rcp_f32_e32 v152, v22
	v_add_f32_e32 v22, 1.0, v123
	v_rcp_f32_e32 v153, v22
	v_cvt_f32_f16_e32 v156, v102
	v_mul_f32_e32 v155, v107, v141
	v_cvt_f32_f16_e32 v126, v103
	v_pk_mul_f32 v[150:151], v[150:151], v[152:153]
	v_cvt_f32_f16_sdwa v152, v23 dst_sel:DWORD dst_unused:UNUSED_PAD src0_sel:WORD_1
	v_cvt_f32_f16_e32 v153, v24
	v_pk_fma_f32 v[22:23], v[106:107], v[128:129], v[120:121] op_sel_hi:[0,1,0]
	v_pk_fma_f32 v[22:23], v[106:107], v[148:149], v[22:23] op_sel:[1,0,0]
	v_cvt_f32_f16_sdwa v158, v103 dst_sel:DWORD dst_unused:UNUSED_PAD src0_sel:WORD_1
	v_pk_fma_f32 v[22:23], v[108:109], v[138:139], v[22:23] op_sel_hi:[0,1,1]
	v_pk_mov_b32 v[128:129], v[138:139], v[152:153] op_sel:[1,0]
	v_cvt_f32_f16_e32 v159, v104
	v_pk_fma_f32 v[148:149], v[122:123], v[128:129], v[22:23] op_sel_hi:[0,1,1]
	v_mul_f32_e32 v22, 0xbfb8aa3b, v148
	v_exp_f32_e32 v23, v22
	v_mul_f32_e32 v22, 0xbfb8aa3b, v149
	v_exp_f32_e32 v123, v22
	v_cvt_pk_f16_f32 v22, v150, v151
	v_add_f32_e32 v23, 1.0, v23
	v_rcp_f32_e32 v150, v23
	v_add_f32_e32 v23, 1.0, v123
	v_rcp_f32_e32 v151, v23
	v_lshrrev_b32_e32 v123, 16, v22
	v_mov_b32_e32 v103, v158
	v_cvt_f32_f16_sdwa v127, v105 dst_sel:DWORD dst_unused:UNUSED_PAD src0_sel:WORD_1
	v_pk_mul_f32 v[148:149], v[148:149], v[150:151]
	v_cvt_f32_f16_sdwa v150, v24 dst_sel:DWORD dst_unused:UNUSED_PAD src0_sel:WORD_1
	v_cvt_f32_f16_e32 v151, v25
	v_pk_fma_f32 v[24:25], v[106:107], v[138:139], v[120:121] op_sel_hi:[0,1,0]
	v_pk_fma_f32 v[24:25], v[106:107], v[128:129], v[24:25] op_sel:[1,0,0]
	v_cvt_f32_f16_e32 v145, v115
	v_pk_fma_f32 v[24:25], v[108:109], v[152:153], v[24:25] op_sel_hi:[0,1,1]
	v_pk_mov_b32 v[128:129], v[152:153], v[150:151] op_sel:[1,0]
	v_mov_b32_e32 v140, v151
	v_pk_fma_f32 v[24:25], v[122:123], v[128:129], v[24:25] op_sel_hi:[0,1,1]
	v_mul_f32_e32 v23, 0xbfb8aa3b, v24
	v_exp_f32_e32 v124, v23
	v_mul_f32_e32 v23, 0xbfb8aa3b, v25
	v_exp_f32_e32 v137, v23
	v_cvt_pk_f16_f32 v23, v148, v149
	v_add_f32_e32 v124, 1.0, v124
	v_rcp_f32_e32 v138, v124
	v_add_f32_e32 v124, 1.0, v137
	v_rcp_f32_e32 v139, v124
	v_pk_fma_f32 v[148:149], v[106:107], v[152:153], v[120:121] op_sel_hi:[0,1,0]
	v_pk_fma_f32 v[128:129], v[106:107], v[128:129], v[148:149] op_sel:[1,0,0]
	v_cvt_f32_f16_sdwa v125, v117 dst_sel:DWORD dst_unused:UNUSED_PAD src0_sel:WORD_1
	v_pk_mul_f32 v[24:25], v[24:25], v[138:139]
	v_mul_f32_e32 v139, v109, v141
	v_pk_fma_f32 v[128:129], v[108:109], v[150:151], v[128:129] op_sel_hi:[0,1,1]
	v_mul_f32_e32 v138, v109, v151
	v_pk_add_f32 v[128:129], v[128:129], v[138:139]
	v_cvt_pk_f16_f32 v24, v24, v25
	v_mul_f32_e32 v124, 0xbfb8aa3b, v128
	v_exp_f32_e32 v124, v124
	v_mul_f32_e32 v138, 0xbfb8aa3b, v129
	v_exp_f32_e32 v138, v138
	v_pk_fma_f32 v[150:151], v[106:107], v[150:151], v[120:121] op_sel_hi:[0,1,0]
	v_add_f32_e32 v25, 1.0, v124
	v_rcp_f32_e32 v148, v25
	v_add_f32_e32 v25, 1.0, v138
	v_rcp_f32_e32 v149, v25
	v_cvt_f32_f16_e32 v146, v111
	v_cvt_f32_f16_sdwa v144, v113 dst_sel:DWORD dst_unused:UNUSED_PAD src0_sel:WORD_1
	v_cvt_f32_f16_e32 v113, v113
	v_pk_mul_f32 v[148:149], v[128:129], v[148:149]
	v_pk_mov_b32 v[128:129], v[106:107], v[108:109] op_sel:[1,0]
	v_lshlrev_b32_e32 v143, 1, v0
	v_pk_mul_f32 v[152:153], v[128:129], v[140:141]
	v_mov_b32_e32 v140, v141
	v_mov_b32_e32 v154, v152
	v_pk_add_f32 v[150:151], v[150:151], v[154:155]
	v_pk_mul_f32 v[154:155], v[108:109], v[156:157]
	v_lshrrev_b32_e32 v137, 16, v23
	v_pk_mov_b32 v[152:153], v[152:153], v[154:155] op_sel:[1,0]
	v_mul_f32_e32 v155, v108, v126
	v_pk_add_f32 v[150:151], v[150:151], v[152:153]
	v_pk_mul_f32 v[152:153], v[106:107], v[156:157]
	v_pk_fma_f32 v[150:151], v[122:123], v[156:157], v[150:151] op_sel_hi:[0,1,1]
	v_mul_f32_e32 v25, 0xbfb8aa3b, v150
	v_exp_f32_e32 v102, v25
	v_mul_f32_e32 v25, 0xbfb8aa3b, v151
	v_exp_f32_e32 v124, v25
	v_cvt_pk_f16_f32 v25, v148, v149
	v_add_f32_e32 v102, 1.0, v102
	v_rcp_f32_e32 v148, v102
	v_add_f32_e32 v102, 1.0, v124
	v_rcp_f32_e32 v149, v102
	v_lshrrev_b32_e32 v138, 16, v24
	v_lshrrev_b32_e32 v139, 16, v25
	ds_write_b16 v143, v22
	v_pk_mul_f32 v[148:149], v[150:151], v[148:149]
	ds_write_b16 v143, v123 offset:1040
	v_cvt_pk_f16_f32 v102, v148, v149
	v_pk_mov_b32 v[148:149], v[156:157], v[156:157] op_sel:[1,0]
	v_mov_b32_e32 v157, v152
	v_mov_b32_e32 v141, v149
	v_pk_mul_f32 v[140:141], v[106:107], v[140:141]
	v_mov_b32_e32 v149, v126
	v_mov_b32_e32 v156, v140
	v_pk_mul_f32 v[150:151], v[108:109], v[148:149]
	v_pk_add_f32 v[156:157], v[120:121], v[156:157] op_sel_hi:[0,1]
	v_mov_b32_e32 v152, v141
	v_pk_add_f32 v[140:141], v[156:157], v[152:153]
	v_mov_b32_e32 v154, v150
	v_pk_mul_f32 v[152:153], v[108:109], v[102:103]
	v_pk_add_f32 v[140:141], v[140:141], v[154:155]
	v_mov_b32_e32 v152, v151
	v_pk_add_f32 v[150:151], v[140:141], v[152:153]
	v_pk_mul_f32 v[148:149], v[106:107], v[148:149]
	v_mul_f32_e32 v124, 0xbfb8aa3b, v150
	v_exp_f32_e32 v124, v124
	v_mul_f32_e32 v140, 0xbfb8aa3b, v151
	v_exp_f32_e32 v141, v140
	v_cvt_f32_f16_sdwa v156, v104 dst_sel:DWORD dst_unused:UNUSED_PAD src0_sel:WORD_1
	v_add_f32_e32 v124, 1.0, v124
	v_rcp_f32_e32 v152, v124
	v_add_f32_e32 v124, 1.0, v141
	v_rcp_f32_e32 v153, v124
	v_cvt_f32_f16_e32 v157, v105
	v_pk_mul_f32 v[154:155], v[106:107], v[102:103]
	v_lshrrev_b32_e32 v140, 16, v102
	v_pk_mul_f32 v[150:151], v[150:151], v[152:153]
	v_mul_f32_e32 v153, v106, v126
	v_mov_b32_e32 v152, v148
	v_pk_add_f32 v[152:153], v[120:121], v[152:153] op_sel_hi:[0,1]
	v_mov_b32_e32 v154, v149
	v_pk_add_f32 v[104:105], v[152:153], v[154:155]
	v_pk_mov_b32 v[148:149], v[158:159], v[156:157] op_sel:[1,0]
	v_pk_fma_f32 v[104:105], v[108:109], v[158:159], v[104:105] op_sel_hi:[0,1,1]
	v_pk_fma_f32 v[104:105], v[122:123], v[148:149], v[104:105] op_sel_hi:[0,1,1]
	v_mul_f32_e32 v103, 0xbfb8aa3b, v104
	v_exp_f32_e32 v124, v103
	v_mul_f32_e32 v103, 0xbfb8aa3b, v105
	v_exp_f32_e32 v126, v103
	v_cvt_pk_f16_f32 v103, v150, v151
	v_add_f32_e32 v124, 1.0, v124
	v_rcp_f32_e32 v150, v124
	v_add_f32_e32 v124, 1.0, v126
	v_rcp_f32_e32 v151, v124
	v_pk_fma_f32 v[152:153], v[106:107], v[158:159], v[120:121] op_sel_hi:[0,1,0]
	v_pk_fma_f32 v[148:149], v[106:107], v[148:149], v[152:153] op_sel:[1,0,0]
	v_cvt_f32_f16_sdwa v155, v114 dst_sel:DWORD dst_unused:UNUSED_PAD src0_sel:WORD_1
	v_pk_mul_f32 v[104:105], v[104:105], v[150:151]
	v_mul_f32_e32 v151, v109, v127
	v_pk_fma_f32 v[148:149], v[108:109], v[156:157], v[148:149] op_sel_hi:[0,1,1]
	v_mul_f32_e32 v150, v109, v157
	v_pk_add_f32 v[148:149], v[148:149], v[150:151]
	v_cvt_pk_f16_f32 v104, v104, v105
	v_mul_f32_e32 v124, 0xbfb8aa3b, v148
	v_exp_f32_e32 v124, v124
	v_mul_f32_e32 v126, 0xbfb8aa3b, v149
	v_exp_f32_e32 v126, v126
	v_cvt_f32_f16_e32 v154, v114
	v_add_f32_e32 v105, 1.0, v124
	v_rcp_f32_e32 v150, v105
	v_add_f32_e32 v105, 1.0, v126
	v_rcp_f32_e32 v151, v105
	v_mov_b32_e32 v126, v157
	v_mul_f32_e32 v153, v107, v127
	v_pk_fma_f32 v[156:157], v[106:107], v[156:157], v[120:121] op_sel_hi:[0,1,0]
	v_pk_mul_f32 v[148:149], v[148:149], v[150:151]
	v_pk_mul_f32 v[150:151], v[128:129], v[126:127]
	v_lshrrev_b32_e32 v141, 16, v103
	v_mov_b32_e32 v152, v150
	v_pk_add_f32 v[152:153], v[156:157], v[152:153]
	v_pk_mul_f32 v[156:157], v[108:109], v[154:155]
	v_lshrrev_b32_e32 v142, 16, v104
	v_pk_mov_b32 v[150:151], v[150:151], v[156:157] op_sel:[1,0]
	v_mul_f32_e32 v157, v108, v145
	v_pk_add_f32 v[150:151], v[152:153], v[150:151]
	ds_write_b16 v143, v23 offset:2080
	v_pk_fma_f32 v[150:151], v[122:123], v[154:155], v[150:151] op_sel_hi:[0,1,1]
	v_mul_f32_e32 v105, 0xbfb8aa3b, v150
	v_exp_f32_e32 v114, v105
	v_mul_f32_e32 v105, 0xbfb8aa3b, v151
	v_exp_f32_e32 v124, v105
	v_cvt_pk_f16_f32 v105, v148, v149
	v_add_f32_e32 v114, 1.0, v114
	v_rcp_f32_e32 v148, v114
	v_add_f32_e32 v114, 1.0, v124
	v_rcp_f32_e32 v149, v114
	v_lshrrev_b32_e32 v126, 16, v105
	ds_write_b16 v143, v137 offset:3120
	ds_write_b16 v143, v24 offset:4160
	v_pk_mul_f32 v[148:149], v[150:151], v[148:149]
	v_mov_b32_e32 v150, v127
	v_cvt_pk_f16_f32 v114, v148, v149
	v_pk_mov_b32 v[148:149], v[154:155], v[154:155] op_sel:[1,0]
	v_pk_mul_f32 v[154:155], v[106:107], v[154:155]
	v_mov_b32_e32 v151, v149
	v_pk_mul_f32 v[150:151], v[106:107], v[150:151]
	v_mov_b32_e32 v149, v145
	v_mov_b32_e32 v158, v150
	v_cvt_f32_f16_sdwa v150, v115 dst_sel:DWORD dst_unused:UNUSED_PAD src0_sel:WORD_1
	v_mov_b32_e32 v159, v154
	v_pk_mul_f32 v[152:153], v[108:109], v[148:149]
	v_pk_add_f32 v[158:159], v[120:121], v[158:159] op_sel_hi:[0,1]
	v_mov_b32_e32 v154, v151
	v_pk_add_f32 v[154:155], v[158:159], v[154:155]
	v_mov_b32_e32 v156, v152
	v_mov_b32_e32 v115, v150
	v_pk_add_f32 v[154:155], v[154:155], v[156:157]
	v_pk_mul_f32 v[156:157], v[108:109], v[114:115]
	v_pk_mul_f32 v[148:149], v[106:107], v[148:149]
	v_mov_b32_e32 v156, v153
	v_pk_add_f32 v[152:153], v[154:155], v[156:157]
	v_cvt_f32_f16_e32 v151, v116
	v_mul_f32_e32 v124, 0xbfb8aa3b, v152
	v_exp_f32_e32 v124, v124
	v_mul_f32_e32 v127, 0xbfb8aa3b, v153
	v_exp_f32_e32 v147, v127
	v_cvt_f32_f16_sdwa v158, v116 dst_sel:DWORD dst_unused:UNUSED_PAD src0_sel:WORD_1
	v_add_f32_e32 v124, 1.0, v124
	v_rcp_f32_e32 v154, v124
	v_add_f32_e32 v124, 1.0, v147
	v_rcp_f32_e32 v155, v124
	v_cvt_f32_f16_e32 v159, v117
	v_pk_mul_f32 v[156:157], v[106:107], v[114:115]
	v_lshrrev_b32_e32 v127, 16, v114
	v_pk_mul_f32 v[152:153], v[152:153], v[154:155]
	v_mul_f32_e32 v155, v106, v145
	v_mov_b32_e32 v154, v148
	v_pk_add_f32 v[154:155], v[120:121], v[154:155] op_sel_hi:[0,1]
	v_mov_b32_e32 v156, v149
	v_pk_add_f32 v[116:117], v[154:155], v[156:157]
	v_pk_mov_b32 v[148:149], v[150:151], v[158:159] op_sel:[1,0]
	v_pk_fma_f32 v[116:117], v[108:109], v[150:151], v[116:117] op_sel_hi:[0,1,1]
	v_pk_fma_f32 v[116:117], v[122:123], v[148:149], v[116:117] op_sel_hi:[0,1,1]
	v_mul_f32_e32 v115, 0xbfb8aa3b, v116
	v_exp_f32_e32 v124, v115
	v_mul_f32_e32 v115, 0xbfb8aa3b, v117
	v_exp_f32_e32 v145, v115
	v_cvt_pk_f16_f32 v115, v152, v153
	v_add_f32_e32 v124, 1.0, v124
	v_rcp_f32_e32 v152, v124
	v_add_f32_e32 v124, 1.0, v145
	v_rcp_f32_e32 v153, v124
	v_pk_fma_f32 v[150:151], v[106:107], v[150:151], v[120:121] op_sel_hi:[0,1,0]
	v_pk_fma_f32 v[148:149], v[106:107], v[148:149], v[150:151] op_sel:[1,0,0]
	v_pk_fma_f32 v[154:155], v[106:107], v[158:159], v[120:121] op_sel_hi:[0,1,0]
	v_pk_mul_f32 v[116:117], v[116:117], v[152:153]
	v_mul_f32_e32 v153, v109, v125
	v_pk_fma_f32 v[148:149], v[108:109], v[158:159], v[148:149] op_sel_hi:[0,1,1]
	v_mul_f32_e32 v152, v109, v159
	v_pk_add_f32 v[148:149], v[148:149], v[152:153]
	v_cvt_pk_f16_f32 v116, v116, v117
	v_mul_f32_e32 v124, 0xbfb8aa3b, v148
	v_exp_f32_e32 v124, v124
	v_mul_f32_e32 v147, 0xbfb8aa3b, v149
	v_exp_f32_e32 v147, v147
	v_cvt_f32_f16_sdwa v153, v110 dst_sel:DWORD dst_unused:UNUSED_PAD src0_sel:WORD_1
	v_add_f32_e32 v117, 1.0, v124
	v_rcp_f32_e32 v150, v117
	v_add_f32_e32 v117, 1.0, v147
	v_rcp_f32_e32 v151, v117
	v_cvt_f32_f16_e32 v152, v110
	v_mov_b32_e32 v124, v159
	v_pk_mul_f32 v[128:129], v[128:129], v[124:125]
	v_pk_mul_f32 v[148:149], v[148:149], v[150:151]
	v_mul_f32_e32 v151, v107, v125
	v_mov_b32_e32 v150, v128
	v_pk_add_f32 v[150:151], v[154:155], v[150:151]
	v_pk_mul_f32 v[154:155], v[108:109], v[152:153]
	v_lshrrev_b32_e32 v145, 16, v115
	v_pk_mov_b32 v[128:129], v[128:129], v[154:155] op_sel:[1,0]
	v_mul_f32_e32 v155, v108, v146
	v_pk_add_f32 v[128:129], v[150:151], v[128:129]
	v_lshrrev_b32_e32 v147, 16, v116
	v_pk_fma_f32 v[128:129], v[122:123], v[152:153], v[128:129] op_sel_hi:[0,1,1]
	v_mul_f32_e32 v110, 0xbfb8aa3b, v128
	v_exp_f32_e32 v110, v110
	v_mul_f32_e32 v117, 0xbfb8aa3b, v129
	v_exp_f32_e32 v124, v117
	v_cvt_pk_f16_f32 v117, v148, v149
	v_add_f32_e32 v110, 1.0, v110
	v_rcp_f32_e32 v148, v110
	v_add_f32_e32 v110, 1.0, v124
	v_rcp_f32_e32 v149, v110
	v_lshrrev_b32_e32 v124, 16, v117
	ds_write_b16 v143, v138 offset:5200
	ds_write_b16 v143, v25 offset:6240
	v_pk_mul_f32 v[128:129], v[128:129], v[148:149]
	v_mov_b32_e32 v148, v125
	v_cvt_pk_f16_f32 v110, v128, v129
	v_pk_mov_b32 v[128:129], v[152:153], v[152:153] op_sel:[1,0]
	v_pk_mul_f32 v[152:153], v[106:107], v[152:153]
	v_mov_b32_e32 v149, v129
	v_pk_mul_f32 v[148:149], v[106:107], v[148:149]
	v_mov_b32_e32 v129, v146
	v_mov_b32_e32 v156, v148
	v_cvt_f32_f16_sdwa v148, v111 dst_sel:DWORD dst_unused:UNUSED_PAD src0_sel:WORD_1
	v_mov_b32_e32 v157, v152
	v_pk_mul_f32 v[150:151], v[108:109], v[128:129]
	v_pk_add_f32 v[156:157], v[120:121], v[156:157] op_sel_hi:[0,1]
	v_mov_b32_e32 v152, v149
	v_pk_add_f32 v[152:153], v[156:157], v[152:153]
	v_mov_b32_e32 v154, v150
	v_mov_b32_e32 v111, v148
	v_pk_add_f32 v[152:153], v[152:153], v[154:155]
	v_pk_mul_f32 v[154:155], v[108:109], v[110:111]
	v_pk_mul_f32 v[128:129], v[106:107], v[128:129]
	v_mov_b32_e32 v154, v151
	v_pk_add_f32 v[150:151], v[152:153], v[154:155]
	v_pk_mul_f32 v[154:155], v[106:107], v[110:111]
	v_mul_f32_e32 v125, 0xbfb8aa3b, v150
	v_exp_f32_e32 v149, v125
	v_mul_f32_e32 v125, 0xbfb8aa3b, v151
	v_exp_f32_e32 v153, v125
	v_mov_b32_e32 v154, v129
	v_add_f32_e32 v149, 1.0, v149
	v_rcp_f32_e32 v152, v149
	v_add_f32_e32 v149, 1.0, v153
	v_rcp_f32_e32 v153, v149
	v_cvt_f32_f16_e32 v149, v112
	v_cvt_f32_f16_sdwa v112, v112 dst_sel:DWORD dst_unused:UNUSED_PAD src0_sel:WORD_1
	v_lshrrev_b32_e32 v125, 16, v110
	v_pk_mul_f32 v[150:151], v[150:151], v[152:153]
	v_mul_f32_e32 v153, v106, v146
	v_mov_b32_e32 v152, v128
	v_pk_add_f32 v[152:153], v[120:121], v[152:153] op_sel_hi:[0,1]
	v_pk_add_f32 v[128:129], v[152:153], v[154:155]
	v_pk_mov_b32 v[152:153], v[148:149], v[112:113] op_sel:[1,0]
	v_pk_fma_f32 v[128:129], v[108:109], v[148:149], v[128:129] op_sel_hi:[0,1,1]
	v_pk_fma_f32 v[128:129], v[122:123], v[152:153], v[128:129] op_sel_hi:[0,1,1]
	v_mul_f32_e32 v111, 0xbfb8aa3b, v128
	v_exp_f32_e32 v122, v111
	v_mul_f32_e32 v111, 0xbfb8aa3b, v129
	v_exp_f32_e32 v146, v111
	v_cvt_pk_f16_f32 v111, v150, v151
	v_add_f32_e32 v122, 1.0, v122
	v_rcp_f32_e32 v150, v122
	v_add_f32_e32 v122, 1.0, v146
	v_rcp_f32_e32 v151, v122
	v_pk_fma_f32 v[148:149], v[106:107], v[148:149], v[120:121] op_sel_hi:[0,1,0]
	v_pk_fma_f32 v[106:107], v[106:107], v[152:153], v[148:149] op_sel:[1,0,0]
	v_lshrrev_b32_e32 v122, 16, v111
	v_pk_mul_f32 v[128:129], v[128:129], v[150:151]
	v_mul_f32_e32 v151, v109, v144
	v_pk_fma_f32 v[106:107], v[108:109], v[112:113], v[106:107] op_sel_hi:[0,1,1]
	v_mul_f32_e32 v150, v109, v113
	v_pk_add_f32 v[106:107], v[106:107], v[150:151]
	v_cvt_pk_f16_f32 v112, v128, v129
	v_mul_f32_e32 v108, 0xbfb8aa3b, v106
	v_exp_f32_e32 v108, v108
	v_mul_f32_e32 v109, 0xbfb8aa3b, v107
	v_exp_f32_e32 v109, v109
	ds_write_b16 v143, v139 offset:7280
	v_add_f32_e32 v108, 1.0, v108
	v_rcp_f32_e32 v128, v108
	v_add_f32_e32 v108, 1.0, v109
	v_rcp_f32_e32 v129, v108
	v_lshrrev_b32_e32 v108, 16, v112
	v_and_b32_e32 v109, 15, v0
	ds_write_b16 v143, v102 offset:8320
	v_pk_mul_f32 v[106:107], v[106:107], v[128:129]
	v_lshl_add_u64 v[128:129], s[2:3], 0, v[118:119]
	v_lshl_add_u64 v[148:149], v[128:129], 0, s[6:7]
	v_cvt_pk_f16_f32 v113, v106, v107
	global_store_dwordx4 v[148:149], v[22:25], off sc1
	v_lshl_add_u64 v[148:149], v[128:129], 0, s[14:15]
	v_lshrrev_b32_e32 v106, 16, v113
	global_store_dwordx4 v[148:149], v[102:105], off sc1
	v_lshl_add_u64 v[148:149], v[128:129], 0, s[16:17]
	v_lshl_add_u64 v[128:129], v[128:129], 0, s[18:19]
	v_lshrrev_b32_e32 v107, 4, v130
	ds_write_b16 v143, v140 offset:9360
	ds_write_b16 v143, v103 offset:10400
	ds_write_b16 v143, v141 offset:11440
	ds_write_b16 v143, v104 offset:12480
	ds_write_b16 v143, v142 offset:13520
	ds_write_b16 v143, v105 offset:14560
	ds_write_b16 v143, v126 offset:15600
	ds_write_b16 v143, v114 offset:16640
	ds_write_b16 v143, v127 offset:17680
	ds_write_b16 v143, v115 offset:18720
	ds_write_b16 v143, v145 offset:19760
	ds_write_b16 v143, v116 offset:20800
	ds_write_b16 v143, v147 offset:21840
	ds_write_b16 v143, v117 offset:22880
	ds_write_b16 v143, v124 offset:23920
	ds_write_b16 v143, v110 offset:24960
	ds_write_b16 v143, v125 offset:26000
	ds_write_b16 v143, v111 offset:27040
	ds_write_b16 v143, v122 offset:28080
	ds_write_b16 v143, v112 offset:29120
	ds_write_b16 v143, v108 offset:30160
	ds_write_b16 v143, v113 offset:31200
	ds_write_b16 v143, v106 offset:32240
	global_store_dwordx4 v[148:149], v[114:117], off sc1
	global_store_dwordx4 v[128:129], v[110:113], off sc1
	s_waitcnt lgkmcnt(0)
	s_barrier
	s_and_saveexec_b64 s[2:3], s[4:5]
	s_cbranch_execz .LBB2_7
	s_movk_i32 s4, 0xbf
	v_cmp_lt_u32_e32 vcc, s4, v0
	v_and_b32_e32 v129, 48, v0
	s_movk_i32 s4, 0x410
	v_cndmask_b32_e64 v120, 0, 16, vcc
	v_or_b32_e32 v128, v120, v109
	v_mad_u32_u24 v128, v128, s4, v129
	s_lshl_b32 s4, s24, 5
	s_and_b32 s5, s4, 0x1e0
	v_lshl_add_u32 v129, s5, 1, v128
	ds_read_b128 v[148:151], v129
	s_add_i32 s8, s4, 32
	s_and_b32 s8, s8, 0x1e0
	v_lshl_add_u32 v129, s8, 1, v128
	ds_read_b128 v[152:155], v129
	s_add_i32 s8, s4, 64
	s_waitcnt lgkmcnt(1)
	v_mfma_f32_16x16x32_f16 v[38:41], v[148:151], v[38:41], 0
	s_and_b32 s8, s8, 0x1e0
	s_xor_b32 s5, s5, 0x100
	s_waitcnt lgkmcnt(0)
	v_mfma_f32_16x16x32_f16 v[38:41], v[152:155], v[42:45], v[38:41]
	v_lshl_add_u32 v42, s8, 1, v128
	ds_read_b128 v[42:45], v42
	s_add_i32 s8, s4, 0x60
	s_and_b32 s8, s8, 0x1e0
	v_lshl_add_u32 v129, s8, 1, v128
	ds_read_b128 v[148:151], v129
	s_add_i32 s8, s4, 0x80
	s_and_b32 s8, s8, 0x1e0
	s_waitcnt lgkmcnt(1)
	v_mfma_f32_16x16x32_f16 v[38:41], v[42:45], v[46:49], v[38:41]
	v_lshl_add_u32 v42, s8, 1, v128
	ds_read_b128 v[42:45], v42
	s_add_i32 s8, s4, 0xa0
	s_and_b32 s8, s8, 0x1e0
	v_lshl_add_u32 v46, s8, 1, v128
	ds_read_b128 v[46:49], v46
	s_waitcnt lgkmcnt(2)
	v_mfma_f32_16x16x32_f16 v[38:41], v[148:151], v[50:53], v[38:41]
	s_add_i32 s8, s4, 0xc0
	s_and_b32 s8, s8, 0x1e0
	s_waitcnt lgkmcnt(1)
	v_mfma_f32_16x16x32_f16 v[38:41], v[42:45], v[54:57], v[38:41]
	v_lshl_add_u32 v42, s8, 1, v128
	ds_read_b128 v[42:45], v42
	s_add_i32 s8, s4, 0xe0
	s_and_b32 s8, s8, 0x1e0
	s_waitcnt lgkmcnt(1)
	v_mfma_f32_16x16x32_f16 v[38:41], v[46:49], v[58:61], v[38:41]
	v_lshl_add_u32 v46, s8, 1, v128
	ds_read_b128 v[46:49], v46
	s_waitcnt lgkmcnt(1)
	v_mfma_f32_16x16x32_f16 v[38:41], v[42:45], v[62:65], v[38:41]
	v_lshl_add_u32 v42, s5, 1, v128
	ds_read_b128 v[42:45], v42
	s_add_i32 s5, s4, 0x120
	s_and_b32 s5, s5, 0x1e0
	s_waitcnt lgkmcnt(1)
	v_mfma_f32_16x16x32_f16 v[38:41], v[46:49], v[66:69], v[38:41]
	v_lshl_add_u32 v46, s5, 1, v128
	ds_read_b128 v[46:49], v46
	s_add_i32 s5, s4, 0x140
	s_and_b32 s5, s5, 0x1e0
	s_waitcnt lgkmcnt(1)
	v_mfma_f32_16x16x32_f16 v[38:41], v[42:45], v[70:73], v[38:41]
	v_lshl_add_u32 v42, s5, 1, v128
	ds_read_b128 v[42:45], v42
	s_add_i32 s5, s4, 0x160
	s_and_b32 s5, s5, 0x1e0
	s_waitcnt lgkmcnt(1)
	v_mfma_f32_16x16x32_f16 v[38:41], v[46:49], v[74:77], v[38:41]
	v_lshl_add_u32 v46, s5, 1, v128
	ds_read_b128 v[46:49], v46
	s_add_i32 s5, s4, 0x180
	s_and_b32 s5, s5, 0x1e0
	s_waitcnt lgkmcnt(1)
	v_mfma_f32_16x16x32_f16 v[38:41], v[42:45], v[78:81], v[38:41]
	v_lshl_add_u32 v42, s5, 1, v128
	ds_read_b128 v[42:45], v42
	s_add_i32 s5, s4, 0x1a0
	s_and_b32 s5, s5, 0x1e0
	s_waitcnt lgkmcnt(1)
	v_mfma_f32_16x16x32_f16 v[38:41], v[46:49], v[82:85], v[38:41]
	v_lshl_add_u32 v46, s5, 1, v128
	ds_read_b128 v[46:49], v46
	s_add_i32 s5, s4, 0x1c0
	s_and_b32 s5, s5, 0x1e0
	s_waitcnt lgkmcnt(1)
	v_mfma_f32_16x16x32_f16 v[38:41], v[42:45], v[86:89], v[38:41]
	v_lshl_add_u32 v42, s5, 1, v128
	ds_read_b128 v[42:45], v42
	s_addk_i32 s4, 0x1e0
	s_and_b32 s4, s4, 0x1e0
	s_waitcnt lgkmcnt(1)
	v_mfma_f32_16x16x32_f16 v[38:41], v[46:49], v[90:93], v[38:41]
	v_lshl_add_u32 v46, s4, 1, v128
	ds_read_b128 v[46:49], v46
	s_waitcnt lgkmcnt(1)
	v_mfma_f32_16x16x32_f16 v[38:41], v[42:45], v[94:97], v[38:41]
	v_mul_lo_u16_e32 v42, 0x56, v132
	v_mov_b32_e32 v43, 3
	v_mul_lo_u16_sdwa v42, v42, v43 dst_sel:DWORD dst_unused:UNUSED_PAD src0_sel:BYTE_1 src1_sel:DWORD
	v_sub_u16_e32 v42, v132, v42
	v_mov_b32_e32 v45, 6
	s_waitcnt lgkmcnt(0)
	v_mfma_f32_16x16x32_f16 v[38:41], v[46:49], v[98:101], v[38:41]
	v_mul_u32_u24_e32 v43, 0xd0, v120
	v_mul_u32_u24_e32 v44, 0x340, v107
	v_lshlrev_b32_sdwa v42, v45, v42 dst_sel:DWORD dst_unused:UNUSED_PAD src0_sel:DWORD src1_sel:BYTE_0
	v_add3_u32 v42, v44, v43, v42
	v_lshl_or_b32 v42, v109, 2, v42
	v_add_u32_e32 v42, 0xa000, v42
	s_nop 1
	ds_write2_b32 v42, v38, v39 offset1:52
	ds_write2_b32 v42, v40, v41 offset0:104 offset1:156
.LBB2_7:
	s_or_b64 exec, exec, s[2:3]
	s_movk_i32 s2, 0x100
	v_cmp_gt_u32_e32 vcc, s2, v0
	s_waitcnt lgkmcnt(0)
	s_barrier
	s_and_saveexec_b64 s[2:3], vcc
	s_cbranch_execz .LBB2_9
	s_load_dwordx2 s[4:5], s[0:1], 0x40
	v_lshrrev_b32_e32 v38, 3, v0
	v_and_b32_e32 v42, 0x70, v118
	s_movk_i32 s8, 0xd0
	v_mad_u32_u24 v39, v38, s8, v42
	v_or_b32_e32 v44, s25, v38
	ds_read_b128 v[38:41], v39 offset:41024
	v_mov_b32_e32 v45, 0
	v_lshlrev_b64 v[46:47], 7, v[44:45]
	s_waitcnt lgkmcnt(0)
	v_lshl_add_u64 v[46:47], s[4:5], 0, v[46:47]
	v_mov_b32_e32 v43, v45
	v_lshl_add_u64 v[42:43], v[46:47], 0, v[42:43]
	global_store_dwordx4 v[42:43], v[38:41], off sc1

.LBB2_13:
	s_or_b64 exec, exec, s[10:11]
	v_mfma_f32_16x16x32_f16 v[92:95], v[42:45], v[34:37], 0
	v_cvt_f32_f16_e32 v89, v24
	v_lshlrev_b32_e32 v52, 3, v107
	s_movk_i32 s0, 0x50
	v_mfma_f32_16x16x32_f16 v[34:37], v[38:41], v[34:37], 0
	v_cvt_f32_f16_e32 v49, v108
	s_nop 2
	v_add_f32_e32 v24, v92, v134
	v_min_f32_e32 v46, 0x42a00000, v24
	v_mul_f32_e32 v46, 0x3fb8aa3b, v46
	v_exp_f32_e32 v46, v46
	v_add_f32_e32 v48, v93, v134
	v_min_f32_e32 v50, 0x42a00000, v48
	v_mul_f32_e32 v50, 0x3fb8aa3b, v50
	v_add_f32_e32 v46, 1.0, v46
	v_log_f32_e32 v46, v46
	v_exp_f32_e32 v50, v50
	v_add_f32_e32 v56, v95, v134
	v_min_f32_e32 v58, 0x42a00000, v56
	v_mul_f32_e32 v46, 0x3f317218, v46
	v_max_f32_e32 v24, v24, v46
	v_add_f32_e32 v46, 1.0, v50
	v_add_f32_e32 v50, v94, v134
	v_min_f32_e32 v54, 0x42a00000, v50
	v_mul_f32_e32 v54, 0x3fb8aa3b, v54
	v_exp_f32_e32 v54, v54
	v_mul_f32_e32 v58, 0x3fb8aa3b, v58
	v_exp_f32_e32 v58, v58
	v_log_f32_e32 v46, v46
	v_add_f32_e32 v54, 1.0, v54
	v_log_f32_e32 v54, v54
	v_add_f32_e32 v58, 1.0, v58
	v_log_f32_e32 v58, v58
	v_mul_f32_e32 v46, 0x3f317218, v46
	v_mfma_f32_16x16x32_f16 v[92:95], v[42:45], v[30:33], 0
	v_max_f32_e32 v46, v48, v46
	v_mul_f32_e32 v48, 0x3f317218, v54
	v_max_f32_e32 v48, v50, v48
	v_mul_f32_e32 v50, 0x3f317218, v58
	v_max_f32_e32 v50, v56, v50
	v_cvt_pk_f16_f32 v97, v48, v50
	s_nop 1
	v_add_f32_e32 v48, v92, v133
	v_min_f32_e32 v50, 0x42a00000, v48
	v_mul_f32_e32 v50, 0x3fb8aa3b, v50
	v_exp_f32_e32 v50, v50
	v_cvt_pk_f16_f32 v96, v24, v46
	v_add_f32_e32 v58, v95, v133
	v_min_f32_e32 v60, 0x42a00000, v58
	v_add_f32_e32 v46, 1.0, v50
	v_add_f32_e32 v50, v93, v133
	v_min_f32_e32 v54, 0x42a00000, v50
	v_log_f32_e32 v46, v46
	v_mul_f32_e32 v54, 0x3fb8aa3b, v54
	v_exp_f32_e32 v54, v54
	v_mul_f32_e32 v60, 0x3fb8aa3b, v60
	v_mul_f32_e32 v46, 0x3f317218, v46
	v_max_f32_e32 v46, v48, v46
	v_add_f32_e32 v48, 1.0, v54
	v_add_f32_e32 v54, v94, v133
	v_min_f32_e32 v56, 0x42a00000, v54
	v_mul_f32_e32 v56, 0x3fb8aa3b, v56
	v_exp_f32_e32 v56, v56
	v_exp_f32_e32 v60, v60
	v_log_f32_e32 v48, v48
	s_waitcnt vmcnt(9)
	v_mfma_f32_16x16x32_f16 v[92:95], v[42:45], v[26:29], 0
	v_add_f32_e32 v56, 1.0, v56
	v_log_f32_e32 v56, v56
	v_add_f32_e32 v60, 1.0, v60
	v_log_f32_e32 v60, v60
	v_mul_f32_e32 v48, 0x3f317218, v48
	v_max_f32_e32 v48, v50, v48
	v_mul_f32_e32 v50, 0x3f317218, v56
	s_nop 0
	v_add_f32_e32 v56, v92, v131
	v_max_f32_e32 v50, v54, v50
	v_mul_f32_e32 v54, 0x3f317218, v60
	v_min_f32_e32 v60, 0x42a00000, v56
	v_mul_f32_e32 v60, 0x3fb8aa3b, v60
	v_exp_f32_e32 v60, v60
	v_mad_u32_u24 v24, v136, s0, v52
	ds_write_b64 v24, v[96:97]
	v_cvt_pk_f16_f32 v96, v46, v48
	v_add_f32_e32 v46, 1.0, v60
	v_log_f32_e32 v46, v46
	v_max_f32_e32 v54, v58, v54
	v_add_f32_e32 v48, v93, v131
	v_cvt_pk_f16_f32 v97, v50, v54
	v_min_f32_e32 v50, 0x42a00000, v48
	v_mul_f32_e32 v46, 0x3f317218, v46
	v_add_f32_e32 v54, v94, v131
	v_mul_f32_e32 v50, 0x3fb8aa3b, v50
	v_max_f32_e32 v46, v56, v46
	v_min_f32_e32 v56, 0x42a00000, v54
	v_exp_f32_e32 v50, v50
	v_mul_f32_e32 v56, 0x3fb8aa3b, v56
	v_exp_f32_e32 v56, v56
	s_waitcnt vmcnt(8)
	v_mfma_f32_16x16x32_f16 v[42:45], v[42:45], v[18:21], 0
	v_add_f32_e32 v50, 1.0, v50
	v_log_f32_e32 v50, v50
	v_add_f32_e32 v56, 1.0, v56
	v_log_f32_e32 v56, v56
	v_add_f32_e32 v58, v95, v131
	v_mul_f32_e32 v50, 0x3f317218, v50
	s_nop 1
	v_add_f32_e32 v42, v42, v121
	v_min_f32_e32 v60, 0x42a00000, v58
	v_max_f32_e32 v48, v48, v50
	v_mul_f32_e32 v50, 0x3f317218, v56
	v_min_f32_e32 v56, 0x42a00000, v42
	v_mul_f32_e32 v60, 0x3fb8aa3b, v60
	v_mul_f32_e32 v56, 0x3fb8aa3b, v56
	v_exp_f32_e32 v60, v60
	v_exp_f32_e32 v56, v56
	v_add_f32_e32 v43, v43, v121
	v_cvt_pk_f16_f32 v92, v46, v48
	v_add_f32_e32 v60, 1.0, v60
	v_add_f32_e32 v46, 1.0, v56
	v_min_f32_e32 v48, 0x42a00000, v43
	v_log_f32_e32 v60, v60
	v_log_f32_e32 v46, v46
	v_mul_f32_e32 v48, 0x3fb8aa3b, v48
	v_exp_f32_e32 v48, v48
	v_max_f32_e32 v50, v54, v50
	v_mul_f32_e32 v54, 0x3f317218, v60
	v_mul_f32_e32 v46, 0x3f317218, v46
	v_add_f32_e32 v44, v44, v121
	v_max_f32_e32 v54, v58, v54
	v_max_f32_e32 v42, v42, v46
	v_add_f32_e32 v46, 1.0, v48
	v_min_f32_e32 v48, 0x42a00000, v44
	v_add_f32_e32 v45, v45, v121
	v_cvt_pk_f16_f32 v93, v50, v54
	v_mul_f32_e32 v48, 0x3fb8aa3b, v48
	v_min_f32_e32 v50, 0x42a00000, v45
	v_exp_f32_e32 v48, v48
	v_mul_f32_e32 v50, 0x3fb8aa3b, v50
	v_exp_f32_e32 v50, v50
	v_log_f32_e32 v46, v46
	v_add_f32_e32 v48, 1.0, v48
	v_log_f32_e32 v48, v48
	v_add_f32_e32 v50, 1.0, v50
	v_log_f32_e32 v50, v50
	v_mul_f32_e32 v46, 0x3f317218, v46
	v_max_f32_e32 v46, v43, v46
	v_mul_f32_e32 v43, 0x3f317218, v48
	v_max_f32_e32 v43, v44, v43
	v_mul_f32_e32 v44, 0x3f317218, v50
	v_add_f32_e32 v34, v34, v134
	v_max_f32_e32 v44, v45, v44
	v_min_f32_e32 v45, 0x42a00000, v34
	v_mul_f32_e32 v45, 0x3fb8aa3b, v45
	v_exp_f32_e32 v45, v45
	v_add_f32_e32 v35, v35, v134
	v_cvt_pk_f16_f32 v43, v43, v44
	v_cvt_pk_f16_f32 v42, v42, v46
	v_mad_u32_u24 v44, v135, s0, v52
	v_add_f32_e32 v45, 1.0, v45
	v_min_f32_e32 v46, 0x42a00000, v35
	v_add_f32_e32 v36, v36, v134
	ds_write_b64 v24, v[96:97] offset:1280
	ds_write_b64 v24, v[92:93] offset:2560
	v_log_f32_e32 v45, v45
	v_mul_f32_e32 v46, 0x3fb8aa3b, v46
	ds_write_b64 v44, v[42:43]
	v_min_f32_e32 v43, 0x42a00000, v36
	v_exp_f32_e32 v46, v46
	v_mul_f32_e32 v43, 0x3fb8aa3b, v43
	v_exp_f32_e32 v43, v43
	v_add_f32_e32 v37, v37, v134
	v_mul_f32_e32 v42, 0x3f317218, v45
	v_min_f32_e32 v45, 0x42a00000, v37
	v_max_f32_e32 v34, v34, v42
	v_add_f32_e32 v42, 1.0, v46
	v_mul_f32_e32 v45, 0x3fb8aa3b, v45
	v_log_f32_e32 v42, v42
	v_exp_f32_e32 v45, v45
	v_add_f32_e32 v43, 1.0, v43
	v_mfma_f32_16x16x32_f16 v[30:33], v[38:41], v[30:33], 0
	v_log_f32_e32 v43, v43
	v_mul_f32_e32 v42, 0x3f317218, v42
	v_add_f32_e32 v45, 1.0, v45
	v_log_f32_e32 v45, v45
	v_max_f32_e32 v42, v35, v42
	s_nop 2
	v_add_f32_e32 v30, v30, v133
	v_mul_f32_e32 v35, 0x3f317218, v43
	v_min_f32_e32 v43, 0x42a00000, v30
	v_mul_f32_e32 v43, 0x3fb8aa3b, v43
	v_exp_f32_e32 v43, v43
	v_max_f32_e32 v35, v36, v35
	v_mul_f32_e32 v36, 0x3f317218, v45
	v_max_f32_e32 v36, v37, v36
	v_add_f32_e32 v31, v31, v133
	v_cvt_pk_f16_f32 v35, v35, v36
	v_cvt_pk_f16_f32 v34, v34, v42
	v_add_f32_e32 v36, 1.0, v43
	v_min_f32_e32 v37, 0x42a00000, v31
	v_add_f32_e32 v32, v32, v133
	v_log_f32_e32 v36, v36
	v_mul_f32_e32 v37, 0x3fb8aa3b, v37
	ds_write_b64 v24, v[34:35] offset:32
	v_min_f32_e32 v35, 0x42a00000, v32
	v_exp_f32_e32 v37, v37
	v_mul_f32_e32 v35, 0x3fb8aa3b, v35
	v_exp_f32_e32 v35, v35
	v_add_f32_e32 v33, v33, v133
	v_mul_f32_e32 v34, 0x3f317218, v36
	v_min_f32_e32 v36, 0x42a00000, v33
	v_max_f32_e32 v30, v30, v34
	v_add_f32_e32 v34, 1.0, v37
	v_mul_f32_e32 v36, 0x3fb8aa3b, v36
	v_log_f32_e32 v34, v34
	v_exp_f32_e32 v36, v36
	v_add_f32_e32 v35, 1.0, v35
	v_mfma_f32_16x16x32_f16 v[26:29], v[38:41], v[26:29], 0
	v_log_f32_e32 v35, v35
	v_mul_f32_e32 v34, 0x3f317218, v34
	v_add_f32_e32 v36, 1.0, v36
	v_log_f32_e32 v36, v36
	v_max_f32_e32 v34, v31, v34
	s_nop 2
	v_add_f32_e32 v26, v26, v131
	v_mul_f32_e32 v31, 0x3f317218, v35
	v_min_f32_e32 v35, 0x42a00000, v26
	v_mul_f32_e32 v35, 0x3fb8aa3b, v35
	v_exp_f32_e32 v35, v35
	v_max_f32_e32 v31, v32, v31
	v_mul_f32_e32 v32, 0x3f317218, v36
	v_max_f32_e32 v32, v33, v32
	v_add_f32_e32 v27, v27, v131
	v_cvt_pk_f16_f32 v31, v31, v32
	v_cvt_pk_f16_f32 v30, v30, v34
	v_add_f32_e32 v32, 1.0, v35
	v_min_f32_e32 v33, 0x42a00000, v27
	v_add_f32_e32 v28, v28, v131
	v_log_f32_e32 v32, v32
	v_mul_f32_e32 v33, 0x3fb8aa3b, v33
	ds_write_b64 v24, v[30:31] offset:1312
	v_min_f32_e32 v31, 0x42a00000, v28
	v_exp_f32_e32 v33, v33
	v_mul_f32_e32 v31, 0x3fb8aa3b, v31
	v_exp_f32_e32 v31, v31
	v_add_f32_e32 v29, v29, v131
	v_mul_f32_e32 v30, 0x3f317218, v32
	v_min_f32_e32 v32, 0x42a00000, v29
	v_max_f32_e32 v26, v26, v30
	v_add_f32_e32 v30, 1.0, v33
	v_mul_f32_e32 v32, 0x3fb8aa3b, v32
	v_log_f32_e32 v30, v30
	v_exp_f32_e32 v32, v32
	v_add_f32_e32 v31, 1.0, v31
	v_mfma_f32_16x16x32_f16 v[18:21], v[38:41], v[18:21], 0
	v_log_f32_e32 v31, v31
	v_mul_f32_e32 v30, 0x3f317218, v30
	v_add_f32_e32 v32, 1.0, v32
	v_log_f32_e32 v32, v32
	v_max_f32_e32 v30, v27, v30
	s_nop 2
	v_add_f32_e32 v18, v18, v121
	v_mul_f32_e32 v27, 0x3f317218, v31
	v_min_f32_e32 v31, 0x42a00000, v18
	v_mul_f32_e32 v31, 0x3fb8aa3b, v31
	v_exp_f32_e32 v31, v31
	v_max_f32_e32 v27, v28, v27
	v_mul_f32_e32 v28, 0x3f317218, v32
	v_max_f32_e32 v28, v29, v28
	v_add_f32_e32 v19, v19, v121
	v_cvt_pk_f16_f32 v27, v27, v28
	v_cvt_pk_f16_f32 v26, v26, v30
	v_add_f32_e32 v28, 1.0, v31
	v_min_f32_e32 v29, 0x42a00000, v19
	v_add_f32_e32 v20, v20, v121
	v_log_f32_e32 v28, v28
	v_mul_f32_e32 v29, 0x3fb8aa3b, v29
	ds_write_b64 v24, v[26:27] offset:2592
	v_min_f32_e32 v26, 0x42a00000, v20
	v_add_f32_e32 v21, v21, v121
	v_exp_f32_e32 v29, v29
	v_mul_f32_e32 v26, 0x3fb8aa3b, v26
	v_min_f32_e32 v27, 0x42a00000, v21
	v_exp_f32_e32 v26, v26
	v_mul_f32_e32 v27, 0x3fb8aa3b, v27
	v_exp_f32_e32 v27, v27
	v_mul_f32_e32 v24, 0x3f317218, v28
	v_max_f32_e32 v18, v18, v24
	v_add_f32_e32 v24, 1.0, v29
	v_log_f32_e32 v24, v24
	v_add_f32_e32 v26, 1.0, v26
	v_log_f32_e32 v26, v26
	v_add_f32_e32 v27, 1.0, v27
	v_log_f32_e32 v27, v27
	v_mul_f32_e32 v24, 0x3f317218, v24
	v_max_f32_e32 v24, v19, v24
	v_mul_f32_e32 v19, 0x3f317218, v26
	v_max_f32_e32 v19, v20, v19
	v_mul_f32_e32 v20, 0x3f317218, v27
	v_max_f32_e32 v20, v21, v20
	v_cvt_pk_f16_f32 v19, v19, v20
	v_cvt_pk_f16_f32 v18, v18, v24
	ds_write_b64 v44, v[18:19] offset:32
	v_mul_u32_u24_e32 v18, 0x50, v0
	s_waitcnt lgkmcnt(0)
	s_barrier
	ds_read_b128 v[92:95], v18
	v_cvt_f32_f16_e32 v55, v111
	v_cvt_f32_f16_e32 v59, v110
	v_cvt_f32_f16_e32 v79, v105
	v_cvt_f32_f16_e32 v82, v104
	v_cvt_f32_f16_e32 v84, v103
	v_cvt_f32_f16_e32 v86, v102
	ds_read_b128 v[96:99], v18 offset:16
	ds_read_b128 v[100:103], v18 offset:32
	ds_read_b128 v[108:111], v18 offset:48
	v_lshl_add_u64 v[104:105], s[8:9], 0, v[118:119]
	v_cvt_f32_f16_e32 v47, v113
	v_cvt_f32_f16_e32 v51, v112
	v_lshl_add_u64 v[112:113], v[104:105], 0, s[6:7]
	s_waitcnt lgkmcnt(3)
	v_cvt_f32_f16_e32 v26, v94
	v_cvt_f32_f16_sdwa v28, v94 dst_sel:DWORD dst_unused:UNUSED_PAD src0_sel:WORD_1
	v_cvt_f32_f16_e32 v30, v95
	v_cvt_f32_f16_sdwa v32, v95 dst_sel:DWORD dst_unused:UNUSED_PAD src0_sel:WORD_1
	global_store_dwordx4 v[112:113], v[92:95], off sc1
	v_cvt_f32_f16_e32 v53, v122
	v_cvt_f32_f16_e32 v57, v125
	v_lshl_add_u64 v[94:95], v[104:105], 0, s[14:15]
	s_waitcnt lgkmcnt(2)
	global_store_dwordx4 v[94:95], v[96:99], off sc1
	v_lshl_add_u64 v[94:95], v[104:105], 0, s[16:17]
	s_waitcnt lgkmcnt(1)
	global_store_dwordx4 v[94:95], v[100:103], off sc1
	v_lshl_add_u64 v[94:95], v[104:105], 0, s[18:19]
	v_cvt_f32_f16_e32 v61, v124
	v_cvt_f32_f16_e32 v63, v117
	v_cvt_f32_f16_e32 v65, v147
	v_cvt_f32_f16_e32 v67, v116
	v_cvt_f32_f16_e32 v69, v145
	v_cvt_f32_f16_e32 v71, v115
	v_cvt_f32_f16_e32 v73, v127
	v_cvt_f32_f16_e32 v75, v114
	v_cvt_f32_f16_e32 v77, v126
	v_cvt_f32_f16_e32 v81, v142
	v_cvt_f32_f16_e32 v83, v141
	v_cvt_f32_f16_e32 v85, v140
	v_cvt_f32_f16_e32 v87, v139
	v_cvt_f32_f16_e32 v25, v25
	v_cvt_f32_f16_e32 v88, v138
	v_cvt_f32_f16_e32 v90, v137
	v_cvt_f32_f16_e32 v23, v23
	v_cvt_f32_f16_e32 v91, v123
	v_cvt_f32_f16_e32 v19, v22
	v_cvt_f32_f16_sdwa v20, v92 dst_sel:DWORD dst_unused:UNUSED_PAD src0_sel:WORD_1
	v_cvt_f32_f16_e32 v22, v93
	v_cvt_f32_f16_sdwa v24, v93 dst_sel:DWORD dst_unused:UNUSED_PAD src0_sel:WORD_1
	v_cvt_f32_f16_e32 v34, v96
	v_cvt_f32_f16_sdwa v36, v96 dst_sel:DWORD dst_unused:UNUSED_PAD src0_sel:WORD_1
	v_cvt_f32_f16_e32 v38, v97
	v_cvt_f32_f16_sdwa v40, v97 dst_sel:DWORD dst_unused:UNUSED_PAD src0_sel:WORD_1
	v_cvt_f32_f16_e32 v42, v98
	v_cvt_f32_f16_sdwa v44, v98 dst_sel:DWORD dst_unused:UNUSED_PAD src0_sel:WORD_1
	v_cvt_f32_f16_e32 v46, v99
	v_cvt_f32_f16_sdwa v48, v99 dst_sel:DWORD dst_unused:UNUSED_PAD src0_sel:WORD_1
	v_cvt_f32_f16_e32 v50, v100
	v_cvt_f32_f16_sdwa v52, v100 dst_sel:DWORD dst_unused:UNUSED_PAD src0_sel:WORD_1
	v_cvt_f32_f16_e32 v54, v101
	v_cvt_f32_f16_sdwa v56, v101 dst_sel:DWORD dst_unused:UNUSED_PAD src0_sel:WORD_1
	v_cvt_f32_f16_e32 v58, v102
	v_cvt_f32_f16_sdwa v60, v102 dst_sel:DWORD dst_unused:UNUSED_PAD src0_sel:WORD_1
	v_cvt_f32_f16_e32 v62, v103
	v_cvt_f32_f16_sdwa v64, v103 dst_sel:DWORD dst_unused:UNUSED_PAD src0_sel:WORD_1
	s_waitcnt lgkmcnt(0)
	v_cvt_f32_f16_e32 v66, v108
	v_cvt_f32_f16_sdwa v68, v108 dst_sel:DWORD dst_unused:UNUSED_PAD src0_sel:WORD_1
	v_cvt_f32_f16_e32 v70, v109
	v_cvt_f32_f16_sdwa v72, v109 dst_sel:DWORD dst_unused:UNUSED_PAD src0_sel:WORD_1
	v_cvt_f32_f16_e32 v74, v110
	v_cvt_f32_f16_sdwa v76, v110 dst_sel:DWORD dst_unused:UNUSED_PAD src0_sel:WORD_1
	v_cvt_f32_f16_e32 v78, v111
	v_cvt_f32_f16_sdwa v18, v111 dst_sel:DWORD dst_unused:UNUSED_PAD src0_sel:WORD_1
	global_store_dwordx4 v[94:95], v[108:111], off sc1
	v_cvt_f32_f16_e32 v80, v92
	v_mov_b32_e32 v21, 0xa000
	v_mov_b32_e32 v27, 0xa0d0
	ds_read_b128 v[92:95], v21 offset:64
	ds_read_b128 v[96:99], v21 offset:80
	ds_read_b128 v[100:103], v21 offset:96
	ds_read_b128 v[108:111], v21 offset:112
	s_waitcnt lgkmcnt(0)
	ds_read_b128 v[112:115], v27 offset:64
	ds_read_b128 v[116:119], v27 offset:80
	ds_read_b128 v[120:123], v27 offset:96
	ds_read_b128 v[124:127], v27 offset:112
	s_lshr_b32 s0, s23, 5
	s_waitcnt vmcnt(11)
	v_pk_mul_f32 v[128:129], v[80:81], v[14:15] op_sel_hi:[0,1]
	v_exp_f32_e32 v128, v128
	v_exp_f32_e32 v129, v129
	v_pk_mul_f32 v[130:131], v[80:81], v[16:17] op_sel_hi:[0,1]
	v_exp_f32_e32 v130, v130
	v_exp_f32_e32 v131, v131
	v_mul_f32_e32 v104, v80, v19
	v_pk_mul_f32 v[92:93], v[104:105], v[92:93] op_sel_hi:[0,1]
	v_pk_fma_f32 v[128:129], v[128:129], 0, v[92:93] op_sel_hi:[1,0,1]
	v_pk_mul_f32 v[92:93], v[104:105], v[94:95] op_sel_hi:[0,1]
	v_pk_fma_f32 v[130:131], v[130:131], 0, v[92:93] op_sel_hi:[1,0,1]
	s_waitcnt vmcnt(10)
	v_pk_mul_f32 v[92:93], v[80:81], v[10:11] op_sel_hi:[0,1]
	v_exp_f32_e32 v92, v92
	v_exp_f32_e32 v93, v93
	v_pk_mul_f32 v[94:95], v[80:81], v[12:13] op_sel_hi:[0,1]
	v_exp_f32_e32 v94, v94
	v_exp_f32_e32 v95, v95
	v_pk_mul_f32 v[96:97], v[104:105], v[96:97] op_sel_hi:[0,1]
	v_pk_fma_f32 v[132:133], v[92:93], 0, v[96:97] op_sel_hi:[1,0,1]
	v_pk_mul_f32 v[92:93], v[104:105], v[98:99] op_sel_hi:[0,1]
	v_pk_fma_f32 v[134:135], v[94:95], 0, v[92:93] op_sel_hi:[1,0,1]
	s_waitcnt vmcnt(9)
	v_pk_mul_f32 v[92:93], v[80:81], v[6:7] op_sel_hi:[0,1]
	v_exp_f32_e32 v92, v92
	v_exp_f32_e32 v93, v93
	v_pk_mul_f32 v[94:95], v[80:81], v[8:9] op_sel_hi:[0,1]
	v_exp_f32_e32 v94, v94
	v_exp_f32_e32 v95, v95
	v_pk_mul_f32 v[96:97], v[104:105], v[100:101] op_sel_hi:[0,1]
	v_pk_fma_f32 v[136:137], v[92:93], 0, v[96:97] op_sel_hi:[1,0,1]
	v_pk_mul_f32 v[92:93], v[104:105], v[102:103] op_sel_hi:[0,1]
	v_pk_fma_f32 v[138:139], v[94:95], 0, v[92:93] op_sel_hi:[1,0,1]
	s_waitcnt vmcnt(8)
	v_pk_mul_f32 v[92:93], v[80:81], v[2:3] op_sel_hi:[0,1]
	v_exp_f32_e32 v92, v92
	v_exp_f32_e32 v93, v93
	v_pk_mul_f32 v[94:95], v[80:81], v[4:5] op_sel_hi:[0,1]
	v_exp_f32_e32 v94, v94
	v_exp_f32_e32 v95, v95
	v_pk_mul_f32 v[96:97], v[104:105], v[108:109] op_sel_hi:[0,1]
	v_pk_fma_f32 v[140:141], v[92:93], 0, v[96:97] op_sel_hi:[1,0,1]
	v_pk_mul_f32 v[92:93], v[104:105], v[110:111] op_sel_hi:[0,1]
	v_pk_fma_f32 v[104:105], v[94:95], 0, v[92:93] op_sel_hi:[1,0,1]
	v_mov_b32_e32 v19, 0xa1a0
	s_waitcnt lgkmcnt(0)
	s_and_b32 s6, s22, 0x7ffffc0
	ds_read_b128 v[92:95], v19 offset:64
	ds_read_b128 v[96:99], v19 offset:80
	ds_read_b128 v[100:103], v19 offset:96
	ds_read_b128 v[108:111], v19 offset:112
	v_mov_b32_e32 v19, 0xa270
	v_pk_mul_f32 v[142:143], v[20:21], v[14:15] op_sel_hi:[0,1]
	v_exp_f32_e32 v142, v142
	v_exp_f32_e32 v143, v143
	v_mul_f32_e32 v144, v20, v91
	v_pk_mul_f32 v[112:113], v[144:145], v[112:113] op_sel_hi:[0,1]
	v_pk_mul_f32 v[114:115], v[144:145], v[114:115] op_sel_hi:[0,1]
	v_pk_fma_f32 v[128:129], v[128:129], v[142:143], v[112:113]
	v_pk_mul_f32 v[112:113], v[20:21], v[16:17] op_sel_hi:[0,1]
	v_exp_f32_e32 v112, v112
	v_exp_f32_e32 v113, v113
	v_pk_mul_f32 v[116:117], v[144:145], v[116:117] op_sel_hi:[0,1]
	s_or_b32 s0, s0, s6
	s_lshl_b64 s[6:7], s[0:1], 14
	v_pk_fma_f32 v[130:131], v[130:131], v[112:113], v[114:115]
	v_pk_mul_f32 v[112:113], v[20:21], v[10:11] op_sel_hi:[0,1]
	v_exp_f32_e32 v112, v112
	v_exp_f32_e32 v113, v113
	v_pk_mul_f32 v[114:115], v[20:21], v[12:13] op_sel_hi:[0,1]
	v_exp_f32_e32 v114, v114
	v_exp_f32_e32 v115, v115
	v_pk_fma_f32 v[132:133], v[132:133], v[112:113], v[116:117]
	v_pk_mul_f32 v[112:113], v[144:145], v[118:119] op_sel_hi:[0,1]
	v_pk_mul_f32 v[116:117], v[144:145], v[120:121] op_sel_hi:[0,1]
	v_pk_fma_f32 v[134:135], v[134:135], v[114:115], v[112:113]
	v_pk_mul_f32 v[112:113], v[20:21], v[6:7] op_sel_hi:[0,1]
	v_exp_f32_e32 v112, v112
	v_exp_f32_e32 v113, v113
	v_pk_mul_f32 v[114:115], v[20:21], v[8:9] op_sel_hi:[0,1]
	v_exp_f32_e32 v114, v114
	v_exp_f32_e32 v115, v115
	v_pk_fma_f32 v[136:137], v[136:137], v[112:113], v[116:117]
	v_pk_mul_f32 v[112:113], v[144:145], v[122:123] op_sel_hi:[0,1]
	v_pk_mul_f32 v[116:117], v[144:145], v[124:125] op_sel_hi:[0,1]
	v_pk_fma_f32 v[138:139], v[138:139], v[114:115], v[112:113]
	v_pk_mul_f32 v[112:113], v[20:21], v[2:3] op_sel_hi:[0,1]
	v_exp_f32_e32 v112, v112
	v_exp_f32_e32 v113, v113
	v_pk_mul_f32 v[114:115], v[20:21], v[4:5] op_sel_hi:[0,1]
	v_exp_f32_e32 v114, v114
	v_exp_f32_e32 v115, v115
	v_pk_fma_f32 v[140:141], v[140:141], v[112:113], v[116:117]
	v_pk_mul_f32 v[112:113], v[144:145], v[126:127] op_sel_hi:[0,1]
	s_lshl_b64 s[0:1], s[0:1], 11
	v_pk_fma_f32 v[104:105], v[104:105], v[114:115], v[112:113]
	s_add_u32 s0, s2, s0
	s_waitcnt lgkmcnt(0)
	s_addc_u32 s1, s3, s1
	ds_read_b128 v[112:115], v19 offset:64
	ds_read_b128 v[116:119], v19 offset:80
	ds_read_b128 v[120:123], v19 offset:96
	ds_read_b128 v[124:127], v19 offset:112
	v_mov_b32_e32 v19, 0xa340
	v_pk_mul_f32 v[142:143], v[22:23], v[14:15] op_sel_hi:[0,1]
	v_exp_f32_e32 v142, v142
	v_exp_f32_e32 v143, v143
	v_mul_f32_e32 v144, v22, v23
	v_pk_mul_f32 v[92:93], v[144:145], v[92:93] op_sel_hi:[0,1]
	v_pk_mul_f32 v[94:95], v[144:145], v[94:95] op_sel_hi:[0,1]
	v_pk_fma_f32 v[128:129], v[128:129], v[142:143], v[92:93]
	v_pk_mul_f32 v[92:93], v[22:23], v[16:17] op_sel_hi:[0,1]
	v_exp_f32_e32 v92, v92
	v_exp_f32_e32 v93, v93
	v_pk_mul_f32 v[96:97], v[144:145], v[96:97] op_sel_hi:[0,1]
	v_pk_fma_f32 v[130:131], v[130:131], v[92:93], v[94:95]
	v_pk_mul_f32 v[92:93], v[22:23], v[10:11] op_sel_hi:[0,1]
	v_exp_f32_e32 v92, v92
	v_exp_f32_e32 v93, v93
	v_pk_mul_f32 v[94:95], v[22:23], v[12:13] op_sel_hi:[0,1]
	v_exp_f32_e32 v94, v94
	v_exp_f32_e32 v95, v95
	v_pk_fma_f32 v[132:133], v[132:133], v[92:93], v[96:97]
	v_pk_mul_f32 v[92:93], v[144:145], v[98:99] op_sel_hi:[0,1]
	v_pk_mul_f32 v[96:97], v[144:145], v[100:101] op_sel_hi:[0,1]
	v_pk_fma_f32 v[134:135], v[134:135], v[94:95], v[92:93]
	v_pk_mul_f32 v[92:93], v[22:23], v[6:7] op_sel_hi:[0,1]
	v_exp_f32_e32 v92, v92
	v_exp_f32_e32 v93, v93
	v_pk_mul_f32 v[94:95], v[22:23], v[8:9] op_sel_hi:[0,1]
	v_exp_f32_e32 v94, v94
	v_exp_f32_e32 v95, v95
	v_pk_fma_f32 v[136:137], v[136:137], v[92:93], v[96:97]
	v_pk_mul_f32 v[92:93], v[144:145], v[102:103] op_sel_hi:[0,1]
	v_pk_mul_f32 v[96:97], v[144:145], v[108:109] op_sel_hi:[0,1]
	v_pk_fma_f32 v[138:139], v[138:139], v[94:95], v[92:93]
	v_pk_mul_f32 v[92:93], v[22:23], v[2:3] op_sel_hi:[0,1]
	v_exp_f32_e32 v92, v92
	v_exp_f32_e32 v93, v93
	v_pk_mul_f32 v[94:95], v[22:23], v[4:5] op_sel_hi:[0,1]
	v_exp_f32_e32 v94, v94
	v_exp_f32_e32 v95, v95
	v_pk_fma_f32 v[140:141], v[140:141], v[92:93], v[96:97]
	v_pk_mul_f32 v[92:93], v[144:145], v[110:111] op_sel_hi:[0,1]
	v_pk_fma_f32 v[104:105], v[104:105], v[94:95], v[92:93]
	s_nop 0
	s_waitcnt lgkmcnt(0)
	s_nop 0
	ds_read_b128 v[92:95], v19 offset:64
	ds_read_b128 v[96:99], v19 offset:80
	ds_read_b128 v[100:103], v19 offset:96
	ds_read_b128 v[108:111], v19 offset:112
	v_mov_b32_e32 v19, 0xa410
	v_pk_mul_f32 v[142:143], v[24:25], v[14:15] op_sel_hi:[0,1]
	v_exp_f32_e32 v142, v142
	v_exp_f32_e32 v143, v143
	v_mul_f32_e32 v90, v24, v90
	v_pk_mul_f32 v[112:113], v[90:91], v[112:113] op_sel_hi:[0,1]
	v_pk_mul_f32 v[114:115], v[90:91], v[114:115] op_sel_hi:[0,1]
	v_pk_fma_f32 v[128:129], v[128:129], v[142:143], v[112:113]
	v_pk_mul_f32 v[112:113], v[24:25], v[16:17] op_sel_hi:[0,1]
	v_exp_f32_e32 v112, v112
	v_exp_f32_e32 v113, v113
	v_pk_mul_f32 v[116:117], v[90:91], v[116:117] op_sel_hi:[0,1]
	v_pk_fma_f32 v[130:131], v[130:131], v[112:113], v[114:115]
	v_pk_mul_f32 v[112:113], v[24:25], v[10:11] op_sel_hi:[0,1]
	v_exp_f32_e32 v112, v112
	v_exp_f32_e32 v113, v113
	v_pk_mul_f32 v[114:115], v[24:25], v[12:13] op_sel_hi:[0,1]
	v_exp_f32_e32 v114, v114
	v_exp_f32_e32 v115, v115
	v_pk_fma_f32 v[132:133], v[132:133], v[112:113], v[116:117]
	v_pk_mul_f32 v[112:113], v[90:91], v[118:119] op_sel_hi:[0,1]
	v_pk_mul_f32 v[116:117], v[90:91], v[120:121] op_sel_hi:[0,1]
	v_pk_fma_f32 v[134:135], v[134:135], v[114:115], v[112:113]
	v_pk_mul_f32 v[112:113], v[24:25], v[6:7] op_sel_hi:[0,1]
	v_exp_f32_e32 v112, v112
	v_exp_f32_e32 v113, v113
	v_pk_mul_f32 v[114:115], v[24:25], v[8:9] op_sel_hi:[0,1]
	v_exp_f32_e32 v114, v114
	v_exp_f32_e32 v115, v115
	v_pk_fma_f32 v[136:137], v[136:137], v[112:113], v[116:117]
	v_pk_mul_f32 v[112:113], v[90:91], v[122:123] op_sel_hi:[0,1]
	v_pk_mul_f32 v[116:117], v[90:91], v[124:125] op_sel_hi:[0,1]
	v_pk_fma_f32 v[138:139], v[138:139], v[114:115], v[112:113]
	v_pk_mul_f32 v[112:113], v[24:25], v[2:3] op_sel_hi:[0,1]
	v_pk_mul_f32 v[114:115], v[24:25], v[4:5] op_sel_hi:[0,1]
	v_exp_f32_e32 v112, v112
	v_exp_f32_e32 v113, v113
	v_exp_f32_e32 v114, v114
	v_exp_f32_e32 v115, v115
	v_pk_mul_f32 v[90:91], v[90:91], v[126:127] op_sel_hi:[0,1]
	v_pk_fma_f32 v[140:141], v[140:141], v[112:113], v[116:117]
	v_pk_fma_f32 v[90:91], v[104:105], v[114:115], v[90:91]
	s_nop 0
	s_waitcnt lgkmcnt(0)
	s_nop 0
	ds_read_b128 v[112:115], v19 offset:64
	ds_read_b128 v[116:119], v19 offset:80
	ds_read_b128 v[120:123], v19 offset:96
	ds_read_b128 v[124:127], v19 offset:112
	v_mov_b32_e32 v19, 0xa4e0
	v_pk_mul_f32 v[104:105], v[26:27], v[14:15] op_sel_hi:[0,1]
	v_exp_f32_e32 v104, v104
	v_exp_f32_e32 v105, v105
	v_mul_f32_e32 v142, v26, v89
	v_pk_mul_f32 v[92:93], v[142:143], v[92:93] op_sel_hi:[0,1]
	v_pk_mul_f32 v[94:95], v[142:143], v[94:95] op_sel_hi:[0,1]
	v_pk_fma_f32 v[128:129], v[128:129], v[104:105], v[92:93]
	v_pk_mul_f32 v[92:93], v[26:27], v[16:17] op_sel_hi:[0,1]
	v_exp_f32_e32 v92, v92
	v_exp_f32_e32 v93, v93
	v_pk_mul_f32 v[96:97], v[142:143], v[96:97] op_sel_hi:[0,1]
	v_pk_fma_f32 v[130:131], v[130:131], v[92:93], v[94:95]
	v_pk_mul_f32 v[92:93], v[26:27], v[10:11] op_sel_hi:[0,1]
	v_exp_f32_e32 v92, v92
	v_exp_f32_e32 v93, v93
	v_pk_mul_f32 v[94:95], v[26:27], v[12:13] op_sel_hi:[0,1]
	v_exp_f32_e32 v94, v94
	v_exp_f32_e32 v95, v95
	v_pk_fma_f32 v[132:133], v[132:133], v[92:93], v[96:97]
	v_pk_mul_f32 v[92:93], v[142:143], v[98:99] op_sel_hi:[0,1]
	v_pk_mul_f32 v[96:97], v[142:143], v[100:101] op_sel_hi:[0,1]
	v_pk_fma_f32 v[134:135], v[134:135], v[94:95], v[92:93]
	v_pk_mul_f32 v[92:93], v[26:27], v[6:7] op_sel_hi:[0,1]
	v_exp_f32_e32 v92, v92
	v_exp_f32_e32 v93, v93
	v_pk_mul_f32 v[94:95], v[26:27], v[8:9] op_sel_hi:[0,1]
	v_exp_f32_e32 v94, v94
	v_exp_f32_e32 v95, v95
	v_pk_fma_f32 v[136:137], v[136:137], v[92:93], v[96:97]
	v_pk_mul_f32 v[92:93], v[142:143], v[102:103] op_sel_hi:[0,1]
	v_pk_mul_f32 v[96:97], v[142:143], v[108:109] op_sel_hi:[0,1]
	v_pk_fma_f32 v[138:139], v[138:139], v[94:95], v[92:93]
	v_pk_mul_f32 v[92:93], v[26:27], v[2:3] op_sel_hi:[0,1]
	v_exp_f32_e32 v92, v92
	v_exp_f32_e32 v93, v93
	v_pk_mul_f32 v[94:95], v[26:27], v[4:5] op_sel_hi:[0,1]
	v_exp_f32_e32 v94, v94
	v_exp_f32_e32 v95, v95
	v_pk_fma_f32 v[108:109], v[140:141], v[92:93], v[96:97]
	v_pk_mul_f32 v[92:93], v[142:143], v[110:111] op_sel_hi:[0,1]
	v_pk_fma_f32 v[110:111], v[90:91], v[94:95], v[92:93]
	s_nop 0
	s_waitcnt lgkmcnt(0)
	s_nop 0
	ds_read_b128 v[90:93], v19 offset:64
	ds_read_b128 v[94:97], v19 offset:80
	ds_read_b128 v[98:101], v19 offset:96
	ds_read_b128 v[102:105], v19 offset:112
	v_mov_b32_e32 v19, 0xa5b0
	v_pk_mul_f32 v[140:141], v[28:29], v[14:15] op_sel_hi:[0,1]
	v_exp_f32_e32 v140, v140
	v_exp_f32_e32 v141, v141
	v_pk_mul_f32 v[142:143], v[28:29], v[16:17] op_sel_hi:[0,1]
	v_exp_f32_e32 v142, v142
	v_exp_f32_e32 v143, v143
	v_mul_f32_e32 v88, v28, v88
	v_pk_mul_f32 v[112:113], v[88:89], v[112:113] op_sel_hi:[0,1]
	v_pk_fma_f32 v[128:129], v[128:129], v[140:141], v[112:113]
	v_pk_mul_f32 v[112:113], v[88:89], v[114:115] op_sel_hi:[0,1]
	v_pk_fma_f32 v[130:131], v[130:131], v[142:143], v[112:113]
	v_pk_mul_f32 v[112:113], v[28:29], v[10:11] op_sel_hi:[0,1]
	v_exp_f32_e32 v112, v112
	v_exp_f32_e32 v113, v113
	v_pk_mul_f32 v[114:115], v[28:29], v[12:13] op_sel_hi:[0,1]
	v_exp_f32_e32 v114, v114
	v_exp_f32_e32 v115, v115
	v_pk_mul_f32 v[116:117], v[88:89], v[116:117] op_sel_hi:[0,1]
	v_pk_fma_f32 v[132:133], v[132:133], v[112:113], v[116:117]
	v_pk_mul_f32 v[112:113], v[88:89], v[118:119] op_sel_hi:[0,1]
	v_pk_fma_f32 v[134:135], v[134:135], v[114:115], v[112:113]
	v_pk_mul_f32 v[112:113], v[28:29], v[6:7] op_sel_hi:[0,1]
	v_exp_f32_e32 v112, v112
	v_exp_f32_e32 v113, v113
	v_pk_mul_f32 v[114:115], v[28:29], v[8:9] op_sel_hi:[0,1]
	v_exp_f32_e32 v114, v114
	v_exp_f32_e32 v115, v115
	v_pk_mul_f32 v[116:117], v[88:89], v[120:121] op_sel_hi:[0,1]
	v_pk_fma_f32 v[136:137], v[136:137], v[112:113], v[116:117]
	v_pk_mul_f32 v[112:113], v[88:89], v[122:123] op_sel_hi:[0,1]
	v_pk_fma_f32 v[138:139], v[138:139], v[114:115], v[112:113]
	v_pk_mul_f32 v[112:113], v[28:29], v[2:3] op_sel_hi:[0,1]
	v_pk_mul_f32 v[114:115], v[28:29], v[4:5] op_sel_hi:[0,1]
	v_exp_f32_e32 v112, v112
	v_exp_f32_e32 v113, v113
	v_exp_f32_e32 v114, v114
	v_exp_f32_e32 v115, v115
	v_pk_mul_f32 v[116:117], v[88:89], v[124:125] op_sel_hi:[0,1]
	v_pk_mul_f32 v[88:89], v[88:89], v[126:127] op_sel_hi:[0,1]
	v_pk_fma_f32 v[124:125], v[108:109], v[112:113], v[116:117]
	v_pk_fma_f32 v[88:89], v[110:111], v[114:115], v[88:89]
	s_nop 0
	s_waitcnt lgkmcnt(0)
	s_nop 0
	ds_read_b128 v[108:111], v19 offset:64
	ds_read_b128 v[112:115], v19 offset:80
	ds_read_b128 v[116:119], v19 offset:96
	ds_read_b128 v[120:123], v19 offset:112
	v_mov_b32_e32 v19, 0xa680
	v_pk_mul_f32 v[140:141], v[30:31], v[14:15] op_sel_hi:[0,1]
	v_exp_f32_e32 v140, v140
	v_exp_f32_e32 v141, v141
	v_pk_mul_f32 v[142:143], v[30:31], v[16:17] op_sel_hi:[0,1]
	v_exp_f32_e32 v142, v142
	v_exp_f32_e32 v143, v143
	v_mul_f32_e32 v126, v30, v25
	v_pk_mul_f32 v[90:91], v[126:127], v[90:91] op_sel_hi:[0,1]
	v_pk_fma_f32 v[128:129], v[128:129], v[140:141], v[90:91]
	v_pk_mul_f32 v[90:91], v[126:127], v[92:93] op_sel_hi:[0,1]
	v_pk_fma_f32 v[130:131], v[130:131], v[142:143], v[90:91]
	v_pk_mul_f32 v[90:91], v[30:31], v[10:11] op_sel_hi:[0,1]
	v_exp_f32_e32 v90, v90
	v_exp_f32_e32 v91, v91
	v_pk_mul_f32 v[92:93], v[30:31], v[12:13] op_sel_hi:[0,1]
	v_exp_f32_e32 v92, v92
	v_exp_f32_e32 v93, v93
	v_pk_mul_f32 v[94:95], v[126:127], v[94:95] op_sel_hi:[0,1]
	v_pk_fma_f32 v[132:133], v[132:133], v[90:91], v[94:95]
	v_pk_mul_f32 v[90:91], v[126:127], v[96:97] op_sel_hi:[0,1]
	v_pk_fma_f32 v[134:135], v[134:135], v[92:93], v[90:91]
	v_pk_mul_f32 v[90:91], v[30:31], v[6:7] op_sel_hi:[0,1]
	v_exp_f32_e32 v90, v90
	v_exp_f32_e32 v91, v91
	v_pk_mul_f32 v[92:93], v[30:31], v[8:9] op_sel_hi:[0,1]
	v_exp_f32_e32 v92, v92
	v_exp_f32_e32 v93, v93
	v_pk_mul_f32 v[94:95], v[126:127], v[98:99] op_sel_hi:[0,1]
	v_pk_fma_f32 v[136:137], v[136:137], v[90:91], v[94:95]
	v_pk_mul_f32 v[90:91], v[126:127], v[100:101] op_sel_hi:[0,1]
	v_pk_fma_f32 v[138:139], v[138:139], v[92:93], v[90:91]
	v_pk_mul_f32 v[90:91], v[30:31], v[2:3] op_sel_hi:[0,1]
	v_exp_f32_e32 v90, v90
	v_exp_f32_e32 v91, v91
	v_pk_mul_f32 v[92:93], v[30:31], v[4:5] op_sel_hi:[0,1]
	v_exp_f32_e32 v92, v92
	v_exp_f32_e32 v93, v93
	v_pk_mul_f32 v[94:95], v[126:127], v[102:103] op_sel_hi:[0,1]
	v_pk_fma_f32 v[124:125], v[124:125], v[90:91], v[94:95]
	v_pk_mul_f32 v[90:91], v[126:127], v[104:105] op_sel_hi:[0,1]
	v_pk_fma_f32 v[104:105], v[88:89], v[92:93], v[90:91]
	s_nop 0
	s_waitcnt lgkmcnt(0)
	s_nop 0
	ds_read_b128 v[88:91], v19 offset:64
	ds_read_b128 v[92:95], v19 offset:80
	ds_read_b128 v[96:99], v19 offset:96
	ds_read_b128 v[100:103], v19 offset:112
	v_mov_b32_e32 v19, 0xa750
	v_pk_mul_f32 v[140:141], v[32:33], v[14:15] op_sel_hi:[0,1]
	v_exp_f32_e32 v140, v140
	v_exp_f32_e32 v141, v141
	v_pk_mul_f32 v[142:143], v[32:33], v[16:17] op_sel_hi:[0,1]
	v_exp_f32_e32 v142, v142
	v_exp_f32_e32 v143, v143
	v_mul_f32_e32 v126, v32, v87
	v_pk_mul_f32 v[108:109], v[126:127], v[108:109] op_sel_hi:[0,1]
	v_pk_fma_f32 v[128:129], v[128:129], v[140:141], v[108:109]
	v_pk_mul_f32 v[108:109], v[126:127], v[110:111] op_sel_hi:[0,1]
	v_pk_fma_f32 v[130:131], v[130:131], v[142:143], v[108:109]
	v_pk_mul_f32 v[108:109], v[32:33], v[10:11] op_sel_hi:[0,1]
	v_exp_f32_e32 v108, v108
	v_exp_f32_e32 v109, v109
	v_pk_mul_f32 v[110:111], v[32:33], v[12:13] op_sel_hi:[0,1]
	v_exp_f32_e32 v110, v110
	v_exp_f32_e32 v111, v111
	v_pk_mul_f32 v[112:113], v[126:127], v[112:113] op_sel_hi:[0,1]
	v_pk_fma_f32 v[132:133], v[132:133], v[108:109], v[112:113]
	v_pk_mul_f32 v[108:109], v[126:127], v[114:115] op_sel_hi:[0,1]
	v_pk_fma_f32 v[134:135], v[134:135], v[110:111], v[108:109]
	v_pk_mul_f32 v[108:109], v[32:33], v[6:7] op_sel_hi:[0,1]
	v_exp_f32_e32 v108, v108
	v_exp_f32_e32 v109, v109
	v_pk_mul_f32 v[110:111], v[32:33], v[8:9] op_sel_hi:[0,1]
	v_exp_f32_e32 v110, v110
	v_exp_f32_e32 v111, v111
	v_pk_mul_f32 v[112:113], v[126:127], v[116:117] op_sel_hi:[0,1]
	v_pk_fma_f32 v[136:137], v[136:137], v[108:109], v[112:113]
	v_pk_mul_f32 v[108:109], v[126:127], v[118:119] op_sel_hi:[0,1]
	v_pk_fma_f32 v[138:139], v[138:139], v[110:111], v[108:109]
	v_pk_mul_f32 v[108:109], v[32:33], v[2:3] op_sel_hi:[0,1]
	v_exp_f32_e32 v108, v108
	v_exp_f32_e32 v109, v109
	v_pk_mul_f32 v[110:111], v[32:33], v[4:5] op_sel_hi:[0,1]
	v_exp_f32_e32 v110, v110
	v_exp_f32_e32 v111, v111
	v_pk_mul_f32 v[112:113], v[126:127], v[120:121] op_sel_hi:[0,1]
	v_pk_fma_f32 v[124:125], v[124:125], v[108:109], v[112:113]
	v_pk_mul_f32 v[108:109], v[126:127], v[122:123] op_sel_hi:[0,1]
	v_pk_fma_f32 v[104:105], v[104:105], v[110:111], v[108:109]
	s_nop 0
	s_waitcnt lgkmcnt(0)
	s_nop 0
	ds_read_b128 v[108:111], v19 offset:64
	ds_read_b128 v[112:115], v19 offset:80
	ds_read_b128 v[116:119], v19 offset:96
	ds_read_b128 v[120:123], v19 offset:112
	v_mov_b32_e32 v19, 0xa820
	v_pk_mul_f32 v[126:127], v[34:35], v[14:15] op_sel_hi:[0,1]
	v_exp_f32_e32 v126, v126
	v_exp_f32_e32 v127, v127
	v_pk_mul_f32 v[140:141], v[34:35], v[16:17] op_sel_hi:[0,1]
	v_exp_f32_e32 v140, v140
	v_exp_f32_e32 v141, v141
	v_mul_f32_e32 v86, v34, v86
	v_pk_mul_f32 v[88:89], v[86:87], v[88:89] op_sel_hi:[0,1]
	v_pk_fma_f32 v[126:127], v[128:129], v[126:127], v[88:89]
	v_pk_mul_f32 v[88:89], v[86:87], v[90:91] op_sel_hi:[0,1]
	v_pk_fma_f32 v[128:129], v[130:131], v[140:141], v[88:89]
	v_pk_mul_f32 v[88:89], v[34:35], v[10:11] op_sel_hi:[0,1]
	v_exp_f32_e32 v88, v88
	v_exp_f32_e32 v89, v89
	v_pk_mul_f32 v[90:91], v[34:35], v[12:13] op_sel_hi:[0,1]
	v_exp_f32_e32 v90, v90
	v_exp_f32_e32 v91, v91
	v_pk_mul_f32 v[92:93], v[86:87], v[92:93] op_sel_hi:[0,1]
	v_pk_fma_f32 v[130:131], v[132:133], v[88:89], v[92:93]
	v_pk_mul_f32 v[88:89], v[86:87], v[94:95] op_sel_hi:[0,1]
	v_pk_fma_f32 v[132:133], v[134:135], v[90:91], v[88:89]
	v_pk_mul_f32 v[88:89], v[34:35], v[6:7] op_sel_hi:[0,1]
	v_exp_f32_e32 v88, v88
	v_exp_f32_e32 v89, v89
	v_pk_mul_f32 v[90:91], v[34:35], v[8:9] op_sel_hi:[0,1]
	v_exp_f32_e32 v90, v90
	v_exp_f32_e32 v91, v91
	v_pk_mul_f32 v[92:93], v[86:87], v[96:97] op_sel_hi:[0,1]
	v_pk_fma_f32 v[134:135], v[136:137], v[88:89], v[92:93]
	v_pk_mul_f32 v[88:89], v[86:87], v[98:99] op_sel_hi:[0,1]
	v_pk_fma_f32 v[136:137], v[138:139], v[90:91], v[88:89]
	v_pk_mul_f32 v[88:89], v[34:35], v[2:3] op_sel_hi:[0,1]
	v_pk_mul_f32 v[90:91], v[34:35], v[4:5] op_sel_hi:[0,1]
	v_exp_f32_e32 v88, v88
	v_exp_f32_e32 v89, v89
	v_exp_f32_e32 v90, v90
	v_exp_f32_e32 v91, v91
	v_pk_mul_f32 v[92:93], v[86:87], v[100:101] op_sel_hi:[0,1]
	v_pk_mul_f32 v[86:87], v[86:87], v[102:103] op_sel_hi:[0,1]
	v_pk_fma_f32 v[124:125], v[124:125], v[88:89], v[92:93]
	v_pk_fma_f32 v[102:103], v[104:105], v[90:91], v[86:87]
	s_nop 0
	s_waitcnt lgkmcnt(0)
	s_nop 0
	ds_read_b128 v[86:89], v19 offset:64
	ds_read_b128 v[90:93], v19 offset:80
	ds_read_b128 v[94:97], v19 offset:96
	ds_read_b128 v[98:101], v19 offset:112
	v_mov_b32_e32 v19, 0xa8f0
	v_pk_mul_f32 v[138:139], v[36:37], v[14:15] op_sel_hi:[0,1]
	v_exp_f32_e32 v138, v138
	v_exp_f32_e32 v139, v139
	v_pk_mul_f32 v[140:141], v[36:37], v[16:17] op_sel_hi:[0,1]
	v_exp_f32_e32 v140, v140
	v_exp_f32_e32 v141, v141
	v_mul_f32_e32 v104, v36, v85
	v_pk_mul_f32 v[108:109], v[104:105], v[108:109] op_sel_hi:[0,1]
	v_pk_fma_f32 v[126:127], v[126:127], v[138:139], v[108:109]
	v_pk_mul_f32 v[108:109], v[104:105], v[110:111] op_sel_hi:[0,1]
	v_pk_fma_f32 v[128:129], v[128:129], v[140:141], v[108:109]
	v_pk_mul_f32 v[108:109], v[36:37], v[10:11] op_sel_hi:[0,1]
	v_exp_f32_e32 v108, v108
	v_exp_f32_e32 v109, v109
	v_pk_mul_f32 v[110:111], v[36:37], v[12:13] op_sel_hi:[0,1]
	v_exp_f32_e32 v110, v110
	v_exp_f32_e32 v111, v111
	v_pk_mul_f32 v[112:113], v[104:105], v[112:113] op_sel_hi:[0,1]
	v_pk_fma_f32 v[130:131], v[130:131], v[108:109], v[112:113]
	v_pk_mul_f32 v[108:109], v[104:105], v[114:115] op_sel_hi:[0,1]
	v_pk_fma_f32 v[132:133], v[132:133], v[110:111], v[108:109]
	v_pk_mul_f32 v[108:109], v[36:37], v[6:7] op_sel_hi:[0,1]
	v_exp_f32_e32 v108, v108
	v_exp_f32_e32 v109, v109
	v_pk_mul_f32 v[110:111], v[36:37], v[8:9] op_sel_hi:[0,1]
	v_exp_f32_e32 v110, v110
	v_exp_f32_e32 v111, v111
	v_pk_mul_f32 v[112:113], v[104:105], v[116:117] op_sel_hi:[0,1]
	v_pk_fma_f32 v[134:135], v[134:135], v[108:109], v[112:113]
	v_pk_mul_f32 v[108:109], v[104:105], v[118:119] op_sel_hi:[0,1]
	v_pk_fma_f32 v[136:137], v[136:137], v[110:111], v[108:109]
	v_pk_mul_f32 v[108:109], v[36:37], v[2:3] op_sel_hi:[0,1]
	v_pk_mul_f32 v[110:111], v[36:37], v[4:5] op_sel_hi:[0,1]
	v_exp_f32_e32 v108, v108
	v_exp_f32_e32 v109, v109
	v_exp_f32_e32 v110, v110
	v_exp_f32_e32 v111, v111
	v_pk_mul_f32 v[112:113], v[104:105], v[120:121] op_sel_hi:[0,1]
	v_pk_mul_f32 v[104:105], v[104:105], v[122:123] op_sel_hi:[0,1]
	v_pk_fma_f32 v[120:121], v[124:125], v[108:109], v[112:113]
	v_pk_fma_f32 v[122:123], v[102:103], v[110:111], v[104:105]
	s_nop 0
	s_waitcnt lgkmcnt(0)
	s_nop 0
	ds_read_b128 v[102:105], v19 offset:64
	ds_read_b128 v[108:111], v19 offset:80
	ds_read_b128 v[112:115], v19 offset:96
	ds_read_b128 v[116:119], v19 offset:112
	v_mov_b32_e32 v19, 0xa9c0
	v_pk_mul_f32 v[124:125], v[38:39], v[14:15] op_sel_hi:[0,1]
	v_exp_f32_e32 v124, v124
	v_exp_f32_e32 v125, v125
	v_pk_mul_f32 v[138:139], v[38:39], v[16:17] op_sel_hi:[0,1]
	v_exp_f32_e32 v138, v138
	v_exp_f32_e32 v139, v139
	v_mul_f32_e32 v84, v38, v84
	v_pk_mul_f32 v[86:87], v[84:85], v[86:87] op_sel_hi:[0,1]
	v_pk_fma_f32 v[124:125], v[126:127], v[124:125], v[86:87]
	v_pk_mul_f32 v[86:87], v[84:85], v[88:89] op_sel_hi:[0,1]
	v_pk_fma_f32 v[126:127], v[128:129], v[138:139], v[86:87]
	v_pk_mul_f32 v[86:87], v[38:39], v[10:11] op_sel_hi:[0,1]
	v_exp_f32_e32 v86, v86
	v_exp_f32_e32 v87, v87
	v_pk_mul_f32 v[88:89], v[38:39], v[12:13] op_sel_hi:[0,1]
	v_exp_f32_e32 v88, v88
	v_exp_f32_e32 v89, v89
	v_pk_mul_f32 v[90:91], v[84:85], v[90:91] op_sel_hi:[0,1]
	v_pk_fma_f32 v[128:129], v[130:131], v[86:87], v[90:91]
	v_pk_mul_f32 v[86:87], v[84:85], v[92:93] op_sel_hi:[0,1]
	v_pk_fma_f32 v[130:131], v[132:133], v[88:89], v[86:87]
	v_pk_mul_f32 v[86:87], v[38:39], v[6:7] op_sel_hi:[0,1]
	v_exp_f32_e32 v86, v86
	v_exp_f32_e32 v87, v87
	v_pk_mul_f32 v[88:89], v[38:39], v[8:9] op_sel_hi:[0,1]
	v_exp_f32_e32 v88, v88
	v_exp_f32_e32 v89, v89
	v_pk_mul_f32 v[90:91], v[84:85], v[94:95] op_sel_hi:[0,1]
	v_pk_fma_f32 v[132:133], v[134:135], v[86:87], v[90:91]
	v_pk_mul_f32 v[86:87], v[84:85], v[96:97] op_sel_hi:[0,1]
	v_pk_fma_f32 v[134:135], v[136:137], v[88:89], v[86:87]
	v_pk_mul_f32 v[86:87], v[38:39], v[2:3] op_sel_hi:[0,1]
	v_pk_mul_f32 v[88:89], v[38:39], v[4:5] op_sel_hi:[0,1]
	v_exp_f32_e32 v86, v86
	v_exp_f32_e32 v87, v87
	v_exp_f32_e32 v88, v88
	v_exp_f32_e32 v89, v89
	v_pk_mul_f32 v[90:91], v[84:85], v[98:99] op_sel_hi:[0,1]
	v_pk_mul_f32 v[84:85], v[84:85], v[100:101] op_sel_hi:[0,1]
	v_pk_fma_f32 v[120:121], v[120:121], v[86:87], v[90:91]
	v_pk_fma_f32 v[100:101], v[122:123], v[88:89], v[84:85]
	s_nop 0
	s_waitcnt lgkmcnt(0)
	s_nop 0
	ds_read_b128 v[84:87], v19 offset:64
	ds_read_b128 v[88:91], v19 offset:80
	ds_read_b128 v[92:95], v19 offset:96
	ds_read_b128 v[96:99], v19 offset:112
	v_mov_b32_e32 v19, 0xaa90
	v_pk_mul_f32 v[136:137], v[40:41], v[14:15] op_sel_hi:[0,1]
	v_exp_f32_e32 v136, v136
	v_exp_f32_e32 v137, v137
	v_pk_mul_f32 v[138:139], v[40:41], v[16:17] op_sel_hi:[0,1]
	v_exp_f32_e32 v138, v138
	v_exp_f32_e32 v139, v139
	v_mul_f32_e32 v122, v40, v83
	v_pk_mul_f32 v[102:103], v[122:123], v[102:103] op_sel_hi:[0,1]
	v_pk_fma_f32 v[124:125], v[124:125], v[136:137], v[102:103]
	v_pk_mul_f32 v[102:103], v[122:123], v[104:105] op_sel_hi:[0,1]
	v_pk_fma_f32 v[104:105], v[126:127], v[138:139], v[102:103]
	v_pk_mul_f32 v[102:103], v[40:41], v[10:11] op_sel_hi:[0,1]
	v_exp_f32_e32 v102, v102
	v_exp_f32_e32 v103, v103
	v_pk_mul_f32 v[126:127], v[40:41], v[12:13] op_sel_hi:[0,1]
	v_exp_f32_e32 v126, v126
	v_exp_f32_e32 v127, v127
	v_pk_mul_f32 v[108:109], v[122:123], v[108:109] op_sel_hi:[0,1]
	v_pk_fma_f32 v[128:129], v[128:129], v[102:103], v[108:109]
	v_pk_mul_f32 v[102:103], v[122:123], v[110:111] op_sel_hi:[0,1]
	v_pk_fma_f32 v[126:127], v[130:131], v[126:127], v[102:103]
	v_pk_mul_f32 v[102:103], v[40:41], v[6:7] op_sel_hi:[0,1]
	v_exp_f32_e32 v102, v102
	v_exp_f32_e32 v103, v103
	v_pk_mul_f32 v[108:109], v[40:41], v[8:9] op_sel_hi:[0,1]
	v_exp_f32_e32 v108, v108
	v_exp_f32_e32 v109, v109
	v_pk_mul_f32 v[110:111], v[122:123], v[112:113] op_sel_hi:[0,1]
	v_pk_fma_f32 v[130:131], v[132:133], v[102:103], v[110:111]
	v_pk_mul_f32 v[102:103], v[122:123], v[114:115] op_sel_hi:[0,1]
	v_pk_fma_f32 v[132:133], v[134:135], v[108:109], v[102:103]
	v_pk_mul_f32 v[102:103], v[40:41], v[2:3] op_sel_hi:[0,1]
	v_exp_f32_e32 v102, v102
	v_exp_f32_e32 v103, v103
	v_pk_mul_f32 v[108:109], v[40:41], v[4:5] op_sel_hi:[0,1]
	v_exp_f32_e32 v108, v108
	v_exp_f32_e32 v109, v109
	v_pk_mul_f32 v[110:111], v[122:123], v[116:117] op_sel_hi:[0,1]
	v_pk_fma_f32 v[120:121], v[120:121], v[102:103], v[110:111]
	v_pk_mul_f32 v[102:103], v[122:123], v[118:119] op_sel_hi:[0,1]
	v_pk_fma_f32 v[122:123], v[100:101], v[108:109], v[102:103]
	s_nop 0
	s_waitcnt lgkmcnt(0)
	s_nop 0
	ds_read_b128 v[100:103], v19 offset:64
	ds_read_b128 v[108:111], v19 offset:80
	ds_read_b128 v[112:115], v19 offset:96
	ds_read_b128 v[116:119], v19 offset:112
	v_mov_b32_e32 v19, 0xab60
	v_pk_mul_f32 v[134:135], v[42:43], v[14:15] op_sel_hi:[0,1]
	v_exp_f32_e32 v134, v134
	v_exp_f32_e32 v135, v135
	v_pk_mul_f32 v[136:137], v[42:43], v[16:17] op_sel_hi:[0,1]
	v_exp_f32_e32 v136, v136
	v_exp_f32_e32 v137, v137
	v_mul_f32_e32 v82, v42, v82
	v_pk_mul_f32 v[84:85], v[82:83], v[84:85] op_sel_hi:[0,1]
	v_pk_fma_f32 v[124:125], v[124:125], v[134:135], v[84:85]
	v_pk_mul_f32 v[84:85], v[82:83], v[86:87] op_sel_hi:[0,1]
	v_pk_fma_f32 v[104:105], v[104:105], v[136:137], v[84:85]
	v_pk_mul_f32 v[84:85], v[42:43], v[10:11] op_sel_hi:[0,1]
	v_exp_f32_e32 v84, v84
	v_exp_f32_e32 v85, v85
	v_pk_mul_f32 v[86:87], v[42:43], v[12:13] op_sel_hi:[0,1]
	v_exp_f32_e32 v86, v86
	v_exp_f32_e32 v87, v87
	v_pk_mul_f32 v[88:89], v[82:83], v[88:89] op_sel_hi:[0,1]
	v_pk_fma_f32 v[128:129], v[128:129], v[84:85], v[88:89]
	v_pk_mul_f32 v[84:85], v[82:83], v[90:91] op_sel_hi:[0,1]
	v_pk_fma_f32 v[126:127], v[126:127], v[86:87], v[84:85]
	v_pk_mul_f32 v[84:85], v[42:43], v[6:7] op_sel_hi:[0,1]
	v_exp_f32_e32 v84, v84
	v_exp_f32_e32 v85, v85
	v_pk_mul_f32 v[86:87], v[42:43], v[8:9] op_sel_hi:[0,1]
	v_exp_f32_e32 v86, v86
	v_exp_f32_e32 v87, v87
	v_pk_mul_f32 v[88:89], v[82:83], v[92:93] op_sel_hi:[0,1]
	v_pk_fma_f32 v[130:131], v[130:131], v[84:85], v[88:89]
	v_pk_mul_f32 v[84:85], v[82:83], v[94:95] op_sel_hi:[0,1]
	v_pk_fma_f32 v[132:133], v[132:133], v[86:87], v[84:85]
	v_pk_mul_f32 v[84:85], v[42:43], v[2:3] op_sel_hi:[0,1]
	v_pk_mul_f32 v[86:87], v[42:43], v[4:5] op_sel_hi:[0,1]
	v_exp_f32_e32 v84, v84
	v_exp_f32_e32 v85, v85
	v_exp_f32_e32 v86, v86
	v_exp_f32_e32 v87, v87
	v_pk_mul_f32 v[88:89], v[82:83], v[96:97] op_sel_hi:[0,1]
	v_pk_mul_f32 v[82:83], v[82:83], v[98:99] op_sel_hi:[0,1]
	v_pk_fma_f32 v[120:121], v[120:121], v[84:85], v[88:89]
	v_pk_fma_f32 v[98:99], v[122:123], v[86:87], v[82:83]
	s_nop 0
	s_waitcnt lgkmcnt(0)
	s_nop 0
	ds_read_b128 v[82:85], v19 offset:64
	ds_read_b128 v[86:89], v19 offset:80
	ds_read_b128 v[90:93], v19 offset:96
	ds_read_b128 v[94:97], v19 offset:112
	v_mov_b32_e32 v19, 0xac30
	v_pk_mul_f32 v[134:135], v[44:45], v[14:15] op_sel_hi:[0,1]
	v_exp_f32_e32 v134, v134
	v_exp_f32_e32 v135, v135
	v_pk_mul_f32 v[136:137], v[44:45], v[16:17] op_sel_hi:[0,1]
	v_exp_f32_e32 v136, v136
	v_exp_f32_e32 v137, v137
	v_mul_f32_e32 v122, v44, v81
	v_pk_mul_f32 v[100:101], v[122:123], v[100:101] op_sel_hi:[0,1]
	v_pk_fma_f32 v[124:125], v[124:125], v[134:135], v[100:101]
	v_pk_mul_f32 v[100:101], v[122:123], v[102:103] op_sel_hi:[0,1]
	v_pk_fma_f32 v[134:135], v[104:105], v[136:137], v[100:101]
	v_pk_mul_f32 v[100:101], v[44:45], v[10:11] op_sel_hi:[0,1]
	v_exp_f32_e32 v100, v100
	v_exp_f32_e32 v101, v101
	v_pk_mul_f32 v[102:103], v[44:45], v[12:13] op_sel_hi:[0,1]
	v_exp_f32_e32 v102, v102
	v_exp_f32_e32 v103, v103
	v_pk_mul_f32 v[104:105], v[122:123], v[108:109] op_sel_hi:[0,1]
	v_pk_fma_f32 v[128:129], v[128:129], v[100:101], v[104:105]
	v_pk_mul_f32 v[100:101], v[122:123], v[110:111] op_sel_hi:[0,1]
	v_pk_fma_f32 v[126:127], v[126:127], v[102:103], v[100:101]
	v_pk_mul_f32 v[100:101], v[44:45], v[6:7] op_sel_hi:[0,1]
	v_exp_f32_e32 v100, v100
	v_exp_f32_e32 v101, v101
	v_pk_mul_f32 v[102:103], v[44:45], v[8:9] op_sel_hi:[0,1]
	v_exp_f32_e32 v102, v102
	v_exp_f32_e32 v103, v103
	v_pk_mul_f32 v[104:105], v[122:123], v[112:113] op_sel_hi:[0,1]
	v_pk_fma_f32 v[130:131], v[130:131], v[100:101], v[104:105]
	v_pk_mul_f32 v[100:101], v[122:123], v[114:115] op_sel_hi:[0,1]
	v_pk_fma_f32 v[132:133], v[132:133], v[102:103], v[100:101]
	v_pk_mul_f32 v[100:101], v[44:45], v[2:3] op_sel_hi:[0,1]
	v_exp_f32_e32 v100, v100
	v_exp_f32_e32 v101, v101
	v_pk_mul_f32 v[102:103], v[44:45], v[4:5] op_sel_hi:[0,1]
	v_exp_f32_e32 v102, v102
	v_exp_f32_e32 v103, v103
	v_pk_mul_f32 v[104:105], v[122:123], v[116:117] op_sel_hi:[0,1]
	v_pk_fma_f32 v[116:117], v[120:121], v[100:101], v[104:105]
	v_pk_mul_f32 v[100:101], v[122:123], v[118:119] op_sel_hi:[0,1]
	v_pk_fma_f32 v[118:119], v[98:99], v[102:103], v[100:101]
	s_nop 0
	s_waitcnt lgkmcnt(0)
	s_nop 0
	ds_read_b128 v[98:101], v19 offset:64
	ds_read_b128 v[102:105], v19 offset:80
	ds_read_b128 v[108:111], v19 offset:96
	ds_read_b128 v[112:115], v19 offset:112
	v_mov_b32_e32 v19, 0xad00
	v_pk_mul_f32 v[122:123], v[46:47], v[14:15] op_sel_hi:[0,1]
	v_exp_f32_e32 v122, v122
	v_exp_f32_e32 v123, v123
	v_pk_mul_f32 v[136:137], v[46:47], v[16:17] op_sel_hi:[0,1]
	v_exp_f32_e32 v136, v136
	v_exp_f32_e32 v137, v137
	v_mul_f32_e32 v120, v46, v79
	v_pk_mul_f32 v[82:83], v[120:121], v[82:83] op_sel_hi:[0,1]
	v_pk_fma_f32 v[122:123], v[124:125], v[122:123], v[82:83]
	v_pk_mul_f32 v[82:83], v[120:121], v[84:85] op_sel_hi:[0,1]
	v_pk_fma_f32 v[124:125], v[134:135], v[136:137], v[82:83]
	v_pk_mul_f32 v[82:83], v[46:47], v[10:11] op_sel_hi:[0,1]
	v_exp_f32_e32 v82, v82
	v_exp_f32_e32 v83, v83
	v_pk_mul_f32 v[84:85], v[46:47], v[12:13] op_sel_hi:[0,1]
	v_exp_f32_e32 v84, v84
	v_exp_f32_e32 v85, v85
	v_pk_mul_f32 v[86:87], v[120:121], v[86:87] op_sel_hi:[0,1]
	v_pk_fma_f32 v[128:129], v[128:129], v[82:83], v[86:87]
	v_pk_mul_f32 v[82:83], v[120:121], v[88:89] op_sel_hi:[0,1]
	v_pk_fma_f32 v[126:127], v[126:127], v[84:85], v[82:83]
	v_pk_mul_f32 v[82:83], v[46:47], v[6:7] op_sel_hi:[0,1]
	v_exp_f32_e32 v82, v82
	v_exp_f32_e32 v83, v83
	v_pk_mul_f32 v[84:85], v[46:47], v[8:9] op_sel_hi:[0,1]
	v_exp_f32_e32 v84, v84
	v_exp_f32_e32 v85, v85
	v_pk_mul_f32 v[86:87], v[120:121], v[90:91] op_sel_hi:[0,1]
	v_pk_fma_f32 v[130:131], v[130:131], v[82:83], v[86:87]
	v_pk_mul_f32 v[82:83], v[120:121], v[92:93] op_sel_hi:[0,1]
	v_pk_fma_f32 v[132:133], v[132:133], v[84:85], v[82:83]
	v_pk_mul_f32 v[82:83], v[46:47], v[2:3] op_sel_hi:[0,1]
	v_exp_f32_e32 v82, v82
	v_exp_f32_e32 v83, v83
	v_pk_mul_f32 v[84:85], v[46:47], v[4:5] op_sel_hi:[0,1]
	v_exp_f32_e32 v84, v84
	v_exp_f32_e32 v85, v85
	v_pk_mul_f32 v[86:87], v[120:121], v[94:95] op_sel_hi:[0,1]
	v_pk_fma_f32 v[116:117], v[116:117], v[82:83], v[86:87]
	v_pk_mul_f32 v[82:83], v[120:121], v[96:97] op_sel_hi:[0,1]
	v_pk_fma_f32 v[118:119], v[118:119], v[84:85], v[82:83]
	s_nop 0
	s_waitcnt lgkmcnt(0)
	s_nop 0
	ds_read_b128 v[82:85], v19 offset:64
	ds_read_b128 v[86:89], v19 offset:80
	ds_read_b128 v[90:93], v19 offset:96
	ds_read_b128 v[94:97], v19 offset:112
	v_mov_b32_e32 v19, 0xadd0
	v_pk_mul_f32 v[134:135], v[48:49], v[14:15] op_sel_hi:[0,1]
	v_exp_f32_e32 v134, v134
	v_exp_f32_e32 v135, v135
	v_pk_mul_f32 v[136:137], v[48:49], v[16:17] op_sel_hi:[0,1]
	v_exp_f32_e32 v136, v136
	v_exp_f32_e32 v137, v137
	v_mul_f32_e32 v120, v48, v77
	v_pk_mul_f32 v[98:99], v[120:121], v[98:99] op_sel_hi:[0,1]
	v_pk_fma_f32 v[122:123], v[122:123], v[134:135], v[98:99]
	v_pk_mul_f32 v[98:99], v[120:121], v[100:101] op_sel_hi:[0,1]
	v_pk_fma_f32 v[124:125], v[124:125], v[136:137], v[98:99]
	v_pk_mul_f32 v[98:99], v[48:49], v[10:11] op_sel_hi:[0,1]
	v_exp_f32_e32 v98, v98
	v_exp_f32_e32 v99, v99
	v_pk_mul_f32 v[100:101], v[48:49], v[12:13] op_sel_hi:[0,1]
	v_exp_f32_e32 v100, v100
	v_exp_f32_e32 v101, v101
	v_pk_mul_f32 v[102:103], v[120:121], v[102:103] op_sel_hi:[0,1]
	v_pk_fma_f32 v[128:129], v[128:129], v[98:99], v[102:103]
	v_pk_mul_f32 v[98:99], v[120:121], v[104:105] op_sel_hi:[0,1]
	v_pk_fma_f32 v[126:127], v[126:127], v[100:101], v[98:99]
	v_pk_mul_f32 v[98:99], v[48:49], v[6:7] op_sel_hi:[0,1]
	v_exp_f32_e32 v98, v98
	v_exp_f32_e32 v99, v99
	v_pk_mul_f32 v[100:101], v[48:49], v[8:9] op_sel_hi:[0,1]
	v_exp_f32_e32 v100, v100
	v_exp_f32_e32 v101, v101
	v_pk_mul_f32 v[102:103], v[120:121], v[108:109] op_sel_hi:[0,1]
	v_pk_fma_f32 v[130:131], v[130:131], v[98:99], v[102:103]
	v_pk_mul_f32 v[98:99], v[120:121], v[110:111] op_sel_hi:[0,1]
	v_pk_fma_f32 v[132:133], v[132:133], v[100:101], v[98:99]
	v_pk_mul_f32 v[98:99], v[48:49], v[2:3] op_sel_hi:[0,1]
	v_exp_f32_e32 v98, v98
	v_exp_f32_e32 v99, v99
	v_pk_mul_f32 v[100:101], v[48:49], v[4:5] op_sel_hi:[0,1]
	v_exp_f32_e32 v100, v100
	v_exp_f32_e32 v101, v101
	v_pk_mul_f32 v[102:103], v[120:121], v[112:113] op_sel_hi:[0,1]
	v_pk_fma_f32 v[116:117], v[116:117], v[98:99], v[102:103]
	v_pk_mul_f32 v[98:99], v[120:121], v[114:115] op_sel_hi:[0,1]
	v_pk_fma_f32 v[118:119], v[118:119], v[100:101], v[98:99]
	s_nop 0
	s_waitcnt lgkmcnt(0)
	s_nop 0
	ds_read_b128 v[98:101], v19 offset:64
	ds_read_b128 v[102:105], v19 offset:80
	ds_read_b128 v[108:111], v19 offset:96
	ds_read_b128 v[112:115], v19 offset:112
	v_mov_b32_e32 v19, 0xaea0
	v_pk_mul_f32 v[134:135], v[50:51], v[14:15] op_sel_hi:[0,1]
	v_exp_f32_e32 v134, v134
	v_exp_f32_e32 v135, v135
	v_pk_mul_f32 v[136:137], v[50:51], v[16:17] op_sel_hi:[0,1]
	v_exp_f32_e32 v136, v136
	v_exp_f32_e32 v137, v137
	v_mul_f32_e32 v120, v50, v75
	v_pk_mul_f32 v[82:83], v[120:121], v[82:83] op_sel_hi:[0,1]
	v_pk_fma_f32 v[122:123], v[122:123], v[134:135], v[82:83]
	v_pk_mul_f32 v[82:83], v[120:121], v[84:85] op_sel_hi:[0,1]
	v_pk_fma_f32 v[124:125], v[124:125], v[136:137], v[82:83]
	v_pk_mul_f32 v[82:83], v[50:51], v[10:11] op_sel_hi:[0,1]
	v_exp_f32_e32 v82, v82
	v_exp_f32_e32 v83, v83
	v_pk_mul_f32 v[84:85], v[50:51], v[12:13] op_sel_hi:[0,1]
	v_exp_f32_e32 v84, v84
	v_exp_f32_e32 v85, v85
	v_pk_mul_f32 v[86:87], v[120:121], v[86:87] op_sel_hi:[0,1]
	v_pk_fma_f32 v[128:129], v[128:129], v[82:83], v[86:87]
	v_pk_mul_f32 v[82:83], v[120:121], v[88:89] op_sel_hi:[0,1]
	v_pk_fma_f32 v[126:127], v[126:127], v[84:85], v[82:83]
	v_pk_mul_f32 v[82:83], v[50:51], v[6:7] op_sel_hi:[0,1]
	v_exp_f32_e32 v82, v82
	v_exp_f32_e32 v83, v83
	v_pk_mul_f32 v[84:85], v[50:51], v[8:9] op_sel_hi:[0,1]
	v_exp_f32_e32 v84, v84
	v_exp_f32_e32 v85, v85
	v_pk_mul_f32 v[86:87], v[120:121], v[90:91] op_sel_hi:[0,1]
	v_pk_fma_f32 v[130:131], v[130:131], v[82:83], v[86:87]
	v_pk_mul_f32 v[82:83], v[120:121], v[92:93] op_sel_hi:[0,1]
	v_pk_fma_f32 v[132:133], v[132:133], v[84:85], v[82:83]
	v_pk_mul_f32 v[82:83], v[50:51], v[2:3] op_sel_hi:[0,1]
	v_exp_f32_e32 v82, v82
	v_exp_f32_e32 v83, v83
	v_pk_mul_f32 v[84:85], v[50:51], v[4:5] op_sel_hi:[0,1]
	v_exp_f32_e32 v84, v84
	v_exp_f32_e32 v85, v85
	v_pk_mul_f32 v[86:87], v[120:121], v[94:95] op_sel_hi:[0,1]
	v_pk_fma_f32 v[116:117], v[116:117], v[82:83], v[86:87]
	v_pk_mul_f32 v[82:83], v[120:121], v[96:97] op_sel_hi:[0,1]
	v_pk_fma_f32 v[118:119], v[118:119], v[84:85], v[82:83]
	s_nop 0
	s_waitcnt lgkmcnt(0)
	s_nop 0
	ds_read_b128 v[82:85], v19 offset:64
	ds_read_b128 v[86:89], v19 offset:80
	ds_read_b128 v[90:93], v19 offset:96
	ds_read_b128 v[94:97], v19 offset:112
	v_mov_b32_e32 v19, 0xaf70
	v_pk_mul_f32 v[134:135], v[52:53], v[14:15] op_sel_hi:[0,1]
	v_exp_f32_e32 v134, v134
	v_exp_f32_e32 v135, v135
	v_pk_mul_f32 v[136:137], v[52:53], v[16:17] op_sel_hi:[0,1]
	v_exp_f32_e32 v136, v136
	v_exp_f32_e32 v137, v137
	v_mul_f32_e32 v120, v52, v73
	v_pk_mul_f32 v[98:99], v[120:121], v[98:99] op_sel_hi:[0,1]
	v_pk_fma_f32 v[122:123], v[122:123], v[134:135], v[98:99]
	v_pk_mul_f32 v[98:99], v[120:121], v[100:101] op_sel_hi:[0,1]
	v_pk_fma_f32 v[124:125], v[124:125], v[136:137], v[98:99]
	v_pk_mul_f32 v[98:99], v[52:53], v[10:11] op_sel_hi:[0,1]
	v_exp_f32_e32 v98, v98
	v_exp_f32_e32 v99, v99
	v_pk_mul_f32 v[100:101], v[52:53], v[12:13] op_sel_hi:[0,1]
	v_exp_f32_e32 v100, v100
	v_exp_f32_e32 v101, v101
	v_pk_mul_f32 v[102:103], v[120:121], v[102:103] op_sel_hi:[0,1]
	v_pk_fma_f32 v[128:129], v[128:129], v[98:99], v[102:103]
	v_pk_mul_f32 v[98:99], v[120:121], v[104:105] op_sel_hi:[0,1]
	v_pk_fma_f32 v[126:127], v[126:127], v[100:101], v[98:99]
	v_pk_mul_f32 v[98:99], v[52:53], v[6:7] op_sel_hi:[0,1]
	v_exp_f32_e32 v98, v98
	v_exp_f32_e32 v99, v99
	v_pk_mul_f32 v[100:101], v[52:53], v[8:9] op_sel_hi:[0,1]
	v_exp_f32_e32 v100, v100
	v_exp_f32_e32 v101, v101
	v_pk_mul_f32 v[102:103], v[120:121], v[108:109] op_sel_hi:[0,1]
	v_pk_fma_f32 v[130:131], v[130:131], v[98:99], v[102:103]
	v_pk_mul_f32 v[98:99], v[120:121], v[110:111] op_sel_hi:[0,1]
	v_pk_fma_f32 v[132:133], v[132:133], v[100:101], v[98:99]
	v_pk_mul_f32 v[98:99], v[52:53], v[2:3] op_sel_hi:[0,1]
	v_exp_f32_e32 v98, v98
	v_exp_f32_e32 v99, v99
	v_pk_mul_f32 v[100:101], v[52:53], v[4:5] op_sel_hi:[0,1]
	v_exp_f32_e32 v100, v100
	v_exp_f32_e32 v101, v101
	v_pk_mul_f32 v[102:103], v[120:121], v[112:113] op_sel_hi:[0,1]
	v_pk_fma_f32 v[116:117], v[116:117], v[98:99], v[102:103]
	v_pk_mul_f32 v[98:99], v[120:121], v[114:115] op_sel_hi:[0,1]
	v_pk_fma_f32 v[118:119], v[118:119], v[100:101], v[98:99]
	s_nop 0
	s_waitcnt lgkmcnt(0)
	s_nop 0
	ds_read_b128 v[98:101], v19 offset:64
	ds_read_b128 v[102:105], v19 offset:80
	ds_read_b128 v[108:111], v19 offset:96
	ds_read_b128 v[112:115], v19 offset:112
	v_mov_b32_e32 v19, 0xb040
	v_pk_mul_f32 v[134:135], v[54:55], v[14:15] op_sel_hi:[0,1]
	v_exp_f32_e32 v134, v134
	v_exp_f32_e32 v135, v135
	v_pk_mul_f32 v[136:137], v[54:55], v[16:17] op_sel_hi:[0,1]
	v_exp_f32_e32 v136, v136
	v_exp_f32_e32 v137, v137
	v_mul_f32_e32 v120, v54, v71
	v_pk_mul_f32 v[82:83], v[120:121], v[82:83] op_sel_hi:[0,1]
	v_pk_fma_f32 v[122:123], v[122:123], v[134:135], v[82:83]
	v_pk_mul_f32 v[82:83], v[120:121], v[84:85] op_sel_hi:[0,1]
	v_pk_fma_f32 v[124:125], v[124:125], v[136:137], v[82:83]
	v_pk_mul_f32 v[82:83], v[54:55], v[10:11] op_sel_hi:[0,1]
	v_exp_f32_e32 v82, v82
	v_exp_f32_e32 v83, v83
	v_pk_mul_f32 v[84:85], v[54:55], v[12:13] op_sel_hi:[0,1]
	v_exp_f32_e32 v84, v84
	v_exp_f32_e32 v85, v85
	v_pk_mul_f32 v[86:87], v[120:121], v[86:87] op_sel_hi:[0,1]
	v_pk_fma_f32 v[128:129], v[128:129], v[82:83], v[86:87]
	v_pk_mul_f32 v[82:83], v[120:121], v[88:89] op_sel_hi:[0,1]
	v_pk_fma_f32 v[126:127], v[126:127], v[84:85], v[82:83]
	v_pk_mul_f32 v[82:83], v[54:55], v[6:7] op_sel_hi:[0,1]
	v_exp_f32_e32 v82, v82
	v_exp_f32_e32 v83, v83
	v_pk_mul_f32 v[84:85], v[54:55], v[8:9] op_sel_hi:[0,1]
	v_exp_f32_e32 v84, v84
	v_exp_f32_e32 v85, v85
	v_pk_mul_f32 v[86:87], v[120:121], v[90:91] op_sel_hi:[0,1]
	v_pk_fma_f32 v[130:131], v[130:131], v[82:83], v[86:87]
	v_pk_mul_f32 v[82:83], v[120:121], v[92:93] op_sel_hi:[0,1]
	v_pk_fma_f32 v[132:133], v[132:133], v[84:85], v[82:83]
	v_pk_mul_f32 v[82:83], v[54:55], v[2:3] op_sel_hi:[0,1]
	v_exp_f32_e32 v82, v82
	v_exp_f32_e32 v83, v83
	v_pk_mul_f32 v[84:85], v[54:55], v[4:5] op_sel_hi:[0,1]
	v_exp_f32_e32 v84, v84
	v_exp_f32_e32 v85, v85
	v_pk_mul_f32 v[86:87], v[120:121], v[94:95] op_sel_hi:[0,1]
	v_pk_fma_f32 v[116:117], v[116:117], v[82:83], v[86:87]
	v_pk_mul_f32 v[82:83], v[120:121], v[96:97] op_sel_hi:[0,1]
	v_pk_fma_f32 v[118:119], v[118:119], v[84:85], v[82:83]
	s_nop 0
	s_waitcnt lgkmcnt(0)
	s_nop 0
	ds_read_b128 v[82:85], v19 offset:64
	ds_read_b128 v[86:89], v19 offset:80
	ds_read_b128 v[90:93], v19 offset:96
	ds_read_b128 v[94:97], v19 offset:112
	v_mov_b32_e32 v19, 0xb110
	v_pk_mul_f32 v[134:135], v[56:57], v[14:15] op_sel_hi:[0,1]
	v_exp_f32_e32 v134, v134
	v_exp_f32_e32 v135, v135
	v_pk_mul_f32 v[136:137], v[56:57], v[16:17] op_sel_hi:[0,1]
	v_exp_f32_e32 v136, v136
	v_exp_f32_e32 v137, v137
	v_mul_f32_e32 v120, v56, v69
	v_pk_mul_f32 v[98:99], v[120:121], v[98:99] op_sel_hi:[0,1]
	v_pk_fma_f32 v[122:123], v[122:123], v[134:135], v[98:99]
	v_pk_mul_f32 v[98:99], v[120:121], v[100:101] op_sel_hi:[0,1]
	v_pk_fma_f32 v[124:125], v[124:125], v[136:137], v[98:99]
	v_pk_mul_f32 v[98:99], v[56:57], v[10:11] op_sel_hi:[0,1]
	v_exp_f32_e32 v98, v98
	v_exp_f32_e32 v99, v99
	v_pk_mul_f32 v[100:101], v[56:57], v[12:13] op_sel_hi:[0,1]
	v_exp_f32_e32 v100, v100
	v_exp_f32_e32 v101, v101
	v_pk_mul_f32 v[102:103], v[120:121], v[102:103] op_sel_hi:[0,1]
	v_pk_fma_f32 v[128:129], v[128:129], v[98:99], v[102:103]
	v_pk_mul_f32 v[98:99], v[120:121], v[104:105] op_sel_hi:[0,1]
	v_pk_fma_f32 v[126:127], v[126:127], v[100:101], v[98:99]
	v_pk_mul_f32 v[98:99], v[56:57], v[6:7] op_sel_hi:[0,1]
	v_exp_f32_e32 v98, v98
	v_exp_f32_e32 v99, v99
	v_pk_mul_f32 v[100:101], v[56:57], v[8:9] op_sel_hi:[0,1]
	v_exp_f32_e32 v100, v100
	v_exp_f32_e32 v101, v101
	v_pk_mul_f32 v[102:103], v[120:121], v[108:109] op_sel_hi:[0,1]
	v_pk_fma_f32 v[130:131], v[130:131], v[98:99], v[102:103]
	v_pk_mul_f32 v[98:99], v[120:121], v[110:111] op_sel_hi:[0,1]
	v_pk_fma_f32 v[132:133], v[132:133], v[100:101], v[98:99]
	v_pk_mul_f32 v[98:99], v[56:57], v[2:3] op_sel_hi:[0,1]
	v_exp_f32_e32 v98, v98
	v_exp_f32_e32 v99, v99
	v_pk_mul_f32 v[100:101], v[56:57], v[4:5] op_sel_hi:[0,1]
	v_exp_f32_e32 v100, v100
	v_exp_f32_e32 v101, v101
	v_pk_mul_f32 v[102:103], v[120:121], v[112:113] op_sel_hi:[0,1]
	v_pk_fma_f32 v[116:117], v[116:117], v[98:99], v[102:103]
	v_pk_mul_f32 v[98:99], v[120:121], v[114:115] op_sel_hi:[0,1]
	v_pk_fma_f32 v[118:119], v[118:119], v[100:101], v[98:99]
	s_nop 0
	s_waitcnt lgkmcnt(0)
	s_nop 0
	ds_read_b128 v[98:101], v19 offset:64
	ds_read_b128 v[102:105], v19 offset:80
	ds_read_b128 v[108:111], v19 offset:96
	ds_read_b128 v[112:115], v19 offset:112
	v_mov_b32_e32 v19, 0xb1e0
	v_pk_mul_f32 v[134:135], v[58:59], v[14:15] op_sel_hi:[0,1]
	v_exp_f32_e32 v134, v134
	v_exp_f32_e32 v135, v135
	v_pk_mul_f32 v[136:137], v[58:59], v[16:17] op_sel_hi:[0,1]
	v_exp_f32_e32 v136, v136
	v_exp_f32_e32 v137, v137
	v_mul_f32_e32 v120, v58, v67
	v_pk_mul_f32 v[82:83], v[120:121], v[82:83] op_sel_hi:[0,1]
	v_pk_fma_f32 v[122:123], v[122:123], v[134:135], v[82:83]
	v_pk_mul_f32 v[82:83], v[120:121], v[84:85] op_sel_hi:[0,1]
	v_pk_fma_f32 v[124:125], v[124:125], v[136:137], v[82:83]
	v_pk_mul_f32 v[82:83], v[58:59], v[10:11] op_sel_hi:[0,1]
	v_exp_f32_e32 v82, v82
	v_exp_f32_e32 v83, v83
	v_pk_mul_f32 v[84:85], v[58:59], v[12:13] op_sel_hi:[0,1]
	v_exp_f32_e32 v84, v84
	v_exp_f32_e32 v85, v85
	v_pk_mul_f32 v[86:87], v[120:121], v[86:87] op_sel_hi:[0,1]
	v_pk_fma_f32 v[128:129], v[128:129], v[82:83], v[86:87]
	v_pk_mul_f32 v[82:83], v[120:121], v[88:89] op_sel_hi:[0,1]
	v_pk_fma_f32 v[126:127], v[126:127], v[84:85], v[82:83]
	v_pk_mul_f32 v[82:83], v[58:59], v[6:7] op_sel_hi:[0,1]
	v_exp_f32_e32 v82, v82
	v_exp_f32_e32 v83, v83
	v_pk_mul_f32 v[84:85], v[58:59], v[8:9] op_sel_hi:[0,1]
	v_exp_f32_e32 v84, v84
	v_exp_f32_e32 v85, v85
	v_pk_mul_f32 v[86:87], v[120:121], v[90:91] op_sel_hi:[0,1]
	v_pk_fma_f32 v[130:131], v[130:131], v[82:83], v[86:87]
	v_pk_mul_f32 v[82:83], v[120:121], v[92:93] op_sel_hi:[0,1]
	v_pk_fma_f32 v[132:133], v[132:133], v[84:85], v[82:83]
	v_pk_mul_f32 v[82:83], v[58:59], v[2:3] op_sel_hi:[0,1]
	v_exp_f32_e32 v82, v82
	v_exp_f32_e32 v83, v83
	v_pk_mul_f32 v[84:85], v[58:59], v[4:5] op_sel_hi:[0,1]
	v_exp_f32_e32 v84, v84
	v_exp_f32_e32 v85, v85
	v_pk_mul_f32 v[86:87], v[120:121], v[94:95] op_sel_hi:[0,1]
	v_pk_fma_f32 v[116:117], v[116:117], v[82:83], v[86:87]
	v_pk_mul_f32 v[82:83], v[120:121], v[96:97] op_sel_hi:[0,1]
	v_pk_fma_f32 v[118:119], v[118:119], v[84:85], v[82:83]
	s_nop 0
	s_waitcnt lgkmcnt(0)
	s_nop 0
	ds_read_b128 v[82:85], v19 offset:64
	ds_read_b128 v[86:89], v19 offset:80
	ds_read_b128 v[90:93], v19 offset:96
	ds_read_b128 v[94:97], v19 offset:112
	v_mov_b32_e32 v19, 0xb2b0
	v_pk_mul_f32 v[134:135], v[60:61], v[14:15] op_sel_hi:[0,1]
	v_exp_f32_e32 v134, v134
	v_exp_f32_e32 v135, v135
	v_pk_mul_f32 v[136:137], v[60:61], v[16:17] op_sel_hi:[0,1]
	v_exp_f32_e32 v136, v136
	v_exp_f32_e32 v137, v137
	v_mul_f32_e32 v120, v60, v65
	v_pk_mul_f32 v[98:99], v[120:121], v[98:99] op_sel_hi:[0,1]
	v_pk_fma_f32 v[122:123], v[122:123], v[134:135], v[98:99]
	v_pk_mul_f32 v[98:99], v[120:121], v[100:101] op_sel_hi:[0,1]
	v_pk_fma_f32 v[124:125], v[124:125], v[136:137], v[98:99]
	v_pk_mul_f32 v[98:99], v[60:61], v[10:11] op_sel_hi:[0,1]
	v_exp_f32_e32 v98, v98
	v_exp_f32_e32 v99, v99
	v_pk_mul_f32 v[100:101], v[60:61], v[12:13] op_sel_hi:[0,1]
	v_exp_f32_e32 v100, v100
	v_exp_f32_e32 v101, v101
	v_pk_mul_f32 v[102:103], v[120:121], v[102:103] op_sel_hi:[0,1]
	v_pk_fma_f32 v[128:129], v[128:129], v[98:99], v[102:103]
	v_pk_mul_f32 v[98:99], v[120:121], v[104:105] op_sel_hi:[0,1]
	v_pk_fma_f32 v[126:127], v[126:127], v[100:101], v[98:99]
	v_pk_mul_f32 v[98:99], v[60:61], v[6:7] op_sel_hi:[0,1]
	v_exp_f32_e32 v98, v98
	v_exp_f32_e32 v99, v99
	v_pk_mul_f32 v[100:101], v[60:61], v[8:9] op_sel_hi:[0,1]
	v_exp_f32_e32 v100, v100
	v_exp_f32_e32 v101, v101
	v_pk_mul_f32 v[102:103], v[120:121], v[108:109] op_sel_hi:[0,1]
	v_pk_fma_f32 v[130:131], v[130:131], v[98:99], v[102:103]
	v_pk_mul_f32 v[98:99], v[120:121], v[110:111] op_sel_hi:[0,1]
	v_pk_fma_f32 v[132:133], v[132:133], v[100:101], v[98:99]
	v_pk_mul_f32 v[98:99], v[60:61], v[2:3] op_sel_hi:[0,1]
	v_exp_f32_e32 v98, v98
	v_exp_f32_e32 v99, v99
	v_pk_mul_f32 v[100:101], v[60:61], v[4:5] op_sel_hi:[0,1]
	v_exp_f32_e32 v100, v100
	v_exp_f32_e32 v101, v101
	v_pk_mul_f32 v[102:103], v[120:121], v[112:113] op_sel_hi:[0,1]
	v_pk_fma_f32 v[116:117], v[116:117], v[98:99], v[102:103]
	v_pk_mul_f32 v[98:99], v[120:121], v[114:115] op_sel_hi:[0,1]
	v_pk_fma_f32 v[118:119], v[118:119], v[100:101], v[98:99]
	s_nop 0
	s_waitcnt lgkmcnt(0)
	s_nop 0
	ds_read_b128 v[98:101], v19 offset:64
	ds_read_b128 v[102:105], v19 offset:80
	ds_read_b128 v[108:111], v19 offset:96
	ds_read_b128 v[112:115], v19 offset:112
	v_mov_b32_e32 v19, 0xb380
	v_pk_mul_f32 v[134:135], v[62:63], v[14:15] op_sel_hi:[0,1]
	v_exp_f32_e32 v134, v134
	v_exp_f32_e32 v135, v135
	v_pk_mul_f32 v[136:137], v[62:63], v[16:17] op_sel_hi:[0,1]
	v_exp_f32_e32 v136, v136
	v_exp_f32_e32 v137, v137
	v_mul_f32_e32 v120, v62, v63
	v_pk_mul_f32 v[82:83], v[120:121], v[82:83] op_sel_hi:[0,1]
	v_pk_fma_f32 v[122:123], v[122:123], v[134:135], v[82:83]
	v_pk_mul_f32 v[82:83], v[120:121], v[84:85] op_sel_hi:[0,1]
	v_pk_fma_f32 v[124:125], v[124:125], v[136:137], v[82:83]
	v_pk_mul_f32 v[82:83], v[62:63], v[10:11] op_sel_hi:[0,1]
	v_exp_f32_e32 v82, v82
	v_exp_f32_e32 v83, v83
	v_pk_mul_f32 v[84:85], v[62:63], v[12:13] op_sel_hi:[0,1]
	v_exp_f32_e32 v84, v84
	v_exp_f32_e32 v85, v85
	v_pk_mul_f32 v[86:87], v[120:121], v[86:87] op_sel_hi:[0,1]
	v_pk_fma_f32 v[128:129], v[128:129], v[82:83], v[86:87]
	v_pk_mul_f32 v[82:83], v[120:121], v[88:89] op_sel_hi:[0,1]
	v_pk_fma_f32 v[126:127], v[126:127], v[84:85], v[82:83]
	v_pk_mul_f32 v[82:83], v[62:63], v[6:7] op_sel_hi:[0,1]
	v_exp_f32_e32 v82, v82
	v_exp_f32_e32 v83, v83
	v_pk_mul_f32 v[84:85], v[62:63], v[8:9] op_sel_hi:[0,1]
	v_exp_f32_e32 v84, v84
	v_exp_f32_e32 v85, v85
	v_pk_mul_f32 v[86:87], v[120:121], v[90:91] op_sel_hi:[0,1]
	v_pk_fma_f32 v[130:131], v[130:131], v[82:83], v[86:87]
	v_pk_mul_f32 v[82:83], v[120:121], v[92:93] op_sel_hi:[0,1]
	v_pk_fma_f32 v[132:133], v[132:133], v[84:85], v[82:83]
	v_pk_mul_f32 v[82:83], v[62:63], v[2:3] op_sel_hi:[0,1]
	v_exp_f32_e32 v82, v82
	v_exp_f32_e32 v83, v83
	v_pk_mul_f32 v[84:85], v[62:63], v[4:5] op_sel_hi:[0,1]
	v_exp_f32_e32 v84, v84
	v_exp_f32_e32 v85, v85
	v_pk_mul_f32 v[86:87], v[120:121], v[94:95] op_sel_hi:[0,1]
	v_pk_fma_f32 v[116:117], v[116:117], v[82:83], v[86:87]
	v_pk_mul_f32 v[82:83], v[120:121], v[96:97] op_sel_hi:[0,1]
	v_pk_fma_f32 v[118:119], v[118:119], v[84:85], v[82:83]
	s_nop 0
	s_waitcnt lgkmcnt(0)
	s_nop 0
	ds_read_b128 v[82:85], v19 offset:64
	ds_read_b128 v[86:89], v19 offset:80
	ds_read_b128 v[90:93], v19 offset:96
	ds_read_b128 v[94:97], v19 offset:112
	v_mov_b32_e32 v19, 0xb450
	v_pk_mul_f32 v[134:135], v[64:65], v[14:15] op_sel_hi:[0,1]
	v_exp_f32_e32 v134, v134
	v_exp_f32_e32 v135, v135
	v_pk_mul_f32 v[136:137], v[64:65], v[16:17] op_sel_hi:[0,1]
	v_exp_f32_e32 v136, v136
	v_exp_f32_e32 v137, v137
	v_mul_f32_e32 v120, v64, v61
	v_pk_mul_f32 v[98:99], v[120:121], v[98:99] op_sel_hi:[0,1]
	v_pk_fma_f32 v[122:123], v[122:123], v[134:135], v[98:99]
	v_pk_mul_f32 v[98:99], v[120:121], v[100:101] op_sel_hi:[0,1]
	v_pk_fma_f32 v[124:125], v[124:125], v[136:137], v[98:99]
	v_pk_mul_f32 v[98:99], v[64:65], v[10:11] op_sel_hi:[0,1]
	v_exp_f32_e32 v98, v98
	v_exp_f32_e32 v99, v99
	v_pk_mul_f32 v[100:101], v[64:65], v[12:13] op_sel_hi:[0,1]
	v_exp_f32_e32 v100, v100
	v_exp_f32_e32 v101, v101
	v_pk_mul_f32 v[102:103], v[120:121], v[102:103] op_sel_hi:[0,1]
	v_pk_fma_f32 v[128:129], v[128:129], v[98:99], v[102:103]
	v_pk_mul_f32 v[98:99], v[120:121], v[104:105] op_sel_hi:[0,1]
	v_pk_fma_f32 v[126:127], v[126:127], v[100:101], v[98:99]
	v_pk_mul_f32 v[98:99], v[64:65], v[6:7] op_sel_hi:[0,1]
	v_exp_f32_e32 v98, v98
	v_exp_f32_e32 v99, v99
	v_pk_mul_f32 v[100:101], v[64:65], v[8:9] op_sel_hi:[0,1]
	v_exp_f32_e32 v100, v100
	v_exp_f32_e32 v101, v101
	v_pk_mul_f32 v[102:103], v[120:121], v[108:109] op_sel_hi:[0,1]
	v_pk_fma_f32 v[130:131], v[130:131], v[98:99], v[102:103]
	v_pk_mul_f32 v[98:99], v[120:121], v[110:111] op_sel_hi:[0,1]
	v_pk_fma_f32 v[132:133], v[132:133], v[100:101], v[98:99]
	v_pk_mul_f32 v[98:99], v[64:65], v[2:3] op_sel_hi:[0,1]
	v_exp_f32_e32 v98, v98
	v_exp_f32_e32 v99, v99
	v_pk_mul_f32 v[100:101], v[64:65], v[4:5] op_sel_hi:[0,1]
	v_exp_f32_e32 v100, v100
	v_exp_f32_e32 v101, v101
	v_pk_mul_f32 v[102:103], v[120:121], v[112:113] op_sel_hi:[0,1]
	v_pk_fma_f32 v[116:117], v[116:117], v[98:99], v[102:103]
	v_pk_mul_f32 v[98:99], v[120:121], v[114:115] op_sel_hi:[0,1]
	v_pk_fma_f32 v[118:119], v[118:119], v[100:101], v[98:99]
	s_nop 0
	s_waitcnt lgkmcnt(0)
	s_nop 0
	ds_read_b128 v[98:101], v19 offset:64
	ds_read_b128 v[102:105], v19 offset:80
	ds_read_b128 v[108:111], v19 offset:96
	ds_read_b128 v[112:115], v19 offset:112
	v_mov_b32_e32 v19, 0xb520
	v_pk_mul_f32 v[134:135], v[66:67], v[14:15] op_sel_hi:[0,1]
	v_exp_f32_e32 v134, v134
	v_exp_f32_e32 v135, v135
	v_pk_mul_f32 v[136:137], v[66:67], v[16:17] op_sel_hi:[0,1]
	v_exp_f32_e32 v136, v136
	v_exp_f32_e32 v137, v137
	v_mul_f32_e32 v120, v66, v59
	v_pk_mul_f32 v[82:83], v[120:121], v[82:83] op_sel_hi:[0,1]
	v_pk_fma_f32 v[122:123], v[122:123], v[134:135], v[82:83]
	v_pk_mul_f32 v[82:83], v[120:121], v[84:85] op_sel_hi:[0,1]
	v_pk_fma_f32 v[124:125], v[124:125], v[136:137], v[82:83]
	v_pk_mul_f32 v[82:83], v[66:67], v[10:11] op_sel_hi:[0,1]
	v_exp_f32_e32 v82, v82
	v_exp_f32_e32 v83, v83
	v_pk_mul_f32 v[84:85], v[66:67], v[12:13] op_sel_hi:[0,1]
	v_exp_f32_e32 v84, v84
	v_exp_f32_e32 v85, v85
	v_pk_mul_f32 v[86:87], v[120:121], v[86:87] op_sel_hi:[0,1]
	v_pk_fma_f32 v[128:129], v[128:129], v[82:83], v[86:87]
	v_pk_mul_f32 v[82:83], v[120:121], v[88:89] op_sel_hi:[0,1]
	v_pk_fma_f32 v[126:127], v[126:127], v[84:85], v[82:83]
	v_pk_mul_f32 v[82:83], v[66:67], v[6:7] op_sel_hi:[0,1]
	v_exp_f32_e32 v82, v82
	v_exp_f32_e32 v83, v83
	v_pk_mul_f32 v[84:85], v[66:67], v[8:9] op_sel_hi:[0,1]
	v_exp_f32_e32 v84, v84
	v_exp_f32_e32 v85, v85
	v_pk_mul_f32 v[86:87], v[120:121], v[90:91] op_sel_hi:[0,1]
	v_pk_fma_f32 v[130:131], v[130:131], v[82:83], v[86:87]
	v_pk_mul_f32 v[82:83], v[120:121], v[92:93] op_sel_hi:[0,1]
	v_pk_fma_f32 v[132:133], v[132:133], v[84:85], v[82:83]
	v_pk_mul_f32 v[82:83], v[66:67], v[2:3] op_sel_hi:[0,1]
	v_exp_f32_e32 v82, v82
	v_exp_f32_e32 v83, v83
	v_pk_mul_f32 v[84:85], v[66:67], v[4:5] op_sel_hi:[0,1]
	v_exp_f32_e32 v84, v84
	v_exp_f32_e32 v85, v85
	v_pk_mul_f32 v[86:87], v[120:121], v[94:95] op_sel_hi:[0,1]
	v_pk_fma_f32 v[116:117], v[116:117], v[82:83], v[86:87]
	v_pk_mul_f32 v[82:83], v[120:121], v[96:97] op_sel_hi:[0,1]
	v_pk_fma_f32 v[118:119], v[118:119], v[84:85], v[82:83]
	s_nop 0
	s_waitcnt lgkmcnt(0)
	s_nop 0
	ds_read_b128 v[82:85], v19 offset:64
	ds_read_b128 v[86:89], v19 offset:80
	ds_read_b128 v[90:93], v19 offset:96
	ds_read_b128 v[94:97], v19 offset:112
	v_mov_b32_e32 v19, 0xb5f0
	v_pk_mul_f32 v[134:135], v[68:69], v[14:15] op_sel_hi:[0,1]
	v_exp_f32_e32 v134, v134
	v_exp_f32_e32 v135, v135
	v_pk_mul_f32 v[136:137], v[68:69], v[16:17] op_sel_hi:[0,1]
	v_exp_f32_e32 v136, v136
	v_exp_f32_e32 v137, v137
	v_mul_f32_e32 v120, v68, v57
	v_pk_mul_f32 v[98:99], v[120:121], v[98:99] op_sel_hi:[0,1]
	v_pk_fma_f32 v[122:123], v[122:123], v[134:135], v[98:99]
	v_pk_mul_f32 v[98:99], v[120:121], v[100:101] op_sel_hi:[0,1]
	v_pk_fma_f32 v[124:125], v[124:125], v[136:137], v[98:99]
	v_pk_mul_f32 v[98:99], v[68:69], v[10:11] op_sel_hi:[0,1]
	v_exp_f32_e32 v98, v98
	v_exp_f32_e32 v99, v99
	v_pk_mul_f32 v[100:101], v[68:69], v[12:13] op_sel_hi:[0,1]
	v_exp_f32_e32 v100, v100
	v_exp_f32_e32 v101, v101
	v_pk_mul_f32 v[102:103], v[120:121], v[102:103] op_sel_hi:[0,1]
	v_pk_fma_f32 v[128:129], v[128:129], v[98:99], v[102:103]
	v_pk_mul_f32 v[98:99], v[120:121], v[104:105] op_sel_hi:[0,1]
	v_pk_fma_f32 v[126:127], v[126:127], v[100:101], v[98:99]
	v_pk_mul_f32 v[98:99], v[68:69], v[6:7] op_sel_hi:[0,1]
	v_exp_f32_e32 v98, v98
	v_exp_f32_e32 v99, v99
	v_pk_mul_f32 v[100:101], v[68:69], v[8:9] op_sel_hi:[0,1]
	v_exp_f32_e32 v100, v100
	v_exp_f32_e32 v101, v101
	v_pk_mul_f32 v[102:103], v[120:121], v[108:109] op_sel_hi:[0,1]
	v_pk_fma_f32 v[130:131], v[130:131], v[98:99], v[102:103]
	v_pk_mul_f32 v[98:99], v[120:121], v[110:111] op_sel_hi:[0,1]
	v_pk_fma_f32 v[132:133], v[132:133], v[100:101], v[98:99]
	v_pk_mul_f32 v[98:99], v[68:69], v[2:3] op_sel_hi:[0,1]
	v_exp_f32_e32 v98, v98
	v_exp_f32_e32 v99, v99
	v_pk_mul_f32 v[100:101], v[68:69], v[4:5] op_sel_hi:[0,1]
	v_exp_f32_e32 v100, v100
	v_exp_f32_e32 v101, v101
	v_pk_mul_f32 v[102:103], v[120:121], v[112:113] op_sel_hi:[0,1]
	v_pk_fma_f32 v[116:117], v[116:117], v[98:99], v[102:103]
	v_pk_mul_f32 v[98:99], v[120:121], v[114:115] op_sel_hi:[0,1]
	v_pk_fma_f32 v[118:119], v[118:119], v[100:101], v[98:99]
	s_nop 0
	s_waitcnt lgkmcnt(0)
	s_nop 0
	ds_read_b128 v[98:101], v19 offset:64
	ds_read_b128 v[102:105], v19 offset:80
	ds_read_b128 v[108:111], v19 offset:96
	ds_read_b128 v[112:115], v19 offset:112
	v_mov_b32_e32 v19, 0xb6c0
	v_pk_mul_f32 v[134:135], v[70:71], v[14:15] op_sel_hi:[0,1]
	v_exp_f32_e32 v134, v134
	v_exp_f32_e32 v135, v135
	v_pk_mul_f32 v[136:137], v[70:71], v[16:17] op_sel_hi:[0,1]
	v_exp_f32_e32 v136, v136
	v_exp_f32_e32 v137, v137
	v_mul_f32_e32 v120, v70, v55
	v_pk_mul_f32 v[82:83], v[120:121], v[82:83] op_sel_hi:[0,1]
	v_pk_fma_f32 v[122:123], v[122:123], v[134:135], v[82:83]
	v_pk_mul_f32 v[82:83], v[120:121], v[84:85] op_sel_hi:[0,1]
	v_pk_fma_f32 v[124:125], v[124:125], v[136:137], v[82:83]
	v_pk_mul_f32 v[82:83], v[70:71], v[10:11] op_sel_hi:[0,1]
	v_exp_f32_e32 v82, v82
	v_exp_f32_e32 v83, v83
	v_pk_mul_f32 v[84:85], v[70:71], v[12:13] op_sel_hi:[0,1]
	v_exp_f32_e32 v84, v84
	v_exp_f32_e32 v85, v85
	v_pk_mul_f32 v[86:87], v[120:121], v[86:87] op_sel_hi:[0,1]
	v_pk_fma_f32 v[128:129], v[128:129], v[82:83], v[86:87]
	v_pk_mul_f32 v[82:83], v[120:121], v[88:89] op_sel_hi:[0,1]
	v_pk_fma_f32 v[126:127], v[126:127], v[84:85], v[82:83]
	v_pk_mul_f32 v[82:83], v[70:71], v[6:7] op_sel_hi:[0,1]
	v_exp_f32_e32 v82, v82
	v_exp_f32_e32 v83, v83
	v_pk_mul_f32 v[84:85], v[70:71], v[8:9] op_sel_hi:[0,1]
	v_exp_f32_e32 v84, v84
	v_exp_f32_e32 v85, v85
	v_pk_mul_f32 v[86:87], v[120:121], v[90:91] op_sel_hi:[0,1]
	v_pk_fma_f32 v[130:131], v[130:131], v[82:83], v[86:87]
	v_pk_mul_f32 v[82:83], v[120:121], v[92:93] op_sel_hi:[0,1]
	v_pk_fma_f32 v[132:133], v[132:133], v[84:85], v[82:83]
	v_pk_mul_f32 v[82:83], v[70:71], v[2:3] op_sel_hi:[0,1]
	v_exp_f32_e32 v82, v82
	v_exp_f32_e32 v83, v83
	v_pk_mul_f32 v[84:85], v[70:71], v[4:5] op_sel_hi:[0,1]
	v_exp_f32_e32 v84, v84
	v_exp_f32_e32 v85, v85
	v_pk_mul_f32 v[86:87], v[120:121], v[94:95] op_sel_hi:[0,1]
	v_pk_fma_f32 v[116:117], v[116:117], v[82:83], v[86:87]
	v_pk_mul_f32 v[82:83], v[120:121], v[96:97] op_sel_hi:[0,1]
	v_pk_fma_f32 v[118:119], v[118:119], v[84:85], v[82:83]
	s_nop 0
	s_waitcnt lgkmcnt(0)
	s_nop 0
	ds_read_b128 v[82:85], v19 offset:64
	ds_read_b128 v[86:89], v19 offset:80
	ds_read_b128 v[90:93], v19 offset:96
	ds_read_b128 v[94:97], v19 offset:112
	v_mov_b32_e32 v19, 0xb790
	v_pk_mul_f32 v[134:135], v[72:73], v[14:15] op_sel_hi:[0,1]
	v_exp_f32_e32 v134, v134
	v_exp_f32_e32 v135, v135
	v_pk_mul_f32 v[136:137], v[72:73], v[16:17] op_sel_hi:[0,1]
	v_exp_f32_e32 v136, v136
	v_exp_f32_e32 v137, v137
	v_mul_f32_e32 v120, v72, v53
	v_pk_mul_f32 v[98:99], v[120:121], v[98:99] op_sel_hi:[0,1]
	v_pk_fma_f32 v[122:123], v[122:123], v[134:135], v[98:99]
	v_pk_mul_f32 v[98:99], v[120:121], v[100:101] op_sel_hi:[0,1]
	v_pk_fma_f32 v[124:125], v[124:125], v[136:137], v[98:99]
	v_pk_mul_f32 v[98:99], v[72:73], v[10:11] op_sel_hi:[0,1]
	v_exp_f32_e32 v98, v98
	v_exp_f32_e32 v99, v99
	v_pk_mul_f32 v[100:101], v[72:73], v[12:13] op_sel_hi:[0,1]
	v_exp_f32_e32 v100, v100
	v_exp_f32_e32 v101, v101
	v_pk_mul_f32 v[102:103], v[120:121], v[102:103] op_sel_hi:[0,1]
	v_pk_fma_f32 v[128:129], v[128:129], v[98:99], v[102:103]
	v_pk_mul_f32 v[98:99], v[120:121], v[104:105] op_sel_hi:[0,1]
	v_pk_fma_f32 v[126:127], v[126:127], v[100:101], v[98:99]
	v_pk_mul_f32 v[98:99], v[72:73], v[6:7] op_sel_hi:[0,1]
	v_exp_f32_e32 v98, v98
	v_exp_f32_e32 v99, v99
	v_pk_mul_f32 v[100:101], v[72:73], v[8:9] op_sel_hi:[0,1]
	v_exp_f32_e32 v100, v100
	v_exp_f32_e32 v101, v101
	v_pk_mul_f32 v[102:103], v[120:121], v[108:109] op_sel_hi:[0,1]
	v_pk_fma_f32 v[130:131], v[130:131], v[98:99], v[102:103]
	v_pk_mul_f32 v[98:99], v[120:121], v[110:111] op_sel_hi:[0,1]
	v_pk_fma_f32 v[132:133], v[132:133], v[100:101], v[98:99]
	v_pk_mul_f32 v[98:99], v[72:73], v[2:3] op_sel_hi:[0,1]
	v_exp_f32_e32 v98, v98
	v_exp_f32_e32 v99, v99
	v_pk_mul_f32 v[100:101], v[72:73], v[4:5] op_sel_hi:[0,1]
	v_exp_f32_e32 v100, v100
	v_exp_f32_e32 v101, v101
	v_pk_mul_f32 v[102:103], v[120:121], v[112:113] op_sel_hi:[0,1]
	v_pk_fma_f32 v[116:117], v[116:117], v[98:99], v[102:103]
	v_pk_mul_f32 v[98:99], v[120:121], v[114:115] op_sel_hi:[0,1]
	v_pk_fma_f32 v[118:119], v[118:119], v[100:101], v[98:99]
	s_nop 0
	s_waitcnt lgkmcnt(0)
	s_nop 0
	ds_read_b128 v[98:101], v19 offset:64
	ds_read_b128 v[102:105], v19 offset:80
	ds_read_b128 v[108:111], v19 offset:96
	ds_read_b128 v[112:115], v19 offset:112
	v_mov_b32_e32 v19, 0xb860
	v_pk_mul_f32 v[134:135], v[74:75], v[14:15] op_sel_hi:[0,1]
	v_exp_f32_e32 v134, v134
	v_exp_f32_e32 v135, v135
	v_pk_mul_f32 v[136:137], v[74:75], v[16:17] op_sel_hi:[0,1]
	v_exp_f32_e32 v136, v136
	v_exp_f32_e32 v137, v137
	v_mul_f32_e32 v120, v74, v51
	v_pk_mul_f32 v[82:83], v[120:121], v[82:83] op_sel_hi:[0,1]
	v_pk_fma_f32 v[122:123], v[122:123], v[134:135], v[82:83]
	v_pk_mul_f32 v[82:83], v[120:121], v[84:85] op_sel_hi:[0,1]
	v_pk_fma_f32 v[124:125], v[124:125], v[136:137], v[82:83]
	v_pk_mul_f32 v[82:83], v[74:75], v[10:11] op_sel_hi:[0,1]
	v_exp_f32_e32 v82, v82
	v_exp_f32_e32 v83, v83
	v_pk_mul_f32 v[84:85], v[74:75], v[12:13] op_sel_hi:[0,1]
	v_exp_f32_e32 v84, v84
	v_exp_f32_e32 v85, v85
	v_pk_mul_f32 v[86:87], v[120:121], v[86:87] op_sel_hi:[0,1]
	v_pk_fma_f32 v[128:129], v[128:129], v[82:83], v[86:87]
	v_pk_mul_f32 v[82:83], v[120:121], v[88:89] op_sel_hi:[0,1]
	v_pk_fma_f32 v[126:127], v[126:127], v[84:85], v[82:83]
	v_pk_mul_f32 v[82:83], v[74:75], v[6:7] op_sel_hi:[0,1]
	v_exp_f32_e32 v82, v82
	v_exp_f32_e32 v83, v83
	v_pk_mul_f32 v[84:85], v[74:75], v[8:9] op_sel_hi:[0,1]
	v_exp_f32_e32 v84, v84
	v_exp_f32_e32 v85, v85
	v_pk_mul_f32 v[86:87], v[120:121], v[90:91] op_sel_hi:[0,1]
	v_pk_fma_f32 v[130:131], v[130:131], v[82:83], v[86:87]
	v_pk_mul_f32 v[82:83], v[120:121], v[92:93] op_sel_hi:[0,1]
	v_pk_fma_f32 v[132:133], v[132:133], v[84:85], v[82:83]
	v_pk_mul_f32 v[82:83], v[74:75], v[2:3] op_sel_hi:[0,1]
	v_exp_f32_e32 v82, v82
	v_exp_f32_e32 v83, v83
	v_pk_mul_f32 v[84:85], v[74:75], v[4:5] op_sel_hi:[0,1]
	v_exp_f32_e32 v84, v84
	v_exp_f32_e32 v85, v85
	v_pk_mul_f32 v[86:87], v[120:121], v[94:95] op_sel_hi:[0,1]
	v_pk_fma_f32 v[116:117], v[116:117], v[82:83], v[86:87]
	v_pk_mul_f32 v[82:83], v[120:121], v[96:97] op_sel_hi:[0,1]
	v_pk_fma_f32 v[118:119], v[118:119], v[84:85], v[82:83]
	s_nop 0
	s_waitcnt lgkmcnt(0)
	s_nop 0
	ds_read_b128 v[82:85], v19 offset:64
	ds_read_b128 v[86:89], v19 offset:80
	ds_read_b128 v[90:93], v19 offset:96
	ds_read_b128 v[94:97], v19 offset:112
	v_mov_b32_e32 v19, 0xb930
	v_pk_mul_f32 v[134:135], v[76:77], v[14:15] op_sel_hi:[0,1]
	v_exp_f32_e32 v134, v134
	v_exp_f32_e32 v135, v135
	v_pk_mul_f32 v[136:137], v[76:77], v[16:17] op_sel_hi:[0,1]
	v_exp_f32_e32 v136, v136
	v_exp_f32_e32 v137, v137
	v_mul_f32_e32 v120, v76, v49
	v_pk_mul_f32 v[98:99], v[120:121], v[98:99] op_sel_hi:[0,1]
	v_pk_fma_f32 v[122:123], v[122:123], v[134:135], v[98:99]
	v_pk_mul_f32 v[98:99], v[120:121], v[100:101] op_sel_hi:[0,1]
	v_pk_fma_f32 v[124:125], v[124:125], v[136:137], v[98:99]
	v_pk_mul_f32 v[98:99], v[76:77], v[10:11] op_sel_hi:[0,1]
	v_exp_f32_e32 v98, v98
	v_exp_f32_e32 v99, v99
	v_pk_mul_f32 v[100:101], v[76:77], v[12:13] op_sel_hi:[0,1]
	v_exp_f32_e32 v100, v100
	v_exp_f32_e32 v101, v101
	v_pk_mul_f32 v[102:103], v[120:121], v[102:103] op_sel_hi:[0,1]
	v_pk_fma_f32 v[128:129], v[128:129], v[98:99], v[102:103]
	v_pk_mul_f32 v[98:99], v[120:121], v[104:105] op_sel_hi:[0,1]
	v_pk_fma_f32 v[126:127], v[126:127], v[100:101], v[98:99]
	v_pk_mul_f32 v[98:99], v[76:77], v[6:7] op_sel_hi:[0,1]
	v_exp_f32_e32 v98, v98
	v_exp_f32_e32 v99, v99
	v_pk_mul_f32 v[100:101], v[76:77], v[8:9] op_sel_hi:[0,1]
	v_exp_f32_e32 v100, v100
	v_exp_f32_e32 v101, v101
	v_pk_mul_f32 v[102:103], v[120:121], v[108:109] op_sel_hi:[0,1]
	v_pk_fma_f32 v[130:131], v[130:131], v[98:99], v[102:103]
	v_pk_mul_f32 v[98:99], v[120:121], v[110:111] op_sel_hi:[0,1]
	v_pk_fma_f32 v[132:133], v[132:133], v[100:101], v[98:99]
	v_pk_mul_f32 v[98:99], v[76:77], v[2:3] op_sel_hi:[0,1]
	v_exp_f32_e32 v98, v98
	v_exp_f32_e32 v99, v99
	v_pk_mul_f32 v[100:101], v[76:77], v[4:5] op_sel_hi:[0,1]
	v_exp_f32_e32 v100, v100
	v_exp_f32_e32 v101, v101
	v_pk_mul_f32 v[102:103], v[120:121], v[112:113] op_sel_hi:[0,1]
	v_pk_fma_f32 v[116:117], v[116:117], v[98:99], v[102:103]
	v_pk_mul_f32 v[98:99], v[120:121], v[114:115] op_sel_hi:[0,1]
	v_pk_fma_f32 v[118:119], v[118:119], v[100:101], v[98:99]
	s_nop 0
	s_waitcnt lgkmcnt(0)
	s_nop 0
	ds_read_b128 v[98:101], v19 offset:64
	ds_read_b128 v[102:105], v19 offset:80
	ds_read_b128 v[108:111], v19 offset:96
	ds_read_b128 v[112:115], v19 offset:112
	v_add_f32_e32 v19, 0, v80
	v_add_f32_e32 v19, v19, v20
	v_add_f32_e32 v19, v19, v22
	v_add_f32_e32 v19, v19, v24
	v_add_f32_e32 v19, v19, v26
	v_add_f32_e32 v19, v19, v28
	v_add_f32_e32 v19, v19, v30
	v_add_f32_e32 v19, v19, v32
	v_add_f32_e32 v19, v19, v34
	v_add_f32_e32 v19, v19, v36
	v_pk_mul_f32 v[134:135], v[78:79], v[14:15] op_sel_hi:[0,1]
	v_pk_mul_f32 v[136:137], v[78:79], v[16:17] op_sel_hi:[0,1]
	v_add_f32_e32 v19, v19, v38
	v_exp_f32_e32 v134, v134
	v_exp_f32_e32 v135, v135
	v_exp_f32_e32 v136, v136
	v_exp_f32_e32 v137, v137
	v_add_f32_e32 v19, v19, v40
	v_add_f32_e32 v19, v19, v42
	v_mul_f32_e32 v120, v78, v47
	v_add_f32_e32 v19, v19, v44
	v_pk_mul_f32 v[82:83], v[120:121], v[82:83] op_sel_hi:[0,1]
	v_pk_mul_f32 v[84:85], v[120:121], v[84:85] op_sel_hi:[0,1]
	v_add_f32_e32 v19, v19, v46
	v_pk_fma_f32 v[82:83], v[122:123], v[134:135], v[82:83]
	v_pk_fma_f32 v[84:85], v[124:125], v[136:137], v[84:85]
	v_pk_mul_f32 v[122:123], v[78:79], v[10:11] op_sel_hi:[0,1]
	v_pk_mul_f32 v[124:125], v[78:79], v[12:13] op_sel_hi:[0,1]
	v_add_f32_e32 v19, v19, v48
	v_exp_f32_e32 v122, v122
	v_exp_f32_e32 v123, v123
	v_exp_f32_e32 v124, v124
	v_exp_f32_e32 v125, v125
	v_add_f32_e32 v19, v19, v50
	v_add_f32_e32 v19, v19, v52
	v_add_f32_e32 v19, v19, v54
	v_pk_mul_f32 v[86:87], v[120:121], v[86:87] op_sel_hi:[0,1]
	v_pk_mul_f32 v[88:89], v[120:121], v[88:89] op_sel_hi:[0,1]
	v_add_f32_e32 v19, v19, v56
	v_pk_fma_f32 v[86:87], v[128:129], v[122:123], v[86:87]
	v_pk_fma_f32 v[88:89], v[126:127], v[124:125], v[88:89]
	v_pk_mul_f32 v[122:123], v[78:79], v[6:7] op_sel_hi:[0,1]
	v_pk_mul_f32 v[124:125], v[78:79], v[8:9] op_sel_hi:[0,1]
	v_add_f32_e32 v19, v19, v58
	v_exp_f32_e32 v122, v122
	v_exp_f32_e32 v123, v123
	v_exp_f32_e32 v124, v124
	v_exp_f32_e32 v125, v125
	v_add_f32_e32 v19, v19, v60
	v_add_f32_e32 v19, v19, v62
	v_add_f32_e32 v19, v19, v64
	v_pk_mul_f32 v[90:91], v[120:121], v[90:91] op_sel_hi:[0,1]
	v_pk_mul_f32 v[92:93], v[120:121], v[92:93] op_sel_hi:[0,1]
	v_add_f32_e32 v19, v19, v66
	v_pk_fma_f32 v[90:91], v[130:131], v[122:123], v[90:91]
	v_pk_fma_f32 v[92:93], v[132:133], v[124:125], v[92:93]
	v_pk_mul_f32 v[122:123], v[78:79], v[2:3] op_sel_hi:[0,1]
	v_pk_mul_f32 v[124:125], v[78:79], v[4:5] op_sel_hi:[0,1]
	v_add_f32_e32 v19, v19, v68
	v_exp_f32_e32 v122, v122
	v_exp_f32_e32 v123, v123
	v_exp_f32_e32 v124, v124
	v_exp_f32_e32 v125, v125
	v_add_f32_e32 v19, v19, v70
	v_add_f32_e32 v19, v19, v72
	v_add_f32_e32 v19, v19, v74
	v_pk_mul_f32 v[94:95], v[120:121], v[94:95] op_sel_hi:[0,1]
	v_pk_mul_f32 v[96:97], v[120:121], v[96:97] op_sel_hi:[0,1]
	v_add_f32_e32 v19, v19, v76
	v_pk_fma_f32 v[94:95], v[116:117], v[122:123], v[94:95]
	v_pk_fma_f32 v[96:97], v[118:119], v[124:125], v[96:97]
	v_add_f32_e32 v19, v19, v78
	s_waitcnt lgkmcnt(0)
	v_cvt_f32_f16_e32 v20, v106
	v_add_f32_e32 v19, v19, v18
	v_pk_mul_f32 v[4:5], v[18:19], v[4:5] op_sel_hi:[0,1]
	v_exp_f32_e32 v4, v4
	v_exp_f32_e32 v5, v5
	v_pk_mul_f32 v[14:15], v[18:19], v[14:15] op_sel_hi:[0,1]
	v_exp_f32_e32 v14, v14
	v_exp_f32_e32 v15, v15
	v_mul_f32_e32 v20, v18, v20
	v_pk_mul_f32 v[22:23], v[20:21], v[114:115] op_sel_hi:[0,1]
	v_pk_fma_f32 v[22:23], v[96:97], v[4:5], v[22:23]
	v_pk_mul_f32 v[4:5], v[20:21], v[98:99] op_sel_hi:[0,1]
	v_pk_fma_f32 v[14:15], v[82:83], v[14:15], v[4:5]
	v_pk_mul_f32 v[4:5], v[18:19], v[16:17] op_sel_hi:[0,1]
	v_exp_f32_e32 v4, v4
	v_exp_f32_e32 v5, v5
	v_pk_mul_f32 v[10:11], v[18:19], v[10:11] op_sel_hi:[0,1]
	v_exp_f32_e32 v10, v10
	v_exp_f32_e32 v11, v11
	v_pk_mul_f32 v[16:17], v[20:21], v[100:101] op_sel_hi:[0,1]
	v_pk_fma_f32 v[16:17], v[84:85], v[4:5], v[16:17]
	v_pk_mul_f32 v[4:5], v[20:21], v[102:103] op_sel_hi:[0,1]
	v_pk_fma_f32 v[10:11], v[86:87], v[10:11], v[4:5]
	v_pk_mul_f32 v[4:5], v[18:19], v[12:13] op_sel_hi:[0,1]
	v_exp_f32_e32 v4, v4
	v_exp_f32_e32 v5, v5
	v_pk_mul_f32 v[6:7], v[18:19], v[6:7] op_sel_hi:[0,1]
	v_exp_f32_e32 v6, v6
	v_exp_f32_e32 v7, v7
	v_pk_mul_f32 v[8:9], v[18:19], v[8:9] op_sel_hi:[0,1]
	v_exp_f32_e32 v8, v8
	v_exp_f32_e32 v9, v9
	v_pk_mul_f32 v[2:3], v[18:19], v[2:3] op_sel_hi:[0,1]
	v_pk_mul_f32 v[12:13], v[20:21], v[104:105] op_sel_hi:[0,1]
	v_exp_f32_e32 v2, v2
	v_exp_f32_e32 v3, v3
	v_pk_fma_f32 v[4:5], v[88:89], v[4:5], v[12:13]
	v_pk_mul_f32 v[12:13], v[20:21], v[108:109] op_sel_hi:[0,1]
	v_pk_fma_f32 v[6:7], v[90:91], v[6:7], v[12:13]
	v_pk_mul_f32 v[12:13], v[20:21], v[110:111] op_sel_hi:[0,1]
	v_pk_fma_f32 v[8:9], v[92:93], v[8:9], v[12:13]
	v_pk_mul_f32 v[12:13], v[20:21], v[112:113] op_sel_hi:[0,1]
	v_cvt_pk_f16_f32 v5, v4, v5
	v_cvt_pk_f16_f32 v4, v10, v11
	v_lshl_or_b32 v10, v0, 4, s6
	v_mov_b32_e32 v11, s7
	v_pk_fma_f32 v[12:13], v[94:95], v[2:3], v[12:13]
	v_cvt_pk_f16_f32 v3, v16, v17
	v_cvt_pk_f16_f32 v2, v14, v15
	v_lshl_add_u64 v[10:11], s[4:5], 0, v[10:11]
	s_movk_i32 s4, 0x2000
	global_store_dwordx4 v[10:11], v[2:5], off sc1
	global_store_dword v1, v19, s[0:1] sc1
	s_nop 0
	v_cvt_pk_f16_f32 v2, v6, v7
	v_add_co_u32_e32 v6, vcc, s4, v10
	v_cvt_pk_f16_f32 v5, v22, v23
	v_cvt_pk_f16_f32 v4, v12, v13
	v_cvt_pk_f16_f32 v3, v8, v9
	v_addc_co_u32_e32 v7, vcc, 0, v11, vcc
	global_store_dwordx4 v[6:7], v[2:5], off sc1
	s_endpgm

.LBB3_10:
	s_or_b64 exec, exec, s[0:1]
	v_lshl_add_u64 v[0:1], v[6:7], 1, s[10:11]
	v_cvt_pk_f16_f32 v5, v80, v81
	v_cvt_pk_f16_f32 v4, v78, v79
	v_lshl_add_u64 v[6:7], v[0:1], 0, v[8:9]
	global_store_dwordx2 v[6:7], v[4:5], off sc1
	v_cvt_pk_f16_f32 v3, v2, v3
	v_cvt_pk_f16_f32 v2, v82, v83
	v_lshl_add_u64 v[4:5], v[0:1], 0, v[10:11]
	global_store_dwordx2 v[4:5], v[2:3], off sc1
	v_cvt_pk_f16_f32 v3, v84, v85
	v_cvt_pk_f16_f32 v2, v86, v87
	v_lshl_add_u64 v[4:5], v[0:1], 0, v[12:13]
	global_store_dwordx2 v[4:5], v[2:3], off sc1
	v_cvt_pk_f16_f32 v3, v88, v89
	v_cvt_pk_f16_f32 v2, v90, v91
	v_lshl_add_u64 v[4:5], v[0:1], 0, v[14:15]
	global_store_dwordx2 v[4:5], v[2:3], off sc1
	v_cvt_pk_f16_f32 v3, v92, v93
	v_cvt_pk_f16_f32 v2, v94, v95
	v_lshl_add_u64 v[4:5], v[0:1], 0, v[16:17]
	global_store_dwordx2 v[4:5], v[2:3], off sc1
	v_cvt_pk_f16_f32 v3, v96, v97
	v_cvt_pk_f16_f32 v2, v98, v99
	v_lshl_add_u64 v[4:5], v[0:1], 0, v[18:19]
	global_store_dwordx2 v[4:5], v[2:3], off sc1
	v_cvt_pk_f16_f32 v3, v100, v101
	v_cvt_pk_f16_f32 v2, v102, v103
	v_lshl_add_u64 v[4:5], v[0:1], 0, v[20:21]
	global_store_dwordx2 v[4:5], v[2:3], off sc1
	v_cvt_pk_f16_f32 v3, v104, v105
	v_cvt_pk_f16_f32 v2, v106, v107
	v_lshl_add_u64 v[0:1], v[0:1], 0, v[22:23]
	global_store_dwordx2 v[0:1], v[2:3], off sc1
	s_endpgm

.Lk2f_bc_done:
	s_or_b64 exec, exec, s[56:57]
	s_waitcnt lgkmcnt(0)
	s_barrier
	s_waitcnt vmcnt(18)
	v_cvt_f32_f16_e32 v134, v68
	v_cvt_f32_f16_sdwa v135, v68 dst_sel:DWORD dst_unused:UNUSED_PAD src0_sel:WORD_1
	v_cvt_f32_f16_e32 v136, v69
	v_cvt_f32_f16_sdwa v137, v69 dst_sel:DWORD dst_unused:UNUSED_PAD src0_sel:WORD_1
	v_cvt_f32_f16_e32 v138, v70
	v_cvt_f32_f16_sdwa v139, v70 dst_sel:DWORD dst_unused:UNUSED_PAD src0_sel:WORD_1
	v_cvt_f32_f16_e32 v140, v71
	v_cvt_f32_f16_sdwa v141, v71 dst_sel:DWORD dst_unused:UNUSED_PAD src0_sel:WORD_1
	s_waitcnt vmcnt(17)
	v_cvt_f32_f16_e32 v142, v72
	v_cvt_f32_f16_sdwa v143, v72 dst_sel:DWORD dst_unused:UNUSED_PAD src0_sel:WORD_1
	v_cvt_f32_f16_e32 v144, v73
	v_cvt_f32_f16_sdwa v145, v73 dst_sel:DWORD dst_unused:UNUSED_PAD src0_sel:WORD_1
	v_cvt_f32_f16_e32 v146, v74
	v_cvt_f32_f16_sdwa v147, v74 dst_sel:DWORD dst_unused:UNUSED_PAD src0_sel:WORD_1
	v_cvt_f32_f16_e32 v148, v75
	v_cvt_f32_f16_sdwa v149, v75 dst_sel:DWORD dst_unused:UNUSED_PAD src0_sel:WORD_1
	ds_read_b128 v[70:73], v67
	ds_read_b128 v[74:77], v67 offset:16
	ds_read_b128 v[78:81], v67 offset:32
	ds_read_b128 v[82:85], v67 offset:48
	ds_read_b128 v[86:89], v67 offset:64
	ds_read_b128 v[90:93], v67 offset:80
	ds_read_b128 v[94:97], v67 offset:96
	ds_read_b128 v[98:101], v67 offset:112
	ds_read_b128 v[102:105], v67 offset:128
	ds_read_b128 v[106:109], v67 offset:144
	ds_read_b128 v[110:113], v67 offset:160
	ds_read_b128 v[114:117], v67 offset:176
	ds_read_b128 v[118:121], v67 offset:192
	ds_read_b128 v[122:125], v67 offset:208
	ds_read_b128 v[126:129], v67 offset:224
	ds_read_b128 v[130:133], v67 offset:240
	v_lshlrev_b32_e32 v68, 1, v0
	s_waitcnt vmcnt(11)
	v_cvt_f32_f16_e32 v150, v62
	s_waitcnt vmcnt(10)
	v_cvt_f32_f16_e32 v69, v54
	v_pk_mul_f32 v[154:155], v[150:151], v[14:15] op_sel_hi:[0,1]
	v_exp_f32_e32 v154, v154
	v_exp_f32_e32 v155, v155
	v_pk_mul_f32 v[156:157], v[150:151], v[16:17] op_sel_hi:[0,1]
	v_exp_f32_e32 v156, v156
	v_exp_f32_e32 v157, v157
	v_mul_f32_e32 v152, v150, v69
	v_pk_mul_f32 v[134:135], v[154:155], v[134:135]
	s_waitcnt lgkmcnt(14)
	v_pk_fma_f32 v[134:135], v[152:153], v[70:71], v[134:135] op_sel_hi:[0,1,1]
	s_waitcnt lgkmcnt(11)
	v_pk_fma_f32 v[70:71], v[86:87], v[134:135], 0 op_sel_hi:[1,1,0]
	v_pk_mul_f32 v[86:87], v[156:157], v[136:137]
	s_nop 0
	v_pk_fma_f32 v[136:137], v[152:153], v[72:73], v[86:87] op_sel_hi:[0,1,1]
	v_pk_mul_f32 v[72:73], v[150:151], v[10:11] op_sel_hi:[0,1]
	v_exp_f32_e32 v72, v72
	v_exp_f32_e32 v73, v73
	v_pk_mul_f32 v[86:87], v[150:151], v[12:13] op_sel_hi:[0,1]
	v_exp_f32_e32 v86, v86
	v_exp_f32_e32 v87, v87
	v_pk_mul_f32 v[72:73], v[72:73], v[138:139]
	v_pk_fma_f32 v[70:71], v[88:89], v[136:137], v[70:71]
	v_pk_fma_f32 v[138:139], v[152:153], v[74:75], v[72:73] op_sel_hi:[0,1,1]
	v_pk_mul_f32 v[72:73], v[86:87], v[140:141]
	v_pk_mul_f32 v[74:75], v[150:151], v[8:9] op_sel_hi:[0,1]
	v_pk_fma_f32 v[140:141], v[152:153], v[76:77], v[72:73] op_sel_hi:[0,1,1]
	v_pk_mul_f32 v[72:73], v[150:151], v[6:7] op_sel_hi:[0,1]
	v_exp_f32_e32 v72, v72
	v_exp_f32_e32 v73, v73
	v_exp_f32_e32 v74, v74
	v_exp_f32_e32 v75, v75
	s_waitcnt lgkmcnt(10)
	v_pk_fma_f32 v[70:71], v[90:91], v[138:139], v[70:71]
	v_pk_mul_f32 v[72:73], v[72:73], v[142:143]
	v_pk_fma_f32 v[70:71], v[92:93], v[140:141], v[70:71]
	v_pk_fma_f32 v[142:143], v[152:153], v[78:79], v[72:73] op_sel_hi:[0,1,1]
	v_pk_mul_f32 v[72:73], v[74:75], v[144:145]
	v_pk_mul_f32 v[74:75], v[150:151], v[4:5] op_sel_hi:[0,1]
	v_pk_fma_f32 v[144:145], v[152:153], v[80:81], v[72:73] op_sel_hi:[0,1,1]
	v_pk_mul_f32 v[72:73], v[150:151], v[2:3] op_sel_hi:[0,1]
	v_exp_f32_e32 v72, v72
	v_exp_f32_e32 v73, v73
	v_exp_f32_e32 v74, v74
	v_exp_f32_e32 v75, v75
	s_waitcnt lgkmcnt(9)
	v_pk_fma_f32 v[70:71], v[94:95], v[142:143], v[70:71]
	v_pk_mul_f32 v[72:73], v[72:73], v[146:147]
	v_pk_fma_f32 v[70:71], v[96:97], v[144:145], v[70:71]
	v_pk_fma_f32 v[146:147], v[152:153], v[82:83], v[72:73] op_sel_hi:[0,1,1]
	v_pk_mul_f32 v[72:73], v[74:75], v[148:149]
	s_waitcnt lgkmcnt(8)
	v_pk_fma_f32 v[70:71], v[98:99], v[146:147], v[70:71]
	v_pk_fma_f32 v[148:149], v[152:153], v[84:85], v[72:73] op_sel_hi:[0,1,1]
	v_pk_fma_f32 v[70:71], v[100:101], v[148:149], v[70:71]
	s_nop 0
	v_add_f32_e32 v69, v70, v71
	v_fma_mix_f32 v69, v1, v54, v69 op_sel_hi:[0,1,0]
	s_waitcnt vmcnt(9)
	v_fma_mixlo_f16 v69, v69, v58, 0 op_sel_hi:[0,1,0]
	ds_write_b16 v68, v69 offset:4096
	ds_read_b128 v[70:73], v67 offset:256
	ds_read_b128 v[74:77], v67 offset:272
	ds_read_b128 v[78:81], v67 offset:288
	ds_read_b128 v[82:85], v67 offset:304
	ds_read_b128 v[86:89], v67 offset:320
	ds_read_b128 v[90:93], v67 offset:336
	ds_read_b128 v[94:97], v67 offset:352
	ds_read_b128 v[98:101], v67 offset:368
	v_cvt_f32_f16_sdwa v62, v62 dst_sel:DWORD dst_unused:UNUSED_PAD src0_sel:WORD_1
	v_cvt_f32_f16_sdwa v69, v54 dst_sel:DWORD dst_unused:UNUSED_PAD src0_sel:WORD_1
	v_pk_mul_f32 v[152:153], v[62:63], v[14:15] op_sel_hi:[0,1]
	v_exp_f32_e32 v152, v152
	v_exp_f32_e32 v153, v153
	v_pk_mul_f32 v[154:155], v[62:63], v[16:17] op_sel_hi:[0,1]
	v_exp_f32_e32 v154, v154
	v_exp_f32_e32 v155, v155
	v_mul_f32_e32 v150, v62, v69
	v_pk_mul_f32 v[134:135], v[152:153], v[134:135]
	s_waitcnt lgkmcnt(14)
	v_pk_fma_f32 v[134:135], v[150:151], v[102:103], v[134:135] op_sel_hi:[0,1,1]
	s_waitcnt lgkmcnt(12)
	v_pk_fma_f32 v[102:103], v[118:119], v[134:135], 0 op_sel_hi:[1,1,0]
	v_pk_mul_f32 v[118:119], v[154:155], v[136:137]
	s_nop 0
	v_pk_fma_f32 v[136:137], v[150:151], v[104:105], v[118:119] op_sel_hi:[0,1,1]
	v_pk_mul_f32 v[104:105], v[62:63], v[10:11] op_sel_hi:[0,1]
	v_exp_f32_e32 v104, v104
	v_exp_f32_e32 v105, v105
	v_pk_mul_f32 v[118:119], v[62:63], v[12:13] op_sel_hi:[0,1]
	v_exp_f32_e32 v118, v118
	v_exp_f32_e32 v119, v119
	v_pk_mul_f32 v[104:105], v[104:105], v[138:139]
	v_pk_fma_f32 v[102:103], v[120:121], v[136:137], v[102:103]
	v_pk_fma_f32 v[138:139], v[150:151], v[106:107], v[104:105] op_sel_hi:[0,1,1]
	v_pk_mul_f32 v[104:105], v[118:119], v[140:141]
	v_pk_mul_f32 v[106:107], v[62:63], v[8:9] op_sel_hi:[0,1]
	v_pk_fma_f32 v[140:141], v[150:151], v[108:109], v[104:105] op_sel_hi:[0,1,1]
	v_pk_mul_f32 v[104:105], v[62:63], v[6:7] op_sel_hi:[0,1]
	v_exp_f32_e32 v104, v104
	v_exp_f32_e32 v105, v105
	v_exp_f32_e32 v106, v106
	v_exp_f32_e32 v107, v107
	s_waitcnt lgkmcnt(11)
	v_pk_fma_f32 v[102:103], v[122:123], v[138:139], v[102:103]
	v_pk_mul_f32 v[104:105], v[104:105], v[142:143]
	v_pk_fma_f32 v[102:103], v[124:125], v[140:141], v[102:103]
	v_pk_fma_f32 v[142:143], v[150:151], v[110:111], v[104:105] op_sel_hi:[0,1,1]
	v_pk_mul_f32 v[104:105], v[106:107], v[144:145]
	v_pk_mul_f32 v[106:107], v[62:63], v[4:5] op_sel_hi:[0,1]
	v_pk_fma_f32 v[144:145], v[150:151], v[112:113], v[104:105] op_sel_hi:[0,1,1]
	v_pk_mul_f32 v[104:105], v[62:63], v[2:3] op_sel_hi:[0,1]
	v_exp_f32_e32 v104, v104
	v_exp_f32_e32 v105, v105
	v_exp_f32_e32 v106, v106
	v_exp_f32_e32 v107, v107
	s_waitcnt lgkmcnt(10)
	v_pk_fma_f32 v[102:103], v[126:127], v[142:143], v[102:103]
	v_pk_mul_f32 v[104:105], v[104:105], v[146:147]
	v_pk_fma_f32 v[102:103], v[128:129], v[144:145], v[102:103]
	v_pk_fma_f32 v[146:147], v[150:151], v[114:115], v[104:105] op_sel_hi:[0,1,1]
	v_pk_mul_f32 v[104:105], v[106:107], v[148:149]
	s_waitcnt lgkmcnt(9)
	v_pk_fma_f32 v[102:103], v[130:131], v[146:147], v[102:103]
	v_pk_fma_f32 v[148:149], v[150:151], v[116:117], v[104:105] op_sel_hi:[0,1,1]
	v_pk_fma_f32 v[102:103], v[132:133], v[148:149], v[102:103]
	s_nop 0
	v_add_f32_e32 v62, v102, v103
	v_fma_mix_f32 v54, v1, v54, v62 op_sel:[0,1,0] op_sel_hi:[0,1,0]
	v_fma_mixlo_f16 v54, v54, v58, 0 op_sel:[0,1,0] op_sel_hi:[0,1,0]
	ds_write_b16 v68, v54 offset:5136
	ds_read_b128 v[102:105], v67 offset:384
	ds_read_b128 v[106:109], v67 offset:400
	ds_read_b128 v[110:113], v67 offset:416
	ds_read_b128 v[114:117], v67 offset:432
	ds_read_b128 v[118:121], v67 offset:448
	ds_read_b128 v[122:125], v67 offset:464
	ds_read_b128 v[126:129], v67 offset:480
	ds_read_b128 v[130:133], v67 offset:496
	v_cvt_f32_f16_e32 v54, v63
	v_cvt_f32_f16_e32 v58, v55
	v_pk_mul_f32 v[150:151], v[54:55], v[14:15] op_sel_hi:[0,1]
	v_exp_f32_e32 v150, v150
	v_exp_f32_e32 v151, v151
	v_pk_mul_f32 v[152:153], v[54:55], v[16:17] op_sel_hi:[0,1]
	v_exp_f32_e32 v152, v152
	v_exp_f32_e32 v153, v153
	v_mul_f32_e32 v58, v54, v58
	v_pk_mul_f32 v[134:135], v[150:151], v[134:135]
	s_waitcnt lgkmcnt(14)
	v_pk_fma_f32 v[134:135], v[58:59], v[70:71], v[134:135] op_sel_hi:[0,1,1]
	s_waitcnt lgkmcnt(12)
	v_pk_fma_f32 v[70:71], v[86:87], v[134:135], 0 op_sel_hi:[1,1,0]
	v_pk_mul_f32 v[86:87], v[152:153], v[136:137]
	s_nop 0
	v_pk_fma_f32 v[136:137], v[58:59], v[72:73], v[86:87] op_sel_hi:[0,1,1]
	v_pk_mul_f32 v[72:73], v[54:55], v[10:11] op_sel_hi:[0,1]
	v_exp_f32_e32 v72, v72
	v_exp_f32_e32 v73, v73
	v_pk_mul_f32 v[86:87], v[54:55], v[12:13] op_sel_hi:[0,1]
	v_exp_f32_e32 v86, v86
	v_exp_f32_e32 v87, v87
	v_pk_mul_f32 v[72:73], v[72:73], v[138:139]
	v_pk_fma_f32 v[70:71], v[88:89], v[136:137], v[70:71]
	v_pk_fma_f32 v[138:139], v[58:59], v[74:75], v[72:73] op_sel_hi:[0,1,1]
	v_pk_mul_f32 v[72:73], v[86:87], v[140:141]
	v_pk_mul_f32 v[74:75], v[54:55], v[8:9] op_sel_hi:[0,1]
	v_pk_fma_f32 v[140:141], v[58:59], v[76:77], v[72:73] op_sel_hi:[0,1,1]
	v_pk_mul_f32 v[72:73], v[54:55], v[6:7] op_sel_hi:[0,1]
	v_exp_f32_e32 v72, v72
	v_exp_f32_e32 v73, v73
	v_exp_f32_e32 v74, v74
	v_exp_f32_e32 v75, v75
	s_waitcnt lgkmcnt(11)
	v_pk_fma_f32 v[70:71], v[90:91], v[138:139], v[70:71]
	v_pk_mul_f32 v[72:73], v[72:73], v[142:143]
	v_pk_fma_f32 v[70:71], v[92:93], v[140:141], v[70:71]
	v_pk_fma_f32 v[142:143], v[58:59], v[78:79], v[72:73] op_sel_hi:[0,1,1]
	v_pk_mul_f32 v[72:73], v[74:75], v[144:145]
	v_pk_mul_f32 v[74:75], v[54:55], v[4:5] op_sel_hi:[0,1]
	v_pk_fma_f32 v[144:145], v[58:59], v[80:81], v[72:73] op_sel_hi:[0,1,1]
	v_pk_mul_f32 v[72:73], v[54:55], v[2:3] op_sel_hi:[0,1]
	v_exp_f32_e32 v72, v72
	v_exp_f32_e32 v73, v73
	v_exp_f32_e32 v74, v74
	v_exp_f32_e32 v75, v75
	s_waitcnt lgkmcnt(10)
	v_pk_fma_f32 v[70:71], v[94:95], v[142:143], v[70:71]
	v_pk_mul_f32 v[72:73], v[72:73], v[146:147]
	v_pk_fma_f32 v[70:71], v[96:97], v[144:145], v[70:71]
	v_pk_fma_f32 v[146:147], v[58:59], v[82:83], v[72:73] op_sel_hi:[0,1,1]
	v_pk_mul_f32 v[72:73], v[74:75], v[148:149]
	s_waitcnt lgkmcnt(9)
	v_pk_fma_f32 v[70:71], v[98:99], v[146:147], v[70:71]
	v_pk_fma_f32 v[148:149], v[58:59], v[84:85], v[72:73] op_sel_hi:[0,1,1]
	v_pk_fma_f32 v[70:71], v[100:101], v[148:149], v[70:71]
	s_nop 0
	v_add_f32_e32 v54, v70, v71
	v_fma_mix_f32 v54, v1, v55, v54 op_sel_hi:[0,1,0]
	v_fma_mixlo_f16 v54, v54, v59, 0 op_sel_hi:[0,1,0]
	ds_write_b16 v68, v54 offset:6176
	ds_read_b128 v[70:73], v67 offset:512
	ds_read_b128 v[74:77], v67 offset:528
	ds_read_b128 v[78:81], v67 offset:544
	ds_read_b128 v[82:85], v67 offset:560
	ds_read_b128 v[86:89], v67 offset:576
	ds_read_b128 v[90:93], v67 offset:592
	ds_read_b128 v[94:97], v67 offset:608
	ds_read_b128 v[98:101], v67 offset:624
	v_cvt_f32_f16_sdwa v54, v63 dst_sel:DWORD dst_unused:UNUSED_PAD src0_sel:WORD_1
	v_cvt_f32_f16_sdwa v58, v55 dst_sel:DWORD dst_unused:UNUSED_PAD src0_sel:WORD_1
	v_pk_mul_f32 v[62:63], v[54:55], v[14:15] op_sel_hi:[0,1]
	v_exp_f32_e32 v62, v62
	v_exp_f32_e32 v63, v63
	v_pk_mul_f32 v[150:151], v[54:55], v[16:17] op_sel_hi:[0,1]
	v_exp_f32_e32 v150, v150
	v_exp_f32_e32 v151, v151
	v_mul_f32_e32 v58, v54, v58
	v_pk_mul_f32 v[62:63], v[62:63], v[134:135]
	s_waitcnt lgkmcnt(14)
	v_pk_fma_f32 v[62:63], v[58:59], v[102:103], v[62:63] op_sel_hi:[0,1,1]
	s_waitcnt lgkmcnt(12)
	v_pk_fma_f32 v[102:103], v[118:119], v[62:63], 0 op_sel_hi:[1,1,0]
	v_pk_mul_f32 v[118:119], v[150:151], v[136:137]
	s_nop 0
	v_pk_fma_f32 v[134:135], v[58:59], v[104:105], v[118:119] op_sel_hi:[0,1,1]
	v_pk_mul_f32 v[104:105], v[54:55], v[10:11] op_sel_hi:[0,1]
	v_exp_f32_e32 v104, v104
	v_exp_f32_e32 v105, v105
	v_pk_mul_f32 v[118:119], v[54:55], v[12:13] op_sel_hi:[0,1]
	v_exp_f32_e32 v118, v118
	v_exp_f32_e32 v119, v119
	v_pk_mul_f32 v[104:105], v[104:105], v[138:139]
	v_pk_fma_f32 v[102:103], v[120:121], v[134:135], v[102:103]
	v_pk_fma_f32 v[136:137], v[58:59], v[106:107], v[104:105] op_sel_hi:[0,1,1]
	v_pk_mul_f32 v[104:105], v[118:119], v[140:141]
	v_pk_mul_f32 v[106:107], v[54:55], v[8:9] op_sel_hi:[0,1]
	v_pk_fma_f32 v[138:139], v[58:59], v[108:109], v[104:105] op_sel_hi:[0,1,1]
	v_pk_mul_f32 v[104:105], v[54:55], v[6:7] op_sel_hi:[0,1]
	v_exp_f32_e32 v104, v104
	v_exp_f32_e32 v105, v105
	v_exp_f32_e32 v106, v106
	v_exp_f32_e32 v107, v107
	s_waitcnt lgkmcnt(11)
	v_pk_fma_f32 v[102:103], v[122:123], v[136:137], v[102:103]
	v_pk_mul_f32 v[104:105], v[104:105], v[142:143]
	v_pk_fma_f32 v[102:103], v[124:125], v[138:139], v[102:103]
	v_pk_fma_f32 v[140:141], v[58:59], v[110:111], v[104:105] op_sel_hi:[0,1,1]
	v_pk_mul_f32 v[104:105], v[106:107], v[144:145]
	v_pk_mul_f32 v[106:107], v[54:55], v[4:5] op_sel_hi:[0,1]
	v_pk_fma_f32 v[142:143], v[58:59], v[112:113], v[104:105] op_sel_hi:[0,1,1]
	v_pk_mul_f32 v[104:105], v[54:55], v[2:3] op_sel_hi:[0,1]
	v_exp_f32_e32 v104, v104
	v_exp_f32_e32 v105, v105
	v_exp_f32_e32 v106, v106
	v_exp_f32_e32 v107, v107
	s_waitcnt lgkmcnt(10)
	v_pk_fma_f32 v[102:103], v[126:127], v[140:141], v[102:103]
	v_pk_mul_f32 v[104:105], v[104:105], v[146:147]
	v_pk_fma_f32 v[102:103], v[128:129], v[142:143], v[102:103]
	v_pk_fma_f32 v[144:145], v[58:59], v[114:115], v[104:105] op_sel_hi:[0,1,1]
	v_pk_mul_f32 v[104:105], v[106:107], v[148:149]
	s_waitcnt lgkmcnt(9)
	v_pk_fma_f32 v[102:103], v[130:131], v[144:145], v[102:103]
	v_pk_fma_f32 v[146:147], v[58:59], v[116:117], v[104:105] op_sel_hi:[0,1,1]
	v_pk_fma_f32 v[102:103], v[132:133], v[146:147], v[102:103]
	s_nop 0
	v_add_f32_e32 v54, v102, v103
	v_fma_mix_f32 v54, v1, v55, v54 op_sel:[0,1,0] op_sel_hi:[0,1,0]
	v_fma_mixlo_f16 v54, v54, v59, 0 op_sel:[0,1,0] op_sel_hi:[0,1,0]
	ds_write_b16 v68, v54 offset:7216
	ds_read_b128 v[102:105], v67 offset:640
	ds_read_b128 v[106:109], v67 offset:656
	ds_read_b128 v[110:113], v67 offset:672
	ds_read_b128 v[114:117], v67 offset:688
	ds_read_b128 v[118:121], v67 offset:704
	ds_read_b128 v[122:125], v67 offset:720
	ds_read_b128 v[126:129], v67 offset:736
	ds_read_b128 v[130:133], v67 offset:752
	v_cvt_f32_f16_e32 v54, v64
	v_cvt_f32_f16_e32 v55, v56
	v_pk_mul_f32 v[148:149], v[54:55], v[14:15] op_sel_hi:[0,1]
	v_exp_f32_e32 v148, v148
	v_exp_f32_e32 v149, v149
	v_pk_mul_f32 v[150:151], v[54:55], v[16:17] op_sel_hi:[0,1]
	v_exp_f32_e32 v150, v150
	v_exp_f32_e32 v151, v151
	v_mul_f32_e32 v58, v54, v55
	v_pk_mul_f32 v[62:63], v[148:149], v[62:63]
	s_waitcnt lgkmcnt(14)
	v_pk_fma_f32 v[62:63], v[58:59], v[70:71], v[62:63] op_sel_hi:[0,1,1]
	s_waitcnt lgkmcnt(12)
	v_pk_fma_f32 v[70:71], v[86:87], v[62:63], 0 op_sel_hi:[1,1,0]
	v_pk_mul_f32 v[86:87], v[150:151], v[134:135]
	s_nop 0
	v_pk_fma_f32 v[134:135], v[58:59], v[72:73], v[86:87] op_sel_hi:[0,1,1]
	v_pk_mul_f32 v[72:73], v[54:55], v[10:11] op_sel_hi:[0,1]
	v_exp_f32_e32 v72, v72
	v_exp_f32_e32 v73, v73
	v_pk_mul_f32 v[86:87], v[54:55], v[12:13] op_sel_hi:[0,1]
	v_exp_f32_e32 v86, v86
	v_exp_f32_e32 v87, v87
	v_pk_mul_f32 v[72:73], v[72:73], v[136:137]
	v_pk_fma_f32 v[70:71], v[88:89], v[134:135], v[70:71]
	v_pk_fma_f32 v[136:137], v[58:59], v[74:75], v[72:73] op_sel_hi:[0,1,1]
	v_pk_mul_f32 v[72:73], v[86:87], v[138:139]
	v_pk_mul_f32 v[74:75], v[54:55], v[8:9] op_sel_hi:[0,1]
	v_pk_fma_f32 v[138:139], v[58:59], v[76:77], v[72:73] op_sel_hi:[0,1,1]
	v_pk_mul_f32 v[72:73], v[54:55], v[6:7] op_sel_hi:[0,1]
	v_exp_f32_e32 v72, v72
	v_exp_f32_e32 v73, v73
	v_exp_f32_e32 v74, v74
	v_exp_f32_e32 v75, v75
	s_waitcnt lgkmcnt(11)
	v_pk_fma_f32 v[70:71], v[90:91], v[136:137], v[70:71]
	v_pk_mul_f32 v[72:73], v[72:73], v[140:141]
	v_pk_fma_f32 v[70:71], v[92:93], v[138:139], v[70:71]
	v_pk_fma_f32 v[140:141], v[58:59], v[78:79], v[72:73] op_sel_hi:[0,1,1]
	v_pk_mul_f32 v[72:73], v[74:75], v[142:143]
	s_waitcnt lgkmcnt(10)
	v_pk_fma_f32 v[70:71], v[94:95], v[140:141], v[70:71]
	v_pk_fma_f32 v[142:143], v[58:59], v[80:81], v[72:73] op_sel_hi:[0,1,1]
	v_pk_mul_f32 v[72:73], v[54:55], v[2:3] op_sel_hi:[0,1]
	v_exp_f32_e32 v72, v72
	v_exp_f32_e32 v73, v73
	v_pk_mul_f32 v[54:55], v[54:55], v[4:5] op_sel_hi:[0,1]
	v_exp_f32_e32 v54, v54
	v_exp_f32_e32 v55, v55
	v_pk_mul_f32 v[72:73], v[72:73], v[144:145]
	v_pk_fma_f32 v[70:71], v[96:97], v[142:143], v[70:71]
	v_pk_fma_f32 v[144:145], v[58:59], v[82:83], v[72:73] op_sel_hi:[0,1,1]
	v_pk_mul_f32 v[54:55], v[54:55], v[146:147]
	s_waitcnt lgkmcnt(9)
	v_pk_fma_f32 v[70:71], v[98:99], v[144:145], v[70:71]
	v_pk_fma_f32 v[54:55], v[58:59], v[84:85], v[54:55] op_sel_hi:[0,1,1]
	v_pk_fma_f32 v[58:59], v[100:101], v[54:55], v[70:71]
	s_nop 0
	v_add_f32_e32 v58, v58, v59
	v_fma_mix_f32 v58, v1, v56, v58 op_sel_hi:[0,1,0]
	v_fma_mixlo_f16 v58, v58, v60, 0 op_sel_hi:[0,1,0]
	ds_write_b16 v68, v58 offset:8256
	ds_read_b128 v[70:73], v67 offset:768
	ds_read_b128 v[74:77], v67 offset:784
	ds_read_b128 v[78:81], v67 offset:800
	ds_read_b128 v[82:85], v67 offset:816
	ds_read_b128 v[86:89], v67 offset:832
	ds_read_b128 v[90:93], v67 offset:848
	ds_read_b128 v[94:97], v67 offset:864
	ds_read_b128 v[98:101], v67 offset:880
	v_cvt_f32_f16_sdwa v58, v64 dst_sel:DWORD dst_unused:UNUSED_PAD src0_sel:WORD_1
	v_cvt_f32_f16_sdwa v59, v56 dst_sel:DWORD dst_unused:UNUSED_PAD src0_sel:WORD_1
	v_pk_mul_f32 v[146:147], v[58:59], v[14:15] op_sel_hi:[0,1]
	v_exp_f32_e32 v146, v146
	v_exp_f32_e32 v147, v147
	v_pk_mul_f32 v[148:149], v[58:59], v[16:17] op_sel_hi:[0,1]
	v_exp_f32_e32 v148, v148
	v_exp_f32_e32 v149, v149
	v_mul_f32_e32 v64, v58, v59
	v_pk_mul_f32 v[62:63], v[146:147], v[62:63]
	s_waitcnt lgkmcnt(14)
	v_pk_fma_f32 v[62:63], v[64:65], v[102:103], v[62:63] op_sel_hi:[0,1,1]
	s_waitcnt lgkmcnt(12)
	v_pk_fma_f32 v[102:103], v[118:119], v[62:63], 0 op_sel_hi:[1,1,0]
	v_pk_mul_f32 v[118:119], v[148:149], v[134:135]
	s_nop 0
	v_pk_fma_f32 v[134:135], v[64:65], v[104:105], v[118:119] op_sel_hi:[0,1,1]
	v_pk_mul_f32 v[104:105], v[58:59], v[10:11] op_sel_hi:[0,1]
	v_exp_f32_e32 v104, v104
	v_exp_f32_e32 v105, v105
	v_pk_mul_f32 v[118:119], v[58:59], v[12:13] op_sel_hi:[0,1]
	v_exp_f32_e32 v118, v118
	v_exp_f32_e32 v119, v119
	v_pk_mul_f32 v[104:105], v[104:105], v[136:137]
	v_pk_fma_f32 v[102:103], v[120:121], v[134:135], v[102:103]
	v_pk_fma_f32 v[136:137], v[64:65], v[106:107], v[104:105] op_sel_hi:[0,1,1]
	v_pk_mul_f32 v[104:105], v[118:119], v[138:139]
	v_pk_mul_f32 v[106:107], v[58:59], v[8:9] op_sel_hi:[0,1]
	v_pk_fma_f32 v[138:139], v[64:65], v[108:109], v[104:105] op_sel_hi:[0,1,1]
	v_pk_mul_f32 v[104:105], v[58:59], v[6:7] op_sel_hi:[0,1]
	v_exp_f32_e32 v104, v104
	v_exp_f32_e32 v105, v105
	v_exp_f32_e32 v106, v106
	v_exp_f32_e32 v107, v107
	s_waitcnt lgkmcnt(11)
	v_pk_fma_f32 v[102:103], v[122:123], v[136:137], v[102:103]
	v_pk_mul_f32 v[104:105], v[104:105], v[140:141]
	v_pk_fma_f32 v[102:103], v[124:125], v[138:139], v[102:103]
	v_pk_fma_f32 v[140:141], v[64:65], v[110:111], v[104:105] op_sel_hi:[0,1,1]
	v_pk_mul_f32 v[104:105], v[106:107], v[142:143]
	s_waitcnt lgkmcnt(10)
	v_pk_fma_f32 v[102:103], v[126:127], v[140:141], v[102:103]
	v_pk_fma_f32 v[142:143], v[64:65], v[112:113], v[104:105] op_sel_hi:[0,1,1]
	v_pk_mul_f32 v[104:105], v[58:59], v[2:3] op_sel_hi:[0,1]
	v_exp_f32_e32 v104, v104
	v_exp_f32_e32 v105, v105
	v_pk_mul_f32 v[58:59], v[58:59], v[4:5] op_sel_hi:[0,1]
	v_exp_f32_e32 v58, v58
	v_exp_f32_e32 v59, v59
	v_pk_mul_f32 v[104:105], v[104:105], v[144:145]
	v_pk_fma_f32 v[102:103], v[128:129], v[142:143], v[102:103]
	v_pk_fma_f32 v[144:145], v[64:65], v[114:115], v[104:105] op_sel_hi:[0,1,1]
	v_pk_mul_f32 v[54:55], v[58:59], v[54:55]
	s_waitcnt lgkmcnt(9)
	v_pk_fma_f32 v[102:103], v[130:131], v[144:145], v[102:103]
	v_pk_fma_f32 v[54:55], v[64:65], v[116:117], v[54:55] op_sel_hi:[0,1,1]
	v_pk_fma_f32 v[58:59], v[132:133], v[54:55], v[102:103]
	s_nop 0
	v_add_f32_e32 v58, v58, v59
	v_fma_mix_f32 v56, v1, v56, v58 op_sel:[0,1,0] op_sel_hi:[0,1,0]
	v_fma_mixlo_f16 v56, v56, v60, 0 op_sel:[0,1,0] op_sel_hi:[0,1,0]
	ds_write_b16 v68, v56 offset:9296
	ds_read_b128 v[102:105], v67 offset:896
	ds_read_b128 v[106:109], v67 offset:912
	ds_read_b128 v[110:113], v67 offset:928
	ds_read_b128 v[114:117], v67 offset:944
	ds_read_b128 v[118:121], v67 offset:960
	ds_read_b128 v[122:125], v67 offset:976
	ds_read_b128 v[126:129], v67 offset:992
	ds_read_b128 v[130:133], v67 offset:1008
	v_cvt_f32_f16_e32 v56, v65
	v_cvt_f32_f16_e32 v58, v57
	v_pk_mul_f32 v[146:147], v[56:57], v[14:15] op_sel_hi:[0,1]
	v_exp_f32_e32 v146, v146
	v_exp_f32_e32 v147, v147
	v_pk_mul_f32 v[148:149], v[56:57], v[16:17] op_sel_hi:[0,1]
	v_exp_f32_e32 v148, v148
	v_exp_f32_e32 v149, v149
	v_mul_f32_e32 v58, v56, v58
	v_pk_mul_f32 v[62:63], v[146:147], v[62:63]
	s_waitcnt lgkmcnt(14)
	v_pk_fma_f32 v[62:63], v[58:59], v[70:71], v[62:63] op_sel_hi:[0,1,1]
	s_waitcnt lgkmcnt(12)
	v_pk_fma_f32 v[70:71], v[86:87], v[62:63], 0 op_sel_hi:[1,1,0]
	v_pk_mul_f32 v[86:87], v[148:149], v[134:135]
	s_nop 0
	v_pk_fma_f32 v[134:135], v[58:59], v[72:73], v[86:87] op_sel_hi:[0,1,1]
	v_pk_mul_f32 v[72:73], v[56:57], v[10:11] op_sel_hi:[0,1]
	v_exp_f32_e32 v72, v72
	v_exp_f32_e32 v73, v73
	v_pk_mul_f32 v[86:87], v[56:57], v[12:13] op_sel_hi:[0,1]
	v_exp_f32_e32 v86, v86
	v_exp_f32_e32 v87, v87
	v_pk_mul_f32 v[72:73], v[72:73], v[136:137]
	v_pk_fma_f32 v[70:71], v[88:89], v[134:135], v[70:71]
	v_pk_fma_f32 v[136:137], v[58:59], v[74:75], v[72:73] op_sel_hi:[0,1,1]
	v_pk_mul_f32 v[72:73], v[86:87], v[138:139]
	v_pk_mul_f32 v[74:75], v[56:57], v[8:9] op_sel_hi:[0,1]
	v_pk_fma_f32 v[138:139], v[58:59], v[76:77], v[72:73] op_sel_hi:[0,1,1]
	v_pk_mul_f32 v[72:73], v[56:57], v[6:7] op_sel_hi:[0,1]
	v_exp_f32_e32 v72, v72
	v_exp_f32_e32 v73, v73
	v_exp_f32_e32 v74, v74
	v_exp_f32_e32 v75, v75
	s_waitcnt lgkmcnt(11)
	v_pk_fma_f32 v[70:71], v[90:91], v[136:137], v[70:71]
	v_pk_mul_f32 v[72:73], v[72:73], v[140:141]
	v_pk_fma_f32 v[70:71], v[92:93], v[138:139], v[70:71]
	v_pk_fma_f32 v[140:141], v[58:59], v[78:79], v[72:73] op_sel_hi:[0,1,1]
	v_pk_mul_f32 v[72:73], v[74:75], v[142:143]
	v_pk_mul_f32 v[74:75], v[56:57], v[4:5] op_sel_hi:[0,1]
	v_pk_fma_f32 v[142:143], v[58:59], v[80:81], v[72:73] op_sel_hi:[0,1,1]
	v_pk_mul_f32 v[72:73], v[56:57], v[2:3] op_sel_hi:[0,1]
	v_exp_f32_e32 v72, v72
	v_exp_f32_e32 v73, v73
	v_exp_f32_e32 v74, v74
	v_exp_f32_e32 v75, v75
	s_waitcnt lgkmcnt(10)
	v_pk_fma_f32 v[70:71], v[94:95], v[140:141], v[70:71]
	v_pk_mul_f32 v[72:73], v[72:73], v[144:145]
	v_pk_fma_f32 v[70:71], v[96:97], v[142:143], v[70:71]
	v_pk_fma_f32 v[144:145], v[58:59], v[82:83], v[72:73] op_sel_hi:[0,1,1]
	v_pk_mul_f32 v[54:55], v[74:75], v[54:55]
	s_waitcnt lgkmcnt(9)
	v_pk_fma_f32 v[70:71], v[98:99], v[144:145], v[70:71]
	v_pk_fma_f32 v[54:55], v[58:59], v[84:85], v[54:55] op_sel_hi:[0,1,1]
	v_pk_fma_f32 v[58:59], v[100:101], v[54:55], v[70:71]
	s_nop 0
	v_add_f32_e32 v56, v58, v59
	v_fma_mix_f32 v56, v1, v57, v56 op_sel_hi:[0,1,0]
	v_fma_mixlo_f16 v56, v56, v61, 0 op_sel_hi:[0,1,0]
	ds_write_b16 v68, v56 offset:10336
	ds_read_b128 v[70:73], v67 offset:1024
	ds_read_b128 v[74:77], v67 offset:1040
	ds_read_b128 v[78:81], v67 offset:1056
	ds_read_b128 v[82:85], v67 offset:1072
	ds_read_b128 v[86:89], v67 offset:1088
	ds_read_b128 v[90:93], v67 offset:1104
	ds_read_b128 v[94:97], v67 offset:1120
	ds_read_b128 v[98:101], v67 offset:1136
	v_cvt_f32_f16_sdwa v56, v65 dst_sel:DWORD dst_unused:UNUSED_PAD src0_sel:WORD_1
	v_cvt_f32_f16_sdwa v58, v57 dst_sel:DWORD dst_unused:UNUSED_PAD src0_sel:WORD_1
	v_pk_mul_f32 v[64:65], v[56:57], v[14:15] op_sel_hi:[0,1]
	v_pk_mul_f32 v[146:147], v[56:57], v[16:17] op_sel_hi:[0,1]
	v_exp_f32_e32 v64, v64
	v_exp_f32_e32 v65, v65
	v_exp_f32_e32 v146, v146
	v_exp_f32_e32 v147, v147
	v_mul_f32_e32 v58, v56, v58
	v_pk_mul_f32 v[62:63], v[64:65], v[62:63]
	v_pk_mul_f32 v[64:65], v[146:147], v[134:135]
	s_waitcnt lgkmcnt(14)
	v_pk_fma_f32 v[134:135], v[58:59], v[104:105], v[64:65] op_sel_hi:[0,1,1]
	v_pk_mul_f32 v[64:65], v[56:57], v[10:11] op_sel_hi:[0,1]
	v_pk_fma_f32 v[148:149], v[58:59], v[102:103], v[62:63] op_sel_hi:[0,1,1]
	v_exp_f32_e32 v64, v64
	v_exp_f32_e32 v65, v65
	v_pk_mul_f32 v[102:103], v[56:57], v[12:13] op_sel_hi:[0,1]
	v_exp_f32_e32 v102, v102
	v_exp_f32_e32 v103, v103
	s_waitcnt lgkmcnt(12)
	v_pk_fma_f32 v[62:63], v[118:119], v[148:149], 0 op_sel_hi:[1,1,0]
	v_pk_mul_f32 v[64:65], v[64:65], v[136:137]
	v_pk_fma_f32 v[62:63], v[120:121], v[134:135], v[62:63]
	v_pk_fma_f32 v[136:137], v[58:59], v[106:107], v[64:65] op_sel_hi:[0,1,1]
	v_pk_mul_f32 v[64:65], v[102:103], v[138:139]
	s_waitcnt lgkmcnt(11)
	v_pk_fma_f32 v[62:63], v[122:123], v[136:137], v[62:63]
	v_pk_fma_f32 v[122:123], v[58:59], v[108:109], v[64:65] op_sel_hi:[0,1,1]
	v_pk_mul_f32 v[64:65], v[56:57], v[6:7] op_sel_hi:[0,1]
	v_exp_f32_e32 v64, v64
	v_exp_f32_e32 v65, v65
	v_pk_mul_f32 v[102:103], v[56:57], v[8:9] op_sel_hi:[0,1]
	v_exp_f32_e32 v102, v102
	v_exp_f32_e32 v103, v103
	v_pk_mul_f32 v[64:65], v[64:65], v[140:141]
	v_pk_fma_f32 v[62:63], v[124:125], v[122:123], v[62:63]
	v_pk_fma_f32 v[124:125], v[58:59], v[110:111], v[64:65] op_sel_hi:[0,1,1]
	v_pk_mul_f32 v[64:65], v[102:103], v[142:143]
	s_waitcnt lgkmcnt(10)
	v_pk_fma_f32 v[62:63], v[126:127], v[124:125], v[62:63]
	v_pk_fma_f32 v[126:127], v[58:59], v[112:113], v[64:65] op_sel_hi:[0,1,1]
	v_pk_mul_f32 v[64:65], v[56:57], v[2:3] op_sel_hi:[0,1]
	v_exp_f32_e32 v64, v64
	v_exp_f32_e32 v65, v65
	v_pk_mul_f32 v[102:103], v[56:57], v[4:5] op_sel_hi:[0,1]
	v_exp_f32_e32 v102, v102
	v_exp_f32_e32 v103, v103
	v_pk_mul_f32 v[64:65], v[64:65], v[144:145]
	v_pk_fma_f32 v[62:63], v[128:129], v[126:127], v[62:63]
	v_pk_fma_f32 v[128:129], v[58:59], v[114:115], v[64:65] op_sel_hi:[0,1,1]
	v_pk_mul_f32 v[54:55], v[102:103], v[54:55]
	s_waitcnt lgkmcnt(9)
	v_pk_fma_f32 v[62:63], v[130:131], v[128:129], v[62:63]
	v_pk_fma_f32 v[130:131], v[58:59], v[116:117], v[54:55] op_sel_hi:[0,1,1]
	v_pk_fma_f32 v[54:55], v[132:133], v[130:131], v[62:63]
	s_nop 0
	v_add_f32_e32 v54, v54, v55
	v_fma_mix_f32 v54, v1, v57, v54 op_sel:[0,1,0] op_sel_hi:[0,1,0]
	v_fma_mixlo_f16 v54, v54, v61, 0 op_sel:[0,1,0] op_sel_hi:[0,1,0]
	ds_write_b16 v68, v54 offset:11376
	ds_read_b128 v[54:57], v67 offset:1152
	ds_read_b128 v[58:61], v67 offset:1168
	ds_read_b128 v[62:65], v67 offset:1184
	ds_read_b128 v[102:105], v67 offset:1200
	ds_read_b128 v[106:109], v67 offset:1216
	ds_read_b128 v[110:113], v67 offset:1232
	ds_read_b128 v[114:117], v67 offset:1248
	ds_read_b128 v[118:121], v67 offset:1264
	s_waitcnt vmcnt(8)
	v_cvt_f32_f16_e32 v132, v50
	s_waitcnt vmcnt(7)
	v_cvt_f32_f16_e32 v69, v42
	v_pk_mul_f32 v[140:141], v[132:133], v[14:15] op_sel_hi:[0,1]
	v_exp_f32_e32 v140, v140
	v_exp_f32_e32 v141, v141
	v_pk_mul_f32 v[142:143], v[132:133], v[16:17] op_sel_hi:[0,1]
	v_exp_f32_e32 v142, v142
	v_exp_f32_e32 v143, v143
	v_mul_f32_e32 v138, v132, v69
	v_pk_mul_f32 v[140:141], v[140:141], v[148:149]
	s_waitcnt lgkmcnt(14)
	v_pk_fma_f32 v[140:141], v[138:139], v[70:71], v[140:141] op_sel_hi:[0,1,1]
	s_waitcnt lgkmcnt(12)
	v_pk_fma_f32 v[70:71], v[86:87], v[140:141], 0 op_sel_hi:[1,1,0]
	v_pk_mul_f32 v[86:87], v[142:143], v[134:135]
	s_nop 0
	v_pk_fma_f32 v[134:135], v[138:139], v[72:73], v[86:87] op_sel_hi:[0,1,1]
	v_pk_mul_f32 v[72:73], v[132:133], v[10:11] op_sel_hi:[0,1]
	v_exp_f32_e32 v72, v72
	v_exp_f32_e32 v73, v73
	v_pk_mul_f32 v[86:87], v[132:133], v[12:13] op_sel_hi:[0,1]
	v_exp_f32_e32 v86, v86
	v_exp_f32_e32 v87, v87
	v_pk_mul_f32 v[72:73], v[72:73], v[136:137]
	v_pk_fma_f32 v[70:71], v[88:89], v[134:135], v[70:71]
	v_pk_fma_f32 v[136:137], v[138:139], v[74:75], v[72:73] op_sel_hi:[0,1,1]
	v_pk_mul_f32 v[72:73], v[86:87], v[122:123]
	v_pk_mul_f32 v[74:75], v[132:133], v[8:9] op_sel_hi:[0,1]
	v_pk_fma_f32 v[122:123], v[138:139], v[76:77], v[72:73] op_sel_hi:[0,1,1]
	v_pk_mul_f32 v[72:73], v[132:133], v[6:7] op_sel_hi:[0,1]
	v_exp_f32_e32 v72, v72
	v_exp_f32_e32 v73, v73
	v_exp_f32_e32 v74, v74
	v_exp_f32_e32 v75, v75
	s_waitcnt lgkmcnt(11)
	v_pk_fma_f32 v[70:71], v[90:91], v[136:137], v[70:71]
	v_pk_mul_f32 v[72:73], v[72:73], v[124:125]
	v_pk_fma_f32 v[70:71], v[92:93], v[122:123], v[70:71]
	v_pk_fma_f32 v[124:125], v[138:139], v[78:79], v[72:73] op_sel_hi:[0,1,1]
	v_pk_mul_f32 v[72:73], v[74:75], v[126:127]
	v_pk_mul_f32 v[74:75], v[132:133], v[4:5] op_sel_hi:[0,1]
	v_pk_fma_f32 v[126:127], v[138:139], v[80:81], v[72:73] op_sel_hi:[0,1,1]
	v_pk_mul_f32 v[72:73], v[132:133], v[2:3] op_sel_hi:[0,1]
	v_exp_f32_e32 v72, v72
	v_exp_f32_e32 v73, v73
	v_exp_f32_e32 v74, v74
	v_exp_f32_e32 v75, v75
	s_waitcnt lgkmcnt(10)
	v_pk_fma_f32 v[70:71], v[94:95], v[124:125], v[70:71]
	v_pk_mul_f32 v[72:73], v[72:73], v[128:129]
	v_pk_fma_f32 v[70:71], v[96:97], v[126:127], v[70:71]
	v_pk_fma_f32 v[128:129], v[138:139], v[82:83], v[72:73] op_sel_hi:[0,1,1]
	v_pk_mul_f32 v[72:73], v[74:75], v[130:131]
	s_waitcnt lgkmcnt(9)
	v_pk_fma_f32 v[70:71], v[98:99], v[128:129], v[70:71]
	v_pk_fma_f32 v[130:131], v[138:139], v[84:85], v[72:73] op_sel_hi:[0,1,1]
	v_pk_fma_f32 v[70:71], v[100:101], v[130:131], v[70:71]
	s_nop 0
	v_add_f32_e32 v69, v70, v71
	v_fma_mix_f32 v69, v1, v42, v69 op_sel_hi:[0,1,0]
	s_waitcnt vmcnt(6)
	v_fma_mixlo_f16 v69, v69, v46, 0 op_sel_hi:[0,1,0]
	ds_write_b16 v68, v69 offset:12416
	ds_read_b128 v[70:73], v67 offset:1280
	ds_read_b128 v[74:77], v67 offset:1296
	ds_read_b128 v[78:81], v67 offset:1312
	ds_read_b128 v[82:85], v67 offset:1328
	ds_read_b128 v[86:89], v67 offset:1344
	ds_read_b128 v[90:93], v67 offset:1360
	ds_read_b128 v[94:97], v67 offset:1376
	ds_read_b128 v[98:101], v67 offset:1392
	v_cvt_f32_f16_sdwa v50, v50 dst_sel:DWORD dst_unused:UNUSED_PAD src0_sel:WORD_1
	v_cvt_f32_f16_sdwa v69, v42 dst_sel:DWORD dst_unused:UNUSED_PAD src0_sel:WORD_1
	v_pk_mul_f32 v[138:139], v[50:51], v[14:15] op_sel_hi:[0,1]
	v_exp_f32_e32 v138, v138
	v_exp_f32_e32 v139, v139
	v_pk_mul_f32 v[142:143], v[50:51], v[16:17] op_sel_hi:[0,1]
	v_exp_f32_e32 v142, v142
	v_exp_f32_e32 v143, v143
	v_mul_f32_e32 v132, v50, v69
	v_pk_mul_f32 v[138:139], v[138:139], v[140:141]
	s_waitcnt lgkmcnt(14)
	v_pk_fma_f32 v[138:139], v[132:133], v[54:55], v[138:139] op_sel_hi:[0,1,1]
	s_waitcnt lgkmcnt(12)
	v_pk_fma_f32 v[54:55], v[106:107], v[138:139], 0 op_sel_hi:[1,1,0]
	v_pk_mul_f32 v[106:107], v[142:143], v[134:135]
	s_nop 0
	v_pk_fma_f32 v[134:135], v[132:133], v[56:57], v[106:107] op_sel_hi:[0,1,1]
	v_pk_mul_f32 v[56:57], v[50:51], v[10:11] op_sel_hi:[0,1]
	v_exp_f32_e32 v56, v56
	v_exp_f32_e32 v57, v57
	v_pk_mul_f32 v[106:107], v[50:51], v[12:13] op_sel_hi:[0,1]
	v_exp_f32_e32 v106, v106
	v_exp_f32_e32 v107, v107
	v_pk_mul_f32 v[56:57], v[56:57], v[136:137]
	v_pk_fma_f32 v[54:55], v[108:109], v[134:135], v[54:55]
	v_pk_fma_f32 v[136:137], v[132:133], v[58:59], v[56:57] op_sel_hi:[0,1,1]
	v_pk_mul_f32 v[56:57], v[106:107], v[122:123]
	v_pk_mul_f32 v[58:59], v[50:51], v[8:9] op_sel_hi:[0,1]
	v_pk_fma_f32 v[122:123], v[132:133], v[60:61], v[56:57] op_sel_hi:[0,1,1]
	v_pk_mul_f32 v[56:57], v[50:51], v[6:7] op_sel_hi:[0,1]
	v_exp_f32_e32 v56, v56
	v_exp_f32_e32 v57, v57
	v_exp_f32_e32 v58, v58
	v_exp_f32_e32 v59, v59
	s_waitcnt lgkmcnt(11)
	v_pk_fma_f32 v[54:55], v[110:111], v[136:137], v[54:55]
	v_pk_mul_f32 v[56:57], v[56:57], v[124:125]
	v_pk_fma_f32 v[54:55], v[112:113], v[122:123], v[54:55]
	v_pk_fma_f32 v[124:125], v[132:133], v[62:63], v[56:57] op_sel_hi:[0,1,1]
	v_pk_mul_f32 v[56:57], v[58:59], v[126:127]
	v_pk_mul_f32 v[58:59], v[50:51], v[4:5] op_sel_hi:[0,1]
	v_pk_fma_f32 v[126:127], v[132:133], v[64:65], v[56:57] op_sel_hi:[0,1,1]
	v_pk_mul_f32 v[56:57], v[50:51], v[2:3] op_sel_hi:[0,1]
	v_exp_f32_e32 v56, v56
	v_exp_f32_e32 v57, v57
	v_exp_f32_e32 v58, v58
	v_exp_f32_e32 v59, v59
	s_waitcnt lgkmcnt(10)
	v_pk_fma_f32 v[54:55], v[114:115], v[124:125], v[54:55]
	v_pk_mul_f32 v[56:57], v[56:57], v[128:129]
	v_pk_fma_f32 v[54:55], v[116:117], v[126:127], v[54:55]
	v_pk_fma_f32 v[128:129], v[132:133], v[102:103], v[56:57] op_sel_hi:[0,1,1]
	v_pk_mul_f32 v[56:57], v[58:59], v[130:131]
	s_waitcnt lgkmcnt(9)
	v_pk_fma_f32 v[54:55], v[118:119], v[128:129], v[54:55]
	v_pk_fma_f32 v[130:131], v[132:133], v[104:105], v[56:57] op_sel_hi:[0,1,1]
	v_pk_fma_f32 v[54:55], v[120:121], v[130:131], v[54:55]
	s_nop 0
	v_add_f32_e32 v50, v54, v55
	v_fma_mix_f32 v42, v1, v42, v50 op_sel:[0,1,0] op_sel_hi:[0,1,0]
	v_fma_mixlo_f16 v42, v42, v46, 0 op_sel:[0,1,0] op_sel_hi:[0,1,0]
	ds_write_b16 v68, v42 offset:13456
	ds_read_b128 v[54:57], v67 offset:1408
	ds_read_b128 v[58:61], v67 offset:1424
	ds_read_b128 v[62:65], v67 offset:1440
	ds_read_b128 v[102:105], v67 offset:1456
	ds_read_b128 v[106:109], v67 offset:1472
	ds_read_b128 v[110:113], v67 offset:1488
	ds_read_b128 v[114:117], v67 offset:1504
	ds_read_b128 v[118:121], v67 offset:1520
	v_cvt_f32_f16_e32 v42, v51
	v_cvt_f32_f16_e32 v46, v43
	v_pk_mul_f32 v[132:133], v[42:43], v[14:15] op_sel_hi:[0,1]
	v_exp_f32_e32 v132, v132
	v_exp_f32_e32 v133, v133
	v_pk_mul_f32 v[140:141], v[42:43], v[16:17] op_sel_hi:[0,1]
	v_exp_f32_e32 v140, v140
	v_exp_f32_e32 v141, v141
	v_mul_f32_e32 v46, v42, v46
	v_pk_mul_f32 v[132:133], v[132:133], v[138:139]
	s_waitcnt lgkmcnt(14)
	v_pk_fma_f32 v[132:133], v[46:47], v[70:71], v[132:133] op_sel_hi:[0,1,1]
	s_waitcnt lgkmcnt(12)
	v_pk_fma_f32 v[70:71], v[86:87], v[132:133], 0 op_sel_hi:[1,1,0]
	v_pk_mul_f32 v[86:87], v[140:141], v[134:135]
	s_nop 0
	v_pk_fma_f32 v[134:135], v[46:47], v[72:73], v[86:87] op_sel_hi:[0,1,1]
	v_pk_mul_f32 v[72:73], v[42:43], v[10:11] op_sel_hi:[0,1]
	v_exp_f32_e32 v72, v72
	v_exp_f32_e32 v73, v73
	v_pk_mul_f32 v[86:87], v[42:43], v[12:13] op_sel_hi:[0,1]
	v_exp_f32_e32 v86, v86
	v_exp_f32_e32 v87, v87
	v_pk_mul_f32 v[72:73], v[72:73], v[136:137]
	v_pk_fma_f32 v[70:71], v[88:89], v[134:135], v[70:71]
	v_pk_fma_f32 v[136:137], v[46:47], v[74:75], v[72:73] op_sel_hi:[0,1,1]
	v_pk_mul_f32 v[72:73], v[86:87], v[122:123]
	v_pk_mul_f32 v[74:75], v[42:43], v[8:9] op_sel_hi:[0,1]
	v_pk_fma_f32 v[122:123], v[46:47], v[76:77], v[72:73] op_sel_hi:[0,1,1]
	v_pk_mul_f32 v[72:73], v[42:43], v[6:7] op_sel_hi:[0,1]
	v_exp_f32_e32 v72, v72
	v_exp_f32_e32 v73, v73
	v_exp_f32_e32 v74, v74
	v_exp_f32_e32 v75, v75
	s_waitcnt lgkmcnt(11)
	v_pk_fma_f32 v[70:71], v[90:91], v[136:137], v[70:71]
	v_pk_mul_f32 v[72:73], v[72:73], v[124:125]
	v_pk_fma_f32 v[70:71], v[92:93], v[122:123], v[70:71]
	v_pk_fma_f32 v[124:125], v[46:47], v[78:79], v[72:73] op_sel_hi:[0,1,1]
	v_pk_mul_f32 v[72:73], v[74:75], v[126:127]
	v_pk_mul_f32 v[74:75], v[42:43], v[4:5] op_sel_hi:[0,1]
	v_pk_fma_f32 v[126:127], v[46:47], v[80:81], v[72:73] op_sel_hi:[0,1,1]
	v_pk_mul_f32 v[72:73], v[42:43], v[2:3] op_sel_hi:[0,1]
	v_exp_f32_e32 v72, v72
	v_exp_f32_e32 v73, v73
	v_exp_f32_e32 v74, v74
	v_exp_f32_e32 v75, v75
	s_waitcnt lgkmcnt(10)
	v_pk_fma_f32 v[70:71], v[94:95], v[124:125], v[70:71]
	v_pk_mul_f32 v[72:73], v[72:73], v[128:129]
	v_pk_fma_f32 v[70:71], v[96:97], v[126:127], v[70:71]
	v_pk_fma_f32 v[128:129], v[46:47], v[82:83], v[72:73] op_sel_hi:[0,1,1]
	v_pk_mul_f32 v[72:73], v[74:75], v[130:131]
	s_waitcnt lgkmcnt(9)
	v_pk_fma_f32 v[70:71], v[98:99], v[128:129], v[70:71]
	v_pk_fma_f32 v[130:131], v[46:47], v[84:85], v[72:73] op_sel_hi:[0,1,1]
	v_pk_fma_f32 v[70:71], v[100:101], v[130:131], v[70:71]
	s_nop 0
	v_add_f32_e32 v42, v70, v71
	v_fma_mix_f32 v42, v1, v43, v42 op_sel_hi:[0,1,0]
	v_fma_mixlo_f16 v42, v42, v47, 0 op_sel_hi:[0,1,0]
	ds_write_b16 v68, v42 offset:14496
	ds_read_b128 v[70:73], v67 offset:1536
	ds_read_b128 v[74:77], v67 offset:1552
	ds_read_b128 v[78:81], v67 offset:1568
	ds_read_b128 v[82:85], v67 offset:1584
	ds_read_b128 v[86:89], v67 offset:1600
	ds_read_b128 v[90:93], v67 offset:1616
	ds_read_b128 v[94:97], v67 offset:1632
	ds_read_b128 v[98:101], v67 offset:1648
	v_cvt_f32_f16_sdwa v42, v51 dst_sel:DWORD dst_unused:UNUSED_PAD src0_sel:WORD_1
	v_cvt_f32_f16_sdwa v46, v43 dst_sel:DWORD dst_unused:UNUSED_PAD src0_sel:WORD_1
	v_pk_mul_f32 v[50:51], v[42:43], v[14:15] op_sel_hi:[0,1]
	v_exp_f32_e32 v50, v50
	v_exp_f32_e32 v51, v51
	v_pk_mul_f32 v[138:139], v[42:43], v[16:17] op_sel_hi:[0,1]
	v_exp_f32_e32 v138, v138
	v_exp_f32_e32 v139, v139
	v_mul_f32_e32 v46, v42, v46
	v_pk_mul_f32 v[50:51], v[50:51], v[132:133]
	s_waitcnt lgkmcnt(14)
	v_pk_fma_f32 v[50:51], v[46:47], v[54:55], v[50:51] op_sel_hi:[0,1,1]
	s_waitcnt lgkmcnt(12)
	v_pk_fma_f32 v[54:55], v[106:107], v[50:51], 0 op_sel_hi:[1,1,0]
	v_pk_mul_f32 v[106:107], v[138:139], v[134:135]
	s_nop 0
	v_pk_fma_f32 v[132:133], v[46:47], v[56:57], v[106:107] op_sel_hi:[0,1,1]
	v_pk_mul_f32 v[56:57], v[42:43], v[10:11] op_sel_hi:[0,1]
	v_exp_f32_e32 v56, v56
	v_exp_f32_e32 v57, v57
	v_pk_mul_f32 v[106:107], v[42:43], v[12:13] op_sel_hi:[0,1]
	v_exp_f32_e32 v106, v106
	v_exp_f32_e32 v107, v107
	v_pk_mul_f32 v[56:57], v[56:57], v[136:137]
	v_pk_fma_f32 v[54:55], v[108:109], v[132:133], v[54:55]
	v_pk_fma_f32 v[134:135], v[46:47], v[58:59], v[56:57] op_sel_hi:[0,1,1]
	v_pk_mul_f32 v[56:57], v[106:107], v[122:123]
	v_pk_mul_f32 v[58:59], v[42:43], v[8:9] op_sel_hi:[0,1]
	v_pk_fma_f32 v[122:123], v[46:47], v[60:61], v[56:57] op_sel_hi:[0,1,1]
	v_pk_mul_f32 v[56:57], v[42:43], v[6:7] op_sel_hi:[0,1]
	v_exp_f32_e32 v56, v56
	v_exp_f32_e32 v57, v57
	v_exp_f32_e32 v58, v58
	v_exp_f32_e32 v59, v59
	s_waitcnt lgkmcnt(11)
	v_pk_fma_f32 v[54:55], v[110:111], v[134:135], v[54:55]
	v_pk_mul_f32 v[56:57], v[56:57], v[124:125]
	v_pk_fma_f32 v[54:55], v[112:113], v[122:123], v[54:55]
	v_pk_fma_f32 v[124:125], v[46:47], v[62:63], v[56:57] op_sel_hi:[0,1,1]
	v_pk_mul_f32 v[56:57], v[58:59], v[126:127]
	v_pk_mul_f32 v[58:59], v[42:43], v[4:5] op_sel_hi:[0,1]
	v_pk_fma_f32 v[126:127], v[46:47], v[64:65], v[56:57] op_sel_hi:[0,1,1]
	v_pk_mul_f32 v[56:57], v[42:43], v[2:3] op_sel_hi:[0,1]
	v_exp_f32_e32 v56, v56
	v_exp_f32_e32 v57, v57
	v_exp_f32_e32 v58, v58
	v_exp_f32_e32 v59, v59
	s_waitcnt lgkmcnt(10)
	v_pk_fma_f32 v[54:55], v[114:115], v[124:125], v[54:55]
	v_pk_mul_f32 v[56:57], v[56:57], v[128:129]
	v_pk_fma_f32 v[54:55], v[116:117], v[126:127], v[54:55]
	v_pk_fma_f32 v[128:129], v[46:47], v[102:103], v[56:57] op_sel_hi:[0,1,1]
	v_pk_mul_f32 v[56:57], v[58:59], v[130:131]
	s_waitcnt lgkmcnt(9)
	v_pk_fma_f32 v[54:55], v[118:119], v[128:129], v[54:55]
	v_pk_fma_f32 v[130:131], v[46:47], v[104:105], v[56:57] op_sel_hi:[0,1,1]
	v_pk_fma_f32 v[54:55], v[120:121], v[130:131], v[54:55]
	s_nop 0
	v_add_f32_e32 v42, v54, v55
	v_fma_mix_f32 v42, v1, v43, v42 op_sel:[0,1,0] op_sel_hi:[0,1,0]
	v_fma_mixlo_f16 v42, v42, v47, 0 op_sel:[0,1,0] op_sel_hi:[0,1,0]
	ds_write_b16 v68, v42 offset:15536
	ds_read_b128 v[54:57], v67 offset:1664
	ds_read_b128 v[58:61], v67 offset:1680
	ds_read_b128 v[62:65], v67 offset:1696
	ds_read_b128 v[102:105], v67 offset:1712
	ds_read_b128 v[106:109], v67 offset:1728
	ds_read_b128 v[110:113], v67 offset:1744
	ds_read_b128 v[114:117], v67 offset:1760
	ds_read_b128 v[118:121], v67 offset:1776
	v_cvt_f32_f16_e32 v42, v52
	v_cvt_f32_f16_e32 v43, v44
	v_pk_mul_f32 v[136:137], v[42:43], v[14:15] op_sel_hi:[0,1]
	v_exp_f32_e32 v136, v136
	v_exp_f32_e32 v137, v137
	v_pk_mul_f32 v[138:139], v[42:43], v[16:17] op_sel_hi:[0,1]
	v_exp_f32_e32 v138, v138
	v_exp_f32_e32 v139, v139
	v_mul_f32_e32 v46, v42, v43
	v_pk_mul_f32 v[50:51], v[136:137], v[50:51]
	s_waitcnt lgkmcnt(14)
	v_pk_fma_f32 v[50:51], v[46:47], v[70:71], v[50:51] op_sel_hi:[0,1,1]
	s_waitcnt lgkmcnt(12)
	v_pk_fma_f32 v[70:71], v[86:87], v[50:51], 0 op_sel_hi:[1,1,0]
	v_pk_mul_f32 v[86:87], v[138:139], v[132:133]
	s_nop 0
	v_pk_fma_f32 v[132:133], v[46:47], v[72:73], v[86:87] op_sel_hi:[0,1,1]
	v_pk_mul_f32 v[72:73], v[42:43], v[10:11] op_sel_hi:[0,1]
	v_exp_f32_e32 v72, v72
	v_exp_f32_e32 v73, v73
	v_pk_mul_f32 v[86:87], v[42:43], v[12:13] op_sel_hi:[0,1]
	v_exp_f32_e32 v86, v86
	v_exp_f32_e32 v87, v87
	v_pk_mul_f32 v[72:73], v[72:73], v[134:135]
	v_pk_fma_f32 v[70:71], v[88:89], v[132:133], v[70:71]
	v_pk_fma_f32 v[134:135], v[46:47], v[74:75], v[72:73] op_sel_hi:[0,1,1]
	v_pk_mul_f32 v[72:73], v[86:87], v[122:123]
	v_pk_mul_f32 v[74:75], v[42:43], v[8:9] op_sel_hi:[0,1]
	v_pk_fma_f32 v[122:123], v[46:47], v[76:77], v[72:73] op_sel_hi:[0,1,1]
	v_pk_mul_f32 v[72:73], v[42:43], v[6:7] op_sel_hi:[0,1]
	v_exp_f32_e32 v72, v72
	v_exp_f32_e32 v73, v73
	v_exp_f32_e32 v74, v74
	v_exp_f32_e32 v75, v75
	s_waitcnt lgkmcnt(11)
	v_pk_fma_f32 v[70:71], v[90:91], v[134:135], v[70:71]
	v_pk_mul_f32 v[72:73], v[72:73], v[124:125]
	v_pk_fma_f32 v[70:71], v[92:93], v[122:123], v[70:71]
	v_pk_fma_f32 v[124:125], v[46:47], v[78:79], v[72:73] op_sel_hi:[0,1,1]
	v_pk_mul_f32 v[72:73], v[74:75], v[126:127]
	s_waitcnt lgkmcnt(10)
	v_pk_fma_f32 v[70:71], v[94:95], v[124:125], v[70:71]
	v_pk_fma_f32 v[126:127], v[46:47], v[80:81], v[72:73] op_sel_hi:[0,1,1]
	v_pk_mul_f32 v[72:73], v[42:43], v[2:3] op_sel_hi:[0,1]
	v_exp_f32_e32 v72, v72
	v_exp_f32_e32 v73, v73
	v_pk_mul_f32 v[42:43], v[42:43], v[4:5] op_sel_hi:[0,1]
	v_exp_f32_e32 v42, v42
	v_exp_f32_e32 v43, v43
	v_pk_mul_f32 v[72:73], v[72:73], v[128:129]
	v_pk_fma_f32 v[70:71], v[96:97], v[126:127], v[70:71]
	v_pk_fma_f32 v[128:129], v[46:47], v[82:83], v[72:73] op_sel_hi:[0,1,1]
	v_pk_mul_f32 v[42:43], v[42:43], v[130:131]
	s_waitcnt lgkmcnt(9)
	v_pk_fma_f32 v[70:71], v[98:99], v[128:129], v[70:71]
	v_pk_fma_f32 v[42:43], v[46:47], v[84:85], v[42:43] op_sel_hi:[0,1,1]
	v_pk_fma_f32 v[46:47], v[100:101], v[42:43], v[70:71]
	s_nop 0
	v_add_f32_e32 v46, v46, v47
	v_fma_mix_f32 v46, v1, v44, v46 op_sel_hi:[0,1,0]
	v_fma_mixlo_f16 v46, v46, v48, 0 op_sel_hi:[0,1,0]
	ds_write_b16 v68, v46 offset:16576
	ds_read_b128 v[70:73], v67 offset:1792
	ds_read_b128 v[74:77], v67 offset:1808
	ds_read_b128 v[78:81], v67 offset:1824
	ds_read_b128 v[82:85], v67 offset:1840
	ds_read_b128 v[86:89], v67 offset:1856
	ds_read_b128 v[90:93], v67 offset:1872
	ds_read_b128 v[94:97], v67 offset:1888
	ds_read_b128 v[98:101], v67 offset:1904
	v_cvt_f32_f16_sdwa v46, v52 dst_sel:DWORD dst_unused:UNUSED_PAD src0_sel:WORD_1
	v_cvt_f32_f16_sdwa v47, v44 dst_sel:DWORD dst_unused:UNUSED_PAD src0_sel:WORD_1
	v_pk_mul_f32 v[130:131], v[46:47], v[14:15] op_sel_hi:[0,1]
	v_exp_f32_e32 v130, v130
	v_exp_f32_e32 v131, v131
	v_pk_mul_f32 v[136:137], v[46:47], v[16:17] op_sel_hi:[0,1]
	v_exp_f32_e32 v136, v136
	v_exp_f32_e32 v137, v137
	v_mul_f32_e32 v52, v46, v47
	v_pk_mul_f32 v[50:51], v[130:131], v[50:51]
	s_waitcnt lgkmcnt(14)
	v_pk_fma_f32 v[50:51], v[52:53], v[54:55], v[50:51] op_sel_hi:[0,1,1]
	s_waitcnt lgkmcnt(12)
	v_pk_fma_f32 v[54:55], v[106:107], v[50:51], 0 op_sel_hi:[1,1,0]
	v_pk_mul_f32 v[106:107], v[136:137], v[132:133]
	s_nop 0
	v_pk_fma_f32 v[130:131], v[52:53], v[56:57], v[106:107] op_sel_hi:[0,1,1]
	v_pk_mul_f32 v[56:57], v[46:47], v[10:11] op_sel_hi:[0,1]
	v_exp_f32_e32 v56, v56
	v_exp_f32_e32 v57, v57
	v_pk_mul_f32 v[106:107], v[46:47], v[12:13] op_sel_hi:[0,1]
	v_exp_f32_e32 v106, v106
	v_exp_f32_e32 v107, v107
	v_pk_mul_f32 v[56:57], v[56:57], v[134:135]
	v_pk_fma_f32 v[54:55], v[108:109], v[130:131], v[54:55]
	v_pk_fma_f32 v[132:133], v[52:53], v[58:59], v[56:57] op_sel_hi:[0,1,1]
	v_pk_mul_f32 v[56:57], v[106:107], v[122:123]
	v_pk_mul_f32 v[58:59], v[46:47], v[8:9] op_sel_hi:[0,1]
	v_pk_fma_f32 v[122:123], v[52:53], v[60:61], v[56:57] op_sel_hi:[0,1,1]
	v_pk_mul_f32 v[56:57], v[46:47], v[6:7] op_sel_hi:[0,1]
	v_exp_f32_e32 v56, v56
	v_exp_f32_e32 v57, v57
	v_exp_f32_e32 v58, v58
	v_exp_f32_e32 v59, v59
	s_waitcnt lgkmcnt(11)
	v_pk_fma_f32 v[54:55], v[110:111], v[132:133], v[54:55]
	v_pk_mul_f32 v[56:57], v[56:57], v[124:125]
	v_pk_fma_f32 v[54:55], v[112:113], v[122:123], v[54:55]
	v_pk_fma_f32 v[124:125], v[52:53], v[62:63], v[56:57] op_sel_hi:[0,1,1]
	v_pk_mul_f32 v[56:57], v[58:59], v[126:127]
	s_waitcnt lgkmcnt(10)
	v_pk_fma_f32 v[54:55], v[114:115], v[124:125], v[54:55]
	v_pk_fma_f32 v[126:127], v[52:53], v[64:65], v[56:57] op_sel_hi:[0,1,1]
	v_pk_mul_f32 v[56:57], v[46:47], v[2:3] op_sel_hi:[0,1]
	v_exp_f32_e32 v56, v56
	v_exp_f32_e32 v57, v57
	v_pk_mul_f32 v[46:47], v[46:47], v[4:5] op_sel_hi:[0,1]
	v_exp_f32_e32 v46, v46
	v_exp_f32_e32 v47, v47
	v_pk_mul_f32 v[56:57], v[56:57], v[128:129]
	v_pk_fma_f32 v[54:55], v[116:117], v[126:127], v[54:55]
	v_pk_fma_f32 v[128:129], v[52:53], v[102:103], v[56:57] op_sel_hi:[0,1,1]
	v_pk_mul_f32 v[42:43], v[46:47], v[42:43]
	s_waitcnt lgkmcnt(9)
	v_pk_fma_f32 v[54:55], v[118:119], v[128:129], v[54:55]
	v_pk_fma_f32 v[42:43], v[52:53], v[104:105], v[42:43] op_sel_hi:[0,1,1]
	v_pk_fma_f32 v[46:47], v[120:121], v[42:43], v[54:55]
	s_nop 0
	v_add_f32_e32 v46, v46, v47
	v_fma_mix_f32 v44, v1, v44, v46 op_sel:[0,1,0] op_sel_hi:[0,1,0]
	v_fma_mixlo_f16 v44, v44, v48, 0 op_sel:[0,1,0] op_sel_hi:[0,1,0]
	ds_write_b16 v68, v44 offset:17616
	ds_read_b128 v[54:57], v67 offset:1920
	ds_read_b128 v[58:61], v67 offset:1936
	ds_read_b128 v[62:65], v67 offset:1952
	ds_read_b128 v[102:105], v67 offset:1968
	ds_read_b128 v[106:109], v67 offset:1984
	ds_read_b128 v[110:113], v67 offset:2000
	ds_read_b128 v[114:117], v67 offset:2016
	ds_read_b128 v[118:121], v67 offset:2032
	v_cvt_f32_f16_e32 v44, v53
	v_cvt_f32_f16_e32 v46, v45
	v_pk_mul_f32 v[134:135], v[44:45], v[14:15] op_sel_hi:[0,1]
	v_exp_f32_e32 v134, v134
	v_exp_f32_e32 v135, v135
	v_pk_mul_f32 v[136:137], v[44:45], v[16:17] op_sel_hi:[0,1]
	v_exp_f32_e32 v136, v136
	v_exp_f32_e32 v137, v137
	v_mul_f32_e32 v46, v44, v46
	v_pk_mul_f32 v[50:51], v[134:135], v[50:51]
	s_waitcnt lgkmcnt(14)
	v_pk_fma_f32 v[50:51], v[46:47], v[70:71], v[50:51] op_sel_hi:[0,1,1]
	s_waitcnt lgkmcnt(12)
	v_pk_fma_f32 v[70:71], v[86:87], v[50:51], 0 op_sel_hi:[1,1,0]
	v_pk_mul_f32 v[86:87], v[136:137], v[130:131]
	s_nop 0
	v_pk_fma_f32 v[130:131], v[46:47], v[72:73], v[86:87] op_sel_hi:[0,1,1]
	v_pk_mul_f32 v[72:73], v[44:45], v[10:11] op_sel_hi:[0,1]
	v_exp_f32_e32 v72, v72
	v_exp_f32_e32 v73, v73
	v_pk_mul_f32 v[86:87], v[44:45], v[12:13] op_sel_hi:[0,1]
	v_exp_f32_e32 v86, v86
	v_exp_f32_e32 v87, v87
	v_pk_mul_f32 v[72:73], v[72:73], v[132:133]
	v_pk_fma_f32 v[70:71], v[88:89], v[130:131], v[70:71]
	v_pk_fma_f32 v[132:133], v[46:47], v[74:75], v[72:73] op_sel_hi:[0,1,1]
	v_pk_mul_f32 v[72:73], v[86:87], v[122:123]
	v_pk_mul_f32 v[74:75], v[44:45], v[8:9] op_sel_hi:[0,1]
	v_pk_fma_f32 v[122:123], v[46:47], v[76:77], v[72:73] op_sel_hi:[0,1,1]
	v_pk_mul_f32 v[72:73], v[44:45], v[6:7] op_sel_hi:[0,1]
	v_exp_f32_e32 v72, v72
	v_exp_f32_e32 v73, v73
	v_exp_f32_e32 v74, v74
	v_exp_f32_e32 v75, v75
	s_waitcnt lgkmcnt(11)
	v_pk_fma_f32 v[70:71], v[90:91], v[132:133], v[70:71]
	v_pk_mul_f32 v[72:73], v[72:73], v[124:125]
	v_pk_fma_f32 v[70:71], v[92:93], v[122:123], v[70:71]
	v_pk_fma_f32 v[124:125], v[46:47], v[78:79], v[72:73] op_sel_hi:[0,1,1]
	v_pk_mul_f32 v[72:73], v[74:75], v[126:127]
	v_pk_mul_f32 v[74:75], v[44:45], v[4:5] op_sel_hi:[0,1]
	v_pk_fma_f32 v[126:127], v[46:47], v[80:81], v[72:73] op_sel_hi:[0,1,1]
	v_pk_mul_f32 v[72:73], v[44:45], v[2:3] op_sel_hi:[0,1]
	v_exp_f32_e32 v72, v72
	v_exp_f32_e32 v73, v73
	v_exp_f32_e32 v74, v74
	v_exp_f32_e32 v75, v75
	s_waitcnt lgkmcnt(10)
	v_pk_fma_f32 v[70:71], v[94:95], v[124:125], v[70:71]
	v_pk_mul_f32 v[72:73], v[72:73], v[128:129]
	v_pk_fma_f32 v[70:71], v[96:97], v[126:127], v[70:71]
	v_pk_fma_f32 v[128:129], v[46:47], v[82:83], v[72:73] op_sel_hi:[0,1,1]
	v_pk_mul_f32 v[42:43], v[74:75], v[42:43]
	s_waitcnt lgkmcnt(9)
	v_pk_fma_f32 v[70:71], v[98:99], v[128:129], v[70:71]
	v_pk_fma_f32 v[42:43], v[46:47], v[84:85], v[42:43] op_sel_hi:[0,1,1]
	v_pk_fma_f32 v[46:47], v[100:101], v[42:43], v[70:71]
	s_nop 0
	v_add_f32_e32 v44, v46, v47
	v_fma_mix_f32 v44, v1, v45, v44 op_sel_hi:[0,1,0]
	v_fma_mixlo_f16 v44, v44, v49, 0 op_sel_hi:[0,1,0]
	ds_write_b16 v68, v44 offset:18656
	ds_read_b128 v[70:73], v67 offset:2048
	ds_read_b128 v[74:77], v67 offset:2064
	ds_read_b128 v[78:81], v67 offset:2080
	ds_read_b128 v[82:85], v67 offset:2096
	ds_read_b128 v[86:89], v67 offset:2112
	ds_read_b128 v[90:93], v67 offset:2128
	ds_read_b128 v[94:97], v67 offset:2144
	ds_read_b128 v[98:101], v67 offset:2160
	v_cvt_f32_f16_sdwa v44, v53 dst_sel:DWORD dst_unused:UNUSED_PAD src0_sel:WORD_1
	v_cvt_f32_f16_sdwa v46, v45 dst_sel:DWORD dst_unused:UNUSED_PAD src0_sel:WORD_1
	v_pk_mul_f32 v[52:53], v[44:45], v[14:15] op_sel_hi:[0,1]
	v_pk_mul_f32 v[134:135], v[44:45], v[16:17] op_sel_hi:[0,1]
	v_exp_f32_e32 v52, v52
	v_exp_f32_e32 v53, v53
	v_exp_f32_e32 v134, v134
	v_exp_f32_e32 v135, v135
	v_mul_f32_e32 v46, v44, v46
	v_pk_mul_f32 v[50:51], v[52:53], v[50:51]
	v_pk_mul_f32 v[52:53], v[134:135], v[130:131]
	s_waitcnt lgkmcnt(14)
	v_pk_fma_f32 v[130:131], v[46:47], v[56:57], v[52:53] op_sel_hi:[0,1,1]
	v_pk_mul_f32 v[52:53], v[44:45], v[10:11] op_sel_hi:[0,1]
	v_pk_fma_f32 v[136:137], v[46:47], v[54:55], v[50:51] op_sel_hi:[0,1,1]
	v_exp_f32_e32 v52, v52
	v_exp_f32_e32 v53, v53
	v_pk_mul_f32 v[54:55], v[44:45], v[12:13] op_sel_hi:[0,1]
	v_exp_f32_e32 v54, v54
	v_exp_f32_e32 v55, v55
	s_waitcnt lgkmcnt(12)
	v_pk_fma_f32 v[50:51], v[106:107], v[136:137], 0 op_sel_hi:[1,1,0]
	v_pk_mul_f32 v[52:53], v[52:53], v[132:133]
	v_pk_fma_f32 v[50:51], v[108:109], v[130:131], v[50:51]
	v_pk_fma_f32 v[132:133], v[46:47], v[58:59], v[52:53] op_sel_hi:[0,1,1]
	v_pk_mul_f32 v[52:53], v[54:55], v[122:123]
	s_waitcnt lgkmcnt(11)
	v_pk_fma_f32 v[50:51], v[110:111], v[132:133], v[50:51]
	v_pk_fma_f32 v[110:111], v[46:47], v[60:61], v[52:53] op_sel_hi:[0,1,1]
	v_pk_mul_f32 v[52:53], v[44:45], v[6:7] op_sel_hi:[0,1]
	v_exp_f32_e32 v52, v52
	v_exp_f32_e32 v53, v53
	v_pk_mul_f32 v[54:55], v[44:45], v[8:9] op_sel_hi:[0,1]
	v_exp_f32_e32 v54, v54
	v_exp_f32_e32 v55, v55
	v_pk_mul_f32 v[52:53], v[52:53], v[124:125]
	v_pk_fma_f32 v[50:51], v[112:113], v[110:111], v[50:51]
	v_pk_fma_f32 v[112:113], v[46:47], v[62:63], v[52:53] op_sel_hi:[0,1,1]
	v_pk_mul_f32 v[52:53], v[54:55], v[126:127]
	s_waitcnt lgkmcnt(10)
	v_pk_fma_f32 v[50:51], v[114:115], v[112:113], v[50:51]
	v_pk_fma_f32 v[114:115], v[46:47], v[64:65], v[52:53] op_sel_hi:[0,1,1]
	v_pk_mul_f32 v[52:53], v[44:45], v[2:3] op_sel_hi:[0,1]
	v_exp_f32_e32 v52, v52
	v_exp_f32_e32 v53, v53
	v_pk_mul_f32 v[54:55], v[44:45], v[4:5] op_sel_hi:[0,1]
	v_exp_f32_e32 v54, v54
	v_exp_f32_e32 v55, v55
	v_pk_mul_f32 v[52:53], v[52:53], v[128:129]
	v_pk_fma_f32 v[50:51], v[116:117], v[114:115], v[50:51]
	v_pk_fma_f32 v[116:117], v[46:47], v[102:103], v[52:53] op_sel_hi:[0,1,1]
	v_pk_mul_f32 v[42:43], v[54:55], v[42:43]
	s_waitcnt lgkmcnt(9)
	v_pk_fma_f32 v[50:51], v[118:119], v[116:117], v[50:51]
	v_pk_fma_f32 v[118:119], v[46:47], v[104:105], v[42:43] op_sel_hi:[0,1,1]
	v_pk_fma_f32 v[42:43], v[120:121], v[118:119], v[50:51]
	s_nop 0
	v_add_f32_e32 v42, v42, v43
	v_fma_mix_f32 v42, v1, v45, v42 op_sel:[0,1,0] op_sel_hi:[0,1,0]
	v_fma_mixlo_f16 v42, v42, v49, 0 op_sel:[0,1,0] op_sel_hi:[0,1,0]
	ds_write_b16 v68, v42 offset:19696
	ds_read_b128 v[42:45], v67 offset:2176
	ds_read_b128 v[46:49], v67 offset:2192
	ds_read_b128 v[50:53], v67 offset:2208
	ds_read_b128 v[54:57], v67 offset:2224
	ds_read_b128 v[58:61], v67 offset:2240
	ds_read_b128 v[62:65], v67 offset:2256
	ds_read_b128 v[102:105], v67 offset:2272
	ds_read_b128 v[106:109], v67 offset:2288
	s_waitcnt vmcnt(5)
	v_cvt_f32_f16_e32 v120, v38
	s_waitcnt vmcnt(4)
	v_cvt_f32_f16_e32 v69, v30
	v_pk_mul_f32 v[124:125], v[120:121], v[14:15] op_sel_hi:[0,1]
	v_exp_f32_e32 v124, v124
	v_exp_f32_e32 v125, v125
	v_pk_mul_f32 v[126:127], v[120:121], v[16:17] op_sel_hi:[0,1]
	v_exp_f32_e32 v126, v126
	v_exp_f32_e32 v127, v127
	v_mul_f32_e32 v122, v120, v69
	v_pk_mul_f32 v[124:125], v[124:125], v[136:137]
	s_waitcnt lgkmcnt(14)
	v_pk_fma_f32 v[124:125], v[122:123], v[70:71], v[124:125] op_sel_hi:[0,1,1]
	s_waitcnt lgkmcnt(12)
	v_pk_fma_f32 v[70:71], v[86:87], v[124:125], 0 op_sel_hi:[1,1,0]
	v_pk_mul_f32 v[86:87], v[126:127], v[130:131]
	s_nop 0
	v_pk_fma_f32 v[126:127], v[122:123], v[72:73], v[86:87] op_sel_hi:[0,1,1]
	v_pk_mul_f32 v[72:73], v[120:121], v[10:11] op_sel_hi:[0,1]
	v_exp_f32_e32 v72, v72
	v_exp_f32_e32 v73, v73
	v_pk_mul_f32 v[86:87], v[120:121], v[12:13] op_sel_hi:[0,1]
	v_exp_f32_e32 v86, v86
	v_exp_f32_e32 v87, v87
	v_pk_mul_f32 v[72:73], v[72:73], v[132:133]
	v_pk_fma_f32 v[70:71], v[88:89], v[126:127], v[70:71]
	v_pk_fma_f32 v[128:129], v[122:123], v[74:75], v[72:73] op_sel_hi:[0,1,1]
	v_pk_mul_f32 v[72:73], v[86:87], v[110:111]
	v_pk_mul_f32 v[74:75], v[120:121], v[8:9] op_sel_hi:[0,1]
	v_pk_fma_f32 v[110:111], v[122:123], v[76:77], v[72:73] op_sel_hi:[0,1,1]
	v_pk_mul_f32 v[72:73], v[120:121], v[6:7] op_sel_hi:[0,1]
	v_exp_f32_e32 v72, v72
	v_exp_f32_e32 v73, v73
	v_exp_f32_e32 v74, v74
	v_exp_f32_e32 v75, v75
	s_waitcnt lgkmcnt(11)
	v_pk_fma_f32 v[70:71], v[90:91], v[128:129], v[70:71]
	v_pk_mul_f32 v[72:73], v[72:73], v[112:113]
	v_pk_fma_f32 v[70:71], v[92:93], v[110:111], v[70:71]
	v_pk_fma_f32 v[112:113], v[122:123], v[78:79], v[72:73] op_sel_hi:[0,1,1]
	v_pk_mul_f32 v[72:73], v[74:75], v[114:115]
	v_pk_mul_f32 v[74:75], v[120:121], v[4:5] op_sel_hi:[0,1]
	v_pk_fma_f32 v[114:115], v[122:123], v[80:81], v[72:73] op_sel_hi:[0,1,1]
	v_pk_mul_f32 v[72:73], v[120:121], v[2:3] op_sel_hi:[0,1]
	v_exp_f32_e32 v72, v72
	v_exp_f32_e32 v73, v73
	v_exp_f32_e32 v74, v74
	v_exp_f32_e32 v75, v75
	s_waitcnt lgkmcnt(10)
	v_pk_fma_f32 v[70:71], v[94:95], v[112:113], v[70:71]
	v_pk_mul_f32 v[72:73], v[72:73], v[116:117]
	v_pk_fma_f32 v[70:71], v[96:97], v[114:115], v[70:71]
	v_pk_fma_f32 v[116:117], v[122:123], v[82:83], v[72:73] op_sel_hi:[0,1,1]
	v_pk_mul_f32 v[72:73], v[74:75], v[118:119]
	s_waitcnt lgkmcnt(9)
	v_pk_fma_f32 v[70:71], v[98:99], v[116:117], v[70:71]
	v_pk_fma_f32 v[118:119], v[122:123], v[84:85], v[72:73] op_sel_hi:[0,1,1]
	v_pk_fma_f32 v[70:71], v[100:101], v[118:119], v[70:71]
	s_nop 0
	v_add_f32_e32 v69, v70, v71
	v_fma_mix_f32 v69, v1, v30, v69 op_sel_hi:[0,1,0]
	s_waitcnt vmcnt(3)
	v_fma_mixlo_f16 v69, v69, v34, 0 op_sel_hi:[0,1,0]
	ds_write_b16 v68, v69 offset:20736
	ds_read_b128 v[70:73], v67 offset:2304
	ds_read_b128 v[74:77], v67 offset:2320
	ds_read_b128 v[78:81], v67 offset:2336
	ds_read_b128 v[82:85], v67 offset:2352
	ds_read_b128 v[86:89], v67 offset:2368
	ds_read_b128 v[90:93], v67 offset:2384
	ds_read_b128 v[94:97], v67 offset:2400
	ds_read_b128 v[98:101], v67 offset:2416
	v_cvt_f32_f16_sdwa v38, v38 dst_sel:DWORD dst_unused:UNUSED_PAD src0_sel:WORD_1
	v_cvt_f32_f16_sdwa v69, v30 dst_sel:DWORD dst_unused:UNUSED_PAD src0_sel:WORD_1
	v_pk_mul_f32 v[122:123], v[38:39], v[14:15] op_sel_hi:[0,1]
	v_exp_f32_e32 v122, v122
	v_exp_f32_e32 v123, v123
	v_pk_mul_f32 v[130:131], v[38:39], v[16:17] op_sel_hi:[0,1]
	v_exp_f32_e32 v130, v130
	v_exp_f32_e32 v131, v131
	v_mul_f32_e32 v120, v38, v69
	v_pk_mul_f32 v[122:123], v[122:123], v[124:125]
	s_waitcnt lgkmcnt(14)
	v_pk_fma_f32 v[122:123], v[120:121], v[42:43], v[122:123] op_sel_hi:[0,1,1]
	s_waitcnt lgkmcnt(12)
	v_pk_fma_f32 v[42:43], v[58:59], v[122:123], 0 op_sel_hi:[1,1,0]
	v_pk_mul_f32 v[58:59], v[130:131], v[126:127]
	s_nop 0
	v_pk_fma_f32 v[124:125], v[120:121], v[44:45], v[58:59] op_sel_hi:[0,1,1]
	v_pk_mul_f32 v[44:45], v[38:39], v[10:11] op_sel_hi:[0,1]
	v_exp_f32_e32 v44, v44
	v_exp_f32_e32 v45, v45
	v_pk_mul_f32 v[58:59], v[38:39], v[12:13] op_sel_hi:[0,1]
	v_exp_f32_e32 v58, v58
	v_exp_f32_e32 v59, v59
	v_pk_mul_f32 v[44:45], v[44:45], v[128:129]
	v_pk_fma_f32 v[42:43], v[60:61], v[124:125], v[42:43]
	v_pk_fma_f32 v[126:127], v[120:121], v[46:47], v[44:45] op_sel_hi:[0,1,1]
	v_pk_mul_f32 v[44:45], v[58:59], v[110:111]
	v_pk_mul_f32 v[46:47], v[38:39], v[8:9] op_sel_hi:[0,1]
	v_pk_fma_f32 v[110:111], v[120:121], v[48:49], v[44:45] op_sel_hi:[0,1,1]
	v_pk_mul_f32 v[44:45], v[38:39], v[6:7] op_sel_hi:[0,1]
	v_exp_f32_e32 v44, v44
	v_exp_f32_e32 v45, v45
	v_exp_f32_e32 v46, v46
	v_exp_f32_e32 v47, v47
	s_waitcnt lgkmcnt(11)
	v_pk_fma_f32 v[42:43], v[62:63], v[126:127], v[42:43]
	v_pk_mul_f32 v[44:45], v[44:45], v[112:113]
	v_pk_fma_f32 v[42:43], v[64:65], v[110:111], v[42:43]
	v_pk_fma_f32 v[112:113], v[120:121], v[50:51], v[44:45] op_sel_hi:[0,1,1]
	v_pk_mul_f32 v[44:45], v[46:47], v[114:115]
	v_pk_mul_f32 v[46:47], v[38:39], v[4:5] op_sel_hi:[0,1]
	v_pk_fma_f32 v[114:115], v[120:121], v[52:53], v[44:45] op_sel_hi:[0,1,1]
	v_pk_mul_f32 v[44:45], v[38:39], v[2:3] op_sel_hi:[0,1]
	v_exp_f32_e32 v44, v44
	v_exp_f32_e32 v45, v45
	v_exp_f32_e32 v46, v46
	v_exp_f32_e32 v47, v47
	s_waitcnt lgkmcnt(10)
	v_pk_fma_f32 v[42:43], v[102:103], v[112:113], v[42:43]
	v_pk_mul_f32 v[44:45], v[44:45], v[116:117]
	v_pk_fma_f32 v[42:43], v[104:105], v[114:115], v[42:43]
	v_pk_fma_f32 v[116:117], v[120:121], v[54:55], v[44:45] op_sel_hi:[0,1,1]
	v_pk_mul_f32 v[44:45], v[46:47], v[118:119]
	s_waitcnt lgkmcnt(9)
	v_pk_fma_f32 v[42:43], v[106:107], v[116:117], v[42:43]
	v_pk_fma_f32 v[118:119], v[120:121], v[56:57], v[44:45] op_sel_hi:[0,1,1]
	v_pk_fma_f32 v[42:43], v[108:109], v[118:119], v[42:43]
	s_nop 0
	v_add_f32_e32 v38, v42, v43
	v_fma_mix_f32 v30, v1, v30, v38 op_sel:[0,1,0] op_sel_hi:[0,1,0]
	v_fma_mixlo_f16 v30, v30, v34, 0 op_sel:[0,1,0] op_sel_hi:[0,1,0]
	ds_write_b16 v68, v30 offset:21776
	ds_read_b128 v[42:45], v67 offset:2432
	ds_read_b128 v[46:49], v67 offset:2448
	ds_read_b128 v[50:53], v67 offset:2464
	ds_read_b128 v[54:57], v67 offset:2480
	ds_read_b128 v[58:61], v67 offset:2496
	ds_read_b128 v[62:65], v67 offset:2512
	ds_read_b128 v[102:105], v67 offset:2528
	ds_read_b128 v[106:109], v67 offset:2544
	v_cvt_f32_f16_e32 v30, v39
	v_cvt_f32_f16_e32 v34, v31
	v_pk_mul_f32 v[120:121], v[30:31], v[14:15] op_sel_hi:[0,1]
	v_exp_f32_e32 v120, v120
	v_exp_f32_e32 v121, v121
	v_pk_mul_f32 v[128:129], v[30:31], v[16:17] op_sel_hi:[0,1]
	v_exp_f32_e32 v128, v128
	v_exp_f32_e32 v129, v129
	v_mul_f32_e32 v34, v30, v34
	v_pk_mul_f32 v[120:121], v[120:121], v[122:123]
	s_waitcnt lgkmcnt(14)
	v_pk_fma_f32 v[120:121], v[34:35], v[70:71], v[120:121] op_sel_hi:[0,1,1]
	s_waitcnt lgkmcnt(12)
	v_pk_fma_f32 v[70:71], v[86:87], v[120:121], 0 op_sel_hi:[1,1,0]
	v_pk_mul_f32 v[86:87], v[128:129], v[124:125]
	s_nop 0
	v_pk_fma_f32 v[122:123], v[34:35], v[72:73], v[86:87] op_sel_hi:[0,1,1]
	v_pk_mul_f32 v[72:73], v[30:31], v[10:11] op_sel_hi:[0,1]
	v_exp_f32_e32 v72, v72
	v_exp_f32_e32 v73, v73
	v_pk_mul_f32 v[86:87], v[30:31], v[12:13] op_sel_hi:[0,1]
	v_exp_f32_e32 v86, v86
	v_exp_f32_e32 v87, v87
	v_pk_mul_f32 v[72:73], v[72:73], v[126:127]
	v_pk_fma_f32 v[70:71], v[88:89], v[122:123], v[70:71]
	v_pk_fma_f32 v[124:125], v[34:35], v[74:75], v[72:73] op_sel_hi:[0,1,1]
	v_pk_mul_f32 v[72:73], v[86:87], v[110:111]
	v_pk_mul_f32 v[74:75], v[30:31], v[8:9] op_sel_hi:[0,1]
	v_pk_fma_f32 v[110:111], v[34:35], v[76:77], v[72:73] op_sel_hi:[0,1,1]
	v_pk_mul_f32 v[72:73], v[30:31], v[6:7] op_sel_hi:[0,1]
	v_exp_f32_e32 v72, v72
	v_exp_f32_e32 v73, v73
	v_exp_f32_e32 v74, v74
	v_exp_f32_e32 v75, v75
	s_waitcnt lgkmcnt(11)
	v_pk_fma_f32 v[70:71], v[90:91], v[124:125], v[70:71]
	v_pk_mul_f32 v[72:73], v[72:73], v[112:113]
	v_pk_fma_f32 v[70:71], v[92:93], v[110:111], v[70:71]
	v_pk_fma_f32 v[112:113], v[34:35], v[78:79], v[72:73] op_sel_hi:[0,1,1]
	v_pk_mul_f32 v[72:73], v[74:75], v[114:115]
	v_pk_mul_f32 v[74:75], v[30:31], v[4:5] op_sel_hi:[0,1]
	v_pk_fma_f32 v[114:115], v[34:35], v[80:81], v[72:73] op_sel_hi:[0,1,1]
	v_pk_mul_f32 v[72:73], v[30:31], v[2:3] op_sel_hi:[0,1]
	v_exp_f32_e32 v72, v72
	v_exp_f32_e32 v73, v73
	v_exp_f32_e32 v74, v74
	v_exp_f32_e32 v75, v75
	s_waitcnt lgkmcnt(10)
	v_pk_fma_f32 v[70:71], v[94:95], v[112:113], v[70:71]
	v_pk_mul_f32 v[72:73], v[72:73], v[116:117]
	v_pk_fma_f32 v[70:71], v[96:97], v[114:115], v[70:71]
	v_pk_fma_f32 v[116:117], v[34:35], v[82:83], v[72:73] op_sel_hi:[0,1,1]
	v_pk_mul_f32 v[72:73], v[74:75], v[118:119]
	s_waitcnt lgkmcnt(9)
	v_pk_fma_f32 v[70:71], v[98:99], v[116:117], v[70:71]
	v_pk_fma_f32 v[118:119], v[34:35], v[84:85], v[72:73] op_sel_hi:[0,1,1]
	v_pk_fma_f32 v[70:71], v[100:101], v[118:119], v[70:71]
	s_nop 0
	v_add_f32_e32 v30, v70, v71
	v_fma_mix_f32 v30, v1, v31, v30 op_sel_hi:[0,1,0]
	v_fma_mixlo_f16 v30, v30, v35, 0 op_sel_hi:[0,1,0]
	ds_write_b16 v68, v30 offset:22816
	ds_read_b128 v[70:73], v67 offset:2560
	ds_read_b128 v[74:77], v67 offset:2576
	ds_read_b128 v[78:81], v67 offset:2592
	ds_read_b128 v[82:85], v67 offset:2608
	ds_read_b128 v[86:89], v67 offset:2624
	ds_read_b128 v[90:93], v67 offset:2640
	ds_read_b128 v[94:97], v67 offset:2656
	ds_read_b128 v[98:101], v67 offset:2672
	v_cvt_f32_f16_sdwa v30, v39 dst_sel:DWORD dst_unused:UNUSED_PAD src0_sel:WORD_1
	v_cvt_f32_f16_sdwa v34, v31 dst_sel:DWORD dst_unused:UNUSED_PAD src0_sel:WORD_1
	v_pk_mul_f32 v[38:39], v[30:31], v[14:15] op_sel_hi:[0,1]
	v_exp_f32_e32 v38, v38
	v_exp_f32_e32 v39, v39
	v_pk_mul_f32 v[126:127], v[30:31], v[16:17] op_sel_hi:[0,1]
	v_exp_f32_e32 v126, v126
	v_exp_f32_e32 v127, v127
	v_mul_f32_e32 v34, v30, v34
	v_pk_mul_f32 v[38:39], v[38:39], v[120:121]
	s_waitcnt lgkmcnt(14)
	v_pk_fma_f32 v[38:39], v[34:35], v[42:43], v[38:39] op_sel_hi:[0,1,1]
	s_waitcnt lgkmcnt(12)
	v_pk_fma_f32 v[42:43], v[58:59], v[38:39], 0 op_sel_hi:[1,1,0]
	v_pk_mul_f32 v[58:59], v[126:127], v[122:123]
	s_nop 0
	v_pk_fma_f32 v[120:121], v[34:35], v[44:45], v[58:59] op_sel_hi:[0,1,1]
	v_pk_mul_f32 v[44:45], v[30:31], v[10:11] op_sel_hi:[0,1]
	v_exp_f32_e32 v44, v44
	v_exp_f32_e32 v45, v45
	v_pk_mul_f32 v[58:59], v[30:31], v[12:13] op_sel_hi:[0,1]
	v_exp_f32_e32 v58, v58
	v_exp_f32_e32 v59, v59
	v_pk_mul_f32 v[44:45], v[44:45], v[124:125]
	v_pk_fma_f32 v[42:43], v[60:61], v[120:121], v[42:43]
	v_pk_fma_f32 v[122:123], v[34:35], v[46:47], v[44:45] op_sel_hi:[0,1,1]
	v_pk_mul_f32 v[44:45], v[58:59], v[110:111]
	v_pk_mul_f32 v[46:47], v[30:31], v[8:9] op_sel_hi:[0,1]
	v_pk_fma_f32 v[110:111], v[34:35], v[48:49], v[44:45] op_sel_hi:[0,1,1]
	v_pk_mul_f32 v[44:45], v[30:31], v[6:7] op_sel_hi:[0,1]
	v_exp_f32_e32 v44, v44
	v_exp_f32_e32 v45, v45
	v_exp_f32_e32 v46, v46
	v_exp_f32_e32 v47, v47
	s_waitcnt lgkmcnt(11)
	v_pk_fma_f32 v[42:43], v[62:63], v[122:123], v[42:43]
	v_pk_mul_f32 v[44:45], v[44:45], v[112:113]
	v_pk_fma_f32 v[42:43], v[64:65], v[110:111], v[42:43]
	v_pk_fma_f32 v[112:113], v[34:35], v[50:51], v[44:45] op_sel_hi:[0,1,1]
	v_pk_mul_f32 v[44:45], v[46:47], v[114:115]
	v_pk_mul_f32 v[46:47], v[30:31], v[4:5] op_sel_hi:[0,1]
	v_pk_fma_f32 v[114:115], v[34:35], v[52:53], v[44:45] op_sel_hi:[0,1,1]
	v_pk_mul_f32 v[44:45], v[30:31], v[2:3] op_sel_hi:[0,1]
	v_exp_f32_e32 v44, v44
	v_exp_f32_e32 v45, v45
	v_exp_f32_e32 v46, v46
	v_exp_f32_e32 v47, v47
	s_waitcnt lgkmcnt(10)
	v_pk_fma_f32 v[42:43], v[102:103], v[112:113], v[42:43]
	v_pk_mul_f32 v[44:45], v[44:45], v[116:117]
	v_pk_fma_f32 v[42:43], v[104:105], v[114:115], v[42:43]
	v_pk_fma_f32 v[116:117], v[34:35], v[54:55], v[44:45] op_sel_hi:[0,1,1]
	v_pk_mul_f32 v[44:45], v[46:47], v[118:119]
	s_waitcnt lgkmcnt(9)
	v_pk_fma_f32 v[42:43], v[106:107], v[116:117], v[42:43]
	v_pk_fma_f32 v[118:119], v[34:35], v[56:57], v[44:45] op_sel_hi:[0,1,1]
	v_pk_fma_f32 v[42:43], v[108:109], v[118:119], v[42:43]
	s_nop 0
	v_add_f32_e32 v30, v42, v43
	v_fma_mix_f32 v30, v1, v31, v30 op_sel:[0,1,0] op_sel_hi:[0,1,0]
	v_fma_mixlo_f16 v30, v30, v35, 0 op_sel:[0,1,0] op_sel_hi:[0,1,0]
	ds_write_b16 v68, v30 offset:23856
	ds_read_b128 v[42:45], v67 offset:2688
	ds_read_b128 v[46:49], v67 offset:2704
	ds_read_b128 v[50:53], v67 offset:2720
	ds_read_b128 v[54:57], v67 offset:2736
	ds_read_b128 v[58:61], v67 offset:2752
	ds_read_b128 v[62:65], v67 offset:2768
	ds_read_b128 v[102:105], v67 offset:2784
	ds_read_b128 v[106:109], v67 offset:2800
	v_cvt_f32_f16_e32 v30, v40
	v_cvt_f32_f16_e32 v31, v32
	v_pk_mul_f32 v[124:125], v[30:31], v[14:15] op_sel_hi:[0,1]
	v_exp_f32_e32 v124, v124
	v_exp_f32_e32 v125, v125
	v_pk_mul_f32 v[126:127], v[30:31], v[16:17] op_sel_hi:[0,1]
	v_exp_f32_e32 v126, v126
	v_exp_f32_e32 v127, v127
	v_mul_f32_e32 v34, v30, v31
	v_pk_mul_f32 v[38:39], v[124:125], v[38:39]
	s_waitcnt lgkmcnt(14)
	v_pk_fma_f32 v[38:39], v[34:35], v[70:71], v[38:39] op_sel_hi:[0,1,1]
	s_waitcnt lgkmcnt(12)
	v_pk_fma_f32 v[70:71], v[86:87], v[38:39], 0 op_sel_hi:[1,1,0]
	v_pk_mul_f32 v[86:87], v[126:127], v[120:121]
	s_nop 0
	v_pk_fma_f32 v[120:121], v[34:35], v[72:73], v[86:87] op_sel_hi:[0,1,1]
	v_pk_mul_f32 v[72:73], v[30:31], v[10:11] op_sel_hi:[0,1]
	v_exp_f32_e32 v72, v72
	v_exp_f32_e32 v73, v73
	v_pk_mul_f32 v[86:87], v[30:31], v[12:13] op_sel_hi:[0,1]
	v_exp_f32_e32 v86, v86
	v_exp_f32_e32 v87, v87
	v_pk_mul_f32 v[72:73], v[72:73], v[122:123]
	v_pk_fma_f32 v[70:71], v[88:89], v[120:121], v[70:71]
	v_pk_fma_f32 v[122:123], v[34:35], v[74:75], v[72:73] op_sel_hi:[0,1,1]
	v_pk_mul_f32 v[72:73], v[86:87], v[110:111]
	v_pk_mul_f32 v[74:75], v[30:31], v[8:9] op_sel_hi:[0,1]
	v_pk_fma_f32 v[110:111], v[34:35], v[76:77], v[72:73] op_sel_hi:[0,1,1]
	v_pk_mul_f32 v[72:73], v[30:31], v[6:7] op_sel_hi:[0,1]
	v_exp_f32_e32 v72, v72
	v_exp_f32_e32 v73, v73
	v_exp_f32_e32 v74, v74
	v_exp_f32_e32 v75, v75
	s_waitcnt lgkmcnt(11)
	v_pk_fma_f32 v[70:71], v[90:91], v[122:123], v[70:71]
	v_pk_mul_f32 v[72:73], v[72:73], v[112:113]
	v_pk_fma_f32 v[70:71], v[92:93], v[110:111], v[70:71]
	v_pk_fma_f32 v[112:113], v[34:35], v[78:79], v[72:73] op_sel_hi:[0,1,1]
	v_pk_mul_f32 v[72:73], v[74:75], v[114:115]
	s_waitcnt lgkmcnt(10)
	v_pk_fma_f32 v[70:71], v[94:95], v[112:113], v[70:71]
	v_pk_fma_f32 v[114:115], v[34:35], v[80:81], v[72:73] op_sel_hi:[0,1,1]
	v_pk_mul_f32 v[72:73], v[30:31], v[2:3] op_sel_hi:[0,1]
	v_exp_f32_e32 v72, v72
	v_exp_f32_e32 v73, v73
	v_pk_mul_f32 v[30:31], v[30:31], v[4:5] op_sel_hi:[0,1]
	v_exp_f32_e32 v30, v30
	v_exp_f32_e32 v31, v31
	v_pk_mul_f32 v[72:73], v[72:73], v[116:117]
	v_pk_fma_f32 v[70:71], v[96:97], v[114:115], v[70:71]
	v_pk_fma_f32 v[116:117], v[34:35], v[82:83], v[72:73] op_sel_hi:[0,1,1]
	v_pk_mul_f32 v[30:31], v[30:31], v[118:119]
	s_waitcnt lgkmcnt(9)
	v_pk_fma_f32 v[70:71], v[98:99], v[116:117], v[70:71]
	v_pk_fma_f32 v[30:31], v[34:35], v[84:85], v[30:31] op_sel_hi:[0,1,1]
	v_pk_fma_f32 v[34:35], v[100:101], v[30:31], v[70:71]
	s_nop 0
	v_add_f32_e32 v34, v34, v35
	v_fma_mix_f32 v34, v1, v32, v34 op_sel_hi:[0,1,0]
	v_fma_mixlo_f16 v34, v34, v36, 0 op_sel_hi:[0,1,0]
	ds_write_b16 v68, v34 offset:24896
	ds_read_b128 v[70:73], v67 offset:2816
	ds_read_b128 v[74:77], v67 offset:2832
	ds_read_b128 v[78:81], v67 offset:2848
	ds_read_b128 v[82:85], v67 offset:2864
	ds_read_b128 v[86:89], v67 offset:2880
	ds_read_b128 v[90:93], v67 offset:2896
	ds_read_b128 v[94:97], v67 offset:2912
	ds_read_b128 v[98:101], v67 offset:2928
	v_cvt_f32_f16_sdwa v34, v40 dst_sel:DWORD dst_unused:UNUSED_PAD src0_sel:WORD_1
	v_cvt_f32_f16_sdwa v35, v32 dst_sel:DWORD dst_unused:UNUSED_PAD src0_sel:WORD_1
	v_pk_mul_f32 v[118:119], v[34:35], v[14:15] op_sel_hi:[0,1]
	v_exp_f32_e32 v118, v118
	v_exp_f32_e32 v119, v119
	v_pk_mul_f32 v[124:125], v[34:35], v[16:17] op_sel_hi:[0,1]
	v_exp_f32_e32 v124, v124
	v_exp_f32_e32 v125, v125
	v_mul_f32_e32 v40, v34, v35
	v_pk_mul_f32 v[38:39], v[118:119], v[38:39]
	s_waitcnt lgkmcnt(14)
	v_pk_fma_f32 v[38:39], v[40:41], v[42:43], v[38:39] op_sel_hi:[0,1,1]
	s_waitcnt lgkmcnt(12)
	v_pk_fma_f32 v[42:43], v[58:59], v[38:39], 0 op_sel_hi:[1,1,0]
	v_pk_mul_f32 v[58:59], v[124:125], v[120:121]
	s_nop 0
	v_pk_fma_f32 v[118:119], v[40:41], v[44:45], v[58:59] op_sel_hi:[0,1,1]
	v_pk_mul_f32 v[44:45], v[34:35], v[10:11] op_sel_hi:[0,1]
	v_exp_f32_e32 v44, v44
	v_exp_f32_e32 v45, v45
	v_pk_mul_f32 v[58:59], v[34:35], v[12:13] op_sel_hi:[0,1]
	v_exp_f32_e32 v58, v58
	v_exp_f32_e32 v59, v59
	v_pk_mul_f32 v[44:45], v[44:45], v[122:123]
	v_pk_fma_f32 v[42:43], v[60:61], v[118:119], v[42:43]
	v_pk_fma_f32 v[120:121], v[40:41], v[46:47], v[44:45] op_sel_hi:[0,1,1]
	v_pk_mul_f32 v[44:45], v[58:59], v[110:111]
	v_pk_mul_f32 v[46:47], v[34:35], v[8:9] op_sel_hi:[0,1]
	v_pk_fma_f32 v[110:111], v[40:41], v[48:49], v[44:45] op_sel_hi:[0,1,1]
	v_pk_mul_f32 v[44:45], v[34:35], v[6:7] op_sel_hi:[0,1]
	v_exp_f32_e32 v44, v44
	v_exp_f32_e32 v45, v45
	v_exp_f32_e32 v46, v46
	v_exp_f32_e32 v47, v47
	s_waitcnt lgkmcnt(11)
	v_pk_fma_f32 v[42:43], v[62:63], v[120:121], v[42:43]
	v_pk_mul_f32 v[44:45], v[44:45], v[112:113]
	v_pk_fma_f32 v[42:43], v[64:65], v[110:111], v[42:43]
	v_pk_fma_f32 v[112:113], v[40:41], v[50:51], v[44:45] op_sel_hi:[0,1,1]
	v_pk_mul_f32 v[44:45], v[46:47], v[114:115]
	s_waitcnt lgkmcnt(10)
	v_pk_fma_f32 v[42:43], v[102:103], v[112:113], v[42:43]
	v_pk_fma_f32 v[114:115], v[40:41], v[52:53], v[44:45] op_sel_hi:[0,1,1]
	v_pk_mul_f32 v[44:45], v[34:35], v[2:3] op_sel_hi:[0,1]
	v_exp_f32_e32 v44, v44
	v_exp_f32_e32 v45, v45
	v_pk_mul_f32 v[34:35], v[34:35], v[4:5] op_sel_hi:[0,1]
	v_exp_f32_e32 v34, v34
	v_exp_f32_e32 v35, v35
	v_pk_mul_f32 v[44:45], v[44:45], v[116:117]
	v_pk_fma_f32 v[42:43], v[104:105], v[114:115], v[42:43]
	v_pk_fma_f32 v[116:117], v[40:41], v[54:55], v[44:45] op_sel_hi:[0,1,1]
	v_pk_mul_f32 v[30:31], v[34:35], v[30:31]
	s_waitcnt lgkmcnt(9)
	v_pk_fma_f32 v[42:43], v[106:107], v[116:117], v[42:43]
	v_pk_fma_f32 v[30:31], v[40:41], v[56:57], v[30:31] op_sel_hi:[0,1,1]
	v_pk_fma_f32 v[34:35], v[108:109], v[30:31], v[42:43]
	s_nop 0
	v_add_f32_e32 v34, v34, v35
	v_fma_mix_f32 v32, v1, v32, v34 op_sel:[0,1,0] op_sel_hi:[0,1,0]
	v_fma_mixlo_f16 v32, v32, v36, 0 op_sel:[0,1,0] op_sel_hi:[0,1,0]
	ds_write_b16 v68, v32 offset:25936
	ds_read_b128 v[42:45], v67 offset:2944
	ds_read_b128 v[46:49], v67 offset:2960
	ds_read_b128 v[50:53], v67 offset:2976
	ds_read_b128 v[54:57], v67 offset:2992
	ds_read_b128 v[58:61], v67 offset:3008
	ds_read_b128 v[62:65], v67 offset:3024
	ds_read_b128 v[102:105], v67 offset:3040
	ds_read_b128 v[106:109], v67 offset:3056
	v_cvt_f32_f16_e32 v32, v41
	v_cvt_f32_f16_e32 v34, v33
	v_pk_mul_f32 v[122:123], v[32:33], v[14:15] op_sel_hi:[0,1]
	v_exp_f32_e32 v122, v122
	v_exp_f32_e32 v123, v123
	v_pk_mul_f32 v[124:125], v[32:33], v[16:17] op_sel_hi:[0,1]
	v_exp_f32_e32 v124, v124
	v_exp_f32_e32 v125, v125
	v_mul_f32_e32 v34, v32, v34
	v_pk_mul_f32 v[38:39], v[122:123], v[38:39]
	s_waitcnt lgkmcnt(14)
	v_pk_fma_f32 v[38:39], v[34:35], v[70:71], v[38:39] op_sel_hi:[0,1,1]
	s_waitcnt lgkmcnt(12)
	v_pk_fma_f32 v[70:71], v[86:87], v[38:39], 0 op_sel_hi:[1,1,0]
	v_pk_mul_f32 v[86:87], v[124:125], v[118:119]
	s_nop 0
	v_pk_fma_f32 v[118:119], v[34:35], v[72:73], v[86:87] op_sel_hi:[0,1,1]
	v_pk_mul_f32 v[72:73], v[32:33], v[10:11] op_sel_hi:[0,1]
	v_exp_f32_e32 v72, v72
	v_exp_f32_e32 v73, v73
	v_pk_mul_f32 v[86:87], v[32:33], v[12:13] op_sel_hi:[0,1]
	v_exp_f32_e32 v86, v86
	v_exp_f32_e32 v87, v87
	v_pk_mul_f32 v[72:73], v[72:73], v[120:121]
	v_pk_fma_f32 v[70:71], v[88:89], v[118:119], v[70:71]
	v_pk_fma_f32 v[120:121], v[34:35], v[74:75], v[72:73] op_sel_hi:[0,1,1]
	v_pk_mul_f32 v[72:73], v[86:87], v[110:111]
	v_pk_mul_f32 v[74:75], v[32:33], v[8:9] op_sel_hi:[0,1]
	v_pk_fma_f32 v[110:111], v[34:35], v[76:77], v[72:73] op_sel_hi:[0,1,1]
	v_pk_mul_f32 v[72:73], v[32:33], v[6:7] op_sel_hi:[0,1]
	v_exp_f32_e32 v72, v72
	v_exp_f32_e32 v73, v73
	v_exp_f32_e32 v74, v74
	v_exp_f32_e32 v75, v75
	s_waitcnt lgkmcnt(11)
	v_pk_fma_f32 v[70:71], v[90:91], v[120:121], v[70:71]
	v_pk_mul_f32 v[72:73], v[72:73], v[112:113]
	v_pk_fma_f32 v[70:71], v[92:93], v[110:111], v[70:71]
	v_pk_fma_f32 v[112:113], v[34:35], v[78:79], v[72:73] op_sel_hi:[0,1,1]
	v_pk_mul_f32 v[72:73], v[74:75], v[114:115]
	v_pk_mul_f32 v[74:75], v[32:33], v[4:5] op_sel_hi:[0,1]
	v_pk_fma_f32 v[114:115], v[34:35], v[80:81], v[72:73] op_sel_hi:[0,1,1]
	v_pk_mul_f32 v[72:73], v[32:33], v[2:3] op_sel_hi:[0,1]
	v_exp_f32_e32 v72, v72
	v_exp_f32_e32 v73, v73
	v_exp_f32_e32 v74, v74
	v_exp_f32_e32 v75, v75
	s_waitcnt lgkmcnt(10)
	v_pk_fma_f32 v[70:71], v[94:95], v[112:113], v[70:71]
	v_pk_mul_f32 v[72:73], v[72:73], v[116:117]
	v_pk_fma_f32 v[70:71], v[96:97], v[114:115], v[70:71]
	v_pk_fma_f32 v[116:117], v[34:35], v[82:83], v[72:73] op_sel_hi:[0,1,1]
	v_pk_mul_f32 v[30:31], v[74:75], v[30:31]
	s_waitcnt lgkmcnt(9)
	v_pk_fma_f32 v[70:71], v[98:99], v[116:117], v[70:71]
	v_pk_fma_f32 v[30:31], v[34:35], v[84:85], v[30:31] op_sel_hi:[0,1,1]
	v_pk_fma_f32 v[34:35], v[100:101], v[30:31], v[70:71]
	s_nop 0
	v_add_f32_e32 v32, v34, v35
	v_fma_mix_f32 v32, v1, v33, v32 op_sel_hi:[0,1,0]
	v_fma_mixlo_f16 v32, v32, v37, 0 op_sel_hi:[0,1,0]
	ds_write_b16 v68, v32 offset:26976
	ds_read_b128 v[70:73], v67 offset:3072
	ds_read_b128 v[74:77], v67 offset:3088
	ds_read_b128 v[78:81], v67 offset:3104
	ds_read_b128 v[82:85], v67 offset:3120
	ds_read_b128 v[86:89], v67 offset:3136
	ds_read_b128 v[90:93], v67 offset:3152
	ds_read_b128 v[94:97], v67 offset:3168
	ds_read_b128 v[98:101], v67 offset:3184
	v_cvt_f32_f16_sdwa v32, v41 dst_sel:DWORD dst_unused:UNUSED_PAD src0_sel:WORD_1
	v_cvt_f32_f16_sdwa v34, v33 dst_sel:DWORD dst_unused:UNUSED_PAD src0_sel:WORD_1
	v_pk_mul_f32 v[40:41], v[32:33], v[14:15] op_sel_hi:[0,1]
	v_pk_mul_f32 v[122:123], v[32:33], v[16:17] op_sel_hi:[0,1]
	v_exp_f32_e32 v40, v40
	v_exp_f32_e32 v41, v41
	v_exp_f32_e32 v122, v122
	v_exp_f32_e32 v123, v123
	v_mul_f32_e32 v34, v32, v34
	v_pk_mul_f32 v[38:39], v[40:41], v[38:39]
	v_pk_mul_f32 v[40:41], v[122:123], v[118:119]
	s_waitcnt lgkmcnt(14)
	v_pk_fma_f32 v[118:119], v[34:35], v[44:45], v[40:41] op_sel_hi:[0,1,1]
	v_pk_mul_f32 v[40:41], v[32:33], v[10:11] op_sel_hi:[0,1]
	v_pk_fma_f32 v[124:125], v[34:35], v[42:43], v[38:39] op_sel_hi:[0,1,1]
	v_exp_f32_e32 v40, v40
	v_exp_f32_e32 v41, v41
	v_pk_mul_f32 v[42:43], v[32:33], v[12:13] op_sel_hi:[0,1]
	v_exp_f32_e32 v42, v42
	v_exp_f32_e32 v43, v43
	s_waitcnt lgkmcnt(12)
	v_pk_fma_f32 v[38:39], v[58:59], v[124:125], 0 op_sel_hi:[1,1,0]
	v_pk_mul_f32 v[40:41], v[40:41], v[120:121]
	v_pk_fma_f32 v[38:39], v[60:61], v[118:119], v[38:39]
	v_pk_fma_f32 v[120:121], v[34:35], v[46:47], v[40:41] op_sel_hi:[0,1,1]
	v_pk_mul_f32 v[40:41], v[42:43], v[110:111]
	s_waitcnt lgkmcnt(11)
	v_pk_fma_f32 v[38:39], v[62:63], v[120:121], v[38:39]
	v_pk_fma_f32 v[62:63], v[34:35], v[48:49], v[40:41] op_sel_hi:[0,1,1]
	v_pk_mul_f32 v[40:41], v[32:33], v[6:7] op_sel_hi:[0,1]
	v_exp_f32_e32 v40, v40
	v_exp_f32_e32 v41, v41
	v_pk_mul_f32 v[42:43], v[32:33], v[8:9] op_sel_hi:[0,1]
	v_exp_f32_e32 v42, v42
	v_exp_f32_e32 v43, v43
	v_pk_mul_f32 v[40:41], v[40:41], v[112:113]
	v_pk_fma_f32 v[38:39], v[64:65], v[62:63], v[38:39]
	v_pk_fma_f32 v[64:65], v[34:35], v[50:51], v[40:41] op_sel_hi:[0,1,1]
	v_pk_mul_f32 v[40:41], v[42:43], v[114:115]
	s_waitcnt lgkmcnt(10)
	v_pk_fma_f32 v[38:39], v[102:103], v[64:65], v[38:39]
	v_pk_fma_f32 v[102:103], v[34:35], v[52:53], v[40:41] op_sel_hi:[0,1,1]
	v_pk_mul_f32 v[40:41], v[32:33], v[2:3] op_sel_hi:[0,1]
	v_exp_f32_e32 v40, v40
	v_exp_f32_e32 v41, v41
	v_pk_mul_f32 v[42:43], v[32:33], v[4:5] op_sel_hi:[0,1]
	v_exp_f32_e32 v42, v42
	v_exp_f32_e32 v43, v43
	v_pk_mul_f32 v[40:41], v[40:41], v[116:117]
	v_pk_fma_f32 v[38:39], v[104:105], v[102:103], v[38:39]
	v_pk_fma_f32 v[104:105], v[34:35], v[54:55], v[40:41] op_sel_hi:[0,1,1]
	v_pk_mul_f32 v[30:31], v[42:43], v[30:31]
	s_waitcnt lgkmcnt(9)
	v_pk_fma_f32 v[38:39], v[106:107], v[104:105], v[38:39]
	v_pk_fma_f32 v[106:107], v[34:35], v[56:57], v[30:31] op_sel_hi:[0,1,1]
	v_pk_fma_f32 v[30:31], v[108:109], v[106:107], v[38:39]
	s_nop 0
	v_add_f32_e32 v30, v30, v31
	v_fma_mix_f32 v30, v1, v33, v30 op_sel:[0,1,0] op_sel_hi:[0,1,0]
	v_fma_mixlo_f16 v30, v30, v37, 0 op_sel:[0,1,0] op_sel_hi:[0,1,0]
	ds_write_b16 v68, v30 offset:28016
	ds_read_b128 v[30:33], v67 offset:3200
	ds_read_b128 v[34:37], v67 offset:3216
	ds_read_b128 v[38:41], v67 offset:3232
	ds_read_b128 v[42:45], v67 offset:3248
	ds_read_b128 v[46:49], v67 offset:3264
	ds_read_b128 v[50:53], v67 offset:3280
	ds_read_b128 v[54:57], v67 offset:3296
	ds_read_b128 v[58:61], v67 offset:3312
	s_waitcnt vmcnt(2)
	v_cvt_f32_f16_e32 v108, v26
	s_waitcnt vmcnt(1)
	v_cvt_f32_f16_e32 v69, v18
	v_pk_mul_f32 v[112:113], v[108:109], v[14:15] op_sel_hi:[0,1]
	v_exp_f32_e32 v112, v112
	v_exp_f32_e32 v113, v113
	v_pk_mul_f32 v[114:115], v[108:109], v[16:17] op_sel_hi:[0,1]
	v_exp_f32_e32 v114, v114
	v_exp_f32_e32 v115, v115
	v_mul_f32_e32 v110, v108, v69
	v_pk_mul_f32 v[112:113], v[112:113], v[124:125]
	s_waitcnt lgkmcnt(14)
	v_pk_fma_f32 v[112:113], v[110:111], v[70:71], v[112:113] op_sel_hi:[0,1,1]
	s_waitcnt lgkmcnt(12)
	v_pk_fma_f32 v[70:71], v[86:87], v[112:113], 0 op_sel_hi:[1,1,0]
	v_pk_mul_f32 v[86:87], v[114:115], v[118:119]
	s_nop 0
	v_pk_fma_f32 v[114:115], v[110:111], v[72:73], v[86:87] op_sel_hi:[0,1,1]
	v_pk_mul_f32 v[72:73], v[108:109], v[10:11] op_sel_hi:[0,1]
	v_exp_f32_e32 v72, v72
	v_exp_f32_e32 v73, v73
	v_pk_mul_f32 v[86:87], v[108:109], v[12:13] op_sel_hi:[0,1]
	v_exp_f32_e32 v86, v86
	v_exp_f32_e32 v87, v87
	v_pk_mul_f32 v[72:73], v[72:73], v[120:121]
	v_pk_fma_f32 v[70:71], v[88:89], v[114:115], v[70:71]
	v_pk_fma_f32 v[116:117], v[110:111], v[74:75], v[72:73] op_sel_hi:[0,1,1]
	v_pk_mul_f32 v[62:63], v[86:87], v[62:63]
	s_waitcnt lgkmcnt(11)
	v_pk_fma_f32 v[70:71], v[90:91], v[116:117], v[70:71]
	v_pk_fma_f32 v[118:119], v[110:111], v[76:77], v[62:63] op_sel_hi:[0,1,1]
	v_pk_fma_f32 v[62:63], v[92:93], v[118:119], v[70:71]
	v_pk_mul_f32 v[70:71], v[108:109], v[6:7] op_sel_hi:[0,1]
	v_exp_f32_e32 v70, v70
	v_exp_f32_e32 v71, v71
	v_pk_mul_f32 v[72:73], v[108:109], v[8:9] op_sel_hi:[0,1]
	v_exp_f32_e32 v72, v72
	v_exp_f32_e32 v73, v73
	v_pk_mul_f32 v[64:65], v[70:71], v[64:65]
	v_pk_mul_f32 v[70:71], v[108:109], v[4:5] op_sel_hi:[0,1]
	v_pk_fma_f32 v[120:121], v[110:111], v[78:79], v[64:65] op_sel_hi:[0,1,1]
	v_pk_mul_f32 v[64:65], v[72:73], v[102:103]
	v_exp_f32_e32 v70, v70
	v_pk_fma_f32 v[102:103], v[110:111], v[80:81], v[64:65] op_sel_hi:[0,1,1]
	v_pk_mul_f32 v[64:65], v[108:109], v[2:3] op_sel_hi:[0,1]
	v_exp_f32_e32 v64, v64
	v_exp_f32_e32 v65, v65
	v_exp_f32_e32 v71, v71
	s_waitcnt lgkmcnt(10)
	v_pk_fma_f32 v[62:63], v[94:95], v[120:121], v[62:63]
	v_pk_mul_f32 v[64:65], v[64:65], v[104:105]
	v_pk_fma_f32 v[62:63], v[96:97], v[102:103], v[62:63]
	v_pk_fma_f32 v[104:105], v[110:111], v[82:83], v[64:65] op_sel_hi:[0,1,1]
	v_pk_mul_f32 v[64:65], v[70:71], v[106:107]
	s_waitcnt lgkmcnt(9)
	v_pk_fma_f32 v[62:63], v[98:99], v[104:105], v[62:63]
	v_pk_fma_f32 v[98:99], v[110:111], v[84:85], v[64:65] op_sel_hi:[0,1,1]
	v_pk_fma_f32 v[62:63], v[100:101], v[98:99], v[62:63]
	s_nop 0
	v_add_f32_e32 v62, v62, v63
	v_fma_mix_f32 v62, v1, v18, v62 op_sel_hi:[0,1,0]
	s_waitcnt vmcnt(0)
	v_fma_mixlo_f16 v62, v62, v22, 0 op_sel_hi:[0,1,0]
	ds_write_b16 v68, v62 offset:29056
	v_lshrrev_b32_e32 v196, 6, v0
	v_and_b32_e32 v197, 48, v0
	v_lshl_or_b32 v196, v196, 7, v197
	v_and_b32_e32 v197, 15, v0
	v_or_b32_e32 v197, s28, v197
	v_lshl_or_b32 v196, v197, 10, v196
	v_add_u32_e32 v197, 0x4000, v196
	global_load_dwordx4 v[180:183], v196, s[4:5]
	global_load_dwordx4 v[184:187], v196, s[4:5] offset:64
	global_load_dwordx4 v[188:191], v197, s[4:5]
	global_load_dwordx4 v[192:195], v197, s[4:5] offset:64
	v_and_b32_e32 v196, 63, v0
	v_lshlrev_b32_e32 v196, 4, v196
	global_load_dwordx4 v[204:207], v196, s[6:7]
	global_load_dwordx4 v[208:211], v196, s[8:9]
	ds_read_b128 v[62:65], v67 offset:3328
	ds_read_b128 v[70:73], v67 offset:3344
	ds_read_b128 v[74:77], v67 offset:3360
	ds_read_b128 v[78:81], v67 offset:3376
	ds_read_b128 v[82:85], v67 offset:3392
	ds_read_b128 v[86:89], v67 offset:3408
	ds_read_b128 v[90:93], v67 offset:3424
	ds_read_b128 v[94:97], v67 offset:3440
	v_cvt_f32_f16_sdwa v26, v26 dst_sel:DWORD dst_unused:UNUSED_PAD src0_sel:WORD_1
	v_cvt_f32_f16_sdwa v69, v18 dst_sel:DWORD dst_unused:UNUSED_PAD src0_sel:WORD_1
	v_pk_mul_f32 v[106:107], v[26:27], v[14:15] op_sel_hi:[0,1]
	v_exp_f32_e32 v106, v106
	v_exp_f32_e32 v107, v107
	v_pk_mul_f32 v[108:109], v[26:27], v[16:17] op_sel_hi:[0,1]
	v_exp_f32_e32 v108, v108
	v_exp_f32_e32 v109, v109
	v_mul_f32_e32 v100, v26, v69
	v_pk_mul_f32 v[106:107], v[106:107], v[112:113]
	s_waitcnt lgkmcnt(14)
	v_pk_fma_f32 v[106:107], v[100:101], v[30:31], v[106:107] op_sel_hi:[0,1,1]
	s_waitcnt lgkmcnt(12)
	v_pk_fma_f32 v[30:31], v[46:47], v[106:107], 0 op_sel_hi:[1,1,0]
	v_pk_mul_f32 v[46:47], v[108:109], v[114:115]
	s_nop 0
	v_pk_fma_f32 v[108:109], v[100:101], v[32:33], v[46:47] op_sel_hi:[0,1,1]
	v_pk_mul_f32 v[32:33], v[26:27], v[10:11] op_sel_hi:[0,1]
	v_exp_f32_e32 v32, v32
	v_exp_f32_e32 v33, v33
	v_pk_mul_f32 v[46:47], v[26:27], v[12:13] op_sel_hi:[0,1]
	v_exp_f32_e32 v46, v46
	v_exp_f32_e32 v47, v47
	v_pk_mul_f32 v[32:33], v[32:33], v[116:117]
	v_pk_fma_f32 v[30:31], v[48:49], v[108:109], v[30:31]
	v_pk_fma_f32 v[110:111], v[100:101], v[34:35], v[32:33] op_sel_hi:[0,1,1]
	v_pk_mul_f32 v[32:33], v[46:47], v[118:119]
	v_pk_mul_f32 v[34:35], v[26:27], v[8:9] op_sel_hi:[0,1]
	v_pk_fma_f32 v[112:113], v[100:101], v[36:37], v[32:33] op_sel_hi:[0,1,1]
	v_pk_mul_f32 v[32:33], v[26:27], v[6:7] op_sel_hi:[0,1]
	v_exp_f32_e32 v32, v32
	v_exp_f32_e32 v33, v33
	v_exp_f32_e32 v34, v34
	v_exp_f32_e32 v35, v35
	s_waitcnt lgkmcnt(11)
	v_pk_fma_f32 v[30:31], v[50:51], v[110:111], v[30:31]
	v_pk_mul_f32 v[32:33], v[32:33], v[120:121]
	v_pk_fma_f32 v[30:31], v[52:53], v[112:113], v[30:31]
	v_pk_fma_f32 v[114:115], v[100:101], v[38:39], v[32:33] op_sel_hi:[0,1,1]
	v_pk_mul_f32 v[32:33], v[34:35], v[102:103]
	v_pk_mul_f32 v[34:35], v[26:27], v[4:5] op_sel_hi:[0,1]
	v_pk_fma_f32 v[102:103], v[100:101], v[40:41], v[32:33] op_sel_hi:[0,1,1]
	v_pk_mul_f32 v[32:33], v[26:27], v[2:3] op_sel_hi:[0,1]
	v_exp_f32_e32 v32, v32
	v_exp_f32_e32 v33, v33
	v_exp_f32_e32 v34, v34
	v_exp_f32_e32 v35, v35
	s_waitcnt lgkmcnt(10)
	v_pk_fma_f32 v[30:31], v[54:55], v[114:115], v[30:31]
	v_pk_mul_f32 v[32:33], v[32:33], v[104:105]
	v_pk_fma_f32 v[30:31], v[56:57], v[102:103], v[30:31]
	v_pk_fma_f32 v[104:105], v[100:101], v[42:43], v[32:33] op_sel_hi:[0,1,1]
	v_pk_mul_f32 v[32:33], v[34:35], v[98:99]
	s_waitcnt lgkmcnt(9)
	v_pk_fma_f32 v[30:31], v[58:59], v[104:105], v[30:31]
	v_pk_fma_f32 v[98:99], v[100:101], v[44:45], v[32:33] op_sel_hi:[0,1,1]
	v_pk_fma_f32 v[30:31], v[60:61], v[98:99], v[30:31]
	s_nop 0
	v_add_f32_e32 v26, v30, v31
	v_fma_mix_f32 v18, v1, v18, v26 op_sel:[0,1,0] op_sel_hi:[0,1,0]
	v_fma_mixlo_f16 v18, v18, v22, 0 op_sel:[0,1,0] op_sel_hi:[0,1,0]
	ds_write_b16 v68, v18 offset:30096
	ds_read_b128 v[30:33], v67 offset:3456
	ds_read_b128 v[34:37], v67 offset:3472
	ds_read_b128 v[38:41], v67 offset:3488
	ds_read_b128 v[42:45], v67 offset:3504
	ds_read_b128 v[46:49], v67 offset:3520
	ds_read_b128 v[50:53], v67 offset:3536
	ds_read_b128 v[54:57], v67 offset:3552
	ds_read_b128 v[58:61], v67 offset:3568
	v_cvt_f32_f16_e32 v18, v27
	v_cvt_f32_f16_e32 v22, v19
	v_pk_mul_f32 v[100:101], v[18:19], v[14:15] op_sel_hi:[0,1]
	v_exp_f32_e32 v100, v100
	v_exp_f32_e32 v101, v101
	v_pk_mul_f32 v[116:117], v[18:19], v[16:17] op_sel_hi:[0,1]
	v_exp_f32_e32 v116, v116
	v_exp_f32_e32 v117, v117
	v_mul_f32_e32 v22, v18, v22
	v_pk_mul_f32 v[100:101], v[100:101], v[106:107]
	s_waitcnt lgkmcnt(14)
	v_pk_fma_f32 v[100:101], v[22:23], v[62:63], v[100:101] op_sel_hi:[0,1,1]
	s_waitcnt lgkmcnt(12)
	v_pk_fma_f32 v[62:63], v[82:83], v[100:101], 0 op_sel_hi:[1,1,0]
	v_pk_mul_f32 v[82:83], v[116:117], v[108:109]
	s_nop 0
	v_pk_fma_f32 v[106:107], v[22:23], v[64:65], v[82:83] op_sel_hi:[0,1,1]
	v_pk_mul_f32 v[64:65], v[18:19], v[10:11] op_sel_hi:[0,1]
	v_exp_f32_e32 v64, v64
	v_exp_f32_e32 v65, v65
	v_pk_mul_f32 v[82:83], v[18:19], v[12:13] op_sel_hi:[0,1]
	v_exp_f32_e32 v82, v82
	v_exp_f32_e32 v83, v83
	v_pk_mul_f32 v[64:65], v[64:65], v[110:111]
	v_pk_fma_f32 v[62:63], v[84:85], v[106:107], v[62:63]
	v_pk_fma_f32 v[108:109], v[22:23], v[70:71], v[64:65] op_sel_hi:[0,1,1]
	v_pk_mul_f32 v[64:65], v[82:83], v[112:113]
	v_pk_mul_f32 v[70:71], v[18:19], v[8:9] op_sel_hi:[0,1]
	v_pk_fma_f32 v[110:111], v[22:23], v[72:73], v[64:65] op_sel_hi:[0,1,1]
	v_pk_mul_f32 v[64:65], v[18:19], v[6:7] op_sel_hi:[0,1]
	v_exp_f32_e32 v64, v64
	v_exp_f32_e32 v65, v65
	v_exp_f32_e32 v70, v70
	v_exp_f32_e32 v71, v71
	s_waitcnt lgkmcnt(11)
	v_pk_fma_f32 v[62:63], v[86:87], v[108:109], v[62:63]
	v_pk_mul_f32 v[64:65], v[64:65], v[114:115]
	v_pk_fma_f32 v[62:63], v[88:89], v[110:111], v[62:63]
	v_pk_fma_f32 v[112:113], v[22:23], v[74:75], v[64:65] op_sel_hi:[0,1,1]
	v_pk_mul_f32 v[64:65], v[70:71], v[102:103]
	v_pk_mul_f32 v[70:71], v[18:19], v[4:5] op_sel_hi:[0,1]
	v_pk_fma_f32 v[102:103], v[22:23], v[76:77], v[64:65] op_sel_hi:[0,1,1]
	v_pk_mul_f32 v[64:65], v[18:19], v[2:3] op_sel_hi:[0,1]
	v_exp_f32_e32 v64, v64
	v_exp_f32_e32 v65, v65
	v_exp_f32_e32 v70, v70
	v_exp_f32_e32 v71, v71
	s_waitcnt lgkmcnt(10)
	v_pk_fma_f32 v[62:63], v[90:91], v[112:113], v[62:63]
	v_pk_mul_f32 v[64:65], v[64:65], v[104:105]
	v_pk_fma_f32 v[62:63], v[92:93], v[102:103], v[62:63]
	v_pk_fma_f32 v[104:105], v[22:23], v[78:79], v[64:65] op_sel_hi:[0,1,1]
	v_pk_mul_f32 v[64:65], v[70:71], v[98:99]
	s_waitcnt lgkmcnt(9)
	v_pk_fma_f32 v[62:63], v[94:95], v[104:105], v[62:63]
	v_pk_fma_f32 v[98:99], v[22:23], v[80:81], v[64:65] op_sel_hi:[0,1,1]
	v_pk_fma_f32 v[62:63], v[96:97], v[98:99], v[62:63]
	s_nop 0
	v_add_f32_e32 v18, v62, v63
	v_fma_mix_f32 v18, v1, v19, v18 op_sel_hi:[0,1,0]
	v_fma_mixlo_f16 v18, v18, v23, 0 op_sel_hi:[0,1,0]
	ds_write_b16 v68, v18 offset:31136
	ds_read_b128 v[62:65], v67 offset:3584
	ds_read_b128 v[70:73], v67 offset:3600
	ds_read_b128 v[74:77], v67 offset:3616
	ds_read_b128 v[78:81], v67 offset:3632
	ds_read_b128 v[82:85], v67 offset:3648
	ds_read_b128 v[86:89], v67 offset:3664
	ds_read_b128 v[90:93], v67 offset:3680
	ds_read_b128 v[94:97], v67 offset:3696
	v_cvt_f32_f16_sdwa v18, v27 dst_sel:DWORD dst_unused:UNUSED_PAD src0_sel:WORD_1
	v_cvt_f32_f16_sdwa v22, v19 dst_sel:DWORD dst_unused:UNUSED_PAD src0_sel:WORD_1
	v_pk_mul_f32 v[26:27], v[18:19], v[14:15] op_sel_hi:[0,1]
	v_exp_f32_e32 v26, v26
	v_exp_f32_e32 v27, v27
	v_pk_mul_f32 v[114:115], v[18:19], v[16:17] op_sel_hi:[0,1]
	v_exp_f32_e32 v114, v114
	v_exp_f32_e32 v115, v115
	v_mul_f32_e32 v22, v18, v22
	v_pk_mul_f32 v[26:27], v[26:27], v[100:101]
	s_waitcnt lgkmcnt(14)
	v_pk_fma_f32 v[26:27], v[22:23], v[30:31], v[26:27] op_sel_hi:[0,1,1]
	s_waitcnt lgkmcnt(12)
	v_pk_fma_f32 v[30:31], v[46:47], v[26:27], 0 op_sel_hi:[1,1,0]
	v_pk_mul_f32 v[46:47], v[114:115], v[106:107]
	s_nop 0
	v_pk_fma_f32 v[100:101], v[22:23], v[32:33], v[46:47] op_sel_hi:[0,1,1]
	v_pk_mul_f32 v[32:33], v[18:19], v[10:11] op_sel_hi:[0,1]
	v_exp_f32_e32 v32, v32
	v_exp_f32_e32 v33, v33
	v_pk_mul_f32 v[46:47], v[18:19], v[12:13] op_sel_hi:[0,1]
	v_exp_f32_e32 v46, v46
	v_exp_f32_e32 v47, v47
	v_pk_mul_f32 v[32:33], v[32:33], v[108:109]
	v_pk_fma_f32 v[30:31], v[48:49], v[100:101], v[30:31]
	v_pk_fma_f32 v[106:107], v[22:23], v[34:35], v[32:33] op_sel_hi:[0,1,1]
	v_pk_mul_f32 v[32:33], v[46:47], v[110:111]
	v_pk_mul_f32 v[34:35], v[18:19], v[8:9] op_sel_hi:[0,1]
	v_pk_fma_f32 v[108:109], v[22:23], v[36:37], v[32:33] op_sel_hi:[0,1,1]
	v_pk_mul_f32 v[32:33], v[18:19], v[6:7] op_sel_hi:[0,1]
	v_exp_f32_e32 v32, v32
	v_exp_f32_e32 v33, v33
	v_exp_f32_e32 v34, v34
	v_exp_f32_e32 v35, v35
	s_waitcnt lgkmcnt(11)
	v_pk_fma_f32 v[30:31], v[50:51], v[106:107], v[30:31]
	v_pk_mul_f32 v[32:33], v[32:33], v[112:113]
	v_pk_fma_f32 v[30:31], v[52:53], v[108:109], v[30:31]
	v_pk_fma_f32 v[110:111], v[22:23], v[38:39], v[32:33] op_sel_hi:[0,1,1]
	v_pk_mul_f32 v[32:33], v[34:35], v[102:103]
	v_pk_mul_f32 v[34:35], v[18:19], v[4:5] op_sel_hi:[0,1]
	v_pk_fma_f32 v[102:103], v[22:23], v[40:41], v[32:33] op_sel_hi:[0,1,1]
	v_pk_mul_f32 v[32:33], v[18:19], v[2:3] op_sel_hi:[0,1]
	v_exp_f32_e32 v32, v32
	v_exp_f32_e32 v33, v33
	v_exp_f32_e32 v34, v34
	v_exp_f32_e32 v35, v35
	s_waitcnt lgkmcnt(10)
	v_pk_fma_f32 v[30:31], v[54:55], v[110:111], v[30:31]
	v_pk_mul_f32 v[32:33], v[32:33], v[104:105]
	v_pk_fma_f32 v[30:31], v[56:57], v[102:103], v[30:31]
	v_pk_fma_f32 v[104:105], v[22:23], v[42:43], v[32:33] op_sel_hi:[0,1,1]
	v_pk_mul_f32 v[32:33], v[34:35], v[98:99]
	s_waitcnt lgkmcnt(9)
	v_pk_fma_f32 v[30:31], v[58:59], v[104:105], v[30:31]
	v_pk_fma_f32 v[98:99], v[22:23], v[44:45], v[32:33] op_sel_hi:[0,1,1]
	v_pk_fma_f32 v[30:31], v[60:61], v[98:99], v[30:31]
	s_nop 0
	v_add_f32_e32 v18, v30, v31
	v_fma_mix_f32 v18, v1, v19, v18 op_sel:[0,1,0] op_sel_hi:[0,1,0]
	v_fma_mixlo_f16 v18, v18, v23, 0 op_sel:[0,1,0] op_sel_hi:[0,1,0]
	ds_write_b16 v68, v18 offset:32176
	ds_read_b128 v[30:33], v67 offset:3712
	ds_read_b128 v[34:37], v67 offset:3728
	ds_read_b128 v[38:41], v67 offset:3744
	ds_read_b128 v[42:45], v67 offset:3760
	ds_read_b128 v[46:49], v67 offset:3776
	ds_read_b128 v[50:53], v67 offset:3792
	ds_read_b128 v[54:57], v67 offset:3808
	ds_read_b128 v[58:61], v67 offset:3824
	v_cvt_f32_f16_e32 v18, v28
	v_cvt_f32_f16_e32 v19, v20
	v_pk_mul_f32 v[112:113], v[18:19], v[14:15] op_sel_hi:[0,1]
	v_exp_f32_e32 v112, v112
	v_exp_f32_e32 v113, v113
	v_pk_mul_f32 v[114:115], v[18:19], v[16:17] op_sel_hi:[0,1]
	v_exp_f32_e32 v114, v114
	v_exp_f32_e32 v115, v115
	v_mul_f32_e32 v22, v18, v19
	v_pk_mul_f32 v[26:27], v[112:113], v[26:27]
	s_waitcnt lgkmcnt(14)
	v_pk_fma_f32 v[26:27], v[22:23], v[62:63], v[26:27] op_sel_hi:[0,1,1]
	s_waitcnt lgkmcnt(12)
	v_pk_fma_f32 v[62:63], v[82:83], v[26:27], 0 op_sel_hi:[1,1,0]
	v_pk_mul_f32 v[82:83], v[114:115], v[100:101]
	s_nop 0
	v_pk_fma_f32 v[100:101], v[22:23], v[64:65], v[82:83] op_sel_hi:[0,1,1]
	v_pk_mul_f32 v[64:65], v[18:19], v[10:11] op_sel_hi:[0,1]
	v_exp_f32_e32 v64, v64
	v_exp_f32_e32 v65, v65
	v_pk_mul_f32 v[82:83], v[18:19], v[12:13] op_sel_hi:[0,1]
	v_exp_f32_e32 v82, v82
	v_exp_f32_e32 v83, v83
	v_pk_mul_f32 v[64:65], v[64:65], v[106:107]
	v_pk_fma_f32 v[62:63], v[84:85], v[100:101], v[62:63]
	v_pk_fma_f32 v[106:107], v[22:23], v[70:71], v[64:65] op_sel_hi:[0,1,1]
	v_pk_mul_f32 v[64:65], v[82:83], v[108:109]
	v_pk_mul_f32 v[70:71], v[18:19], v[8:9] op_sel_hi:[0,1]
	v_pk_fma_f32 v[108:109], v[22:23], v[72:73], v[64:65] op_sel_hi:[0,1,1]
	v_pk_mul_f32 v[64:65], v[18:19], v[6:7] op_sel_hi:[0,1]
	v_exp_f32_e32 v64, v64
	v_exp_f32_e32 v65, v65
	v_exp_f32_e32 v70, v70
	v_exp_f32_e32 v71, v71
	s_waitcnt lgkmcnt(11)
	v_pk_fma_f32 v[62:63], v[86:87], v[106:107], v[62:63]
	v_pk_mul_f32 v[64:65], v[64:65], v[110:111]
	v_pk_fma_f32 v[62:63], v[88:89], v[108:109], v[62:63]
	v_pk_fma_f32 v[110:111], v[22:23], v[74:75], v[64:65] op_sel_hi:[0,1,1]
	v_pk_mul_f32 v[64:65], v[70:71], v[102:103]
	s_waitcnt lgkmcnt(10)
	v_pk_fma_f32 v[62:63], v[90:91], v[110:111], v[62:63]
	v_pk_fma_f32 v[102:103], v[22:23], v[76:77], v[64:65] op_sel_hi:[0,1,1]
	v_pk_mul_f32 v[64:65], v[18:19], v[2:3] op_sel_hi:[0,1]
	v_exp_f32_e32 v64, v64
	v_exp_f32_e32 v65, v65
	v_pk_mul_f32 v[18:19], v[18:19], v[4:5] op_sel_hi:[0,1]
	v_exp_f32_e32 v18, v18
	v_exp_f32_e32 v19, v19
	v_pk_mul_f32 v[64:65], v[64:65], v[104:105]
	v_pk_fma_f32 v[62:63], v[92:93], v[102:103], v[62:63]
	v_pk_fma_f32 v[104:105], v[22:23], v[78:79], v[64:65] op_sel_hi:[0,1,1]
	v_pk_mul_f32 v[18:19], v[18:19], v[98:99]
	s_waitcnt lgkmcnt(9)
	v_pk_fma_f32 v[62:63], v[94:95], v[104:105], v[62:63]
	v_pk_fma_f32 v[18:19], v[22:23], v[80:81], v[18:19] op_sel_hi:[0,1,1]
	v_pk_fma_f32 v[22:23], v[96:97], v[18:19], v[62:63]
	s_nop 0
	v_add_f32_e32 v22, v22, v23
	v_fma_mix_f32 v22, v1, v20, v22 op_sel_hi:[0,1,0]
	v_fma_mixlo_f16 v22, v22, v24, 0 op_sel_hi:[0,1,0]
	ds_write_b16 v68, v22 offset:33216
	ds_read_b128 v[62:65], v67 offset:3840
	ds_read_b128 v[70:73], v67 offset:3856
	ds_read_b128 v[74:77], v67 offset:3872
	ds_read_b128 v[78:81], v67 offset:3888
	ds_read_b128 v[82:85], v67 offset:3904
	ds_read_b128 v[86:89], v67 offset:3920
	ds_read_b128 v[90:93], v67 offset:3936
	ds_read_b128 v[94:97], v67 offset:3952
	v_cvt_f32_f16_sdwa v22, v28 dst_sel:DWORD dst_unused:UNUSED_PAD src0_sel:WORD_1
	v_cvt_f32_f16_sdwa v23, v20 dst_sel:DWORD dst_unused:UNUSED_PAD src0_sel:WORD_1
	v_pk_mul_f32 v[98:99], v[22:23], v[14:15] op_sel_hi:[0,1]
	v_exp_f32_e32 v98, v98
	v_exp_f32_e32 v99, v99
	v_pk_mul_f32 v[112:113], v[22:23], v[16:17] op_sel_hi:[0,1]
	v_exp_f32_e32 v112, v112
	v_exp_f32_e32 v113, v113
	v_mul_f32_e32 v28, v22, v23
	v_pk_mul_f32 v[26:27], v[98:99], v[26:27]
	s_waitcnt lgkmcnt(14)
	v_pk_fma_f32 v[26:27], v[28:29], v[30:31], v[26:27] op_sel_hi:[0,1,1]
	s_waitcnt lgkmcnt(12)
	v_pk_fma_f32 v[30:31], v[46:47], v[26:27], 0 op_sel_hi:[1,1,0]
	v_pk_mul_f32 v[46:47], v[112:113], v[100:101]
	s_nop 0
	v_pk_fma_f32 v[98:99], v[28:29], v[32:33], v[46:47] op_sel_hi:[0,1,1]
	v_pk_mul_f32 v[32:33], v[22:23], v[10:11] op_sel_hi:[0,1]
	v_exp_f32_e32 v32, v32
	v_exp_f32_e32 v33, v33
	v_pk_mul_f32 v[46:47], v[22:23], v[12:13] op_sel_hi:[0,1]
	v_exp_f32_e32 v46, v46
	v_exp_f32_e32 v47, v47
	v_pk_mul_f32 v[32:33], v[32:33], v[106:107]
	v_pk_fma_f32 v[30:31], v[48:49], v[98:99], v[30:31]
	v_pk_fma_f32 v[100:101], v[28:29], v[34:35], v[32:33] op_sel_hi:[0,1,1]
	v_pk_mul_f32 v[32:33], v[46:47], v[108:109]
	v_pk_mul_f32 v[34:35], v[22:23], v[8:9] op_sel_hi:[0,1]
	v_pk_fma_f32 v[106:107], v[28:29], v[36:37], v[32:33] op_sel_hi:[0,1,1]
	v_pk_mul_f32 v[32:33], v[22:23], v[6:7] op_sel_hi:[0,1]
	v_exp_f32_e32 v32, v32
	v_exp_f32_e32 v33, v33
	v_exp_f32_e32 v34, v34
	v_exp_f32_e32 v35, v35
	s_waitcnt lgkmcnt(11)
	v_pk_fma_f32 v[30:31], v[50:51], v[100:101], v[30:31]
	v_pk_mul_f32 v[32:33], v[32:33], v[110:111]
	v_pk_fma_f32 v[30:31], v[52:53], v[106:107], v[30:31]
	v_pk_fma_f32 v[108:109], v[28:29], v[38:39], v[32:33] op_sel_hi:[0,1,1]
	v_pk_mul_f32 v[32:33], v[34:35], v[102:103]
	s_waitcnt lgkmcnt(10)
	v_pk_fma_f32 v[30:31], v[54:55], v[108:109], v[30:31]
	v_pk_fma_f32 v[102:103], v[28:29], v[40:41], v[32:33] op_sel_hi:[0,1,1]
	v_pk_mul_f32 v[32:33], v[22:23], v[2:3] op_sel_hi:[0,1]
	v_exp_f32_e32 v32, v32
	v_exp_f32_e32 v33, v33
	v_pk_mul_f32 v[22:23], v[22:23], v[4:5] op_sel_hi:[0,1]
	v_exp_f32_e32 v22, v22
	v_exp_f32_e32 v23, v23
	v_pk_mul_f32 v[32:33], v[32:33], v[104:105]
	v_pk_fma_f32 v[30:31], v[56:57], v[102:103], v[30:31]
	v_pk_fma_f32 v[104:105], v[28:29], v[42:43], v[32:33] op_sel_hi:[0,1,1]
	v_pk_mul_f32 v[18:19], v[22:23], v[18:19]
	s_waitcnt lgkmcnt(9)
	v_pk_fma_f32 v[30:31], v[58:59], v[104:105], v[30:31]
	v_pk_fma_f32 v[18:19], v[28:29], v[44:45], v[18:19] op_sel_hi:[0,1,1]
	v_pk_fma_f32 v[22:23], v[60:61], v[18:19], v[30:31]
	s_nop 0
	v_add_f32_e32 v22, v22, v23
	v_fma_mix_f32 v20, v1, v20, v22 op_sel:[0,1,0] op_sel_hi:[0,1,0]
	v_fma_mixlo_f16 v20, v20, v24, 0 op_sel:[0,1,0] op_sel_hi:[0,1,0]
	ds_write_b16 v68, v20 offset:34256
	ds_read_b128 v[30:33], v67 offset:3968
	ds_read_b128 v[34:37], v67 offset:3984
	ds_read_b128 v[38:41], v67 offset:4000
	ds_read_b128 v[42:45], v67 offset:4016
	ds_read_b128 v[46:49], v67 offset:4032
	ds_read_b128 v[50:53], v67 offset:4048
	ds_read_b128 v[54:57], v67 offset:4064
	ds_read_b128 v[58:61], v67 offset:4080
	v_cvt_f32_f16_e32 v20, v29
	v_cvt_f32_f16_e32 v22, v21
	v_pk_mul_f32 v[110:111], v[20:21], v[14:15] op_sel_hi:[0,1]
	v_exp_f32_e32 v110, v110
	v_exp_f32_e32 v111, v111
	v_pk_mul_f32 v[112:113], v[20:21], v[16:17] op_sel_hi:[0,1]
	v_exp_f32_e32 v112, v112
	v_exp_f32_e32 v113, v113
	v_mul_f32_e32 v22, v20, v22
	v_pk_mul_f32 v[26:27], v[110:111], v[26:27]
	s_waitcnt lgkmcnt(14)
	v_pk_fma_f32 v[26:27], v[22:23], v[62:63], v[26:27] op_sel_hi:[0,1,1]
	s_waitcnt lgkmcnt(12)
	v_pk_fma_f32 v[62:63], v[82:83], v[26:27], 0 op_sel_hi:[1,1,0]
	v_pk_mul_f32 v[82:83], v[112:113], v[98:99]
	s_nop 0
	v_pk_fma_f32 v[64:65], v[22:23], v[64:65], v[82:83] op_sel_hi:[0,1,1]
	v_pk_mul_f32 v[82:83], v[20:21], v[10:11] op_sel_hi:[0,1]
	v_pk_fma_f32 v[62:63], v[84:85], v[64:65], v[62:63]
	v_exp_f32_e32 v82, v82
	v_exp_f32_e32 v83, v83
	v_pk_mul_f32 v[84:85], v[20:21], v[12:13] op_sel_hi:[0,1]
	v_exp_f32_e32 v84, v84
	v_exp_f32_e32 v85, v85
	v_pk_mul_f32 v[82:83], v[82:83], v[100:101]
	s_nop 0
	v_pk_fma_f32 v[70:71], v[22:23], v[70:71], v[82:83] op_sel_hi:[0,1,1]
	v_pk_mul_f32 v[82:83], v[84:85], v[106:107]
	v_pk_mul_f32 v[84:85], v[20:21], v[8:9] op_sel_hi:[0,1]
	v_pk_fma_f32 v[72:73], v[22:23], v[72:73], v[82:83] op_sel_hi:[0,1,1]
	v_pk_mul_f32 v[82:83], v[20:21], v[6:7] op_sel_hi:[0,1]
	v_exp_f32_e32 v82, v82
	v_exp_f32_e32 v83, v83
	v_exp_f32_e32 v84, v84
	v_exp_f32_e32 v85, v85
	s_waitcnt lgkmcnt(11)
	v_pk_fma_f32 v[62:63], v[86:87], v[70:71], v[62:63]
	v_pk_mul_f32 v[82:83], v[82:83], v[108:109]
	v_pk_fma_f32 v[62:63], v[88:89], v[72:73], v[62:63]
	v_pk_fma_f32 v[74:75], v[22:23], v[74:75], v[82:83] op_sel_hi:[0,1,1]
	v_pk_mul_f32 v[82:83], v[84:85], v[102:103]
	v_pk_mul_f32 v[84:85], v[20:21], v[4:5] op_sel_hi:[0,1]
	v_pk_fma_f32 v[76:77], v[22:23], v[76:77], v[82:83] op_sel_hi:[0,1,1]
	v_pk_mul_f32 v[82:83], v[20:21], v[2:3] op_sel_hi:[0,1]
	v_exp_f32_e32 v82, v82
	v_exp_f32_e32 v83, v83
	v_exp_f32_e32 v84, v84
	v_exp_f32_e32 v85, v85
	s_waitcnt lgkmcnt(10)
	v_pk_fma_f32 v[62:63], v[90:91], v[74:75], v[62:63]
	v_pk_mul_f32 v[82:83], v[82:83], v[104:105]
	v_pk_fma_f32 v[62:63], v[92:93], v[76:77], v[62:63]
	v_pk_fma_f32 v[78:79], v[22:23], v[78:79], v[82:83] op_sel_hi:[0,1,1]
	v_pk_mul_f32 v[18:19], v[84:85], v[18:19]
	s_waitcnt lgkmcnt(9)
	v_pk_fma_f32 v[62:63], v[94:95], v[78:79], v[62:63]
	v_pk_fma_f32 v[18:19], v[22:23], v[80:81], v[18:19] op_sel_hi:[0,1,1]
	v_pk_fma_f32 v[22:23], v[96:97], v[18:19], v[62:63]
	s_nop 0
	v_add_f32_e32 v20, v22, v23
	v_fma_mix_f32 v20, v1, v21, v20 op_sel_hi:[0,1,0]
	v_fma_mixlo_f16 v20, v20, v25, 0 op_sel_hi:[0,1,0]
	ds_write_b16 v68, v20 offset:35296
	v_cvt_f32_f16_sdwa v20, v29 dst_sel:DWORD dst_unused:UNUSED_PAD src0_sel:WORD_1
	v_cvt_f32_f16_sdwa v22, v21 dst_sel:DWORD dst_unused:UNUSED_PAD src0_sel:WORD_1
	v_pk_mul_f32 v[14:15], v[20:21], v[14:15] op_sel_hi:[0,1]
	v_exp_f32_e32 v14, v14
	v_exp_f32_e32 v15, v15
	v_pk_mul_f32 v[16:17], v[20:21], v[16:17] op_sel_hi:[0,1]
	v_exp_f32_e32 v16, v16
	v_exp_f32_e32 v17, v17
	v_pk_mul_f32 v[10:11], v[20:21], v[10:11] op_sel_hi:[0,1]
	v_exp_f32_e32 v10, v10
	v_exp_f32_e32 v11, v11
	v_pk_mul_f32 v[12:13], v[20:21], v[12:13] op_sel_hi:[0,1]
	v_exp_f32_e32 v12, v12
	v_exp_f32_e32 v13, v13
	v_pk_mul_f32 v[6:7], v[20:21], v[6:7] op_sel_hi:[0,1]
	v_mul_f32_e32 v22, v20, v22
	v_pk_mul_f32 v[14:15], v[14:15], v[26:27]
	v_exp_f32_e32 v6, v6
	v_exp_f32_e32 v7, v7
	v_pk_mul_f32 v[8:9], v[20:21], v[8:9] op_sel_hi:[0,1]
	s_waitcnt lgkmcnt(8)
	v_pk_fma_f32 v[14:15], v[22:23], v[30:31], v[14:15] op_sel_hi:[0,1,1]
	v_pk_mul_f32 v[16:17], v[16:17], v[64:65]
	v_exp_f32_e32 v8, v8
	v_exp_f32_e32 v9, v9
	v_pk_mul_f32 v[2:3], v[20:21], v[2:3] op_sel_hi:[0,1]
	s_waitcnt lgkmcnt(4)
	v_pk_fma_f32 v[14:15], v[46:47], v[14:15], 0 op_sel_hi:[1,1,0]
	v_pk_fma_f32 v[16:17], v[22:23], v[32:33], v[16:17] op_sel_hi:[0,1,1]
	v_pk_mul_f32 v[10:11], v[10:11], v[70:71]
	v_exp_f32_e32 v2, v2
	v_exp_f32_e32 v3, v3
	v_pk_mul_f32 v[4:5], v[20:21], v[4:5] op_sel_hi:[0,1]
	v_pk_fma_f32 v[14:15], v[48:49], v[16:17], v[14:15]
	v_pk_fma_f32 v[10:11], v[22:23], v[34:35], v[10:11] op_sel_hi:[0,1,1]
	v_pk_mul_f32 v[12:13], v[12:13], v[72:73]
	v_exp_f32_e32 v4, v4
	v_exp_f32_e32 v5, v5
	s_waitcnt lgkmcnt(3)
	v_pk_fma_f32 v[10:11], v[50:51], v[10:11], v[14:15]
	v_pk_fma_f32 v[12:13], v[22:23], v[36:37], v[12:13] op_sel_hi:[0,1,1]
	v_pk_mul_f32 v[6:7], v[6:7], v[74:75]
	v_pk_fma_f32 v[10:11], v[52:53], v[12:13], v[10:11]
	v_pk_fma_f32 v[6:7], v[22:23], v[38:39], v[6:7] op_sel_hi:[0,1,1]
	v_pk_mul_f32 v[8:9], v[8:9], v[76:77]
	s_waitcnt lgkmcnt(2)
	v_pk_fma_f32 v[6:7], v[54:55], v[6:7], v[10:11]
	v_pk_fma_f32 v[8:9], v[22:23], v[40:41], v[8:9] op_sel_hi:[0,1,1]
	v_pk_mul_f32 v[2:3], v[2:3], v[78:79]
	v_pk_fma_f32 v[6:7], v[56:57], v[8:9], v[6:7]
	v_pk_fma_f32 v[2:3], v[22:23], v[42:43], v[2:3] op_sel_hi:[0,1,1]
	v_pk_mul_f32 v[4:5], v[4:5], v[18:19]
	s_waitcnt lgkmcnt(1)
	v_pk_fma_f32 v[2:3], v[58:59], v[2:3], v[6:7]
	v_pk_fma_f32 v[4:5], v[22:23], v[44:45], v[4:5] op_sel_hi:[0,1,1]
	v_pk_fma_f32 v[2:3], v[60:61], v[4:5], v[2:3]
	s_nop 0
	v_add_f32_e32 v2, v2, v3
	v_fma_mix_f32 v1, v1, v21, v2 op_sel:[0,1,0] op_sel_hi:[0,1,0]
	v_fma_mixlo_f16 v1, v1, v25, 0 op_sel:[0,1,0] op_sel_hi:[0,1,0]
	ds_write_b16 v68, v1 offset:36336
	v_lshlrev_b32_e32 v1, 9, v0
	v_and_b32_e32 v2, 0x38000, v1
	v_mov_b32_e32 v3, v67
	v_and_b32_e32 v1, 63, v0
	s_bfe_u32 s14, s2, 0x40003
	v_lshl_add_u64 v[2:3], s[18:19], 0, v[2:3]
	v_lshlrev_b32_e32 v58, 4, v1
	v_mov_b32_e32 v59, v67
	s_lshl_b32 s13, s14, 6
	v_lshl_add_u64 v[20:21], v[2:3], 0, v[58:59]
	s_lshl_b32 s26, s14, 10
	s_add_i32 s12, s13, 64
	v_lshl_add_u64 v[2:3], v[20:21], 0, s[26:27]
	s_and_b32 s15, s12, 0x3c0
	v_add_co_u32_e32 v4, vcc, s52, v2
	s_lshl_b32 s26, s15, 4
	s_lshl_b32 s12, s12, 4
	v_addc_co_u32_e32 v5, vcc, 0, v3, vcc
	global_load_dwordx4 v[28:31], v[2:3], off
	global_load_dwordx4 v[32:35], v[4:5], off
	v_lshl_add_u64 v[2:3], v[20:21], 0, s[26:27]
	s_or_b32 s26, s12, 0x4000
	s_add_i32 s12, s13, 0x80
	s_and_b32 s15, s12, 0x3c0
	v_lshl_add_u64 v[4:5], v[20:21], 0, s[26:27]
	s_lshl_b32 s26, s15, 4
	s_lshl_b32 s12, s12, 4
	global_load_dwordx4 v[36:39], v[2:3], off
	global_load_dwordx4 v[40:43], v[4:5], off
	v_lshl_add_u64 v[2:3], v[20:21], 0, s[26:27]
	s_or_b32 s26, s12, 0x4000
	s_add_i32 s12, s13, 0xc0
	s_and_b32 s15, s12, 0x3c0
	v_lshl_add_u64 v[4:5], v[20:21], 0, s[26:27]
	s_lshl_b32 s26, s15, 4
	s_lshl_b32 s12, s12, 4
	global_load_dwordx4 v[44:47], v[2:3], off
	global_load_dwordx4 v[48:51], v[4:5], off
	v_lshl_add_u64 v[2:3], v[20:21], 0, s[26:27]
	s_or_b32 s26, s12, 0x4000
	s_add_i32 s12, s13, 0x100
	s_and_b32 s15, s12, 0x3c0
	v_lshl_add_u64 v[4:5], v[20:21], 0, s[26:27]
	s_lshl_b32 s26, s15, 4
	s_lshl_b32 s12, s12, 4
	global_load_dwordx4 v[52:55], v[2:3], off
	global_load_dwordx4 v[60:63], v[4:5], off
	v_lshl_add_u64 v[2:3], v[20:21], 0, s[26:27]
	s_or_b32 s26, s12, 0x4000
	s_add_i32 s12, s13, 0x140
	s_and_b32 s15, s12, 0x3c0
	v_lshl_add_u64 v[4:5], v[20:21], 0, s[26:27]
	s_lshl_b32 s26, s15, 4
	s_lshl_b32 s12, s12, 4
	global_load_dwordx4 v[68:71], v[2:3], off
	global_load_dwordx4 v[72:75], v[4:5], off
	v_lshl_add_u64 v[2:3], v[20:21], 0, s[26:27]
	s_or_b32 s26, s12, 0x4000
	s_add_i32 s12, s13, 0x180
	s_and_b32 s15, s12, 0x3c0
	v_lshl_add_u64 v[4:5], v[20:21], 0, s[26:27]
	s_lshl_b32 s26, s15, 4
	s_lshl_b32 s12, s12, 4
	global_load_dwordx4 v[76:79], v[2:3], off
	global_load_dwordx4 v[82:85], v[4:5], off
	v_lshl_add_u64 v[2:3], v[20:21], 0, s[26:27]
	s_or_b32 s26, s12, 0x4000
	s_add_i32 s12, s13, 0x1c0
	s_and_b32 s15, s12, 0x3c0
	v_lshl_add_u64 v[4:5], v[20:21], 0, s[26:27]
	s_lshl_b32 s26, s15, 4
	s_lshl_b32 s12, s12, 4
	v_lshl_add_u64 v[18:19], v[20:21], 0, s[26:27]
	s_or_b32 s26, s12, 0x4000
	s_xor_b32 s15, s13, 0x200
	v_lshl_add_u64 v[22:23], v[20:21], 0, s[26:27]
	s_lshl_b32 s26, s15, 4
	global_load_dwordx4 v[14:17], v[2:3], off
	global_load_dwordx4 v[10:13], v[4:5], off
	global_load_dwordx4 v[6:9], v[18:19], off
	s_nop 0
	global_load_dwordx4 v[2:5], v[22:23], off
	v_lshl_add_u64 v[18:19], v[20:21], 0, s[26:27]
	v_add_co_u32_e32 v22, vcc, s52, v18
	s_waitcnt lgkmcnt(0)
	s_barrier
	v_addc_co_u32_e32 v23, vcc, 0, v19, vcc
	global_load_dwordx4 v[86:89], v[18:19], off
	global_load_dwordx4 v[90:93], v[22:23], off
	v_lshrrev_b32_e32 v118, 6, v0
	v_lshlrev_b32_e32 v22, 7, v118
	v_mov_b32_e32 v23, v67
	v_and_b32_e32 v81, 15, v0
	v_lshl_add_u64 v[24:25], s[4:5], 0, v[22:23]
	v_and_b32_e32 v18, 48, v0
	v_mov_b32_e32 v19, v67
	s_movk_i32 s12, 0x410
	v_lshl_add_u64 v[56:57], v[24:25], 0, v[18:19]
	v_mad_u32_u24 v19, v81, s12, v18
	v_add_u32_e32 v23, s13, v19
	ds_read_b128 v[94:97], v23 offset:4096
	ds_read_b128 v[98:101], v23 offset:20736
	v_or_b32_e32 v26, s28, v81
	v_mov_b32_e32 v27, v67
	v_lshlrev_b64 v[24:25], 10, v[26:27]
	v_or_b32_e32 v26, 16, v26
	v_lshlrev_b64 v[26:27], 10, v[26:27]
	v_lshrrev_b32_e32 v23, 1, v0
	v_lshl_add_u64 v[24:25], v[56:57], 0, v[24:25]
	v_lshl_add_u64 v[26:27], v[56:57], 0, v[26:27]
	v_and_b32_e32 v80, 24, v23
	s_lshl_b32 s14, s14, 5
	s_setprio 1
	s_waitcnt vmcnt(17) lgkmcnt(1)
	v_mfma_f32_16x16x32_f16 v[102:105], v[28:31], v[94:97], 0
	s_waitcnt lgkmcnt(0)
	v_mfma_f32_16x16x32_f16 v[28:31], v[28:31], v[98:101], 0
	s_waitcnt vmcnt(16)
	v_mfma_f32_16x16x32_f16 v[94:97], v[32:35], v[94:97], 0
	v_mfma_f32_16x16x32_f16 v[32:35], v[32:35], v[98:101], 0
	s_setprio 0
	s_add_i32 s16, s13, 0x240
	s_and_b32 s17, s16, 0x3c0
	s_lshl_b32 s26, s17, 4
	s_lshl_b32 s16, s16, 4
	v_lshl_add_u64 v[56:57], v[20:21], 0, s[26:27]
	s_or_b32 s26, s16, 0x4000
	v_lshl_add_u64 v[64:65], v[20:21], 0, s[26:27]
	global_load_dwordx4 v[98:101], v[56:57], off
	global_load_dwordx4 v[106:109], v[64:65], off
	s_add_i32 s16, s14, 32
	s_and_b32 s16, s16, 0x1e0
	v_lshl_add_u32 v23, s16, 1, v19
	ds_read_b128 v[110:113], v23 offset:4096
	ds_read_b128 v[114:117], v23 offset:20736
	s_setprio 1
	s_waitcnt vmcnt(17) lgkmcnt(1)
	v_mfma_f32_16x16x32_f16 v[102:105], v[36:39], v[110:113], v[102:105]
	s_waitcnt lgkmcnt(0)
	v_mfma_f32_16x16x32_f16 v[28:31], v[36:39], v[114:117], v[28:31]
	s_waitcnt vmcnt(16)
	v_mfma_f32_16x16x32_f16 v[36:39], v[40:43], v[110:113], v[94:97]
	v_mfma_f32_16x16x32_f16 v[32:35], v[40:43], v[114:117], v[32:35]
	s_setprio 0
	s_add_i32 s16, s13, 0x280
	s_and_b32 s17, s16, 0x3c0
	s_lshl_b32 s26, s17, 4
	s_lshl_b32 s16, s16, 4
	v_lshl_add_u64 v[56:57], v[20:21], 0, s[26:27]
	s_or_b32 s26, s16, 0x4000
	v_lshl_add_u64 v[64:65], v[20:21], 0, s[26:27]
	global_load_dwordx4 v[40:43], v[56:57], off
	global_load_dwordx4 v[94:97], v[64:65], off
	s_add_i32 s16, s14, 64
	s_and_b32 s16, s16, 0x1e0
	v_lshl_add_u32 v23, s16, 1, v19
	ds_read_b128 v[110:113], v23 offset:4096
	ds_read_b128 v[114:117], v23 offset:20736
	s_setprio 1
	s_waitcnt vmcnt(17) lgkmcnt(1)
	v_mfma_f32_16x16x32_f16 v[102:105], v[44:47], v[110:113], v[102:105]
	s_waitcnt lgkmcnt(0)
	v_mfma_f32_16x16x32_f16 v[28:31], v[44:47], v[114:117], v[28:31]
	s_waitcnt vmcnt(16)
	v_mfma_f32_16x16x32_f16 v[36:39], v[48:51], v[110:113], v[36:39]
	v_mfma_f32_16x16x32_f16 v[32:35], v[48:51], v[114:117], v[32:35]
	s_setprio 0
	s_add_i32 s16, s13, 0x2c0
	s_and_b32 s17, s16, 0x3c0
	s_lshl_b32 s26, s17, 4
	s_lshl_b32 s16, s16, 4
	v_lshl_add_u64 v[56:57], v[20:21], 0, s[26:27]
	s_or_b32 s26, s16, 0x4000
	v_lshl_add_u64 v[64:65], v[20:21], 0, s[26:27]
	global_load_dwordx4 v[44:47], v[56:57], off
	global_load_dwordx4 v[48:51], v[64:65], off
	s_add_i32 s16, s14, 0x60
	s_and_b32 s16, s16, 0x1e0
	v_lshl_add_u32 v23, s16, 1, v19
	ds_read_b128 v[110:113], v23 offset:4096
	ds_read_b128 v[114:117], v23 offset:20736
	s_setprio 1
	s_waitcnt vmcnt(17) lgkmcnt(1)
	v_mfma_f32_16x16x32_f16 v[102:105], v[52:55], v[110:113], v[102:105]
	s_waitcnt lgkmcnt(0)
	v_mfma_f32_16x16x32_f16 v[28:31], v[52:55], v[114:117], v[28:31]
	s_waitcnt vmcnt(16)
	v_mfma_f32_16x16x32_f16 v[36:39], v[60:63], v[110:113], v[36:39]
	v_mfma_f32_16x16x32_f16 v[32:35], v[60:63], v[114:117], v[32:35]
	s_setprio 0
	s_add_i32 s16, s13, 0x300
	s_and_b32 s17, s16, 0x3c0
	s_lshl_b32 s26, s17, 4
	s_lshl_b32 s16, s16, 4
	v_lshl_add_u64 v[56:57], v[20:21], 0, s[26:27]
	s_or_b32 s26, s16, 0x4000
	v_lshl_add_u64 v[64:65], v[20:21], 0, s[26:27]
	global_load_dwordx4 v[52:55], v[56:57], off
	global_load_dwordx4 v[60:63], v[64:65], off
	s_add_i32 s16, s14, 0x80
	s_and_b32 s16, s16, 0x1e0
	v_lshl_add_u32 v23, s16, 1, v19
	ds_read_b128 v[110:113], v23 offset:4096
	ds_read_b128 v[114:117], v23 offset:20736
	s_setprio 1
	s_waitcnt vmcnt(17) lgkmcnt(1)
	v_mfma_f32_16x16x32_f16 v[102:105], v[68:71], v[110:113], v[102:105]
	s_waitcnt lgkmcnt(0)
	v_mfma_f32_16x16x32_f16 v[28:31], v[68:71], v[114:117], v[28:31]
	s_waitcnt vmcnt(16)
	v_mfma_f32_16x16x32_f16 v[36:39], v[72:75], v[110:113], v[36:39]
	v_mfma_f32_16x16x32_f16 v[32:35], v[72:75], v[114:117], v[32:35]
	s_setprio 0
	s_add_i32 s16, s13, 0x340
	s_and_b32 s17, s16, 0x3c0
	s_lshl_b32 s26, s17, 4
	s_lshl_b32 s16, s16, 4
	v_lshl_add_u64 v[56:57], v[20:21], 0, s[26:27]
	s_or_b32 s26, s16, 0x4000
	v_lshl_add_u64 v[64:65], v[20:21], 0, s[26:27]
	global_load_dwordx4 v[68:71], v[56:57], off
	global_load_dwordx4 v[72:75], v[64:65], off
	s_add_i32 s16, s14, 0xa0
	s_and_b32 s16, s16, 0x1e0
	v_lshl_add_u32 v23, s16, 1, v19
	ds_read_b128 v[110:113], v23 offset:4096
	ds_read_b128 v[114:117], v23 offset:20736
	s_setprio 1
	s_waitcnt vmcnt(17) lgkmcnt(1)
	v_mfma_f32_16x16x32_f16 v[102:105], v[76:79], v[110:113], v[102:105]
	s_waitcnt lgkmcnt(0)
	v_mfma_f32_16x16x32_f16 v[28:31], v[76:79], v[114:117], v[28:31]
	s_waitcnt vmcnt(16)
	v_mfma_f32_16x16x32_f16 v[36:39], v[82:85], v[110:113], v[36:39]
	v_mfma_f32_16x16x32_f16 v[32:35], v[82:85], v[114:117], v[32:35]
	s_setprio 0
	s_add_i32 s16, s13, 0x380
	s_and_b32 s17, s16, 0x3c0
	s_lshl_b32 s26, s17, 4
	s_lshl_b32 s16, s16, 4
	v_lshl_add_u64 v[56:57], v[20:21], 0, s[26:27]
	s_or_b32 s26, s16, 0x4000
	v_lshl_add_u64 v[64:65], v[20:21], 0, s[26:27]
	global_load_dwordx4 v[76:79], v[56:57], off
	global_load_dwordx4 v[82:85], v[64:65], off
	s_add_i32 s16, s14, 0xc0
	s_and_b32 s16, s16, 0x1e0
	v_lshl_add_u32 v23, s16, 1, v19
	ds_read_b128 v[110:113], v23 offset:4096
	ds_read_b128 v[114:117], v23 offset:20736
	s_setprio 1
	s_waitcnt vmcnt(17) lgkmcnt(1)
	v_mfma_f32_16x16x32_f16 v[102:105], v[14:17], v[110:113], v[102:105]
	s_waitcnt lgkmcnt(0)
	v_mfma_f32_16x16x32_f16 v[14:17], v[14:17], v[114:117], v[28:31]
	s_waitcnt vmcnt(16)
	v_mfma_f32_16x16x32_f16 v[28:31], v[10:13], v[110:113], v[36:39]
	v_mfma_f32_16x16x32_f16 v[10:13], v[10:13], v[114:117], v[32:35]
	s_setprio 0
	s_addk_i32 s13, 0x3c0
	s_and_b32 s16, s13, 0x3c0
	s_lshl_b32 s26, s16, 4
	s_lshl_b32 s13, s13, 4
	v_lshl_add_u64 v[56:57], v[20:21], 0, s[26:27]
	s_or_b32 s26, s13, 0x4000
	v_lshl_add_u64 v[20:21], v[20:21], 0, s[26:27]
	global_load_dwordx4 v[32:35], v[56:57], off
	global_load_dwordx4 v[36:39], v[20:21], off
	s_add_i32 s13, s14, 0xe0
	s_and_b32 s13, s13, 0x1e0
	v_lshl_add_u32 v20, s13, 1, v19
	ds_read_b128 v[110:113], v20 offset:4096
	ds_read_b128 v[114:117], v20 offset:20736
	s_setprio 1
	s_waitcnt vmcnt(17) lgkmcnt(1)
	v_mfma_f32_16x16x32_f16 v[102:105], v[6:9], v[110:113], v[102:105]
	s_waitcnt lgkmcnt(0)
	v_mfma_f32_16x16x32_f16 v[6:9], v[6:9], v[114:117], v[14:17]
	s_waitcnt vmcnt(16)
	v_mfma_f32_16x16x32_f16 v[14:17], v[2:5], v[110:113], v[28:31]
	v_mfma_f32_16x16x32_f16 v[2:5], v[2:5], v[114:117], v[10:13]
	s_setprio 0
	v_add_u32_e32 v20, s15, v19
	s_nop 0
	ds_read_b128 v[10:13], v20 offset:4096
	ds_read_b128 v[28:31], v20 offset:20736
	s_setprio 1
	s_waitcnt vmcnt(15) lgkmcnt(1)
	v_mfma_f32_16x16x32_f16 v[102:105], v[86:89], v[10:13], v[102:105]
	s_waitcnt lgkmcnt(0)
	v_mfma_f32_16x16x32_f16 v[6:9], v[86:89], v[28:31], v[6:9]
	s_waitcnt vmcnt(14)
	v_mfma_f32_16x16x32_f16 v[10:13], v[90:93], v[10:13], v[14:17]
	v_mfma_f32_16x16x32_f16 v[2:5], v[90:93], v[28:31], v[2:5]
	s_setprio 0
	s_add_i32 s13, s14, 0x120
	s_and_b32 s13, s13, 0x1e0
	v_lshl_add_u32 v20, s13, 1, v19
	ds_read_b128 v[14:17], v20 offset:4096
	ds_read_b128 v[28:31], v20 offset:20736
	s_setprio 1
	s_waitcnt vmcnt(13) lgkmcnt(1)
	v_mfma_f32_16x16x32_f16 v[86:89], v[98:101], v[14:17], v[102:105]
	s_waitcnt lgkmcnt(0)
	v_mfma_f32_16x16x32_f16 v[6:9], v[98:101], v[28:31], v[6:9]
	s_waitcnt vmcnt(12)
	v_mfma_f32_16x16x32_f16 v[10:13], v[106:109], v[14:17], v[10:13]
	v_mfma_f32_16x16x32_f16 v[2:5], v[106:109], v[28:31], v[2:5]
	s_setprio 0
	s_add_i32 s13, s14, 0x140
	s_and_b32 s13, s13, 0x1e0
	v_lshl_add_u32 v20, s13, 1, v19
	ds_read_b128 v[14:17], v20 offset:4096
	ds_read_b128 v[28:31], v20 offset:20736
	s_setprio 1
	s_waitcnt vmcnt(11) lgkmcnt(1)
	v_mfma_f32_16x16x32_f16 v[86:89], v[40:43], v[14:17], v[86:89]
	s_waitcnt lgkmcnt(0)
	v_mfma_f32_16x16x32_f16 v[6:9], v[40:43], v[28:31], v[6:9]
	s_waitcnt vmcnt(10)
	v_mfma_f32_16x16x32_f16 v[10:13], v[94:97], v[14:17], v[10:13]
	v_mfma_f32_16x16x32_f16 v[2:5], v[94:97], v[28:31], v[2:5]
	s_setprio 0
	s_add_i32 s13, s14, 0x160
	s_and_b32 s13, s13, 0x1e0
	v_lshl_add_u32 v20, s13, 1, v19
	ds_read_b128 v[14:17], v20 offset:4096
	ds_read_b128 v[28:31], v20 offset:20736
	s_setprio 1
	s_waitcnt vmcnt(9) lgkmcnt(1)
	v_mfma_f32_16x16x32_f16 v[40:43], v[44:47], v[14:17], v[86:89]
	s_waitcnt lgkmcnt(0)
	v_mfma_f32_16x16x32_f16 v[6:9], v[44:47], v[28:31], v[6:9]
	s_waitcnt vmcnt(8)
	v_mfma_f32_16x16x32_f16 v[10:13], v[48:51], v[14:17], v[10:13]
	v_mfma_f32_16x16x32_f16 v[2:5], v[48:51], v[28:31], v[2:5]
	s_setprio 0
	s_add_i32 s13, s14, 0x180
	s_and_b32 s13, s13, 0x1e0
	v_lshl_add_u32 v20, s13, 1, v19
	ds_read_b128 v[14:17], v20 offset:4096
	ds_read_b128 v[28:31], v20 offset:20736
	s_setprio 1
	s_waitcnt vmcnt(7) lgkmcnt(1)
	v_mfma_f32_16x16x32_f16 v[40:43], v[52:55], v[14:17], v[40:43]
	s_waitcnt lgkmcnt(0)
	v_mfma_f32_16x16x32_f16 v[6:9], v[52:55], v[28:31], v[6:9]
	s_waitcnt vmcnt(6)
	v_mfma_f32_16x16x32_f16 v[10:13], v[60:63], v[14:17], v[10:13]
	v_mfma_f32_16x16x32_f16 v[2:5], v[60:63], v[28:31], v[2:5]
	s_setprio 0
	s_add_i32 s13, s14, 0x1a0
	s_and_b32 s13, s13, 0x1e0
	v_lshl_add_u32 v20, s13, 1, v19
	ds_read_b128 v[14:17], v20 offset:4096
	ds_read_b128 v[28:31], v20 offset:20736
	s_setprio 1
	s_waitcnt vmcnt(5) lgkmcnt(1)
	v_mfma_f32_16x16x32_f16 v[40:43], v[68:71], v[14:17], v[40:43]
	s_waitcnt lgkmcnt(0)
	v_mfma_f32_16x16x32_f16 v[6:9], v[68:71], v[28:31], v[6:9]
	s_waitcnt vmcnt(4)
	v_mfma_f32_16x16x32_f16 v[10:13], v[72:75], v[14:17], v[10:13]
	v_mfma_f32_16x16x32_f16 v[2:5], v[72:75], v[28:31], v[2:5]
	s_setprio 0
	s_add_i32 s13, s14, 0x1c0
	s_and_b32 s13, s13, 0x1e0
	v_lshl_add_u32 v20, s13, 1, v19
	ds_read_b128 v[14:17], v20 offset:4096
	ds_read_b128 v[28:31], v20 offset:20736
	s_setprio 1
	s_waitcnt vmcnt(3) lgkmcnt(1)
	v_mfma_f32_16x16x32_f16 v[40:43], v[76:79], v[14:17], v[40:43]
	s_waitcnt lgkmcnt(0)
	v_mfma_f32_16x16x32_f16 v[6:9], v[76:79], v[28:31], v[6:9]
	s_waitcnt vmcnt(2)
	v_mfma_f32_16x16x32_f16 v[10:13], v[82:85], v[14:17], v[10:13]
	v_mfma_f32_16x16x32_f16 v[2:5], v[82:85], v[28:31], v[2:5]
	s_setprio 0
	s_addk_i32 s14, 0x1e0
	s_and_b32 s13, s14, 0x1e0
	v_lshl_add_u32 v20, s13, 1, v19
	ds_read_b128 v[14:17], v20 offset:4096
	ds_read_b128 v[28:31], v20 offset:20736
	s_setprio 1
	s_waitcnt vmcnt(1) lgkmcnt(1)
	v_mfma_f32_16x16x32_f16 v[40:43], v[32:35], v[14:17], v[40:43]
	s_waitcnt lgkmcnt(0)
	v_mfma_f32_16x16x32_f16 v[6:9], v[32:35], v[28:31], v[6:9]
	s_waitcnt vmcnt(0)
	v_mfma_f32_16x16x32_f16 v[10:13], v[36:39], v[14:17], v[10:13]
	v_mfma_f32_16x16x32_f16 v[2:5], v[36:39], v[28:31], v[2:5]
	s_setprio 0
	v_add_u32_e32 v19, v19, v22
	v_lshlrev_b32_e32 v20, 15, v118
	v_mov_b32_e32 v21, v67
	s_bfe_u32 s22, s2, 0x30003
	v_lshl_add_u64 v[20:21], s[10:11], 0, v[20:21]
	s_lshl_b32 s26, s22, 10
	v_lshl_add_u64 v[64:65], v[20:21], 0, v[58:59]
	v_lshl_add_u64 v[52:53], v[64:65], 0, s[26:27]
	v_add_co_u32_e32 v76, vcc, s29, v52
	s_lshl_b32 s53, s22, 6
	s_nop 0
	v_addc_co_u32_e32 v77, vcc, 0, v53, vcc
	s_mov_b32 s14, 0x14000
	v_mov_b32_e32 v22, 0x14000
	v_mul_u32_u24_e32 v23, 0x210, v81
	s_add_i32 s38, s53, 64
	v_lshlrev_b32_e32 v83, 2, v118
	s_movk_i32 s16, 0x1040
	s_movk_i32 s18, 0x840
	v_lshl_or_b32 v1, v1, 3, v22
	v_add3_u32 v84, v23, v18, s14
	s_and_b32 s14, s38, 0x1c0
	s_movk_i32 s20, 0x210
	s_mov_b32 s19, s27
	v_mad_u32_u24 v56, v118, s16, v58
	v_or_b32_e32 v22, 1, v83
	v_mad_u32_u24 v98, v118, s18, v1
	s_lshl_b32 s18, s14, 4
	v_mad_u32_u24 v99, v22, s12, v58
	v_mad_u32_u24 v85, v22, s20, v1
	v_lshl_add_u64 v[54:55], v[64:65], 0, s[18:19]
	s_add_i32 s12, s53, 0xc0
	s_and_b32 s2, s3, 0x7ffffff
	s_lshl_b32 s3, s22, 5
	s_and_b32 s39, s12, 0x1c0
	s_lshl_b32 s14, s39, 4
	s_add_i32 s39, s3, 32
	s_and_b32 s39, s39, 0xe0
	v_lshl_add_u32 v82, s39, 1, v84
	s_add_i32 s11, s53, 0x80
	s_lshl_b32 s16, s38, 4
	s_mov_b32 s21, s27
	s_and_b32 s30, s11, 0x1c0
	s_lshl_b32 s11, s11, 4
	s_or_b32 s20, s16, 0x2000
	s_mov_b32 s23, s27
	s_mov_b32 s31, s27
	s_mov_b32 s35, s27
	s_or_b32 s22, s16, 0x6000
	s_lshl_b32 s30, s30, 4
	s_or_b32 s34, s11, 0x2000
	v_lshl_add_u64 v[26:27], v[64:65], 0, s[20:21]
	v_lshl_add_u64 v[28:29], v[64:65], 0, s[22:23]
	v_lshl_add_u64 v[30:31], v[64:65], 0, s[30:31]
	v_lshl_add_u64 v[32:33], v[64:65], 0, s[34:35]
	s_mov_b64 s[40:41], 0x40000
	v_lshl_add_u64 v[60:61], v[64:65], 0, s[40:41]
	s_mov_b32 s37, s27
	s_or_b32 s36, s11, 0x6000
	v_lshl_add_u64 v[74:75], v[64:65], 0, s[36:37]
	s_mov_b32 s15, s27
	s_lshl_b32 s12, s12, 4
	v_lshl_add_u64 v[70:71], v[64:65], 0, s[14:15]
	s_mov_b32 s17, s27
	s_or_b32 s16, s12, 0x2000
	s_mov_b32 s13, s27
	s_or_b32 s12, s12, 0x6000
	v_lshl_add_u64 v[72:73], v[64:65], 0, s[16:17]
	v_lshl_add_u64 v[68:69], v[64:65], 0, s[12:13]
	v_add_u32_e32 v1, s53, v84
	s_xor_b32 s10, s26, 0x1000
	s_mov_b32 s11, s27
	s_mov_b32 s49, s27
	s_mov_b32 s51, s27
	s_mov_b32 s47, s27
	v_pk_add_f32 v[14:15], v[180:181], v[40:41]
	v_pk_add_f32 v[16:17], v[182:183], v[42:43]
	v_pk_add_f32 v[10:11], v[184:185], v[10:11]
	v_pk_add_f32 v[12:13], v[186:187], v[12:13]
	v_pk_add_f32 v[6:7], v[188:189], v[6:7]
	v_pk_add_f32 v[8:9], v[190:191], v[8:9]
	v_pk_add_f32 v[2:3], v[192:193], v[2:3]
	v_pk_add_f32 v[4:5], v[194:195], v[4:5]
	ds_write_b128 v19, v[14:17] offset:37376
	ds_write_b128 v19, v[10:13] offset:37440
	ds_write_b128 v19, v[6:9] offset:54016
	ds_write_b128 v19, v[2:5] offset:54080
	v_mov_b64_e32 v[34:35], v[204:205]
	v_mov_b64_e32 v[36:37], v[206:207]
	v_mov_b64_e32 v[38:39], v[208:209]
	v_mov_b64_e32 v[40:41], v[210:211]
	v_add_co_u32_e32 v2, vcc, s52, v52
	s_waitcnt lgkmcnt(0)
	s_nop 0
	v_addc_co_u32_e32 v3, vcc, 0, v53, vcc
	v_add_co_u32_e32 v4, vcc, s33, v52
	s_barrier
	s_nop 0
	v_addc_co_u32_e32 v5, vcc, 0, v53, vcc
	global_load_dwordx4 v[14:17], v[2:3], off
	global_load_dwordx4 v[18:21], v[4:5], off
	global_load_dwordx4 v[22:25], v[52:53], off
	global_load_dwordx4 v[10:13], v[54:55], off
	ds_read_b128 v[2:5], v56 offset:37376
	ds_read_b128 v[6:9], v99 offset:37376
	v_add_co_u32_e32 v78, vcc, s52, v54
	s_mov_b32 s43, s27
	s_waitcnt lgkmcnt(1)
	v_add_f32_e32 v42, v2, v3
	v_add_f32_e32 v42, v42, v4
	v_add_f32_e32 v42, v42, v5
	v_addc_co_u32_e32 v79, vcc, 0, v55, vcc
	s_nop 0
	v_add_f32_dpp v42, v42, v42 quad_perm:[1,0,3,2] row_mask:0xf bank_mask:0xf bound_ctrl:1
	s_mov_b32 s45, s27
	s_mov_b32 s41, s27
	v_add_f32_dpp v42, v42, v42 quad_perm:[2,3,0,1] row_mask:0xf bank_mask:0xf bound_ctrl:1
	v_lshl_add_u64 v[62:63], v[64:65], 0, s[10:11]
	v_lshl_add_u64 v[58:59], s[4:5], 0, v[58:59]
	v_add_f32_dpp v42, v42, v42 row_half_mirror row_mask:0xf bank_mask:0xf bound_ctrl:1
	v_lshl_add_u64 v[152:153], v[60:61], 0, s[26:27]
	v_lshl_add_u64 v[154:155], v[60:61], 0, s[18:19]
	v_add_f32_dpp v42, v42, v42 row_mirror row_mask:0xf bank_mask:0xf bound_ctrl:1
	v_lshl_add_u64 v[156:157], v[60:61], 0, s[20:21]
	v_readlane_b32 s8, v42, 16
	v_readlane_b32 s9, v42, 48
	v_readlane_b32 s6, v42, 0
	v_readlane_b32 s7, v42, 32
	v_mov_b32_e32 v42, s8
	v_mov_b32_e32 v43, s9
	v_pk_add_f32 v[42:43], s[6:7], v[42:43]
	s_mov_b32 s6, 0x3b800000
	v_add_f32_e32 v42, v42, v43
	v_mul_f32_e32 v42, 0x3b800000, v42
	v_pk_add_f32 v[86:87], v[2:3], v[42:43] op_sel_hi:[1,0] neg_lo:[0,1] neg_hi:[0,1]
	v_pk_add_f32 v[88:89], v[4:5], v[42:43] op_sel_hi:[1,0] neg_lo:[0,1] neg_hi:[0,1]
	v_pk_mul_f32 v[42:43], v[86:87], v[86:87]
	v_pk_mul_f32 v[44:45], v[88:89], v[88:89]
	v_add_f32_e32 v42, v42, v43
	v_add_f32_e32 v42, v44, v42
	s_waitcnt lgkmcnt(0)
	v_add_f32_e32 v44, v6, v7
	v_add_f32_e32 v42, v45, v42
	v_add_f32_e32 v44, v44, v8
	v_add_f32_e32 v44, v44, v9
	v_add_f32_dpp v42, v42, v42 quad_perm:[1,0,3,2] row_mask:0xf bank_mask:0xf bound_ctrl:1
	v_lshl_add_u64 v[158:159], v[60:61], 0, s[22:23]
	v_add_f32_dpp v44, v44, v44 quad_perm:[1,0,3,2] row_mask:0xf bank_mask:0xf bound_ctrl:1
	v_add_f32_dpp v42, v42, v42 quad_perm:[2,3,0,1] row_mask:0xf bank_mask:0xf bound_ctrl:1
	v_lshl_add_u64 v[160:161], v[60:61], 0, s[30:31]
	v_add_f32_dpp v44, v44, v44 quad_perm:[2,3,0,1] row_mask:0xf bank_mask:0xf bound_ctrl:1
	v_add_f32_dpp v42, v42, v42 row_half_mirror row_mask:0xf bank_mask:0xf bound_ctrl:1
	v_lshl_add_u64 v[162:163], v[60:61], 0, s[34:35]
	v_add_f32_dpp v44, v44, v44 row_half_mirror row_mask:0xf bank_mask:0xf bound_ctrl:1
	v_add_f32_dpp v42, v42, v42 row_mirror row_mask:0xf bank_mask:0xf bound_ctrl:1
	v_lshl_add_u64 v[164:165], v[60:61], 0, s[36:37]
	v_readlane_b32 s7, v42, 16
	v_readlane_b32 s39, v42, 48
	v_add_f32_dpp v44, v44, v44 row_mirror row_mask:0xf bank_mask:0xf bound_ctrl:1
	v_readlane_b32 s8, v42, 0
	v_readlane_b32 s9, v42, 32
	v_mov_b32_e32 v42, s7
	v_mov_b32_e32 v43, s39
	v_readlane_b32 s7, v44, 16
	v_readlane_b32 s39, v44, 48
	v_pk_add_f32 v[42:43], s[8:9], v[42:43]
	v_readlane_b32 s8, v44, 0
	v_readlane_b32 s9, v44, 32
	v_mov_b32_e32 v44, s7
	v_mov_b32_e32 v45, s39
	v_pk_add_f32 v[44:45], s[8:9], v[44:45]
	s_nop 0
	v_add_f32_e32 v44, v44, v45
	v_mul_f32_e32 v44, 0x3b800000, v44
	v_pk_add_f32 v[90:91], v[6:7], v[44:45] op_sel_hi:[1,0] neg_lo:[0,1] neg_hi:[0,1]
	v_pk_add_f32 v[92:93], v[8:9], v[44:45] op_sel_hi:[1,0] neg_lo:[0,1] neg_hi:[0,1]
	v_pk_mul_f32 v[46:47], v[90:91], v[90:91]
	v_pk_mul_f32 v[44:45], v[92:93], v[92:93]
	v_add_f32_e32 v46, v46, v47
	v_add_f32_e32 v44, v44, v46
	v_add_f32_e32 v44, v45, v44
	v_mov_b32_e32 v47, v42
	s_nop 0
	v_add_f32_dpp v44, v44, v44 quad_perm:[1,0,3,2] row_mask:0xf bank_mask:0xf bound_ctrl:1
	s_nop 1
	v_add_f32_dpp v44, v44, v44 quad_perm:[2,3,0,1] row_mask:0xf bank_mask:0xf bound_ctrl:1
	s_nop 1
	v_add_f32_dpp v44, v44, v44 row_half_mirror row_mask:0xf bank_mask:0xf bound_ctrl:1
	s_nop 1
	v_add_f32_dpp v44, v44, v44 row_mirror row_mask:0xf bank_mask:0xf bound_ctrl:1
	s_nop 0
	v_readlane_b32 s7, v44, 16
	v_readlane_b32 s39, v44, 48
	v_readlane_b32 s8, v44, 0
	v_readlane_b32 s9, v44, 32
	v_mov_b32_e32 v44, s7
	v_mov_b32_e32 v45, s39
	v_pk_add_f32 v[44:45], s[8:9], v[44:45]
	s_mov_b32 s8, 0x3727c5ac
	v_mov_b32_e32 v46, v44
	v_mov_b32_e32 v42, v45
	v_pk_add_f32 v[42:43], v[46:47], v[42:43]
	v_mov_b64_e32 v[94:95], s[8:9]
	v_pk_fma_f32 v[96:97], v[42:43], s[6:7], v[94:95] op_sel_hi:[1,0,0]
	s_mov_b32 s7, 0x800000
	v_mul_f32_e32 v42, 0x4b800000, v97
	v_cmp_gt_f32_e32 vcc, s7, v97
	s_nop 1
	v_cndmask_b32_e32 v42, v97, v42, vcc
	v_rsq_f32_e32 v97, v42
	global_load_dwordx4 v[54:57], v[26:27], off
	global_load_dwordx4 v[50:53], v[28:29], off
	global_load_dwordx4 v[46:49], v[30:31], off
	global_load_dwordx4 v[42:45], v[32:33], off
	v_mul_f32_e32 v26, 0x45800000, v97
	v_cndmask_b32_e32 v26, v97, v26, vcc
	v_pk_mul_f32 v[28:29], v[86:87], v[26:27] op_sel_hi:[1,0]
	v_cmp_gt_f32_e32 vcc, s7, v96
	s_waitcnt vmcnt(8)
	v_pk_fma_f32 v[28:29], v[34:35], v[28:29], v[38:39]
	v_pk_mul_f32 v[26:27], v[88:89], v[26:27] op_sel_hi:[1,0]
	v_cvt_pk_f16_f32 v28, v28, v29
	v_mul_f32_e32 v29, 0x4b800000, v96
	v_cndmask_b32_e32 v29, v96, v29, vcc
	v_rsq_f32_e32 v32, v29
	v_pk_fma_f32 v[26:27], v[36:37], v[26:27], v[40:41]
	s_nop 0
	v_cvt_pk_f16_f32 v29, v26, v27
	v_mul_f32_e32 v26, 0x45800000, v32
	v_cndmask_b32_e32 v26, v32, v26, vcc
	ds_write_b64 v98, v[28:29]
	v_pk_mul_f32 v[28:29], v[90:91], v[26:27] op_sel_hi:[1,0]
	v_pk_mul_f32 v[26:27], v[92:93], v[26:27] op_sel_hi:[1,0]
	v_pk_fma_f32 v[28:29], v[34:35], v[28:29], v[38:39]
	v_pk_fma_f32 v[26:27], v[36:37], v[26:27], v[40:41]
	v_cvt_pk_f16_f32 v28, v28, v29
	v_cvt_pk_f16_f32 v29, v26, v27
	ds_write_b64 v85, v[28:29]
	ds_read_b128 v[26:29], v99 offset:38416
	v_add_co_u32_e32 v102, vcc, s52, v30
	s_nop 1
	v_addc_co_u32_e32 v103, vcc, 0, v31, vcc
	ds_read_b128 v[30:33], v99 offset:39456
	s_waitcnt lgkmcnt(1)
	v_add_f32_e32 v86, v26, v27
	v_add_f32_e32 v86, v86, v28
	v_add_f32_e32 v86, v86, v29
	s_nop 1
	v_add_f32_dpp v86, v86, v86 quad_perm:[1,0,3,2] row_mask:0xf bank_mask:0xf bound_ctrl:1
	s_nop 1
	v_add_f32_dpp v86, v86, v86 quad_perm:[2,3,0,1] row_mask:0xf bank_mask:0xf bound_ctrl:1
	s_nop 1
	v_add_f32_dpp v86, v86, v86 row_half_mirror row_mask:0xf bank_mask:0xf bound_ctrl:1
	s_nop 1
	v_add_f32_dpp v86, v86, v86 row_mirror row_mask:0xf bank_mask:0xf bound_ctrl:1
	s_nop 0
	v_readlane_b32 s39, v86, 16
	v_readlane_b32 s40, v86, 48
	v_readlane_b32 s8, v86, 0
	v_readlane_b32 s9, v86, 32
	v_mov_b32_e32 v86, s39
	v_mov_b32_e32 v87, s40
	v_pk_add_f32 v[86:87], s[8:9], v[86:87]
	s_nop 0
	v_add_f32_e32 v86, v86, v87
	v_mul_f32_e32 v86, 0x3b800000, v86
	v_pk_add_f32 v[104:105], v[26:27], v[86:87] op_sel_hi:[1,0] neg_lo:[0,1] neg_hi:[0,1]
	v_pk_add_f32 v[106:107], v[28:29], v[86:87] op_sel_hi:[1,0] neg_lo:[0,1] neg_hi:[0,1]
	v_pk_mul_f32 v[88:89], v[104:105], v[104:105]
	v_pk_mul_f32 v[86:87], v[106:107], v[106:107]
	v_add_f32_e32 v88, v88, v89
	v_add_f32_e32 v86, v86, v88
	s_waitcnt lgkmcnt(0)
	v_add_f32_e32 v88, v30, v31
	v_add_f32_e32 v86, v87, v86
	v_add_f32_e32 v88, v88, v32
	v_add_f32_e32 v88, v88, v33
	v_add_f32_dpp v86, v86, v86 quad_perm:[1,0,3,2] row_mask:0xf bank_mask:0xf bound_ctrl:1
	s_nop 0
	v_add_f32_dpp v88, v88, v88 quad_perm:[1,0,3,2] row_mask:0xf bank_mask:0xf bound_ctrl:1
	v_add_f32_dpp v86, v86, v86 quad_perm:[2,3,0,1] row_mask:0xf bank_mask:0xf bound_ctrl:1
	s_nop 0
	v_add_f32_dpp v88, v88, v88 quad_perm:[2,3,0,1] row_mask:0xf bank_mask:0xf bound_ctrl:1
	v_add_f32_dpp v86, v86, v86 row_half_mirror row_mask:0xf bank_mask:0xf bound_ctrl:1
	s_nop 0
	v_add_f32_dpp v88, v88, v88 row_half_mirror row_mask:0xf bank_mask:0xf bound_ctrl:1
	v_add_f32_dpp v86, v86, v86 row_mirror row_mask:0xf bank_mask:0xf bound_ctrl:1
	s_nop 0
	v_readlane_b32 s39, v86, 16
	v_readlane_b32 s40, v86, 48
	v_add_f32_dpp v88, v88, v88 row_mirror row_mask:0xf bank_mask:0xf bound_ctrl:1
	v_readlane_b32 s8, v86, 0
	v_readlane_b32 s9, v86, 32
	v_mov_b32_e32 v86, s39
	v_mov_b32_e32 v87, s40
	v_readlane_b32 s39, v88, 16
	v_readlane_b32 s40, v88, 48
	v_pk_add_f32 v[86:87], s[8:9], v[86:87]
	v_readlane_b32 s8, v88, 0
	v_readlane_b32 s9, v88, 32
	v_mov_b32_e32 v88, s39
	v_mov_b32_e32 v89, s40
	v_pk_add_f32 v[88:89], s[8:9], v[88:89]
	s_nop 0
	v_add_f32_e32 v88, v88, v89
	v_mul_f32_e32 v88, 0x3b800000, v88
	v_pk_add_f32 v[108:109], v[30:31], v[88:89] op_sel_hi:[1,0] neg_lo:[0,1] neg_hi:[0,1]
	v_pk_add_f32 v[110:111], v[32:33], v[88:89] op_sel_hi:[1,0] neg_lo:[0,1] neg_hi:[0,1]
	v_pk_mul_f32 v[90:91], v[108:109], v[108:109]
	v_pk_mul_f32 v[88:89], v[110:111], v[110:111]
	v_add_f32_e32 v90, v90, v91
	v_add_f32_e32 v88, v88, v90
	v_add_f32_e32 v88, v89, v88
	v_mov_b32_e32 v91, v86
	s_nop 0
	v_add_f32_dpp v88, v88, v88 quad_perm:[1,0,3,2] row_mask:0xf bank_mask:0xf bound_ctrl:1
	s_nop 1
	v_add_f32_dpp v88, v88, v88 quad_perm:[2,3,0,1] row_mask:0xf bank_mask:0xf bound_ctrl:1
	s_nop 1
	v_add_f32_dpp v88, v88, v88 row_half_mirror row_mask:0xf bank_mask:0xf bound_ctrl:1
	s_nop 1
	v_add_f32_dpp v88, v88, v88 row_mirror row_mask:0xf bank_mask:0xf bound_ctrl:1
	s_nop 0
	v_readlane_b32 s39, v88, 16
	v_readlane_b32 s40, v88, 48
	v_readlane_b32 s8, v88, 0
	v_readlane_b32 s9, v88, 32
	v_mov_b32_e32 v88, s39
	v_mov_b32_e32 v89, s40
	v_pk_add_f32 v[88:89], s[8:9], v[88:89]
	s_mov_b32 s9, s27
	v_mov_b32_e32 v90, v88
	v_mov_b32_e32 v86, v89
	v_pk_add_f32 v[86:87], v[90:91], v[86:87]
	s_mov_b32 s39, s27
	v_pk_fma_f32 v[112:113], v[86:87], s[6:7], v[94:95] op_sel_hi:[1,0,0]
	s_add_i32 s6, s53, 0x140
	v_mul_f32_e32 v86, 0x4b800000, v113
	v_cmp_gt_f32_e32 vcc, s7, v113
	s_nop 1
	v_cndmask_b32_e32 v86, v113, v86, vcc
	v_rsq_f32_e32 v113, v86
	global_load_dwordx4 v[86:89], v[78:79], off
	global_load_dwordx4 v[90:93], v[102:103], off
	global_load_dwordx4 v[94:97], v[76:77], off
	global_load_dwordx4 v[98:101], v[74:75], off
	v_mul_f32_e32 v74, 0x45800000, v113
	v_cndmask_b32_e32 v74, v113, v74, vcc
	v_pk_mul_f32 v[76:77], v[104:105], v[74:75] op_sel_hi:[1,0]
	v_mul_f32_e32 v75, 0x4b800000, v112
	v_cmp_gt_f32_e32 vcc, s7, v112
	v_pk_fma_f32 v[76:77], v[34:35], v[76:77], v[38:39]
	s_and_b32 s7, s6, 0x1c0
	v_cndmask_b32_e32 v75, v112, v75, vcc
	v_rsq_f32_e32 v78, v75
	v_pk_mul_f32 v[74:75], v[106:107], v[74:75] op_sel_hi:[1,0]
	v_cvt_pk_f16_f32 v76, v76, v77
	v_pk_fma_f32 v[74:75], v[36:37], v[74:75], v[40:41]
	s_lshl_b32 s6, s6, 4
	v_cvt_pk_f16_f32 v77, v74, v75
	v_mul_f32_e32 v74, 0x45800000, v78
	v_cndmask_b32_e32 v74, v78, v74, vcc
	v_pk_mul_f32 v[78:79], v[108:109], v[74:75] op_sel_hi:[1,0]
	s_or_b32 s50, s6, 0x2000
	v_pk_fma_f32 v[34:35], v[34:35], v[78:79], v[38:39]
	v_pk_mul_f32 v[38:39], v[110:111], v[74:75] op_sel_hi:[1,0]
	v_add_co_u32_e32 v78, vcc, s52, v70
	v_pk_fma_f32 v[36:37], v[36:37], v[38:39], v[40:41]
	v_cvt_pk_f16_f32 v34, v34, v35
	v_cvt_pk_f16_f32 v35, v36, v37
	v_addc_co_u32_e32 v79, vcc, 0, v71, vcc
	ds_write2_b64 v85, v[76:77], v[34:35] offset0:66 offset1:132
	s_waitcnt lgkmcnt(0)
	s_barrier
	global_load_dwordx4 v[34:37], v[70:71], off
	global_load_dwordx4 v[38:41], v[72:73], off
	s_nop 0
	global_load_dwordx4 v[70:73], v[78:79], off
	global_load_dwordx4 v[74:77], v[68:69], off
	s_or_b32 s46, s6, 0x6000
	s_sub_i32 s6, s38, s3
	s_and_b32 s6, s6, 0xe0
	v_lshl_add_u32 v172, s6, 1, v84
	s_add_i32 s6, s53, 0x180
	s_lshl_b32 s48, s7, 4
	s_and_b32 s7, s6, 0x1c0
	s_lshl_b32 s6, s6, 4
	s_or_b32 s44, s6, 0x2000
	s_or_b32 s40, s6, 0x6000
	s_add_i32 s6, s3, 0x60
	s_and_b32 s6, s6, 0xe0
	v_lshl_add_u32 v173, s6, 1, v84
	s_add_i32 s6, s53, 0x1c0
	s_xor_b32 s53, s53, 0x100
	v_add_u32_e32 v174, s53, v84
	s_add_i32 s53, s3, 0xa0
	s_lshl_b32 s42, s7, 4
	s_and_b32 s7, s6, 0x1c0
	s_lshl_b32 s6, s6, 4
	s_and_b32 s53, s53, 0xe0
	s_lshl_b32 s8, s7, 4
	s_or_b32 s38, s6, 0x2000
	s_or_b32 s6, s6, 0x6000
	s_mov_b32 s7, s27
	v_lshl_add_u32 v175, s53, 1, v84
	s_add_i32 s53, s3, 0xc0
	s_addk_i32 s3, 0xe0
	v_lshl_add_u64 v[68:69], v[64:65], 0, s[48:49]
	v_lshl_add_u64 v[78:79], v[64:65], 0, s[50:51]
	v_lshl_add_u64 v[138:139], v[64:65], 0, s[46:47]
	v_lshl_add_u64 v[140:141], v[64:65], 0, s[42:43]
	v_lshl_add_u64 v[142:143], v[64:65], 0, s[44:45]
	v_lshl_add_u64 v[144:145], v[64:65], 0, s[40:41]
	v_lshl_add_u64 v[146:147], v[64:65], 0, s[8:9]
	v_lshl_add_u64 v[148:149], v[64:65], 0, s[38:39]
	v_lshl_add_u64 v[150:151], v[64:65], 0, s[6:7]
	s_and_b32 s53, s53, 0xe0
	s_and_b32 s3, s3, 0xe0
	v_add_u32_e32 v64, s28, v83
	v_mov_b32_e32 v65, v67
	v_lshl_add_u32 v176, s53, 1, v84
	v_lshl_add_u32 v177, s3, 1, v84
	v_lshlrev_b64 v[84:85], 10, v[64:65]
	ds_read_b128 v[102:105], v1
	ds_read_b128 v[106:109], v1 offset:8448
	v_lshl_add_u64 v[166:167], v[58:59], 0, v[84:85]
	v_or_b32_e32 v84, 1, v64
	v_mov_b32_e32 v85, v67
	v_lshlrev_b64 v[84:85], 10, v[84:85]
	v_lshl_add_u64 v[168:169], v[58:59], 0, v[84:85]
	v_or_b32_e32 v84, 2, v64
	v_mov_b32_e32 v85, v67
	v_or_b32_e32 v64, 3, v64
	v_lshlrev_b64 v[84:85], 10, v[84:85]
	v_lshlrev_b64 v[64:65], 10, v[64:65]
	v_lshl_add_u64 v[170:171], v[58:59], 0, v[84:85]
	v_lshl_add_u64 v[58:59], v[58:59], 0, v[64:65]
	s_setprio 1
	s_waitcnt vmcnt(13) lgkmcnt(1)
	v_mfma_f32_16x16x32_f16 v[110:113], v[102:105], v[22:25], 0
	s_waitcnt lgkmcnt(0)
	v_mfma_f32_16x16x32_f16 v[22:25], v[106:109], v[22:25], 0
	s_waitcnt vmcnt(5)
	v_mfma_f32_16x16x32_f16 v[114:117], v[102:105], v[94:97], 0
	v_mfma_f32_16x16x32_f16 v[94:97], v[106:109], v[94:97], 0
	v_mfma_f32_16x16x32_f16 v[118:121], v[102:105], v[14:17], 0
	v_mfma_f32_16x16x32_f16 v[14:17], v[106:109], v[14:17], 0
	v_mfma_f32_16x16x32_f16 v[102:105], v[102:105], v[18:21], 0
	v_mfma_f32_16x16x32_f16 v[18:21], v[106:109], v[18:21], 0
	s_setprio 0
	v_add_co_u32_e32 v64, vcc, s29, v62
	global_load_dwordx4 v[106:109], v[62:63], off
	s_nop 0
	v_addc_co_u32_e32 v65, vcc, 0, v63, vcc
	v_add_co_u32_e32 v84, vcc, s52, v62
	s_nop 1
	v_addc_co_u32_e32 v85, vcc, 0, v63, vcc
	v_add_co_u32_e32 v62, vcc, s33, v62
	global_load_dwordx4 v[122:125], v[64:65], off
	global_load_dwordx4 v[126:129], v[84:85], off
	v_addc_co_u32_e32 v63, vcc, 0, v63, vcc
	global_load_dwordx4 v[62:65], v[62:63], off
	ds_read_b128 v[130:133], v82
	ds_read_b128 v[134:137], v82 offset:8448
	s_setprio 1
	s_waitcnt lgkmcnt(1)
	v_mfma_f32_16x16x32_f16 v[110:113], v[130:133], v[10:13], v[110:113]
	s_waitcnt lgkmcnt(0)
	v_mfma_f32_16x16x32_f16 v[10:13], v[134:137], v[10:13], v[22:25]
	v_mfma_f32_16x16x32_f16 v[22:25], v[130:133], v[54:57], v[114:117]
	v_mfma_f32_16x16x32_f16 v[54:57], v[134:137], v[54:57], v[94:97]
	v_mfma_f32_16x16x32_f16 v[94:97], v[130:133], v[86:89], v[118:121]
	v_mfma_f32_16x16x32_f16 v[14:17], v[134:137], v[86:89], v[14:17]
	v_mfma_f32_16x16x32_f16 v[84:87], v[130:133], v[50:53], v[102:105]
	v_mfma_f32_16x16x32_f16 v[18:21], v[134:137], v[50:53], v[18:21]
	s_setprio 0
	global_load_dwordx4 v[50:53], v[68:69], off
	global_load_dwordx4 v[102:105], v[78:79], off
	v_add_co_u32_e32 v68, vcc, s52, v68
	s_nop 1
	v_addc_co_u32_e32 v69, vcc, 0, v69, vcc
	global_load_dwordx4 v[114:117], v[68:69], off
	global_load_dwordx4 v[118:121], v[138:139], off
	ds_read_b128 v[130:133], v172
	ds_read_b128 v[134:137], v172 offset:8448
	s_setprio 1
	s_waitcnt lgkmcnt(1)
	v_mfma_f32_16x16x32_f16 v[110:113], v[130:133], v[46:49], v[110:113]
	s_waitcnt lgkmcnt(0)
	v_mfma_f32_16x16x32_f16 v[10:13], v[134:137], v[46:49], v[10:13]
	v_mfma_f32_16x16x32_f16 v[22:25], v[130:133], v[42:45], v[22:25]
	v_mfma_f32_16x16x32_f16 v[42:45], v[134:137], v[42:45], v[54:57]
	v_mfma_f32_16x16x32_f16 v[46:49], v[130:133], v[90:93], v[94:97]
	v_mfma_f32_16x16x32_f16 v[14:17], v[134:137], v[90:93], v[14:17]
	s_waitcnt vmcnt(12)
	v_mfma_f32_16x16x32_f16 v[54:57], v[130:133], v[98:101], v[84:87]
	v_mfma_f32_16x16x32_f16 v[18:21], v[134:137], v[98:101], v[18:21]
	s_setprio 0
	v_add_co_u32_e32 v68, vcc, s52, v140
	global_load_dwordx4 v[84:87], v[140:141], off
	global_load_dwordx4 v[88:91], v[142:143], off
	v_addc_co_u32_e32 v69, vcc, 0, v141, vcc
	global_load_dwordx4 v[92:95], v[68:69], off
	global_load_dwordx4 v[96:99], v[144:145], off
	ds_read_b128 v[130:133], v173
	ds_read_b128 v[134:137], v173 offset:8448
	s_setprio 1
	s_waitcnt vmcnt(15) lgkmcnt(1)
	v_mfma_f32_16x16x32_f16 v[110:113], v[130:133], v[34:37], v[110:113]
	s_waitcnt lgkmcnt(0)
	v_mfma_f32_16x16x32_f16 v[10:13], v[134:137], v[34:37], v[10:13]
	s_waitcnt vmcnt(14)
	v_mfma_f32_16x16x32_f16 v[22:25], v[130:133], v[38:41], v[22:25]
	v_mfma_f32_16x16x32_f16 v[34:37], v[134:137], v[38:41], v[42:45]
	s_waitcnt vmcnt(13)
	v_mfma_f32_16x16x32_f16 v[38:41], v[130:133], v[70:73], v[46:49]
	v_mfma_f32_16x16x32_f16 v[14:17], v[134:137], v[70:73], v[14:17]
	s_waitcnt vmcnt(12)
	v_mfma_f32_16x16x32_f16 v[42:45], v[130:133], v[74:77], v[54:57]
	v_mfma_f32_16x16x32_f16 v[18:21], v[134:137], v[74:77], v[18:21]
	s_setprio 0
	v_add_co_u32_e32 v68, vcc, s52, v146
	global_load_dwordx4 v[46:49], v[146:147], off
	global_load_dwordx4 v[54:57], v[148:149], off
	v_addc_co_u32_e32 v69, vcc, 0, v147, vcc
	global_load_dwordx4 v[68:71], v[68:69], off
	s_nop 0
	global_load_dwordx4 v[72:75], v[150:151], off
	ds_read_b128 v[76:79], v174
	ds_read_b128 v[130:133], v174 offset:8448
	s_setprio 1
	s_waitcnt vmcnt(15) lgkmcnt(1)
	v_mfma_f32_16x16x32_f16 v[110:113], v[76:79], v[106:109], v[110:113]
	s_waitcnt lgkmcnt(0)
	v_mfma_f32_16x16x32_f16 v[10:13], v[130:133], v[106:109], v[10:13]
	s_waitcnt vmcnt(14)
	v_mfma_f32_16x16x32_f16 v[22:25], v[76:79], v[122:125], v[22:25]
	v_mfma_f32_16x16x32_f16 v[34:37], v[130:133], v[122:125], v[34:37]
	s_waitcnt vmcnt(13)
	v_mfma_f32_16x16x32_f16 v[38:41], v[76:79], v[126:129], v[38:41]
	v_mfma_f32_16x16x32_f16 v[14:17], v[130:133], v[126:129], v[14:17]
	s_waitcnt vmcnt(12)
	v_mfma_f32_16x16x32_f16 v[42:45], v[76:79], v[62:65], v[42:45]
	v_mfma_f32_16x16x32_f16 v[18:21], v[130:133], v[62:65], v[18:21]
	s_setprio 0
	ds_read_b128 v[62:65], v175
	ds_read_b128 v[76:79], v175 offset:8448
	s_setprio 1
	s_waitcnt vmcnt(11) lgkmcnt(1)
	v_mfma_f32_16x16x32_f16 v[106:109], v[62:65], v[50:53], v[110:113]
	s_waitcnt lgkmcnt(0)
	v_mfma_f32_16x16x32_f16 v[10:13], v[76:79], v[50:53], v[10:13]
	s_waitcnt vmcnt(10)
	v_mfma_f32_16x16x32_f16 v[22:25], v[62:65], v[102:105], v[22:25]
	v_mfma_f32_16x16x32_f16 v[34:37], v[76:79], v[102:105], v[34:37]
	s_waitcnt vmcnt(9)
	v_mfma_f32_16x16x32_f16 v[38:41], v[62:65], v[114:117], v[38:41]
	v_mfma_f32_16x16x32_f16 v[14:17], v[76:79], v[114:117], v[14:17]
	s_waitcnt vmcnt(8)
	v_mfma_f32_16x16x32_f16 v[42:45], v[62:65], v[118:121], v[42:45]
	v_mfma_f32_16x16x32_f16 v[18:21], v[76:79], v[118:121], v[18:21]
	s_setprio 0
	ds_read_b128 v[50:53], v176
	ds_read_b128 v[62:65], v176 offset:8448
	s_setprio 1
	s_waitcnt vmcnt(7) lgkmcnt(1)
	v_mfma_f32_16x16x32_f16 v[76:79], v[50:53], v[84:87], v[106:109]
	s_waitcnt lgkmcnt(0)
	v_mfma_f32_16x16x32_f16 v[10:13], v[62:65], v[84:87], v[10:13]
	s_waitcnt vmcnt(6)
	v_mfma_f32_16x16x32_f16 v[22:25], v[50:53], v[88:91], v[22:25]
	v_mfma_f32_16x16x32_f16 v[34:37], v[62:65], v[88:91], v[34:37]
	s_waitcnt vmcnt(5)
	v_mfma_f32_16x16x32_f16 v[38:41], v[50:53], v[92:95], v[38:41]
	v_mfma_f32_16x16x32_f16 v[14:17], v[62:65], v[92:95], v[14:17]
	s_waitcnt vmcnt(4)
	v_mfma_f32_16x16x32_f16 v[42:45], v[50:53], v[96:99], v[42:45]
	v_mfma_f32_16x16x32_f16 v[18:21], v[62:65], v[96:99], v[18:21]
	s_setprio 0
	ds_read_b128 v[50:53], v177
	ds_read_b128 v[62:65], v177 offset:8448
	s_setprio 1
	s_waitcnt vmcnt(3) lgkmcnt(1)
	v_mfma_f32_16x16x32_f16 v[76:79], v[50:53], v[46:49], v[76:79]
	s_waitcnt lgkmcnt(0)
	v_mfma_f32_16x16x32_f16 v[10:13], v[62:65], v[46:49], v[10:13]
	s_waitcnt vmcnt(2)
	v_mfma_f32_16x16x32_f16 v[22:25], v[50:53], v[54:57], v[22:25]
	v_mfma_f32_16x16x32_f16 v[34:37], v[62:65], v[54:57], v[34:37]
	s_waitcnt vmcnt(1)
	v_mfma_f32_16x16x32_f16 v[38:41], v[50:53], v[68:71], v[38:41]
	v_mfma_f32_16x16x32_f16 v[14:17], v[62:65], v[68:71], v[14:17]
	s_waitcnt vmcnt(0)
	v_mfma_f32_16x16x32_f16 v[42:45], v[50:53], v[72:75], v[42:45]
	v_mfma_f32_16x16x32_f16 v[18:21], v[62:65], v[72:75], v[18:21]
	s_setprio 0
	v_add_co_u32_e32 v108, vcc, s29, v152
	v_and_b32_e32 v67, 0x1c0, v0
	s_nop 0
	v_addc_co_u32_e32 v109, vcc, 0, v153, vcc
	v_add_co_u32_e32 v46, vcc, s52, v152
	s_movk_i32 s4, 0x50
	s_nop 0
	v_addc_co_u32_e32 v47, vcc, 0, v153, vcc
	v_add_co_u32_e32 v68, vcc, s33, v152
	v_or_b32_e32 v116, 16, v67
	s_nop 0
	v_addc_co_u32_e32 v69, vcc, 0, v153, vcc
	v_add_co_u32_e32 v110, vcc, s52, v154
	global_load_dwordx4 v[46:49], v[46:47], off
	s_nop 0
	global_load_dwordx4 v[50:53], v[68:69], off
	global_load_dwordx4 v[54:57], v[152:153], off
	global_load_dwordx4 v[62:65], v[154:155], off
	v_addc_co_u32_e32 v111, vcc, 0, v155, vcc
	v_add_co_u32_e32 v112, vcc, s52, v160
	global_load_dwordx4 v[68:71], v[156:157], off
	global_load_dwordx4 v[72:75], v[158:159], off
	global_load_dwordx4 v[84:87], v[160:161], off
	global_load_dwordx4 v[88:91], v[162:163], off
	v_addc_co_u32_e32 v113, vcc, 0, v161, vcc
	global_load_dwordx4 v[92:95], v[110:111], off
	global_load_dwordx4 v[96:99], v[112:113], off
	global_load_dwordx4 v[100:103], v[108:109], off
	global_load_dwordx4 v[104:107], v[164:165], off
	s_nop 0
	global_store_dwordx4 v[166:167], v[2:5], off sc1
	global_store_dwordx4 v[168:169], v[6:9], off sc1
	global_store_dwordx4 v[170:171], v[26:29], off sc1
	global_store_dwordx4 v[58:59], v[30:33], off sc1
	v_and_b32_e32 v4, 0x1cf, v0
	v_cvt_pk_f16_f32 v3, v78, v79
	v_cvt_pk_f16_f32 v2, v76, v77
	v_mad_u32_u24 v4, v4, s4, v80
	v_or_b32_e32 v5, v116, v81
	v_or_b32_e32 v117, 32, v67
	ds_write_b64 v4, v[2:3]
	v_cvt_pk_f16_f32 v3, v24, v25
	v_cvt_pk_f16_f32 v2, v22, v23
	v_mad_u32_u24 v5, v5, s4, v80
	v_or_b32_e32 v6, v117, v81
	v_or_b32_e32 v118, 48, v67
	ds_write_b64 v5, v[2:3]
	v_cvt_pk_f16_f32 v3, v40, v41
	v_cvt_pk_f16_f32 v2, v38, v39
	v_mad_u32_u24 v6, v6, s4, v80
	v_or_b32_e32 v7, v118, v81
	ds_write_b64 v6, v[2:3]
	v_cvt_pk_f16_f32 v3, v44, v45
	v_cvt_pk_f16_f32 v2, v42, v43
	v_mad_u32_u24 v7, v7, s4, v80
	ds_write_b64 v7, v[2:3]
	v_cvt_pk_f16_f32 v3, v12, v13
	v_cvt_pk_f16_f32 v2, v10, v11
	ds_write_b64 v4, v[2:3] offset:32
	v_cvt_pk_f16_f32 v3, v36, v37
	v_cvt_pk_f16_f32 v2, v34, v35
	ds_write_b64 v5, v[2:3] offset:32
	v_cvt_pk_f16_f32 v3, v16, v17
	v_cvt_pk_f16_f32 v2, v14, v15
	v_lshl_add_u64 v[10:11], v[60:61], 0, s[14:15]
	ds_write_b64 v6, v[2:3] offset:32
	v_cvt_pk_f16_f32 v2, v18, v19
	v_add_co_u32_e32 v18, vcc, s52, v10
	v_cvt_pk_f16_f32 v3, v20, v21
	v_lshl_add_u64 v[12:13], v[60:61], 0, s[16:17]
	v_addc_co_u32_e32 v19, vcc, 0, v11, vcc
	ds_write_b64 v7, v[2:3] offset:32
	s_waitcnt lgkmcnt(0)
	s_barrier
	global_load_dwordx4 v[2:5], v[10:11], off
	global_load_dwordx4 v[6:9], v[12:13], off
	v_lshl_add_u64 v[20:21], v[60:61], 0, s[12:13]
	global_load_dwordx4 v[10:13], v[18:19], off
	global_load_dwordx4 v[14:17], v[20:21], off
	ds_read_b128 v[18:21], v1
	ds_read_b128 v[22:25], v1 offset:8448
	s_mov_b32 s3, s27
	s_setprio 1
	s_waitcnt vmcnt(17) lgkmcnt(1)
	v_mfma_f32_16x16x32_f16 v[26:29], v[18:21], v[54:57], 0
	s_waitcnt lgkmcnt(0)
	v_mfma_f32_16x16x32_f16 v[30:33], v[22:25], v[54:57], 0
	s_waitcnt vmcnt(9)
	v_mfma_f32_16x16x32_f16 v[34:37], v[18:21], v[100:103], 0
	v_mfma_f32_16x16x32_f16 v[38:41], v[22:25], v[100:103], 0
	v_mfma_f32_16x16x32_f16 v[42:45], v[18:21], v[46:49], 0
	v_mfma_f32_16x16x32_f16 v[46:49], v[22:25], v[46:49], 0
	v_mfma_f32_16x16x32_f16 v[18:21], v[18:21], v[50:53], 0
	v_mfma_f32_16x16x32_f16 v[22:25], v[22:25], v[50:53], 0
	s_setprio 0
	v_lshl_add_u64 v[58:59], v[60:61], 0, s[10:11]
	v_add_co_u32_e32 v76, vcc, s29, v58
	s_nop 1
	v_addc_co_u32_e32 v77, vcc, 0, v59, vcc
	v_add_co_u32_e32 v108, vcc, s52, v58
	global_load_dwordx4 v[50:53], v[58:59], off
	global_load_dwordx4 v[54:57], v[76:77], off
	v_addc_co_u32_e32 v109, vcc, 0, v59, vcc
	v_add_co_u32_e32 v58, vcc, s33, v58
	s_nop 1
	v_addc_co_u32_e32 v59, vcc, 0, v59, vcc
	global_load_dwordx4 v[76:79], v[108:109], off
	global_load_dwordx4 v[100:103], v[58:59], off
	ds_read_b128 v[108:111], v82
	ds_read_b128 v[112:115], v82 offset:8448
	s_setprio 1
	s_waitcnt lgkmcnt(1)
	v_mfma_f32_16x16x32_f16 v[26:29], v[108:111], v[62:65], v[26:29]
	s_waitcnt lgkmcnt(0)
	v_mfma_f32_16x16x32_f16 v[30:33], v[112:115], v[62:65], v[30:33]
	v_mfma_f32_16x16x32_f16 v[34:37], v[108:111], v[68:71], v[34:37]
	v_mfma_f32_16x16x32_f16 v[38:41], v[112:115], v[68:71], v[38:41]
	v_mfma_f32_16x16x32_f16 v[42:45], v[108:111], v[92:95], v[42:45]
	v_mfma_f32_16x16x32_f16 v[46:49], v[112:115], v[92:95], v[46:49]
	v_mfma_f32_16x16x32_f16 v[18:21], v[108:111], v[72:75], v[18:21]
	v_mfma_f32_16x16x32_f16 v[22:25], v[112:115], v[72:75], v[22:25]
	s_setprio 0
	v_lshl_add_u64 v[58:59], v[60:61], 0, s[48:49]
	v_lshl_add_u64 v[72:73], v[60:61], 0, s[50:51]
	global_load_dwordx4 v[62:65], v[58:59], off
	global_load_dwordx4 v[68:71], v[72:73], off
	v_add_co_u32_e32 v58, vcc, s52, v58
	v_lshl_add_u64 v[82:83], v[60:61], 0, s[46:47]
	s_nop 0
	v_addc_co_u32_e32 v59, vcc, 0, v59, vcc
	global_load_dwordx4 v[72:75], v[58:59], off
	global_load_dwordx4 v[92:95], v[82:83], off
	ds_read_b128 v[108:111], v172
	ds_read_b128 v[112:115], v172 offset:8448
	s_setprio 1
	s_waitcnt lgkmcnt(1)
	v_mfma_f32_16x16x32_f16 v[26:29], v[108:111], v[84:87], v[26:29]
	s_waitcnt lgkmcnt(0)
	v_mfma_f32_16x16x32_f16 v[30:33], v[112:115], v[84:87], v[30:33]
	v_mfma_f32_16x16x32_f16 v[34:37], v[108:111], v[88:91], v[34:37]
	v_mfma_f32_16x16x32_f16 v[38:41], v[112:115], v[88:91], v[38:41]
	v_mfma_f32_16x16x32_f16 v[42:45], v[108:111], v[96:99], v[42:45]
	v_mfma_f32_16x16x32_f16 v[46:49], v[112:115], v[96:99], v[46:49]
	s_waitcnt vmcnt(16)
	v_mfma_f32_16x16x32_f16 v[18:21], v[108:111], v[104:107], v[18:21]
	v_mfma_f32_16x16x32_f16 v[22:25], v[112:115], v[104:107], v[22:25]
	s_setprio 0
	v_lshl_add_u64 v[58:59], v[60:61], 0, s[42:43]
	v_lshl_add_u64 v[90:91], v[60:61], 0, s[44:45]
	global_load_dwordx4 v[82:85], v[58:59], off
	global_load_dwordx4 v[86:89], v[90:91], off
	v_add_co_u32_e32 v58, vcc, s52, v58
	v_lshl_add_u64 v[90:91], v[60:61], 0, s[40:41]
	s_nop 0
	v_addc_co_u32_e32 v59, vcc, 0, v59, vcc
	global_load_dwordx4 v[96:99], v[58:59], off
	global_load_dwordx4 v[104:107], v[90:91], off
	ds_read_b128 v[108:111], v173
	ds_read_b128 v[112:115], v173 offset:8448
	s_setprio 1
	s_waitcnt vmcnt(15) lgkmcnt(1)
	v_mfma_f32_16x16x32_f16 v[26:29], v[108:111], v[2:5], v[26:29]
	s_waitcnt lgkmcnt(0)
	v_mfma_f32_16x16x32_f16 v[2:5], v[112:115], v[2:5], v[30:33]
	s_waitcnt vmcnt(14)
	v_mfma_f32_16x16x32_f16 v[30:33], v[108:111], v[6:9], v[34:37]
	v_mfma_f32_16x16x32_f16 v[6:9], v[112:115], v[6:9], v[38:41]
	s_waitcnt vmcnt(13)
	v_mfma_f32_16x16x32_f16 v[34:37], v[108:111], v[10:13], v[42:45]
	v_mfma_f32_16x16x32_f16 v[10:13], v[112:115], v[10:13], v[46:49]
	s_waitcnt vmcnt(12)
	v_mfma_f32_16x16x32_f16 v[18:21], v[108:111], v[14:17], v[18:21]
	v_mfma_f32_16x16x32_f16 v[14:17], v[112:115], v[14:17], v[22:25]
	s_setprio 0
	v_lshl_add_u64 v[42:43], v[60:61], 0, s[8:9]
	v_add_co_u32_e32 v58, vcc, s52, v42
	v_lshl_add_u64 v[44:45], v[60:61], 0, s[38:39]
	s_nop 0
	v_addc_co_u32_e32 v59, vcc, 0, v43, vcc
	global_load_dwordx4 v[22:25], v[42:43], off
	global_load_dwordx4 v[38:41], v[44:45], off
	v_lshl_add_u64 v[60:61], v[60:61], 0, s[6:7]
	global_load_dwordx4 v[42:45], v[58:59], off
	global_load_dwordx4 v[46:49], v[60:61], off
	ds_read_b128 v[58:61], v174
	ds_read_b128 v[108:111], v174 offset:8448
	s_setprio 1
	s_waitcnt vmcnt(15) lgkmcnt(1)
	v_mfma_f32_16x16x32_f16 v[26:29], v[58:61], v[50:53], v[26:29]
	s_waitcnt lgkmcnt(0)
	v_mfma_f32_16x16x32_f16 v[2:5], v[108:111], v[50:53], v[2:5]
	s_waitcnt vmcnt(14)
	v_mfma_f32_16x16x32_f16 v[30:33], v[58:61], v[54:57], v[30:33]
	v_mfma_f32_16x16x32_f16 v[6:9], v[108:111], v[54:57], v[6:9]
	s_waitcnt vmcnt(13)
	v_mfma_f32_16x16x32_f16 v[34:37], v[58:61], v[76:79], v[34:37]
	v_mfma_f32_16x16x32_f16 v[10:13], v[108:111], v[76:79], v[10:13]
	s_waitcnt vmcnt(12)
	v_mfma_f32_16x16x32_f16 v[18:21], v[58:61], v[100:103], v[18:21]
	v_mfma_f32_16x16x32_f16 v[14:17], v[108:111], v[100:103], v[14:17]
	s_setprio 0
	ds_read_b128 v[50:53], v175
	ds_read_b128 v[54:57], v175 offset:8448
	s_setprio 1
	s_waitcnt vmcnt(11) lgkmcnt(1)
	v_mfma_f32_16x16x32_f16 v[26:29], v[50:53], v[62:65], v[26:29]
	s_waitcnt lgkmcnt(0)
	v_mfma_f32_16x16x32_f16 v[2:5], v[54:57], v[62:65], v[2:5]
	s_waitcnt vmcnt(10)
	v_mfma_f32_16x16x32_f16 v[30:33], v[50:53], v[68:71], v[30:33]
	v_mfma_f32_16x16x32_f16 v[6:9], v[54:57], v[68:71], v[6:9]
	s_waitcnt vmcnt(9)
	v_mfma_f32_16x16x32_f16 v[34:37], v[50:53], v[72:75], v[34:37]
	v_mfma_f32_16x16x32_f16 v[10:13], v[54:57], v[72:75], v[10:13]
	s_waitcnt vmcnt(8)
	v_mfma_f32_16x16x32_f16 v[18:21], v[50:53], v[92:95], v[18:21]
	v_mfma_f32_16x16x32_f16 v[14:17], v[54:57], v[92:95], v[14:17]
	s_setprio 0
	ds_read_b128 v[50:53], v176
	ds_read_b128 v[54:57], v176 offset:8448
	s_setprio 1
	s_waitcnt vmcnt(7) lgkmcnt(1)
	v_mfma_f32_16x16x32_f16 v[26:29], v[50:53], v[82:85], v[26:29]
	s_waitcnt lgkmcnt(0)
	v_mfma_f32_16x16x32_f16 v[2:5], v[54:57], v[82:85], v[2:5]
	s_waitcnt vmcnt(6)
	v_mfma_f32_16x16x32_f16 v[30:33], v[50:53], v[86:89], v[30:33]
	v_mfma_f32_16x16x32_f16 v[6:9], v[54:57], v[86:89], v[6:9]
	s_waitcnt vmcnt(5)
	v_mfma_f32_16x16x32_f16 v[34:37], v[50:53], v[96:99], v[34:37]
	v_mfma_f32_16x16x32_f16 v[58:61], v[54:57], v[96:99], v[10:13]
	s_waitcnt vmcnt(4)
	v_mfma_f32_16x16x32_f16 v[18:21], v[50:53], v[104:107], v[18:21]
	v_mfma_f32_16x16x32_f16 v[50:53], v[54:57], v[104:107], v[14:17]
	s_setprio 0
	ds_read_b128 v[54:57], v177
	ds_read_b128 v[62:65], v177 offset:8448
	s_setprio 1
	s_waitcnt vmcnt(3) lgkmcnt(1)
	v_mfma_f32_16x16x32_f16 v[26:29], v[54:57], v[22:25], v[26:29]
	s_waitcnt lgkmcnt(0)
	v_mfma_f32_16x16x32_f16 v[14:17], v[62:65], v[22:25], v[2:5]
	s_waitcnt vmcnt(2)
	v_mfma_f32_16x16x32_f16 v[22:25], v[54:57], v[38:41], v[30:33]
	v_mfma_f32_16x16x32_f16 v[10:13], v[62:65], v[38:41], v[6:9]
	s_waitcnt vmcnt(1)
	v_mfma_f32_16x16x32_f16 v[30:33], v[54:57], v[42:45], v[34:37]
	v_mfma_f32_16x16x32_f16 v[6:9], v[62:65], v[42:45], v[58:61]
	s_waitcnt vmcnt(0)
	v_mfma_f32_16x16x32_f16 v[34:37], v[54:57], v[46:49], v[18:21]
	v_mfma_f32_16x16x32_f16 v[2:5], v[62:65], v[46:49], v[50:53]
	s_setprio 0
	s_nop 1
	v_mul_u32_u24_e32 v52, 0x50, v0
	ds_read_b128 v[18:21], v52
	s_lshl_b64 s[2:3], s[2:3], 15
	v_or_b32_e32 v0, s2, v66
	v_mov_b32_e32 v1, s3
	v_lshl_add_u64 v[50:51], s[24:25], 0, v[0:1]
	ds_read_b128 v[38:41], v52 offset:16
	ds_read_b128 v[42:45], v52 offset:32
	ds_read_b128 v[46:49], v52 offset:48
	s_waitcnt lgkmcnt(3)
	global_store_dwordx4 v[50:51], v[18:21], off sc1
	s_nop 1
	v_add_co_u32_e32 v18, vcc, s29, v50
	s_nop 1
	v_addc_co_u32_e32 v19, vcc, 0, v51, vcc
	s_waitcnt lgkmcnt(2)
	global_store_dwordx4 v[18:19], v[38:41], off sc1
	v_or_b32_e32 v18, 0x4000, v0
	v_mov_b32_e32 v19, s3
	v_lshl_add_u64 v[20:21], s[24:25], 0, v[18:19]
	s_waitcnt lgkmcnt(1)
	global_store_dwordx4 v[20:21], v[42:45], off sc1
	v_mul_f32_e32 v20, 0xbfb8aa3b, v26
	v_exp_f32_e32 v38, v20
	v_add_co_u32_e32 v20, vcc, s33, v50
	v_or_b32_e32 v39, 0x200, v81
	s_nop 0
	v_addc_co_u32_e32 v21, vcc, 0, v51, vcc
	s_waitcnt lgkmcnt(0)
	global_store_dwordx4 v[20:21], v[46:49], off sc1
	v_add_f32_e32 v20, 1.0, v38
	v_rcp_f32_e32 v20, v20
	v_mul_f32_e32 v21, 0xbfb8aa3b, v27
	v_mul_f32_e32 v38, 0xbfb8aa3b, v28
	v_exp_f32_e32 v21, v21
	v_exp_f32_e32 v38, v38
	v_fma_mixlo_f16 v40, v26, v20, 0
	v_mul_f32_e32 v26, 0xbfb8aa3b, v29
	v_add_f32_e32 v20, 1.0, v21
	v_add_f32_e32 v21, 1.0, v38
	v_exp_f32_e32 v38, v26
	v_rcp_f32_e32 v20, v20
	v_rcp_f32_e32 v21, v21
	v_mov_b32_e32 v26, v27
	v_mov_b32_e32 v27, v28
	v_add_f32_e32 v28, 1.0, v38
	v_rcp_f32_e32 v28, v28
	v_pk_mul_f32 v[20:21], v[26:27], v[20:21]
	v_or_b32_e32 v27, v39, v67
	v_cvt_pk_f16_f32 v21, v20, v21
	v_fma_mixlo_f16 v26, v29, v28, 0
	v_pack_b32_f16 v20, v40, v21
	v_alignbit_b32 v21, v26, v21, 16
	v_mul_f32_e32 v26, 0xbfb8aa3b, v22
	v_exp_f32_e32 v26, v26
	v_mad_u32_u24 v27, v27, s4, v80
	ds_write_b64 v27, v[20:21]
	v_mul_f32_e32 v21, 0xbfb8aa3b, v23
	v_add_f32_e32 v20, 1.0, v26
	v_rcp_f32_e32 v20, v20
	v_mul_f32_e32 v26, 0xbfb8aa3b, v24
	v_exp_f32_e32 v21, v21
	v_exp_f32_e32 v26, v26
	v_fma_mixlo_f16 v28, v22, v20, 0
	v_mul_f32_e32 v22, 0xbfb8aa3b, v25
	v_add_f32_e32 v20, 1.0, v21
	v_add_f32_e32 v21, 1.0, v26
	v_exp_f32_e32 v26, v22
	v_rcp_f32_e32 v20, v20
	v_rcp_f32_e32 v21, v21
	v_mov_b32_e32 v22, v23
	v_mov_b32_e32 v23, v24
	v_add_f32_e32 v24, 1.0, v26
	v_rcp_f32_e32 v24, v24
	v_pk_mul_f32 v[20:21], v[22:23], v[20:21]
	v_or_b32_e32 v23, v116, v39
	v_cvt_pk_f16_f32 v21, v20, v21
	v_fma_mixlo_f16 v22, v25, v24, 0
	v_pack_b32_f16 v20, v28, v21
	v_alignbit_b32 v21, v22, v21, 16
	v_mul_f32_e32 v22, 0xbfb8aa3b, v30
	v_exp_f32_e32 v22, v22
	v_mad_u32_u24 v24, v23, s4, v80
	ds_write_b64 v24, v[20:21]
	v_mul_f32_e32 v21, 0xbfb8aa3b, v31
	v_add_f32_e32 v20, 1.0, v22
	v_mul_f32_e32 v22, 0xbfb8aa3b, v32
	v_rcp_f32_e32 v20, v20
	v_exp_f32_e32 v21, v21
	v_exp_f32_e32 v22, v22
	v_mov_b32_e32 v23, v32
	v_fma_mixlo_f16 v25, v30, v20, 0
	v_add_f32_e32 v20, 1.0, v21
	v_add_f32_e32 v21, 1.0, v22
	v_mul_f32_e32 v22, 0xbfb8aa3b, v33
	v_exp_f32_e32 v26, v22
	v_rcp_f32_e32 v20, v20
	v_rcp_f32_e32 v21, v21
	v_mov_b32_e32 v22, v31
	v_add_f32_e32 v26, 1.0, v26
	v_rcp_f32_e32 v26, v26
	v_pk_mul_f32 v[20:21], v[22:23], v[20:21]
	v_or_b32_e32 v23, v117, v39
	v_cvt_pk_f16_f32 v21, v20, v21
	v_fma_mixlo_f16 v22, v33, v26, 0
	v_pack_b32_f16 v20, v25, v21
	v_alignbit_b32 v21, v22, v21, 16
	v_mul_f32_e32 v22, 0xbfb8aa3b, v34
	v_exp_f32_e32 v22, v22
	v_mad_u32_u24 v25, v23, s4, v80
	ds_write_b64 v25, v[20:21]
	v_mul_f32_e32 v21, 0xbfb8aa3b, v35
	v_add_f32_e32 v20, 1.0, v22
	v_mul_f32_e32 v22, 0xbfb8aa3b, v36
	v_rcp_f32_e32 v20, v20
	v_exp_f32_e32 v21, v21
	v_exp_f32_e32 v22, v22
	v_mov_b32_e32 v23, v36
	v_fma_mixlo_f16 v26, v34, v20, 0
	v_add_f32_e32 v20, 1.0, v21
	v_add_f32_e32 v21, 1.0, v22
	v_mul_f32_e32 v22, 0xbfb8aa3b, v37
	v_exp_f32_e32 v28, v22
	v_rcp_f32_e32 v20, v20
	v_rcp_f32_e32 v21, v21
	v_mov_b32_e32 v22, v35
	v_add_f32_e32 v28, 1.0, v28
	v_rcp_f32_e32 v28, v28
	v_pk_mul_f32 v[20:21], v[22:23], v[20:21]
	v_or_b32_e32 v23, v118, v39
	v_cvt_pk_f16_f32 v21, v20, v21
	v_fma_mixlo_f16 v22, v37, v28, 0
	v_pack_b32_f16 v20, v26, v21
	v_alignbit_b32 v21, v22, v21, 16
	v_mul_f32_e32 v22, 0xbfb8aa3b, v14
	v_exp_f32_e32 v22, v22
	v_mad_u32_u24 v23, v23, s4, v80
	ds_write_b64 v23, v[20:21]
	v_mul_f32_e32 v21, 0xbfb8aa3b, v15
	v_add_f32_e32 v20, 1.0, v22
	v_rcp_f32_e32 v20, v20
	v_exp_f32_e32 v21, v21
	v_mul_f32_e32 v22, 0xbfb8aa3b, v16
	v_exp_f32_e32 v22, v22
	v_fma_mixlo_f16 v26, v14, v20, 0
	v_add_f32_e32 v14, 1.0, v21
	v_rcp_f32_e32 v20, v14
	v_add_f32_e32 v14, 1.0, v22
	v_rcp_f32_e32 v21, v14
	v_mov_b32_e32 v14, v15
	v_mul_f32_e32 v15, 0xbfb8aa3b, v17
	v_exp_f32_e32 v22, v15
	v_mov_b32_e32 v15, v16
	v_pk_mul_f32 v[14:15], v[14:15], v[20:21]
	v_mul_f32_e32 v20, 0xbfb8aa3b, v10
	v_cvt_pk_f16_f32 v15, v14, v15
	v_add_f32_e32 v14, 1.0, v22
	v_rcp_f32_e32 v16, v14
	v_exp_f32_e32 v20, v20
	v_pack_b32_f16 v14, v26, v15
	v_lshl_add_u64 v[0:1], s[0:1], 0, v[0:1]
	v_fma_mixlo_f16 v16, v17, v16, 0
	v_alignbit_b32 v15, v16, v15, 16
	ds_write_b64 v27, v[14:15] offset:32
	v_add_f32_e32 v14, 1.0, v20
	v_mul_f32_e32 v15, 0xbfb8aa3b, v11
	v_rcp_f32_e32 v14, v14
	v_exp_f32_e32 v15, v15
	v_mul_f32_e32 v16, 0xbfb8aa3b, v12
	v_exp_f32_e32 v16, v16
	v_fma_mixlo_f16 v17, v10, v14, 0
	v_add_f32_e32 v10, 1.0, v15
	v_rcp_f32_e32 v14, v10
	v_add_f32_e32 v10, 1.0, v16
	v_rcp_f32_e32 v15, v10
	v_mov_b32_e32 v10, v11
	v_mul_f32_e32 v11, 0xbfb8aa3b, v13
	v_exp_f32_e32 v16, v11
	v_mov_b32_e32 v11, v12
	v_pk_mul_f32 v[10:11], v[10:11], v[14:15]
	v_mul_f32_e32 v14, 0xbfb8aa3b, v6
	v_cvt_pk_f16_f32 v11, v10, v11
	v_add_f32_e32 v10, 1.0, v16
	v_rcp_f32_e32 v12, v10
	v_exp_f32_e32 v14, v14
	v_pack_b32_f16 v10, v17, v11
	v_fma_mixlo_f16 v12, v13, v12, 0
	v_alignbit_b32 v11, v12, v11, 16
	ds_write_b64 v24, v[10:11] offset:32
	v_add_f32_e32 v10, 1.0, v14
	v_mul_f32_e32 v11, 0xbfb8aa3b, v7
	v_rcp_f32_e32 v10, v10
	v_exp_f32_e32 v11, v11
	v_mul_f32_e32 v12, 0xbfb8aa3b, v8
	v_exp_f32_e32 v12, v12
	v_fma_mixlo_f16 v13, v6, v10, 0
	v_add_f32_e32 v6, 1.0, v11
	v_rcp_f32_e32 v10, v6
	v_add_f32_e32 v6, 1.0, v12
	v_rcp_f32_e32 v11, v6
	v_mov_b32_e32 v6, v7
	v_mul_f32_e32 v7, 0xbfb8aa3b, v9
	v_exp_f32_e32 v12, v7
	v_mov_b32_e32 v7, v8
	v_pk_mul_f32 v[6:7], v[6:7], v[10:11]
	v_mul_f32_e32 v10, 0xbfb8aa3b, v2
	v_cvt_pk_f16_f32 v7, v6, v7
	v_add_f32_e32 v6, 1.0, v12
	v_rcp_f32_e32 v8, v6
	v_exp_f32_e32 v10, v10
	v_pack_b32_f16 v6, v13, v7
	v_fma_mixlo_f16 v8, v9, v8, 0
	v_alignbit_b32 v7, v8, v7, 16
	ds_write_b64 v25, v[6:7] offset:32
	v_add_f32_e32 v6, 1.0, v10
	v_mul_f32_e32 v7, 0xbfb8aa3b, v3
	v_rcp_f32_e32 v6, v6
	v_exp_f32_e32 v7, v7
	v_mul_f32_e32 v8, 0xbfb8aa3b, v4
	v_exp_f32_e32 v8, v8
	v_fma_mixlo_f16 v9, v2, v6, 0
	v_add_f32_e32 v2, 1.0, v7
	v_mul_f32_e32 v7, 0xbfb8aa3b, v5
	v_rcp_f32_e32 v6, v2
	v_add_f32_e32 v2, 1.0, v8
	v_exp_f32_e32 v8, v7
	v_rcp_f32_e32 v7, v2
	v_mov_b32_e32 v2, v3
	v_mov_b32_e32 v3, v4
	v_add_f32_e32 v4, 1.0, v8
	v_rcp_f32_e32 v4, v4
	v_pk_mul_f32 v[2:3], v[2:3], v[6:7]
	v_fma_mixlo_f16 v4, v5, v4, 0
	v_cvt_pk_f16_f32 v3, v2, v3
	v_pack_b32_f16 v2, v9, v3
	v_alignbit_b32 v3, v4, v3, 16
	ds_write_b64 v23, v[2:3] offset:32
	s_waitcnt lgkmcnt(0)
	s_barrier
	ds_read_b128 v[2:5], v52 offset:40960
	ds_read_b128 v[6:9], v52 offset:40976
	ds_read_b128 v[10:13], v52 offset:40992
	ds_read_b128 v[14:17], v52 offset:41008
	s_waitcnt lgkmcnt(3)
	global_store_dwordx4 v[0:1], v[2:5], off sc1
	s_nop 1
	v_add_co_u32_e32 v2, vcc, 0x2000, v0
	s_nop 1
	v_addc_co_u32_e32 v3, vcc, 0, v1, vcc
	v_add_co_u32_e32 v0, vcc, 0x6000, v0
	s_waitcnt lgkmcnt(2)
	global_store_dwordx4 v[2:3], v[6:9], off sc1
	v_lshl_add_u64 v[2:3], s[0:1], 0, v[18:19]
	v_addc_co_u32_e32 v1, vcc, 0, v1, vcc
	s_waitcnt lgkmcnt(1)
	global_store_dwordx4 v[2:3], v[10:13], off sc1
	s_waitcnt lgkmcnt(0)
	global_store_dwordx4 v[0:1], v[14:17], off sc1
	s_endpgm
	.p2align	8
